# speedup vs baseline: 1.0287x; 1.0287x over previous
_Z16closed_form_mainPKfS0_PKiPf:
	s_load_dwordx8 s[16:23], s[0:1], 0x0
	s_lshr_b32 s6, s2, 3
	v_readfirstlane_b32 s0, v0
	s_mul_hi_u32 s7, s6, 0x24924925
	s_lshr_b32 s4, s0, 6
	s_and_b32 s0, s2, 7
	s_mul_i32 s1, s7, 7
	s_bfe_u32 s5, s2, 0x10003
	s_sub_i32 s1, s6, s1
	s_mul_i32 s36, s0, 7
	s_xor_b32 s3, s4, s5
	s_add_i32 s36, s36, s1
	s_waitcnt lgkmcnt(0)
	s_mov_b64 s[28:29], s[22:23]
	v_and_b32_e32 v19, 63, v0
	s_cmp_lt_u32 s36, 52
	s_mov_b64 s[0:1], -1
	s_cbranch_scc0 .LBB0_32
	s_mul_hi_u32 s0, s6, 0x20820821
	s_lshr_b32 s38, s0, 3
	s_mul_hi_u32 s0, s7, 0x1c71c71d
	s_mul_i32 s0, s0, 9
	s_sub_i32 s0, s7, s0
	v_add_u32_e32 v2, -3, v19
	v_mad_u64_u32 v[0:1], s[0:1], s0, 57, v[2:3]
	s_mov_b64 s[24:25], s[18:19]
	v_mov_b32_e32 v1, 0x200
	v_med3_i32 v1, v0, 0, v1
	s_mul_i32 s34, s36, 10
	s_and_b32 s17, s17, 0xffff
	s_and_b32 s25, s25, 0xffff
	v_cmp_gt_u32_e64 s[0:1], 57, v2
	s_mov_b32 s19, 0x20000
	s_mov_b32 s18, 0xe0e038
	s_mov_b32 s26, 0x606018
	s_mul_i32 s35, s38, 0x70701c
	s_mul_i32 s33, s38, 0x30300c
	v_lshlrev_b32_e32 v28, 2, v1
	v_mul_u32_u24_e32 v27, 12, v1
	v_lshlrev_b32_e32 v23, 4, v19
	s_cmp_lg_u32 s4, s5
	v_sub_u32_e64 v29, s34, 2 clamp
	s_cbranch_scc0 .LBB0_15
	s_mov_b32 s27, s19
	s_and_b32 s21, s21, 0xffff
	s_mov_b32 s22, 0x202008
	s_mov_b32 s23, s19
	s_mul_i32 s38, s38, 0x101004
	s_movk_i32 s37, 0x80
	v_add_u32_e32 v18, -1, v0
	s_movk_i32 s4, 0x201
	s_movk_i32 s5, 0x1ff
	v_cmp_gt_u32_e64 s[40:41], s4, v0
	v_cmp_gt_u32_e64 s[42:43], s5, v18
	v_mov_b32_e32 v18, 0x42c80000
	v_mov_b32_e32 v22, 0x3de38e39
	v_mov_b32_e32 v26, 0x3a3d6628
	v_mov_b32_e32 v1, 0
	s_add_i32 s4, s34, -3
	s_max_i32 s4, s4, 0
	s_mul_i32 s4, s4, 0x804
	s_add_i32 s4, s4, s38
	buffer_load_dword v29, v28, s[20:23], s4 offen nt
	s_add_i32 s4, s34, -2
	s_max_i32 s4, s4, 0
	s_mul_i32 s4, s4, 0x804
	s_add_i32 s4, s4, s38
	buffer_load_dword v2, v28, s[20:23], s4 offen nt
	s_add_i32 s5, s34, -2
	s_max_i32 s5, s5, 0
	s_mul_i32 s6, s5, 0x804
	s_add_i32 s6, s6, s35
	s_add_i32 s7, s6, 0x505014
	s_add_i32 s8, s6, 0x606018
	s_mul_i32 s9, s5, 0x180c
	s_add_i32 s9, s9, s33
	s_add_i32 s4, s34, -1
	s_max_i32 s4, s4, 0
	s_mul_i32 s4, s4, 0x804
	s_add_i32 s4, s4, s38
	buffer_load_dword v3, v28, s[20:23], s4 offen nt
	buffer_load_dwordx3 v[8:10], v27, s[24:27], s9 offen nt
	buffer_load_dword v4, v28, s[16:19], s7 offen nt
	buffer_load_dword v5, v28, s[16:19], s8 offen nt
	s_add_i32 s5, s34, -1
	s_max_i32 s5, s5, 0
	s_mul_i32 s6, s5, 0x804
	s_add_i32 s6, s6, s35
	s_add_i32 s7, s6, 0x505014
	s_add_i32 s8, s6, 0x606018
	s_mul_i32 s9, s5, 0x180c
	s_add_i32 s9, s9, s33
	s_add_i32 s4, s34, 0
	s_min_i32 s4, s4, 0x200
	s_mul_i32 s4, s4, 0x804
	s_add_i32 s4, s4, s38
	buffer_load_dword v16, v28, s[20:23], s4 offen nt
	buffer_load_dwordx3 v[12:14], v27, s[24:27], s9 offen nt
	buffer_load_dword v6, v28, s[16:19], s7 offen nt
	buffer_load_dword v7, v28, s[16:19], s8 offen nt
	s_waitcnt vmcnt(8)
	s_add_i32 s4, s34, -3
	s_cmpk_lt_u32 s4, 0x201
	s_cselect_b64 s[12:13], s[40:41], 0
	v_cmp_eq_u32_e64 s[14:15], s37, v29
	s_and_b64 s[14:15], s[14:15], s[12:13]
	v_cndmask_b32_e64 v17, 0, 1, s[14:15]
	s_add_i32 s4, s34, -2
	s_cmpk_lt_u32 s4, 0x201
	s_cselect_b64 s[12:13], s[40:41], 0
	v_cmp_eq_u32_e64 s[14:15], s37, v2
	s_and_b64 s[14:15], s[14:15], s[12:13]
	v_cndmask_b32_e64 v20, 0, 1, s[14:15]
	s_nop 0
	v_or_b32_dpp v21, v17, v17 wave_shr:1 row_mask:0xf bank_mask:0xf bound_ctrl:1
	v_or_b32_dpp v24, v20, v20 wave_shr:1 row_mask:0xf bank_mask:0xf bound_ctrl:1
	s_nop 1
	v_or_b32_dpp v21, v17, v21 wave_shl:1 row_mask:0xf bank_mask:0xf bound_ctrl:1
	v_or_b32_dpp v24, v20, v24 wave_shl:1 row_mask:0xf bank_mask:0xf bound_ctrl:1
	s_nop 1
	v_or_b32_dpp v25, v21, v21 wave_shr:1 row_mask:0xf bank_mask:0xf bound_ctrl:1
	v_or_b32_dpp v30, v24, v24 wave_shr:1 row_mask:0xf bank_mask:0xf bound_ctrl:1
	s_nop 1
	v_or_b32_dpp v25, v21, v25 wave_shl:1 row_mask:0xf bank_mask:0xf bound_ctrl:1
	v_or_b32_dpp v30, v24, v30 wave_shl:1 row_mask:0xf bank_mask:0xf bound_ctrl:1
	v_mov_b32_e32 v17, 0
	v_mov_b32_e32 v24, 0
	s_add_i32 s5, s34, 0
	s_min_i32 s5, s5, 0x200
	s_mul_i32 s6, s5, 0x804
	s_add_i32 s6, s6, s35
	s_add_i32 s7, s6, 0x505014
	s_add_i32 s8, s6, 0x606018
	s_mul_i32 s9, s5, 0x180c
	s_add_i32 s9, s9, s33
	s_add_i32 s4, s34, 1
	s_min_i32 s4, s4, 0x200
	s_mul_i32 s4, s4, 0x804
	s_add_i32 s4, s4, s38
	buffer_load_dword v31, v28, s[20:23], s4 offen nt
	buffer_load_dwordx3 v[32:34], v27, s[24:27], s9 offen nt
	buffer_load_dword v20, v28, s[16:19], s7 offen nt
	buffer_load_dword v21, v28, s[16:19], s8 offen nt
	s_waitcnt vmcnt(8)
	v_mov_b32_dpp v36, v8 wave_shr:1 row_mask:0xf bank_mask:0xf bound_ctrl:1
	v_mov_b32_dpp v37, v9 wave_shr:1 row_mask:0xf bank_mask:0xf bound_ctrl:1
	v_mov_b32_dpp v38, v10 wave_shr:1 row_mask:0xf bank_mask:0xf bound_ctrl:1
	v_mov_b32_dpp v40, v8 wave_shl:1 row_mask:0xf bank_mask:0xf bound_ctrl:1
	v_mov_b32_dpp v41, v9 wave_shl:1 row_mask:0xf bank_mask:0xf bound_ctrl:1
	v_mov_b32_dpp v42, v10 wave_shl:1 row_mask:0xf bank_mask:0xf bound_ctrl:1
	s_add_i32 s4, s34, -1
	s_cmpk_lt_u32 s4, 0x201
	s_cselect_b64 s[12:13], s[40:41], 0
	v_cmp_eq_u32_e64 s[14:15], s37, v3
	s_and_b64 s[14:15], s[14:15], s[12:13]
	v_cndmask_b32_e64 v44, 0, 1, s[14:15]
	v_mul_f32_e64 v46, v8, v8
	v_mul_f32_e64 v47, v8, v9
	v_mul_f32_e64 v48, v8, v10
	v_mul_f32_e64 v49, v9, v9
	v_mul_f32_e64 v50, v9, v10
	v_mul_f32_e64 v51, v10, v10
	v_or_b32_dpp v45, v44, v44 wave_shr:1 row_mask:0xf bank_mask:0xf bound_ctrl:1
	s_nop 1
	v_or_b32_dpp v45, v44, v45 wave_shl:1 row_mask:0xf bank_mask:0xf bound_ctrl:1
	s_nop 1
	v_or_b32_dpp v52, v45, v45 wave_shr:1 row_mask:0xf bank_mask:0xf bound_ctrl:1
	s_nop 1
	v_or_b32_dpp v52, v45, v52 wave_shl:1 row_mask:0xf bank_mask:0xf bound_ctrl:1
	v_or3_b32 v53, v52, v30, v25
	v_or3_b32 v53, v53, v17, v24
	s_add_i32 s4, s34, -4
	s_cmpk_lt_u32 s4, 0x1ff
	s_cselect_b64 s[12:13], s[42:43], 0
	v_cmp_ne_u32_e64 s[30:31], 0, v53
	s_and_b64 s[30:31], s[30:31], s[12:13]
	v_cndmask_b32_e64 v53, 0, 1.0, s[30:31]
	v_add_f32_e64 v44, v8, v36
	v_add_f32_e64 v45, v9, v37
	v_add_f32_e64 v54, v10, v38
	v_fma_f32 v46, v36, v36, v46
	v_fma_f32 v47, v36, v37, v47
	v_fma_f32 v48, v36, v38, v48
	v_fma_f32 v49, v37, v37, v49
	v_fma_f32 v50, v37, v38, v50
	v_fma_f32 v51, v38, v38, v51
	v_add_f32_dpp v61, v53, v53 wave_shr:1 row_mask:0xf bank_mask:0xf bound_ctrl:1
	v_add_f32_e64 v44, v44, v40
	v_add_f32_e64 v45, v45, v41
	v_add_f32_e64 v54, v54, v42
	v_fma_f32 v55, v40, v40, v46
	v_fma_f32 v56, v40, v41, v47
	v_fma_f32 v57, v40, v42, v48
	v_fma_f32 v58, v41, v41, v49
	v_fma_f32 v59, v41, v42, v50
	v_fma_f32 v60, v42, v42, v51
	v_add_f32_dpp v61, v53, v61 wave_shl:1 row_mask:0xf bank_mask:0xf bound_ctrl:1
	s_barrier
	v_mov_b32_dpp v46, v4 wave_shr:1 row_mask:0xf bank_mask:0xf bound_ctrl:1
	v_mov_b32_dpp v47, v5 wave_shr:1 row_mask:0xf bank_mask:0xf bound_ctrl:1
	v_mov_b32_dpp v48, v4 wave_shl:1 row_mask:0xf bank_mask:0xf bound_ctrl:1
	v_mov_b32_dpp v49, v5 wave_shl:1 row_mask:0xf bank_mask:0xf bound_ctrl:1
	v_pk_mul_f32 v[50:51], v[4:5], v[8:9] op_sel_hi:[1,0]
	v_pk_mul_f32 v[62:63], v[4:5], v[8:9] op_sel:[0,1]
	v_pk_mul_f32 v[64:65], v[4:5], v[10:11] op_sel_hi:[1,0]
	v_pk_add_f32 v[66:67], v[4:5], v[46:47]
	v_pk_fma_f32 v[50:51], v[46:47], v[36:37], v[50:51] op_sel_hi:[1,0,1]
	v_pk_fma_f32 v[62:63], v[46:47], v[36:37], v[62:63] op_sel:[0,1,0]
	v_pk_fma_f32 v[64:65], v[46:47], v[38:39], v[64:65] op_sel_hi:[1,0,1]
	v_pk_add_f32 v[66:67], v[66:67], v[48:49]
	v_pk_fma_f32 v[50:51], v[48:49], v[40:41], v[50:51] op_sel_hi:[1,0,1]
	v_pk_fma_f32 v[62:63], v[48:49], v[40:41], v[62:63] op_sel:[0,1,0]
	v_pk_fma_f32 v[64:65], v[48:49], v[42:43], v[64:65] op_sel_hi:[1,0,1]
	s_add_i32 s5, s34, 1
	s_min_i32 s5, s5, 0x200
	s_mul_i32 s6, s5, 0x804
	s_add_i32 s6, s6, s35
	s_add_i32 s7, s6, 0x505014
	s_add_i32 s8, s6, 0x606018
	s_mul_i32 s9, s5, 0x180c
	s_add_i32 s9, s9, s33
	s_add_i32 s4, s34, 2
	s_min_i32 s4, s4, 0x200
	s_mul_i32 s4, s4, 0x804
	s_add_i32 s4, s4, s38
	buffer_load_dword v24, v28, s[20:23], s4 offen nt
	buffer_load_dwordx3 v[68:70], v27, s[24:27], s9 offen nt
	buffer_load_dword v46, v28, s[16:19], s7 offen nt
	buffer_load_dword v47, v28, s[16:19], s8 offen nt
	s_waitcnt vmcnt(8)
	v_mov_b32_dpp v72, v12 wave_shr:1 row_mask:0xf bank_mask:0xf bound_ctrl:1
	v_mov_b32_dpp v73, v13 wave_shr:1 row_mask:0xf bank_mask:0xf bound_ctrl:1
	v_mov_b32_dpp v74, v14 wave_shr:1 row_mask:0xf bank_mask:0xf bound_ctrl:1
	v_mov_b32_dpp v76, v12 wave_shl:1 row_mask:0xf bank_mask:0xf bound_ctrl:1
	v_mov_b32_dpp v77, v13 wave_shl:1 row_mask:0xf bank_mask:0xf bound_ctrl:1
	v_mov_b32_dpp v78, v14 wave_shl:1 row_mask:0xf bank_mask:0xf bound_ctrl:1
	s_add_i32 s4, s34, 0
	s_cmpk_lt_u32 s4, 0x201
	s_cselect_b64 s[12:13], s[40:41], 0
	v_cmp_eq_u32_e64 s[14:15], s37, v16
	s_and_b64 s[14:15], s[14:15], s[12:13]
	v_cndmask_b32_e64 v53, 0, 1, s[14:15]
	v_mul_f32_e64 v48, v12, v12
	v_mul_f32_e64 v49, v12, v13
	v_mul_f32_e64 v80, v12, v14
	v_mul_f32_e64 v81, v13, v13
	v_mul_f32_e64 v82, v13, v14
	v_mul_f32_e64 v83, v14, v14
	v_or_b32_dpp v84, v53, v53 wave_shr:1 row_mask:0xf bank_mask:0xf bound_ctrl:1
	s_nop 1
	v_or_b32_dpp v84, v53, v84 wave_shl:1 row_mask:0xf bank_mask:0xf bound_ctrl:1
	s_nop 1
	v_or_b32_dpp v85, v84, v84 wave_shr:1 row_mask:0xf bank_mask:0xf bound_ctrl:1
	s_nop 1
	v_or_b32_dpp v85, v84, v85 wave_shl:1 row_mask:0xf bank_mask:0xf bound_ctrl:1
	v_or3_b32 v53, v85, v52, v30
	v_or3_b32 v53, v53, v25, v17
	s_add_i32 s4, s34, -3
	s_cmpk_lt_u32 s4, 0x1ff
	s_cselect_b64 s[12:13], s[42:43], 0
	v_cmp_ne_u32_e64 s[30:31], 0, v53
	s_and_b64 s[30:31], s[30:31], s[12:13]
	v_cndmask_b32_e64 v53, 0, 1.0, s[30:31]
	v_add_f32_e64 v86, v12, v72
	v_add_f32_e64 v87, v13, v73
	v_add_f32_e64 v88, v14, v74
	v_fma_f32 v48, v72, v72, v48
	v_fma_f32 v49, v72, v73, v49
	v_fma_f32 v80, v72, v74, v80
	v_fma_f32 v81, v73, v73, v81
	v_fma_f32 v82, v73, v74, v82
	v_fma_f32 v83, v74, v74, v83
	v_add_f32_dpp v95, v53, v53 wave_shr:1 row_mask:0xf bank_mask:0xf bound_ctrl:1
	v_add_f32_e64 v86, v86, v76
	v_add_f32_e64 v87, v87, v77
	v_add_f32_e64 v88, v88, v78
	v_fma_f32 v89, v76, v76, v48
	v_fma_f32 v90, v76, v77, v49
	v_fma_f32 v91, v76, v78, v80
	v_fma_f32 v92, v77, v77, v81
	v_fma_f32 v93, v77, v78, v82
	v_fma_f32 v94, v78, v78, v83
	v_add_f32_dpp v95, v53, v95 wave_shl:1 row_mask:0xf bank_mask:0xf bound_ctrl:1
	s_barrier
	v_mov_b32_dpp v48, v6 wave_shr:1 row_mask:0xf bank_mask:0xf bound_ctrl:1
	v_mov_b32_dpp v49, v7 wave_shr:1 row_mask:0xf bank_mask:0xf bound_ctrl:1
	v_mov_b32_dpp v80, v6 wave_shl:1 row_mask:0xf bank_mask:0xf bound_ctrl:1
	v_mov_b32_dpp v81, v7 wave_shl:1 row_mask:0xf bank_mask:0xf bound_ctrl:1
	v_pk_mul_f32 v[82:83], v[6:7], v[12:13] op_sel_hi:[1,0]
	v_pk_mul_f32 v[96:97], v[6:7], v[12:13] op_sel:[0,1]
	v_pk_mul_f32 v[98:99], v[6:7], v[14:15] op_sel_hi:[1,0]
	v_pk_add_f32 v[100:101], v[6:7], v[48:49]
	v_pk_fma_f32 v[82:83], v[48:49], v[72:73], v[82:83] op_sel_hi:[1,0,1]
	v_pk_fma_f32 v[96:97], v[48:49], v[72:73], v[96:97] op_sel:[0,1,0]
	v_pk_fma_f32 v[98:99], v[48:49], v[74:75], v[98:99] op_sel_hi:[1,0,1]
	v_pk_add_f32 v[100:101], v[100:101], v[80:81]
	v_pk_fma_f32 v[82:83], v[80:81], v[76:77], v[82:83] op_sel_hi:[1,0,1]
	v_pk_fma_f32 v[96:97], v[80:81], v[76:77], v[96:97] op_sel:[0,1,0]
	v_pk_fma_f32 v[98:99], v[80:81], v[78:79], v[98:99] op_sel_hi:[1,0,1]
	s_add_i32 s5, s34, 2
	s_min_i32 s5, s5, 0x200
	s_mul_i32 s6, s5, 0x804
	s_add_i32 s6, s6, s35
	s_add_i32 s7, s6, 0x505014
	s_add_i32 s8, s6, 0x606018
	s_mul_i32 s9, s5, 0x180c
	s_add_i32 s9, s9, s33
	s_add_i32 s4, s34, 3
	s_min_i32 s4, s4, 0x200
	s_mul_i32 s4, s4, 0x804
	s_add_i32 s4, s4, s38
	buffer_load_dword v17, v28, s[20:23], s4 offen nt
	buffer_load_dwordx3 v[104:106], v27, s[24:27], s9 offen nt
	buffer_load_dword v48, v28, s[16:19], s7 offen nt
	buffer_load_dword v49, v28, s[16:19], s8 offen nt
	s_waitcnt vmcnt(8)
	v_mov_b32_dpp v108, v32 wave_shr:1 row_mask:0xf bank_mask:0xf bound_ctrl:1
	v_mov_b32_dpp v109, v33 wave_shr:1 row_mask:0xf bank_mask:0xf bound_ctrl:1
	v_mov_b32_dpp v110, v34 wave_shr:1 row_mask:0xf bank_mask:0xf bound_ctrl:1
	v_mov_b32_dpp v112, v32 wave_shl:1 row_mask:0xf bank_mask:0xf bound_ctrl:1
	v_mov_b32_dpp v113, v33 wave_shl:1 row_mask:0xf bank_mask:0xf bound_ctrl:1
	v_mov_b32_dpp v114, v34 wave_shl:1 row_mask:0xf bank_mask:0xf bound_ctrl:1
	s_add_i32 s4, s34, 1
	s_cmpk_lt_u32 s4, 0x201
	s_cselect_b64 s[12:13], s[40:41], 0
	v_cmp_eq_u32_e64 s[14:15], s37, v31
	s_and_b64 s[14:15], s[14:15], s[12:13]
	v_cndmask_b32_e64 v29, 0, 1, s[14:15]
	v_mul_f32_e64 v80, v32, v32
	v_mul_f32_e64 v81, v32, v33
	v_mul_f32_e64 v102, v32, v34
	v_mul_f32_e64 v103, v33, v33
	v_mul_f32_e64 v116, v33, v34
	v_mul_f32_e64 v117, v34, v34
	v_or_b32_dpp v53, v29, v29 wave_shr:1 row_mask:0xf bank_mask:0xf bound_ctrl:1
	s_nop 1
	v_or_b32_dpp v53, v29, v53 wave_shl:1 row_mask:0xf bank_mask:0xf bound_ctrl:1
	s_nop 1
	v_or_b32_dpp v84, v53, v53 wave_shr:1 row_mask:0xf bank_mask:0xf bound_ctrl:1
	s_nop 1
	v_or_b32_dpp v84, v53, v84 wave_shl:1 row_mask:0xf bank_mask:0xf bound_ctrl:1
	v_or3_b32 v29, v84, v85, v52
	v_or3_b32 v29, v29, v30, v25
	s_add_i32 s4, s34, -2
	s_cmpk_lt_u32 s4, 0x1ff
	s_cselect_b64 s[12:13], s[42:43], 0
	v_cmp_ne_u32_e64 s[30:31], 0, v29
	s_and_b64 s[30:31], s[30:31], s[12:13]
	v_cndmask_b32_e64 v29, 0, 1.0, s[30:31]
	v_add_f32_e64 v118, v32, v108
	v_add_f32_e64 v119, v33, v109
	v_add_f32_e64 v120, v34, v110
	v_fma_f32 v80, v108, v108, v80
	v_fma_f32 v81, v108, v109, v81
	v_fma_f32 v102, v108, v110, v102
	v_fma_f32 v103, v109, v109, v103
	v_fma_f32 v116, v109, v110, v116
	v_fma_f32 v117, v110, v110, v117
	v_add_f32_dpp v127, v29, v29 wave_shr:1 row_mask:0xf bank_mask:0xf bound_ctrl:1
	v_add_f32_e64 v118, v118, v112
	v_add_f32_e64 v119, v119, v113
	v_add_f32_e64 v120, v120, v114
	v_fma_f32 v121, v112, v112, v80
	v_fma_f32 v122, v112, v113, v81
	v_fma_f32 v123, v112, v114, v102
	v_fma_f32 v124, v113, v113, v103
	v_fma_f32 v125, v113, v114, v116
	v_fma_f32 v126, v114, v114, v117
	v_add_f32_dpp v127, v29, v127 wave_shl:1 row_mask:0xf bank_mask:0xf bound_ctrl:1
	v_pk_add_f32 v[80:81], v[86:87], v[118:119]
	v_pk_add_f32 v[102:103], v[44:45], v[80:81]
	v_pk_add_f32 v[44:45], v[88:89], v[120:121]
	v_pk_add_f32 v[86:87], v[54:55], v[44:45]
	v_pk_add_f32 v[54:55], v[90:91], v[122:123]
	v_pk_add_f32 v[88:89], v[56:57], v[54:55]
	v_pk_add_f32 v[56:57], v[92:93], v[124:125]
	v_pk_add_f32 v[90:91], v[58:59], v[56:57]
	v_pk_add_f32 v[58:59], v[94:95], v[126:127]
	v_pk_add_f32 v[92:93], v[60:61], v[58:59]
	v_mul_f32_e64 v128, v102, v22
	v_mul_f32_e64 v129, v103, v22
	v_mul_f32_e64 v130, v86, v22
	v_fma_f32 v29, v87, v22, v26
	v_mul_f32_e64 v53, v88, v22
	v_mul_f32_e64 v60, v89, v22
	v_fma_f32 v61, v90, v22, v26
	v_mul_f32_e64 v94, v91, v22
	v_fma_f32 v95, v92, v22, v26
	v_fma_f32 v29, -v128, v128, v29
	v_fma_f32 v53, -v128, v129, v53
	v_fma_f32 v60, -v128, v130, v60
	v_fma_f32 v61, -v129, v129, v61
	v_fma_f32 v94, -v129, v130, v94
	v_fma_f32 v95, -v130, v130, v95
	v_mul_f32_e64 v116, v94, v94
	v_mul_f32_e64 v117, v53, v95
	v_mul_f32_e64 v140, v60, v61
	v_mul_f32_e64 v141, v60, v60
	v_mul_f32_e64 v142, v29, v94
	v_mul_f32_e64 v143, v53, v53
	v_fma_f32 v116, v61, v95, -v116
	v_fma_f32 v117, v60, v94, -v117
	v_fma_f32 v140, v53, v94, -v140
	v_fma_f32 v141, v29, v95, -v141
	v_fma_f32 v142, v53, v60, -v142
	v_fma_f32 v143, v29, v61, -v143
	v_mul_f32_e64 v144, v29, v116
	v_fma_f32 v144, v53, v117, v144
	v_fma_f32 v144, v60, v140, v144
	v_rcp_f32_e32 v144, v144
	v_cmp_ne_u32_e64 vcc, s37, v2
	v_mul_f32_e64 v144, v144, v22
	v_cndmask_b32_e64 v144, 0, v144, s[30:31]
	v_cndmask_b32_e64 v29, 0, v18, vcc
	v_cndmask_b32_e64 v137, 0, v22, s[30:31]
	v_mul_f32_e64 v131, v116, v144
	v_mul_f32_e64 v132, v117, v144
	v_mul_f32_e64 v133, v140, v144
	v_mul_f32_e64 v134, v141, v144
	v_mul_f32_e64 v135, v142, v144
	v_mul_f32_e64 v136, v143, v144
	v_add_f32_e64 v138, v93, v29
	v_mov_b32_e32 v139, v2
	ds_write_b128 v23, v[128:131]
	ds_write_b128 v23, v[132:135] offset:1024
	ds_write_b128 v23, v[136:139] offset:2048
	s_waitcnt lgkmcnt(0)
	s_barrier
	v_mov_b32_dpp v60, v20 wave_shr:1 row_mask:0xf bank_mask:0xf bound_ctrl:1
	v_mov_b32_dpp v61, v21 wave_shr:1 row_mask:0xf bank_mask:0xf bound_ctrl:1
	v_mov_b32_dpp v86, v20 wave_shl:1 row_mask:0xf bank_mask:0xf bound_ctrl:1
	v_mov_b32_dpp v87, v21 wave_shl:1 row_mask:0xf bank_mask:0xf bound_ctrl:1
	v_pk_mul_f32 v[88:89], v[20:21], v[32:33] op_sel_hi:[1,0]
	v_pk_mul_f32 v[90:91], v[20:21], v[32:33] op_sel:[0,1]
	v_pk_mul_f32 v[92:93], v[20:21], v[34:35] op_sel_hi:[1,0]
	v_pk_add_f32 v[94:95], v[20:21], v[60:61]
	v_pk_fma_f32 v[88:89], v[60:61], v[108:109], v[88:89] op_sel_hi:[1,0,1]
	v_pk_fma_f32 v[90:91], v[60:61], v[108:109], v[90:91] op_sel:[0,1,0]
	v_pk_fma_f32 v[92:93], v[60:61], v[110:111], v[92:93] op_sel_hi:[1,0,1]
	v_pk_add_f32 v[94:95], v[94:95], v[86:87]
	v_pk_fma_f32 v[88:89], v[86:87], v[112:113], v[88:89] op_sel_hi:[1,0,1]
	v_pk_fma_f32 v[90:91], v[86:87], v[112:113], v[90:91] op_sel:[0,1,0]
	v_pk_fma_f32 v[92:93], v[86:87], v[114:115], v[92:93] op_sel_hi:[1,0,1]
	v_pk_add_f32 v[60:61], v[100:101], v[94:95]
	v_pk_add_f32 v[86:87], v[66:67], v[60:61]
	v_pk_add_f32 v[66:67], v[82:83], v[88:89]
	v_pk_add_f32 v[100:101], v[50:51], v[66:67]
	v_pk_add_f32 v[50:51], v[96:97], v[90:91]
	v_pk_add_f32 v[82:83], v[62:63], v[50:51]
	v_pk_add_f32 v[62:63], v[98:99], v[92:93]
	v_pk_add_f32 v[96:97], v[64:65], v[62:63]
	v_pk_fma_f32 v[100:101], v[128:129], v[86:87], v[100:101] op_sel_hi:[0,1,1] neg_lo:[1,0,0] neg_hi:[1,0,0]
	v_pk_fma_f32 v[82:83], v[128:129], v[86:87], v[82:83] op_sel:[1,0,0] neg_lo:[1,0,0] neg_hi:[1,0,0]
	v_pk_fma_f32 v[96:97], v[130:131], v[86:87], v[96:97] op_sel_hi:[0,1,1] neg_lo:[1,0,0] neg_hi:[1,0,0]
	v_pk_mul_f32 v[64:65], v[130:131], v[100:101] op_sel:[1,0]
	v_pk_mul_f32 v[98:99], v[132:133], v[100:101] op_sel_hi:[0,1]
	v_pk_mul_f32 v[102:103], v[132:133], v[100:101] op_sel:[1,0]
	v_pk_fma_f32 v[64:65], v[132:133], v[82:83], v[64:65] op_sel_hi:[0,1,1]
	v_pk_fma_f32 v[98:99], v[134:135], v[82:83], v[98:99] op_sel_hi:[0,1,1]
	v_pk_fma_f32 v[102:103], v[134:135], v[82:83], v[102:103] op_sel:[1,0,0]
	v_pk_fma_f32 v[64:65], v[132:133], v[96:97], v[64:65] op_sel:[1,0,0]
	v_pk_fma_f32 v[98:99], v[134:135], v[96:97], v[98:99] op_sel:[1,0,0]
	v_pk_fma_f32 v[102:103], v[136:137], v[96:97], v[102:103] op_sel_hi:[0,1,1]
	v_pk_mul_f32 v[116:117], v[128:129], v[64:65] op_sel_hi:[0,1]
	v_pk_fma_f32 v[116:117], v[128:129], v[98:99], v[116:117] op_sel:[1,0,0]
	v_pk_fma_f32 v[116:117], v[130:131], v[102:103], v[116:117] op_sel_hi:[0,1,1]
	v_pk_fma_f32 v[116:117], v[136:137], v[86:87], v[116:117] op_sel:[1,0,0] neg_lo:[0,0,1] neg_hi:[0,0,1]
	s_add_i32 s5, s34, 3
	s_min_i32 s5, s5, 0x200
	s_mul_i32 s6, s5, 0x804
	s_add_i32 s6, s6, s35
	s_add_i32 s7, s6, 0x505014
	s_add_i32 s8, s6, 0x606018
	s_mul_i32 s9, s5, 0x180c
	s_add_i32 s9, s9, s33
	s_add_i32 s4, s34, 4
	s_min_i32 s4, s4, 0x200
	s_mul_i32 s4, s4, 0x804
	s_add_i32 s4, s4, s38
	buffer_load_dword v2, v28, s[20:23], s4 offen nt
	buffer_load_dwordx3 v[8:10], v27, s[24:27], s9 offen nt
	buffer_load_dword v4, v28, s[16:19], s7 offen nt
	buffer_load_dword v5, v28, s[16:19], s8 offen nt
	s_waitcnt vmcnt(8)
	v_mov_b32_dpp v36, v68 wave_shr:1 row_mask:0xf bank_mask:0xf bound_ctrl:1
	v_mov_b32_dpp v37, v69 wave_shr:1 row_mask:0xf bank_mask:0xf bound_ctrl:1
	v_mov_b32_dpp v38, v70 wave_shr:1 row_mask:0xf bank_mask:0xf bound_ctrl:1
	v_mov_b32_dpp v40, v68 wave_shl:1 row_mask:0xf bank_mask:0xf bound_ctrl:1
	v_mov_b32_dpp v41, v69 wave_shl:1 row_mask:0xf bank_mask:0xf bound_ctrl:1
	v_mov_b32_dpp v42, v70 wave_shl:1 row_mask:0xf bank_mask:0xf bound_ctrl:1
	s_add_i32 s4, s34, 2
	s_cmpk_lt_u32 s4, 0x201
	s_cselect_b64 s[12:13], s[40:41], 0
	v_cmp_eq_u32_e64 s[14:15], s37, v24
	s_and_b64 s[14:15], s[14:15], s[12:13]
	v_cndmask_b32_e64 v25, 0, 1, s[14:15]
	v_mul_f32_e64 v82, v68, v68
	v_mul_f32_e64 v83, v68, v69
	v_mul_f32_e64 v86, v68, v70
	v_mul_f32_e64 v87, v69, v69
	v_mul_f32_e64 v96, v69, v70
	v_mul_f32_e64 v97, v70, v70
	v_or_b32_dpp v29, v25, v25 wave_shr:1 row_mask:0xf bank_mask:0xf bound_ctrl:1
	s_nop 1
	v_or_b32_dpp v29, v25, v29 wave_shl:1 row_mask:0xf bank_mask:0xf bound_ctrl:1
	s_nop 1
	v_or_b32_dpp v53, v29, v29 wave_shr:1 row_mask:0xf bank_mask:0xf bound_ctrl:1
	s_nop 1
	v_or_b32_dpp v53, v29, v53 wave_shl:1 row_mask:0xf bank_mask:0xf bound_ctrl:1
	v_or3_b32 v25, v53, v84, v85
	v_or3_b32 v25, v25, v52, v30
	s_add_i32 s4, s34, -1
	s_cmpk_lt_u32 s4, 0x1ff
	s_cselect_b64 s[12:13], s[42:43], 0
	v_cmp_ne_u32_e64 s[30:31], 0, v25
	s_and_b64 s[30:31], s[30:31], s[12:13]
	v_cndmask_b32_e64 v25, 0, 1.0, s[30:31]
	v_add_f32_e64 v100, v68, v36
	v_add_f32_e64 v101, v69, v37
	v_add_f32_e64 v128, v70, v38
	v_fma_f32 v82, v36, v36, v82
	v_fma_f32 v83, v36, v37, v83
	v_fma_f32 v86, v36, v38, v86
	v_fma_f32 v87, v37, v37, v87
	v_fma_f32 v96, v37, v38, v96
	v_fma_f32 v97, v38, v38, v97
	v_add_f32_dpp v135, v25, v25 wave_shr:1 row_mask:0xf bank_mask:0xf bound_ctrl:1
	v_add_f32_e64 v100, v100, v40
	v_add_f32_e64 v101, v101, v41
	v_add_f32_e64 v128, v128, v42
	v_fma_f32 v129, v40, v40, v82
	v_fma_f32 v130, v40, v41, v83
	v_fma_f32 v131, v40, v42, v86
	v_fma_f32 v132, v41, v41, v87
	v_fma_f32 v133, v41, v42, v96
	v_fma_f32 v134, v42, v42, v97
	v_add_f32_dpp v135, v25, v135 wave_shl:1 row_mask:0xf bank_mask:0xf bound_ctrl:1
	v_pk_add_f32 v[82:83], v[80:81], v[100:101]
	v_pk_add_f32 v[80:81], v[44:45], v[128:129]
	v_pk_add_f32 v[44:45], v[54:55], v[130:131]
	v_pk_add_f32 v[54:55], v[56:57], v[132:133]
	v_pk_add_f32 v[56:57], v[58:59], v[134:135]
	v_mul_f32_e64 v136, v82, v22
	v_mul_f32_e64 v137, v83, v22
	v_mul_f32_e64 v138, v80, v22
	v_fma_f32 v25, v81, v22, v26
	v_mul_f32_e64 v29, v44, v22
	v_mul_f32_e64 v58, v45, v22
	v_fma_f32 v59, v54, v22, v26
	v_mul_f32_e64 v86, v55, v22
	v_fma_f32 v87, v56, v22, v26
	v_fma_f32 v25, -v136, v136, v25
	v_fma_f32 v29, -v136, v137, v29
	v_fma_f32 v58, -v136, v138, v58
	v_fma_f32 v59, -v137, v137, v59
	v_fma_f32 v86, -v137, v138, v86
	v_fma_f32 v87, -v138, v138, v87
	v_mul_f32_e64 v96, v86, v86
	v_mul_f32_e64 v97, v29, v87
	v_mul_f32_e64 v148, v58, v59
	v_mul_f32_e64 v149, v58, v58
	v_mul_f32_e64 v150, v25, v86
	v_mul_f32_e64 v151, v29, v29
	v_fma_f32 v96, v59, v87, -v96
	v_fma_f32 v97, v58, v86, -v97
	v_fma_f32 v148, v29, v86, -v148
	v_fma_f32 v149, v25, v87, -v149
	v_fma_f32 v150, v29, v58, -v150
	v_fma_f32 v151, v25, v59, -v151
	v_mul_f32_e64 v152, v25, v96
	v_fma_f32 v152, v29, v97, v152
	v_fma_f32 v152, v58, v148, v152
	v_rcp_f32_e32 v152, v152
	v_cmp_ne_u32_e64 vcc, s37, v3
	v_mul_f32_e64 v152, v152, v22
	v_cndmask_b32_e64 v152, 0, v152, s[30:31]
	v_cndmask_b32_e64 v25, 0, v18, vcc
	v_cndmask_b32_e64 v145, 0, v22, s[30:31]
	v_mul_f32_e64 v139, v96, v152
	v_mul_f32_e64 v140, v97, v152
	v_mul_f32_e64 v141, v148, v152
	v_mul_f32_e64 v142, v149, v152
	v_mul_f32_e64 v143, v150, v152
	v_mul_f32_e64 v144, v151, v152
	v_add_f32_e64 v146, v57, v25
	v_mov_b32_e32 v147, v3
	ds_write_b128 v23, v[136:139] offset:3072
	ds_write_b128 v23, v[140:143] offset:4096
	ds_write_b128 v23, v[144:147] offset:5120
	s_waitcnt lgkmcnt(0)
	s_barrier
	v_mov_b32_dpp v44, v46 wave_shr:1 row_mask:0xf bank_mask:0xf bound_ctrl:1
	v_mov_b32_dpp v45, v47 wave_shr:1 row_mask:0xf bank_mask:0xf bound_ctrl:1
	v_mov_b32_dpp v54, v46 wave_shl:1 row_mask:0xf bank_mask:0xf bound_ctrl:1
	v_mov_b32_dpp v55, v47 wave_shl:1 row_mask:0xf bank_mask:0xf bound_ctrl:1
	v_pk_mul_f32 v[56:57], v[46:47], v[68:69] op_sel_hi:[1,0]
	v_pk_mul_f32 v[58:59], v[46:47], v[68:69] op_sel:[0,1]
	v_pk_mul_f32 v[80:81], v[46:47], v[70:71] op_sel_hi:[1,0]
	v_pk_add_f32 v[82:83], v[46:47], v[44:45]
	v_pk_fma_f32 v[56:57], v[44:45], v[36:37], v[56:57] op_sel_hi:[1,0,1]
	v_pk_fma_f32 v[58:59], v[44:45], v[36:37], v[58:59] op_sel:[0,1,0]
	v_pk_fma_f32 v[80:81], v[44:45], v[38:39], v[80:81] op_sel_hi:[1,0,1]
	v_pk_add_f32 v[82:83], v[82:83], v[54:55]
	v_pk_fma_f32 v[56:57], v[54:55], v[40:41], v[56:57] op_sel_hi:[1,0,1]
	v_pk_fma_f32 v[58:59], v[54:55], v[40:41], v[58:59] op_sel:[0,1,0]
	v_pk_fma_f32 v[80:81], v[54:55], v[42:43], v[80:81] op_sel_hi:[1,0,1]
	v_pk_add_f32 v[44:45], v[60:61], v[82:83]
	v_pk_add_f32 v[54:55], v[66:67], v[56:57]
	v_pk_add_f32 v[60:61], v[50:51], v[58:59]
	v_pk_add_f32 v[50:51], v[62:63], v[80:81]
	v_pk_fma_f32 v[54:55], v[136:137], v[44:45], v[54:55] op_sel_hi:[0,1,1] neg_lo:[1,0,0] neg_hi:[1,0,0]
	v_pk_fma_f32 v[60:61], v[136:137], v[44:45], v[60:61] op_sel:[1,0,0] neg_lo:[1,0,0] neg_hi:[1,0,0]
	v_pk_fma_f32 v[50:51], v[138:139], v[44:45], v[50:51] op_sel_hi:[0,1,1] neg_lo:[1,0,0] neg_hi:[1,0,0]
	v_pk_mul_f32 v[62:63], v[138:139], v[54:55] op_sel:[1,0]
	v_pk_mul_f32 v[66:67], v[140:141], v[54:55] op_sel_hi:[0,1]
	v_pk_mul_f32 v[86:87], v[140:141], v[54:55] op_sel:[1,0]
	v_pk_fma_f32 v[62:63], v[140:141], v[60:61], v[62:63] op_sel_hi:[0,1,1]
	v_pk_fma_f32 v[66:67], v[142:143], v[60:61], v[66:67] op_sel_hi:[0,1,1]
	v_pk_fma_f32 v[86:87], v[142:143], v[60:61], v[86:87] op_sel:[1,0,0]
	v_pk_fma_f32 v[62:63], v[140:141], v[50:51], v[62:63] op_sel:[1,0,0]
	v_pk_fma_f32 v[66:67], v[142:143], v[50:51], v[66:67] op_sel:[1,0,0]
	v_pk_fma_f32 v[86:87], v[144:145], v[50:51], v[86:87] op_sel_hi:[0,1,1]
	v_pk_mul_f32 v[96:97], v[136:137], v[62:63] op_sel_hi:[0,1]
	v_pk_fma_f32 v[96:97], v[136:137], v[66:67], v[96:97] op_sel:[1,0,0]
	v_pk_fma_f32 v[96:97], v[138:139], v[86:87], v[96:97] op_sel_hi:[0,1,1]
	v_pk_fma_f32 v[96:97], v[144:145], v[44:45], v[96:97] op_sel:[1,0,0] neg_lo:[0,0,1] neg_hi:[0,0,1]
	s_add_i32 s5, s34, 4
	s_min_i32 s5, s5, 0x200
	s_mul_i32 s6, s5, 0x804
	s_add_i32 s6, s6, s35
	s_add_i32 s7, s6, 0x505014
	s_add_i32 s8, s6, 0x606018
	s_mul_i32 s9, s5, 0x180c
	s_add_i32 s9, s9, s33
	s_add_i32 s4, s34, 5
	s_min_i32 s4, s4, 0x200
	s_mul_i32 s4, s4, 0x804
	s_add_i32 s4, s4, s38
	buffer_load_dword v3, v28, s[20:23], s4 offen nt
	buffer_load_dwordx3 v[12:14], v27, s[24:27], s9 offen nt
	buffer_load_dword v6, v28, s[16:19], s7 offen nt
	buffer_load_dword v7, v28, s[16:19], s8 offen nt
	s_waitcnt vmcnt(8)
	v_mov_b32_dpp v72, v104 wave_shr:1 row_mask:0xf bank_mask:0xf bound_ctrl:1
	v_mov_b32_dpp v73, v105 wave_shr:1 row_mask:0xf bank_mask:0xf bound_ctrl:1
	v_mov_b32_dpp v74, v106 wave_shr:1 row_mask:0xf bank_mask:0xf bound_ctrl:1
	v_mov_b32_dpp v76, v104 wave_shl:1 row_mask:0xf bank_mask:0xf bound_ctrl:1
	v_mov_b32_dpp v77, v105 wave_shl:1 row_mask:0xf bank_mask:0xf bound_ctrl:1
	v_mov_b32_dpp v78, v106 wave_shl:1 row_mask:0xf bank_mask:0xf bound_ctrl:1
	s_add_i32 s4, s34, 3
	s_cmpk_lt_u32 s4, 0x201
	s_cselect_b64 s[12:13], s[40:41], 0
	v_cmp_eq_u32_e64 s[14:15], s37, v17
	s_and_b64 s[14:15], s[14:15], s[12:13]
	v_cndmask_b32_e64 v25, 0, 1, s[14:15]
	v_mul_f32_e64 v44, v104, v104
	v_mul_f32_e64 v45, v104, v105
	v_mul_f32_e64 v50, v104, v106
	v_mul_f32_e64 v51, v105, v105
	v_mul_f32_e64 v54, v105, v106
	v_mul_f32_e64 v55, v106, v106
	v_or_b32_dpp v29, v25, v25 wave_shr:1 row_mask:0xf bank_mask:0xf bound_ctrl:1
	s_nop 1
	v_or_b32_dpp v29, v25, v29 wave_shl:1 row_mask:0xf bank_mask:0xf bound_ctrl:1
	s_nop 1
	v_or_b32_dpp v30, v29, v29 wave_shr:1 row_mask:0xf bank_mask:0xf bound_ctrl:1
	s_nop 1
	v_or_b32_dpp v30, v29, v30 wave_shl:1 row_mask:0xf bank_mask:0xf bound_ctrl:1
	v_or3_b32 v25, v30, v53, v84
	v_or3_b32 v25, v25, v85, v52
	s_add_i32 s4, s34, 0
	s_cmpk_lt_u32 s4, 0x1ff
	s_cselect_b64 s[12:13], s[42:43], 0
	v_cmp_ne_u32_e64 s[30:31], 0, v25
	s_and_b64 s[30:31], s[30:31], s[12:13]
	v_cndmask_b32_e64 v25, 0, 1.0, s[30:31]
	v_add_f32_e64 v60, v104, v72
	v_add_f32_e64 v61, v105, v73
	v_add_f32_e64 v136, v106, v74
	v_fma_f32 v44, v72, v72, v44
	v_fma_f32 v45, v72, v73, v45
	v_fma_f32 v50, v72, v74, v50
	v_fma_f32 v51, v73, v73, v51
	v_fma_f32 v54, v73, v74, v54
	v_fma_f32 v55, v74, v74, v55
	v_add_f32_dpp v143, v25, v25 wave_shr:1 row_mask:0xf bank_mask:0xf bound_ctrl:1
	v_add_f32_e64 v60, v60, v76
	v_add_f32_e64 v61, v61, v77
	v_add_f32_e64 v136, v136, v78
	v_fma_f32 v137, v76, v76, v44
	v_fma_f32 v138, v76, v77, v45
	v_fma_f32 v139, v76, v78, v50
	v_fma_f32 v140, v77, v77, v51
	v_fma_f32 v141, v77, v78, v54
	v_fma_f32 v142, v78, v78, v55
	v_add_f32_dpp v143, v25, v143 wave_shl:1 row_mask:0xf bank_mask:0xf bound_ctrl:1
	v_pk_add_f32 v[44:45], v[100:101], v[60:61]
	v_pk_add_f32 v[50:51], v[118:119], v[44:45]
	v_pk_add_f32 v[54:55], v[128:129], v[136:137]
	v_pk_add_f32 v[100:101], v[120:121], v[54:55]
	v_pk_add_f32 v[118:119], v[130:131], v[138:139]
	v_pk_add_f32 v[120:121], v[122:123], v[118:119]
	v_pk_add_f32 v[122:123], v[132:133], v[140:141]
	v_pk_add_f32 v[128:129], v[124:125], v[122:123]
	v_pk_add_f32 v[124:125], v[134:135], v[142:143]
	v_pk_add_f32 v[130:131], v[126:127], v[124:125]
	v_mul_f32_e64 v132, v50, v22
	v_mul_f32_e64 v133, v51, v22
	v_mul_f32_e64 v134, v100, v22
	v_fma_f32 v25, v101, v22, v26
	v_mul_f32_e64 v29, v120, v22
	v_mul_f32_e64 v126, v121, v22
	v_fma_f32 v127, v128, v22, v26
	v_mul_f32_e64 v152, v129, v22
	v_fma_f32 v153, v130, v22, v26
	v_fma_f32 v25, -v132, v132, v25
	v_fma_f32 v29, -v132, v133, v29
	v_fma_f32 v126, -v132, v134, v126
	v_fma_f32 v127, -v133, v133, v127
	v_fma_f32 v152, -v133, v134, v152
	v_fma_f32 v153, -v134, v134, v153
	v_mul_f32_e64 v154, v152, v152
	v_mul_f32_e64 v155, v29, v153
	v_mul_f32_e64 v156, v126, v127
	v_mul_f32_e64 v157, v126, v126
	v_mul_f32_e64 v158, v25, v152
	v_mul_f32_e64 v159, v29, v29
	v_fma_f32 v154, v127, v153, -v154
	v_fma_f32 v155, v126, v152, -v155
	v_fma_f32 v156, v29, v152, -v156
	v_fma_f32 v157, v25, v153, -v157
	v_fma_f32 v158, v29, v126, -v158
	v_fma_f32 v159, v25, v127, -v159
	v_mul_f32_e64 v160, v25, v154
	v_fma_f32 v160, v29, v155, v160
	v_fma_f32 v160, v126, v156, v160
	v_rcp_f32_e32 v160, v160
	v_cmp_ne_u32_e64 vcc, s37, v16
	v_mul_f32_e64 v160, v160, v22
	v_cndmask_b32_e64 v160, 0, v160, s[30:31]
	v_cndmask_b32_e64 v25, 0, v18, vcc
	v_cndmask_b32_e64 v149, 0, v22, s[30:31]
	v_mul_f32_e64 v135, v154, v160
	v_mul_f32_e64 v144, v155, v160
	v_mul_f32_e64 v145, v156, v160
	v_mul_f32_e64 v146, v157, v160
	v_mul_f32_e64 v147, v158, v160
	v_mul_f32_e64 v148, v159, v160
	v_add_f32_e64 v150, v131, v25
	v_mov_b32_e32 v151, v16
	ds_write_b128 v23, v[132:135]
	ds_write_b128 v23, v[144:147] offset:1024
	ds_write_b128 v23, v[148:151] offset:2048
	s_waitcnt lgkmcnt(0)
	s_barrier
	v_mov_b32_dpp v50, v48 wave_shr:1 row_mask:0xf bank_mask:0xf bound_ctrl:1
	v_mov_b32_dpp v51, v49 wave_shr:1 row_mask:0xf bank_mask:0xf bound_ctrl:1
	v_mov_b32_dpp v100, v48 wave_shl:1 row_mask:0xf bank_mask:0xf bound_ctrl:1
	v_mov_b32_dpp v101, v49 wave_shl:1 row_mask:0xf bank_mask:0xf bound_ctrl:1
	v_pk_mul_f32 v[120:121], v[48:49], v[104:105] op_sel_hi:[1,0]
	v_pk_mul_f32 v[126:127], v[48:49], v[104:105] op_sel:[0,1]
	v_pk_mul_f32 v[128:129], v[48:49], v[106:107] op_sel_hi:[1,0]
	v_pk_add_f32 v[130:131], v[48:49], v[50:51]
	v_pk_fma_f32 v[120:121], v[50:51], v[72:73], v[120:121] op_sel_hi:[1,0,1]
	v_pk_fma_f32 v[126:127], v[50:51], v[72:73], v[126:127] op_sel:[0,1,0]
	v_pk_fma_f32 v[128:129], v[50:51], v[74:75], v[128:129] op_sel_hi:[1,0,1]
	v_pk_add_f32 v[130:131], v[130:131], v[100:101]
	v_pk_fma_f32 v[120:121], v[100:101], v[76:77], v[120:121] op_sel_hi:[1,0,1]
	v_pk_fma_f32 v[126:127], v[100:101], v[76:77], v[126:127] op_sel:[0,1,0]
	v_pk_fma_f32 v[128:129], v[100:101], v[78:79], v[128:129] op_sel_hi:[1,0,1]
	v_pk_add_f32 v[50:51], v[82:83], v[130:131]
	v_pk_add_f32 v[100:101], v[94:95], v[50:51]
	v_pk_add_f32 v[82:83], v[56:57], v[120:121]
	v_pk_add_f32 v[94:95], v[88:89], v[82:83]
	v_pk_add_f32 v[56:57], v[58:59], v[126:127]
	v_pk_add_f32 v[88:89], v[90:91], v[56:57]
	v_pk_add_f32 v[58:59], v[80:81], v[128:129]
	v_pk_add_f32 v[90:91], v[92:93], v[58:59]
	v_pk_fma_f32 v[94:95], v[132:133], v[100:101], v[94:95] op_sel_hi:[0,1,1] neg_lo:[1,0,0] neg_hi:[1,0,0]
	v_pk_fma_f32 v[88:89], v[132:133], v[100:101], v[88:89] op_sel:[1,0,0] neg_lo:[1,0,0] neg_hi:[1,0,0]
	v_pk_fma_f32 v[90:91], v[134:135], v[100:101], v[90:91] op_sel_hi:[0,1,1] neg_lo:[1,0,0] neg_hi:[1,0,0]
	v_pk_mul_f32 v[80:81], v[134:135], v[94:95] op_sel:[1,0]
	v_pk_mul_f32 v[92:93], v[144:145], v[94:95] op_sel_hi:[0,1]
	v_pk_mul_f32 v[152:153], v[144:145], v[94:95] op_sel:[1,0]
	v_pk_fma_f32 v[80:81], v[144:145], v[88:89], v[80:81] op_sel_hi:[0,1,1]
	v_pk_fma_f32 v[92:93], v[146:147], v[88:89], v[92:93] op_sel_hi:[0,1,1]
	v_pk_fma_f32 v[152:153], v[146:147], v[88:89], v[152:153] op_sel:[1,0,0]
	v_pk_fma_f32 v[80:81], v[144:145], v[90:91], v[80:81] op_sel:[1,0,0]
	v_pk_fma_f32 v[92:93], v[146:147], v[90:91], v[92:93] op_sel:[1,0,0]
	v_pk_fma_f32 v[152:153], v[148:149], v[90:91], v[152:153] op_sel_hi:[0,1,1]
	v_pk_mul_f32 v[154:155], v[132:133], v[80:81] op_sel_hi:[0,1]
	v_pk_fma_f32 v[154:155], v[132:133], v[92:93], v[154:155] op_sel:[1,0,0]
	v_pk_fma_f32 v[154:155], v[134:135], v[152:153], v[154:155] op_sel_hi:[0,1,1]
	v_pk_fma_f32 v[154:155], v[148:149], v[100:101], v[154:155] op_sel:[1,0,0] neg_lo:[0,0,1] neg_hi:[0,0,1]
	v_cmp_eq_u32_e64 s[10:11], 6, v151
	v_cmp_eq_u32_e64 s[14:15], 7, v151
	v_pk_add_f32 v[88:89], v[62:63], v[80:81]
	v_pk_add_f32 v[90:91], v[64:65], v[88:89]
	v_pk_add_f32 v[62:63], v[66:67], v[92:93]
	v_pk_add_f32 v[64:65], v[98:99], v[62:63]
	v_pk_add_f32 v[66:67], v[86:87], v[152:153]
	v_pk_add_f32 v[94:95], v[102:103], v[66:67]
	v_pk_add_f32 v[86:87], v[96:97], v[154:155]
	v_pk_add_f32 v[98:99], v[116:117], v[86:87]
	v_pk_fma_f32 v[96:97], v[108:109], v[90:91], v[98:99] op_sel_hi:[0,1,1]
	v_pk_fma_f32 v[100:101], v[112:113], v[90:91], v[98:99] op_sel_hi:[0,1,1]
	v_pk_fma_f32 v[96:97], v[108:109], v[64:65], v[96:97] op_sel:[1,0,0]
	v_pk_fma_f32 v[100:101], v[112:113], v[64:65], v[100:101] op_sel:[1,0,0]
	v_pk_fma_f32 v[96:97], v[110:111], v[94:95], v[96:97] op_sel_hi:[0,1,1]
	v_pk_fma_f32 v[100:101], v[114:115], v[94:95], v[100:101] op_sel_hi:[0,1,1]
	v_pk_fma_f32 v[98:99], v[32:33], v[90:91], v[98:99] op_sel_hi:[0,1,1]
	v_pk_fma_f32 v[98:99], v[32:33], v[64:65], v[98:99] op_sel:[1,0,0]
	v_pk_fma_f32 v[98:99], v[34:35], v[94:95], v[98:99] op_sel_hi:[0,1,1]
	v_cndmask_b32_e64 v102, 0, v18, s[10:11]
	v_cndmask_b32_e64 v103, 0, v18, s[14:15]
	v_add_f32_dpp v98, v96, v98 wave_shl:1 row_mask:0xf bank_mask:0xf bound_ctrl:1
	v_add_f32_dpp v99, v97, v99 wave_shl:1 row_mask:0xf bank_mask:0xf bound_ctrl:1
	s_add_i32 s4, s34, 0
	s_cmpk_lt_i32 s4, 0x201
	s_cselect_b64 s[12:13], s[0:1], 0
	v_add_f32_dpp v98, v100, v98 wave_shr:1 row_mask:0xf bank_mask:0xf bound_ctrl:1
	v_add_f32_dpp v99, v101, v99 wave_shr:1 row_mask:0xf bank_mask:0xf bound_ctrl:1
	v_pk_fma_f32 v[98:99], v[20:21], v[150:151], v[98:99] op_sel_hi:[1,0,1] neg_lo:[0,0,1] neg_hi:[0,0,1]
	v_pk_add_f32 v[98:99], v[98:99], v[102:103] neg_lo:[0,1] neg_hi:[0,1]
	v_pk_mul_f32 v[116:117], v[98:99], v[98:99]
	v_add_f32_e32 v116, v116, v117
	v_cndmask_b32_e64 v117, 0, v116, s[12:13]
	v_add_f32_e32 v1, v1, v117
	s_add_i32 s5, s34, 5
	s_min_i32 s5, s5, 0x200
	s_mul_i32 s6, s5, 0x804
	s_add_i32 s6, s6, s35
	s_add_i32 s7, s6, 0x505014
	s_add_i32 s8, s6, 0x606018
	s_mul_i32 s9, s5, 0x180c
	s_add_i32 s9, s9, s33
	s_add_i32 s4, s34, 6
	s_min_i32 s4, s4, 0x200
	s_mul_i32 s4, s4, 0x804
	s_add_i32 s4, s4, s38
	buffer_load_dword v16, v28, s[20:23], s4 offen nt
	buffer_load_dwordx3 v[32:34], v27, s[24:27], s9 offen nt
	buffer_load_dword v20, v28, s[16:19], s7 offen nt
	buffer_load_dword v21, v28, s[16:19], s8 offen nt
	s_waitcnt vmcnt(8)
	v_mov_b32_dpp v96, v8 wave_shr:1 row_mask:0xf bank_mask:0xf bound_ctrl:1
	v_mov_b32_dpp v97, v9 wave_shr:1 row_mask:0xf bank_mask:0xf bound_ctrl:1
	v_mov_b32_dpp v98, v10 wave_shr:1 row_mask:0xf bank_mask:0xf bound_ctrl:1
	v_mov_b32_dpp v100, v8 wave_shl:1 row_mask:0xf bank_mask:0xf bound_ctrl:1
	v_mov_b32_dpp v101, v9 wave_shl:1 row_mask:0xf bank_mask:0xf bound_ctrl:1
	v_mov_b32_dpp v102, v10 wave_shl:1 row_mask:0xf bank_mask:0xf bound_ctrl:1
	s_add_i32 s4, s34, 4
	s_cmpk_lt_u32 s4, 0x201
	s_cselect_b64 s[12:13], s[40:41], 0
	v_cmp_eq_u32_e64 s[14:15], s37, v2
	s_and_b64 s[14:15], s[14:15], s[12:13]
	v_cndmask_b32_e64 v25, 0, 1, s[14:15]
	v_mul_f32_e64 v64, v8, v8
	v_mul_f32_e64 v65, v8, v9
	v_mul_f32_e64 v90, v8, v10
	v_mul_f32_e64 v91, v9, v9
	v_mul_f32_e64 v94, v9, v10
	v_mul_f32_e64 v95, v10, v10
	v_or_b32_dpp v29, v25, v25 wave_shr:1 row_mask:0xf bank_mask:0xf bound_ctrl:1
	s_nop 1
	v_or_b32_dpp v29, v25, v29 wave_shl:1 row_mask:0xf bank_mask:0xf bound_ctrl:1
	s_nop 1
	v_or_b32_dpp v52, v29, v29 wave_shr:1 row_mask:0xf bank_mask:0xf bound_ctrl:1
	s_nop 1
	v_or_b32_dpp v52, v29, v52 wave_shl:1 row_mask:0xf bank_mask:0xf bound_ctrl:1
	v_or3_b32 v25, v52, v30, v53
	v_or3_b32 v25, v25, v84, v85
	s_add_i32 s4, s34, 1
	s_cmpk_lt_u32 s4, 0x1ff
	s_cselect_b64 s[12:13], s[42:43], 0
	v_cmp_ne_u32_e64 s[30:31], 0, v25
	s_and_b64 s[30:31], s[30:31], s[12:13]
	v_cndmask_b32_e64 v25, 0, 1.0, s[30:31]
	v_add_f32_e64 v108, v8, v96
	v_add_f32_e64 v109, v9, v97
	v_add_f32_e64 v110, v10, v98
	v_fma_f32 v64, v96, v96, v64
	v_fma_f32 v65, v96, v97, v65
	v_fma_f32 v90, v96, v98, v90
	v_fma_f32 v91, v97, v97, v91
	v_fma_f32 v94, v97, v98, v94
	v_fma_f32 v95, v98, v98, v95
	v_add_f32_dpp v117, v25, v25 wave_shr:1 row_mask:0xf bank_mask:0xf bound_ctrl:1
	v_add_f32_e64 v108, v108, v100
	v_add_f32_e64 v109, v109, v101
	v_add_f32_e64 v110, v110, v102
	v_fma_f32 v111, v100, v100, v64
	v_fma_f32 v112, v100, v101, v65
	v_fma_f32 v113, v100, v102, v90
	v_fma_f32 v114, v101, v101, v91
	v_fma_f32 v115, v101, v102, v94
	v_fma_f32 v116, v102, v102, v95
	v_add_f32_dpp v117, v25, v117 wave_shl:1 row_mask:0xf bank_mask:0xf bound_ctrl:1
	v_pk_add_f32 v[64:65], v[44:45], v[108:109]
	v_pk_add_f32 v[44:45], v[54:55], v[110:111]
	v_pk_add_f32 v[54:55], v[118:119], v[112:113]
	v_pk_add_f32 v[90:91], v[122:123], v[114:115]
	v_pk_add_f32 v[94:95], v[124:125], v[116:117]
	v_mul_f32_e64 v132, v64, v22
	v_mul_f32_e64 v133, v65, v22
	v_mul_f32_e64 v134, v44, v22
	v_fma_f32 v25, v45, v22, v26
	v_mul_f32_e64 v29, v54, v22
	v_mul_f32_e64 v118, v55, v22
	v_fma_f32 v119, v90, v22, v26
	v_mul_f32_e64 v122, v91, v22
	v_fma_f32 v123, v94, v22, v26
	v_fma_f32 v25, -v132, v132, v25
	v_fma_f32 v29, -v132, v133, v29
	v_fma_f32 v118, -v132, v134, v118
	v_fma_f32 v119, -v133, v133, v119
	v_fma_f32 v122, -v133, v134, v122
	v_fma_f32 v123, -v134, v134, v123
	v_mul_f32_e64 v124, v122, v122
	v_mul_f32_e64 v125, v29, v123
	v_mul_f32_e64 v156, v118, v119
	v_mul_f32_e64 v157, v118, v118
	v_mul_f32_e64 v158, v25, v122
	v_mul_f32_e64 v159, v29, v29
	v_fma_f32 v124, v119, v123, -v124
	v_fma_f32 v125, v118, v122, -v125
	v_fma_f32 v156, v29, v122, -v156
	v_fma_f32 v157, v25, v123, -v157
	v_fma_f32 v158, v29, v118, -v158
	v_fma_f32 v159, v25, v119, -v159
	v_mul_f32_e64 v160, v25, v124
	v_fma_f32 v160, v29, v125, v160
	v_fma_f32 v160, v118, v156, v160
	v_rcp_f32_e32 v160, v160
	v_cmp_ne_u32_e64 vcc, s37, v31
	v_mul_f32_e64 v160, v160, v22
	v_cndmask_b32_e64 v160, 0, v160, s[30:31]
	v_cndmask_b32_e64 v25, 0, v18, vcc
	v_cndmask_b32_e64 v149, 0, v22, s[30:31]
	v_mul_f32_e64 v135, v124, v160
	v_mul_f32_e64 v144, v125, v160
	v_mul_f32_e64 v145, v156, v160
	v_mul_f32_e64 v146, v157, v160
	v_mul_f32_e64 v147, v158, v160
	v_mul_f32_e64 v148, v159, v160
	v_add_f32_e64 v150, v95, v25
	v_mov_b32_e32 v151, v31
	ds_write_b128 v23, v[132:135] offset:3072
	ds_write_b128 v23, v[144:147] offset:4096
	ds_write_b128 v23, v[148:151] offset:5120
	s_waitcnt lgkmcnt(0)
	s_barrier
	v_mov_b32_dpp v44, v4 wave_shr:1 row_mask:0xf bank_mask:0xf bound_ctrl:1
	v_mov_b32_dpp v45, v5 wave_shr:1 row_mask:0xf bank_mask:0xf bound_ctrl:1
	v_mov_b32_dpp v54, v4 wave_shl:1 row_mask:0xf bank_mask:0xf bound_ctrl:1
	v_mov_b32_dpp v55, v5 wave_shl:1 row_mask:0xf bank_mask:0xf bound_ctrl:1
	v_pk_mul_f32 v[64:65], v[4:5], v[8:9] op_sel_hi:[1,0]
	v_pk_mul_f32 v[90:91], v[4:5], v[8:9] op_sel:[0,1]
	v_pk_mul_f32 v[94:95], v[4:5], v[10:11] op_sel_hi:[1,0]
	v_pk_add_f32 v[118:119], v[4:5], v[44:45]
	v_pk_fma_f32 v[64:65], v[44:45], v[96:97], v[64:65] op_sel_hi:[1,0,1]
	v_pk_fma_f32 v[90:91], v[44:45], v[96:97], v[90:91] op_sel:[0,1,0]
	v_pk_fma_f32 v[94:95], v[44:45], v[98:99], v[94:95] op_sel_hi:[1,0,1]
	v_pk_add_f32 v[118:119], v[118:119], v[54:55]
	v_pk_fma_f32 v[64:65], v[54:55], v[100:101], v[64:65] op_sel_hi:[1,0,1]
	v_pk_fma_f32 v[90:91], v[54:55], v[100:101], v[90:91] op_sel:[0,1,0]
	v_pk_fma_f32 v[94:95], v[54:55], v[102:103], v[94:95] op_sel_hi:[1,0,1]
	v_pk_add_f32 v[44:45], v[50:51], v[118:119]
	v_pk_add_f32 v[50:51], v[82:83], v[64:65]
	v_pk_add_f32 v[54:55], v[56:57], v[90:91]
	v_pk_add_f32 v[56:57], v[58:59], v[94:95]
	v_pk_fma_f32 v[50:51], v[132:133], v[44:45], v[50:51] op_sel_hi:[0,1,1] neg_lo:[1,0,0] neg_hi:[1,0,0]
	v_pk_fma_f32 v[54:55], v[132:133], v[44:45], v[54:55] op_sel:[1,0,0] neg_lo:[1,0,0] neg_hi:[1,0,0]
	v_pk_fma_f32 v[56:57], v[134:135], v[44:45], v[56:57] op_sel_hi:[0,1,1] neg_lo:[1,0,0] neg_hi:[1,0,0]
	v_pk_mul_f32 v[58:59], v[134:135], v[50:51] op_sel:[1,0]
	v_pk_mul_f32 v[82:83], v[144:145], v[50:51] op_sel_hi:[0,1]
	v_pk_mul_f32 v[122:123], v[144:145], v[50:51] op_sel:[1,0]
	v_pk_fma_f32 v[58:59], v[144:145], v[54:55], v[58:59] op_sel_hi:[0,1,1]
	v_pk_fma_f32 v[82:83], v[146:147], v[54:55], v[82:83] op_sel_hi:[0,1,1]
	v_pk_fma_f32 v[122:123], v[146:147], v[54:55], v[122:123] op_sel:[1,0,0]
	v_pk_fma_f32 v[58:59], v[144:145], v[56:57], v[58:59] op_sel:[1,0,0]
	v_pk_fma_f32 v[82:83], v[146:147], v[56:57], v[82:83] op_sel:[1,0,0]
	v_pk_fma_f32 v[122:123], v[148:149], v[56:57], v[122:123] op_sel_hi:[0,1,1]
	v_pk_mul_f32 v[124:125], v[132:133], v[58:59] op_sel_hi:[0,1]
	v_pk_fma_f32 v[124:125], v[132:133], v[82:83], v[124:125] op_sel:[1,0,0]
	v_pk_fma_f32 v[124:125], v[134:135], v[122:123], v[124:125] op_sel_hi:[0,1,1]
	v_pk_fma_f32 v[124:125], v[148:149], v[44:45], v[124:125] op_sel:[1,0,0] neg_lo:[0,0,1] neg_hi:[0,0,1]
	v_cmp_eq_u32_e64 s[10:11], 6, v151
	v_cmp_eq_u32_e64 s[14:15], 7, v151
	v_pk_add_f32 v[44:45], v[88:89], v[58:59]
	v_pk_add_f32 v[50:51], v[62:63], v[82:83]
	v_pk_add_f32 v[54:55], v[66:67], v[122:123]
	v_pk_add_f32 v[56:57], v[86:87], v[124:125]
	v_pk_fma_f32 v[62:63], v[36:37], v[44:45], v[56:57] op_sel_hi:[0,1,1]
	v_pk_fma_f32 v[66:67], v[40:41], v[44:45], v[56:57] op_sel_hi:[0,1,1]
	v_pk_fma_f32 v[62:63], v[36:37], v[50:51], v[62:63] op_sel:[1,0,0]
	v_pk_fma_f32 v[66:67], v[40:41], v[50:51], v[66:67] op_sel:[1,0,0]
	v_pk_fma_f32 v[62:63], v[38:39], v[54:55], v[62:63] op_sel_hi:[0,1,1]
	v_pk_fma_f32 v[66:67], v[42:43], v[54:55], v[66:67] op_sel_hi:[0,1,1]
	v_pk_fma_f32 v[56:57], v[68:69], v[44:45], v[56:57] op_sel_hi:[0,1,1]
	v_pk_fma_f32 v[56:57], v[68:69], v[50:51], v[56:57] op_sel:[1,0,0]
	v_pk_fma_f32 v[56:57], v[70:71], v[54:55], v[56:57] op_sel_hi:[0,1,1]
	v_cndmask_b32_e64 v86, 0, v18, s[10:11]
	v_cndmask_b32_e64 v87, 0, v18, s[14:15]
	v_add_f32_dpp v56, v62, v56 wave_shl:1 row_mask:0xf bank_mask:0xf bound_ctrl:1
	v_add_f32_dpp v57, v63, v57 wave_shl:1 row_mask:0xf bank_mask:0xf bound_ctrl:1
	s_add_i32 s4, s34, 1
	s_cmpk_lt_i32 s4, 0x201
	s_cselect_b64 s[12:13], s[0:1], 0
	v_add_f32_dpp v56, v66, v56 wave_shr:1 row_mask:0xf bank_mask:0xf bound_ctrl:1
	v_add_f32_dpp v57, v67, v57 wave_shr:1 row_mask:0xf bank_mask:0xf bound_ctrl:1
	v_pk_fma_f32 v[56:57], v[46:47], v[150:151], v[56:57] op_sel_hi:[1,0,1] neg_lo:[0,0,1] neg_hi:[0,0,1]
	v_pk_add_f32 v[56:57], v[56:57], v[86:87] neg_lo:[0,1] neg_hi:[0,1]
	v_pk_mul_f32 v[88:89], v[56:57], v[56:57]
	v_add_f32_e32 v88, v88, v89
	v_cndmask_b32_e64 v89, 0, v88, s[12:13]
	v_add_f32_e32 v1, v1, v89
	s_add_i32 s5, s34, 6
	s_min_i32 s5, s5, 0x200
	s_mul_i32 s6, s5, 0x804
	s_add_i32 s6, s6, s35
	s_add_i32 s7, s6, 0x505014
	s_add_i32 s8, s6, 0x606018
	s_mul_i32 s9, s5, 0x180c
	s_add_i32 s9, s9, s33
	s_add_i32 s4, s34, 7
	s_min_i32 s4, s4, 0x200
	s_mul_i32 s4, s4, 0x804
	s_add_i32 s4, s4, s38
	buffer_load_dword v25, v28, s[20:23], s4 offen nt
	buffer_load_dwordx3 v[40:42], v27, s[24:27], s9 offen nt
	buffer_load_dword v36, v28, s[16:19], s7 offen nt
	buffer_load_dword v37, v28, s[16:19], s8 offen nt
	s_waitcnt vmcnt(8)
	v_mov_b32_dpp v44, v12 wave_shr:1 row_mask:0xf bank_mask:0xf bound_ctrl:1
	v_mov_b32_dpp v45, v13 wave_shr:1 row_mask:0xf bank_mask:0xf bound_ctrl:1
	v_mov_b32_dpp v46, v14 wave_shr:1 row_mask:0xf bank_mask:0xf bound_ctrl:1
	v_mov_b32_dpp v68, v12 wave_shl:1 row_mask:0xf bank_mask:0xf bound_ctrl:1
	v_mov_b32_dpp v69, v13 wave_shl:1 row_mask:0xf bank_mask:0xf bound_ctrl:1
	v_mov_b32_dpp v70, v14 wave_shl:1 row_mask:0xf bank_mask:0xf bound_ctrl:1
	s_add_i32 s4, s34, 5
	s_cmpk_lt_u32 s4, 0x201
	s_cselect_b64 s[12:13], s[40:41], 0
	v_cmp_eq_u32_e64 s[14:15], s37, v3
	s_and_b64 s[14:15], s[14:15], s[12:13]
	v_cndmask_b32_e64 v29, 0, 1, s[14:15]
	v_mul_f32_e64 v38, v12, v12
	v_mul_f32_e64 v39, v12, v13
	v_mul_f32_e64 v50, v12, v14
	v_mul_f32_e64 v51, v13, v13
	v_mul_f32_e64 v54, v13, v14
	v_mul_f32_e64 v55, v14, v14
	v_or_b32_dpp v31, v29, v29 wave_shr:1 row_mask:0xf bank_mask:0xf bound_ctrl:1
	s_nop 1
	v_or_b32_dpp v31, v29, v31 wave_shl:1 row_mask:0xf bank_mask:0xf bound_ctrl:1
	s_nop 1
	v_or_b32_dpp v85, v31, v31 wave_shr:1 row_mask:0xf bank_mask:0xf bound_ctrl:1
	s_nop 1
	v_or_b32_dpp v85, v31, v85 wave_shl:1 row_mask:0xf bank_mask:0xf bound_ctrl:1
	v_or3_b32 v29, v85, v52, v30
	v_or3_b32 v29, v29, v53, v84
	s_add_i32 s4, s34, 2
	s_cmpk_lt_u32 s4, 0x1ff
	s_cselect_b64 s[12:13], s[42:43], 0
	v_cmp_ne_u32_e64 s[30:31], 0, v29
	s_and_b64 s[30:31], s[30:31], s[12:13]
	v_cndmask_b32_e64 v29, 0, 1.0, s[30:31]
	v_add_f32_e64 v56, v12, v44
	v_add_f32_e64 v57, v13, v45
	v_add_f32_e64 v62, v14, v46
	v_fma_f32 v38, v44, v44, v38
	v_fma_f32 v39, v44, v45, v39
	v_fma_f32 v50, v44, v46, v50
	v_fma_f32 v51, v45, v45, v51
	v_fma_f32 v54, v45, v46, v54
	v_fma_f32 v55, v46, v46, v55
	v_add_f32_dpp v89, v29, v29 wave_shr:1 row_mask:0xf bank_mask:0xf bound_ctrl:1
	v_add_f32_e64 v56, v56, v68
	v_add_f32_e64 v57, v57, v69
	v_add_f32_e64 v62, v62, v70
	v_fma_f32 v63, v68, v68, v38
	v_fma_f32 v66, v68, v69, v39
	v_fma_f32 v67, v68, v70, v50
	v_fma_f32 v86, v69, v69, v51
	v_fma_f32 v87, v69, v70, v54
	v_fma_f32 v88, v70, v70, v55
	v_add_f32_dpp v89, v29, v89 wave_shl:1 row_mask:0xf bank_mask:0xf bound_ctrl:1
	v_pk_add_f32 v[38:39], v[108:109], v[56:57]
	v_pk_add_f32 v[50:51], v[60:61], v[38:39]
	v_pk_add_f32 v[54:55], v[110:111], v[62:63]
	v_pk_add_f32 v[60:61], v[136:137], v[54:55]
	v_pk_add_f32 v[108:109], v[112:113], v[66:67]
	v_pk_add_f32 v[110:111], v[138:139], v[108:109]
	v_pk_add_f32 v[112:113], v[114:115], v[86:87]
	v_pk_add_f32 v[132:133], v[140:141], v[112:113]
	v_pk_add_f32 v[114:115], v[116:117], v[88:89]
	v_pk_add_f32 v[134:135], v[142:143], v[114:115]
	v_mul_f32_e64 v136, v50, v22
	v_mul_f32_e64 v137, v51, v22
	v_mul_f32_e64 v138, v60, v22
	v_fma_f32 v29, v61, v22, v26
	v_mul_f32_e64 v31, v110, v22
	v_mul_f32_e64 v116, v111, v22
	v_fma_f32 v117, v132, v22, v26
	v_mul_f32_e64 v148, v133, v22
	v_fma_f32 v149, v134, v22, v26
	v_fma_f32 v29, -v136, v136, v29
	v_fma_f32 v31, -v136, v137, v31
	v_fma_f32 v116, -v136, v138, v116
	v_fma_f32 v117, -v137, v137, v117
	v_fma_f32 v148, -v137, v138, v148
	v_fma_f32 v149, -v138, v138, v149
	v_mul_f32_e64 v150, v148, v148
	v_mul_f32_e64 v151, v31, v149
	v_mul_f32_e64 v156, v116, v117
	v_mul_f32_e64 v157, v116, v116
	v_mul_f32_e64 v158, v29, v148
	v_mul_f32_e64 v159, v31, v31
	v_fma_f32 v150, v117, v149, -v150
	v_fma_f32 v151, v116, v148, -v151
	v_fma_f32 v156, v31, v148, -v156
	v_fma_f32 v157, v29, v149, -v157
	v_fma_f32 v158, v31, v116, -v158
	v_fma_f32 v159, v29, v117, -v159
	v_mul_f32_e64 v160, v29, v150
	v_fma_f32 v160, v31, v151, v160
	v_fma_f32 v160, v116, v156, v160
	v_rcp_f32_e32 v160, v160
	v_cmp_ne_u32_e64 vcc, s37, v24
	v_mul_f32_e64 v160, v160, v22
	v_cndmask_b32_e64 v160, 0, v160, s[30:31]
	v_cndmask_b32_e64 v29, 0, v18, vcc
	v_cndmask_b32_e64 v145, 0, v22, s[30:31]
	v_mul_f32_e64 v139, v150, v160
	v_mul_f32_e64 v140, v151, v160
	v_mul_f32_e64 v141, v156, v160
	v_mul_f32_e64 v142, v157, v160
	v_mul_f32_e64 v143, v158, v160
	v_mul_f32_e64 v144, v159, v160
	v_add_f32_e64 v146, v135, v29
	v_mov_b32_e32 v147, v24
	ds_write_b128 v23, v[136:139]
	ds_write_b128 v23, v[140:143] offset:1024
	ds_write_b128 v23, v[144:147] offset:2048
	s_waitcnt lgkmcnt(0)
	s_barrier
	v_mov_b32_dpp v50, v6 wave_shr:1 row_mask:0xf bank_mask:0xf bound_ctrl:1
	v_mov_b32_dpp v51, v7 wave_shr:1 row_mask:0xf bank_mask:0xf bound_ctrl:1
	v_mov_b32_dpp v60, v6 wave_shl:1 row_mask:0xf bank_mask:0xf bound_ctrl:1
	v_mov_b32_dpp v61, v7 wave_shl:1 row_mask:0xf bank_mask:0xf bound_ctrl:1
	v_pk_mul_f32 v[110:111], v[6:7], v[12:13] op_sel_hi:[1,0]
	v_pk_mul_f32 v[116:117], v[6:7], v[12:13] op_sel:[0,1]
	v_pk_mul_f32 v[132:133], v[6:7], v[14:15] op_sel_hi:[1,0]
	v_pk_add_f32 v[134:135], v[6:7], v[50:51]
	v_pk_fma_f32 v[110:111], v[50:51], v[44:45], v[110:111] op_sel_hi:[1,0,1]
	v_pk_fma_f32 v[116:117], v[50:51], v[44:45], v[116:117] op_sel:[0,1,0]
	v_pk_fma_f32 v[132:133], v[50:51], v[46:47], v[132:133] op_sel_hi:[1,0,1]
	v_pk_add_f32 v[134:135], v[134:135], v[60:61]
	v_pk_fma_f32 v[110:111], v[60:61], v[68:69], v[110:111] op_sel_hi:[1,0,1]
	v_pk_fma_f32 v[116:117], v[60:61], v[68:69], v[116:117] op_sel:[0,1,0]
	v_pk_fma_f32 v[132:133], v[60:61], v[70:71], v[132:133] op_sel_hi:[1,0,1]
	v_pk_add_f32 v[50:51], v[118:119], v[134:135]
	v_pk_add_f32 v[60:61], v[130:131], v[50:51]
	v_pk_add_f32 v[118:119], v[64:65], v[110:111]
	v_pk_add_f32 v[130:131], v[120:121], v[118:119]
	v_pk_add_f32 v[64:65], v[90:91], v[116:117]
	v_pk_add_f32 v[120:121], v[126:127], v[64:65]
	v_pk_add_f32 v[90:91], v[94:95], v[132:133]
	v_pk_add_f32 v[126:127], v[128:129], v[90:91]
	v_pk_fma_f32 v[130:131], v[136:137], v[60:61], v[130:131] op_sel_hi:[0,1,1] neg_lo:[1,0,0] neg_hi:[1,0,0]
	v_pk_fma_f32 v[120:121], v[136:137], v[60:61], v[120:121] op_sel:[1,0,0] neg_lo:[1,0,0] neg_hi:[1,0,0]
	v_pk_fma_f32 v[126:127], v[138:139], v[60:61], v[126:127] op_sel_hi:[0,1,1] neg_lo:[1,0,0] neg_hi:[1,0,0]
	v_pk_mul_f32 v[94:95], v[138:139], v[130:131] op_sel:[1,0]
	v_pk_mul_f32 v[128:129], v[140:141], v[130:131] op_sel_hi:[0,1]
	v_pk_mul_f32 v[148:149], v[140:141], v[130:131] op_sel:[1,0]
	v_pk_fma_f32 v[94:95], v[140:141], v[120:121], v[94:95] op_sel_hi:[0,1,1]
	v_pk_fma_f32 v[128:129], v[142:143], v[120:121], v[128:129] op_sel_hi:[0,1,1]
	v_pk_fma_f32 v[148:149], v[142:143], v[120:121], v[148:149] op_sel:[1,0,0]
	v_pk_fma_f32 v[94:95], v[140:141], v[126:127], v[94:95] op_sel:[1,0,0]
	v_pk_fma_f32 v[128:129], v[142:143], v[126:127], v[128:129] op_sel:[1,0,0]
	v_pk_fma_f32 v[148:149], v[144:145], v[126:127], v[148:149] op_sel_hi:[0,1,1]
	v_pk_mul_f32 v[150:151], v[136:137], v[94:95] op_sel_hi:[0,1]
	v_pk_fma_f32 v[150:151], v[136:137], v[128:129], v[150:151] op_sel:[1,0,0]
	v_pk_fma_f32 v[150:151], v[138:139], v[148:149], v[150:151] op_sel_hi:[0,1,1]
	v_pk_fma_f32 v[150:151], v[144:145], v[60:61], v[150:151] op_sel:[1,0,0] neg_lo:[0,0,1] neg_hi:[0,0,1]
	v_cmp_eq_u32_e64 s[10:11], 6, v147
	v_cmp_eq_u32_e64 s[14:15], 7, v147
	v_pk_add_f32 v[60:61], v[58:59], v[94:95]
	v_pk_add_f32 v[120:121], v[80:81], v[60:61]
	v_pk_add_f32 v[58:59], v[82:83], v[128:129]
	v_pk_add_f32 v[80:81], v[92:93], v[58:59]
	v_pk_add_f32 v[82:83], v[122:123], v[148:149]
	v_pk_add_f32 v[92:93], v[152:153], v[82:83]
	v_pk_add_f32 v[122:123], v[124:125], v[150:151]
	v_pk_add_f32 v[126:127], v[154:155], v[122:123]
	v_pk_fma_f32 v[124:125], v[72:73], v[120:121], v[126:127] op_sel_hi:[0,1,1]
	v_pk_fma_f32 v[130:131], v[76:77], v[120:121], v[126:127] op_sel_hi:[0,1,1]
	v_pk_fma_f32 v[124:125], v[72:73], v[80:81], v[124:125] op_sel:[1,0,0]
	v_pk_fma_f32 v[130:131], v[76:77], v[80:81], v[130:131] op_sel:[1,0,0]
	v_pk_fma_f32 v[124:125], v[74:75], v[92:93], v[124:125] op_sel_hi:[0,1,1]
	v_pk_fma_f32 v[130:131], v[78:79], v[92:93], v[130:131] op_sel_hi:[0,1,1]
	v_pk_fma_f32 v[126:127], v[104:105], v[120:121], v[126:127] op_sel_hi:[0,1,1]
	v_pk_fma_f32 v[126:127], v[104:105], v[80:81], v[126:127] op_sel:[1,0,0]
	v_pk_fma_f32 v[126:127], v[106:107], v[92:93], v[126:127] op_sel_hi:[0,1,1]
	v_cndmask_b32_e64 v152, 0, v18, s[10:11]
	v_cndmask_b32_e64 v153, 0, v18, s[14:15]
	v_add_f32_dpp v126, v124, v126 wave_shl:1 row_mask:0xf bank_mask:0xf bound_ctrl:1
	v_add_f32_dpp v127, v125, v127 wave_shl:1 row_mask:0xf bank_mask:0xf bound_ctrl:1
	s_add_i32 s4, s34, 2
	s_cmpk_lt_i32 s4, 0x201
	s_cselect_b64 s[12:13], s[0:1], 0
	v_add_f32_dpp v126, v130, v126 wave_shr:1 row_mask:0xf bank_mask:0xf bound_ctrl:1
	v_add_f32_dpp v127, v131, v127 wave_shr:1 row_mask:0xf bank_mask:0xf bound_ctrl:1
	v_pk_fma_f32 v[126:127], v[48:49], v[146:147], v[126:127] op_sel_hi:[1,0,1] neg_lo:[0,0,1] neg_hi:[0,0,1]
	v_pk_add_f32 v[126:127], v[126:127], v[152:153] neg_lo:[0,1] neg_hi:[0,1]
	v_pk_mul_f32 v[154:155], v[126:127], v[126:127]
	v_add_f32_e32 v154, v154, v155
	v_cndmask_b32_e64 v155, 0, v154, s[12:13]
	v_add_f32_e32 v1, v1, v155
	s_add_i32 s5, s34, 7
	s_min_i32 s5, s5, 0x200
	s_mul_i32 s6, s5, 0x804
	s_add_i32 s6, s6, s35
	s_add_i32 s7, s6, 0x505014
	s_add_i32 s8, s6, 0x606018
	s_mul_i32 s9, s5, 0x180c
	s_add_i32 s9, s9, s33
	s_add_i32 s4, s34, 8
	s_min_i32 s4, s4, 0x200
	s_mul_i32 s4, s4, 0x804
	s_add_i32 s4, s4, s38
	buffer_load_dword v24, v28, s[20:23], s4 offen nt
	buffer_load_dwordx3 v[72:74], v27, s[24:27], s9 offen nt
	buffer_load_dword v48, v28, s[16:19], s7 offen nt
	buffer_load_dword v49, v28, s[16:19], s8 offen nt
	s_waitcnt vmcnt(8)
	v_mov_b32_dpp v76, v32 wave_shr:1 row_mask:0xf bank_mask:0xf bound_ctrl:1
	v_mov_b32_dpp v77, v33 wave_shr:1 row_mask:0xf bank_mask:0xf bound_ctrl:1
	v_mov_b32_dpp v78, v34 wave_shr:1 row_mask:0xf bank_mask:0xf bound_ctrl:1
	v_mov_b32_dpp v104, v32 wave_shl:1 row_mask:0xf bank_mask:0xf bound_ctrl:1
	v_mov_b32_dpp v105, v33 wave_shl:1 row_mask:0xf bank_mask:0xf bound_ctrl:1
	v_mov_b32_dpp v106, v34 wave_shl:1 row_mask:0xf bank_mask:0xf bound_ctrl:1
	s_add_i32 s4, s34, 6
	s_cmpk_lt_u32 s4, 0x201
	s_cselect_b64 s[12:13], s[40:41], 0
	v_cmp_eq_u32_e64 s[14:15], s37, v16
	s_and_b64 s[14:15], s[14:15], s[12:13]
	v_cndmask_b32_e64 v29, 0, 1, s[14:15]
	v_mul_f32_e64 v80, v32, v32
	v_mul_f32_e64 v81, v32, v33
	v_mul_f32_e64 v92, v32, v34
	v_mul_f32_e64 v93, v33, v33
	v_mul_f32_e64 v120, v33, v34
	v_mul_f32_e64 v121, v34, v34
	v_or_b32_dpp v31, v29, v29 wave_shr:1 row_mask:0xf bank_mask:0xf bound_ctrl:1
	s_nop 1
	v_or_b32_dpp v31, v29, v31 wave_shl:1 row_mask:0xf bank_mask:0xf bound_ctrl:1
	s_nop 1
	v_or_b32_dpp v84, v31, v31 wave_shr:1 row_mask:0xf bank_mask:0xf bound_ctrl:1
	s_nop 1
	v_or_b32_dpp v84, v31, v84 wave_shl:1 row_mask:0xf bank_mask:0xf bound_ctrl:1
	v_or3_b32 v29, v84, v85, v52
	v_or3_b32 v29, v29, v30, v53
	s_add_i32 s4, s34, 3
	s_cmpk_lt_u32 s4, 0x1ff
	s_cselect_b64 s[12:13], s[42:43], 0
	v_cmp_ne_u32_e64 s[30:31], 0, v29
	s_and_b64 s[30:31], s[30:31], s[12:13]
	v_cndmask_b32_e64 v29, 0, 1.0, s[30:31]
	v_add_f32_e64 v124, v32, v76
	v_add_f32_e64 v125, v33, v77
	v_add_f32_e64 v126, v34, v78
	v_fma_f32 v80, v76, v76, v80
	v_fma_f32 v81, v76, v77, v81
	v_fma_f32 v92, v76, v78, v92
	v_fma_f32 v93, v77, v77, v93
	v_fma_f32 v120, v77, v78, v120
	v_fma_f32 v121, v78, v78, v121
	v_add_f32_dpp v139, v29, v29 wave_shr:1 row_mask:0xf bank_mask:0xf bound_ctrl:1
	v_add_f32_e64 v124, v124, v104
	v_add_f32_e64 v125, v125, v105
	v_add_f32_e64 v126, v126, v106
	v_fma_f32 v127, v104, v104, v80
	v_fma_f32 v130, v104, v105, v81
	v_fma_f32 v131, v104, v106, v92
	v_fma_f32 v136, v105, v105, v93
	v_fma_f32 v137, v105, v106, v120
	v_fma_f32 v138, v106, v106, v121
	v_add_f32_dpp v139, v29, v139 wave_shl:1 row_mask:0xf bank_mask:0xf bound_ctrl:1
	v_pk_add_f32 v[80:81], v[38:39], v[124:125]
	v_pk_add_f32 v[38:39], v[54:55], v[126:127]
	v_pk_add_f32 v[54:55], v[108:109], v[130:131]
	v_pk_add_f32 v[92:93], v[112:113], v[136:137]
	v_pk_add_f32 v[108:109], v[114:115], v[138:139]
	v_mul_f32_e64 v112, v80, v22
	v_mul_f32_e64 v113, v81, v22
	v_mul_f32_e64 v114, v38, v22
	v_fma_f32 v29, v39, v22, v26
	v_mul_f32_e64 v31, v54, v22
	v_mul_f32_e64 v120, v55, v22
	v_fma_f32 v121, v92, v22, v26
	v_mul_f32_e64 v152, v93, v22
	v_fma_f32 v153, v108, v22, v26
	v_fma_f32 v29, -v112, v112, v29
	v_fma_f32 v31, -v112, v113, v31
	v_fma_f32 v120, -v112, v114, v120
	v_fma_f32 v121, -v113, v113, v121
	v_fma_f32 v152, -v113, v114, v152
	v_fma_f32 v153, -v114, v114, v153
	v_mul_f32_e64 v154, v152, v152
	v_mul_f32_e64 v155, v31, v153
	v_mul_f32_e64 v156, v120, v121
	v_mul_f32_e64 v157, v120, v120
	v_mul_f32_e64 v158, v29, v152
	v_mul_f32_e64 v159, v31, v31
	v_fma_f32 v154, v121, v153, -v154
	v_fma_f32 v155, v120, v152, -v155
	v_fma_f32 v156, v31, v152, -v156
	v_fma_f32 v157, v29, v153, -v157
	v_fma_f32 v158, v31, v120, -v158
	v_fma_f32 v159, v29, v121, -v159
	v_mul_f32_e64 v160, v29, v154
	v_fma_f32 v160, v31, v155, v160
	v_fma_f32 v160, v120, v156, v160
	v_rcp_f32_e32 v160, v160
	v_cmp_ne_u32_e64 vcc, s37, v17
	v_mul_f32_e64 v160, v160, v22
	v_cndmask_b32_e64 v160, 0, v160, s[30:31]
	v_cndmask_b32_e64 v29, 0, v18, vcc
	v_cndmask_b32_e64 v145, 0, v22, s[30:31]
	v_mul_f32_e64 v115, v154, v160
	v_mul_f32_e64 v140, v155, v160
	v_mul_f32_e64 v141, v156, v160
	v_mul_f32_e64 v142, v157, v160
	v_mul_f32_e64 v143, v158, v160
	v_mul_f32_e64 v144, v159, v160
	v_add_f32_e64 v146, v109, v29
	v_mov_b32_e32 v147, v17
	ds_write_b128 v23, v[112:115] offset:3072
	ds_write_b128 v23, v[140:143] offset:4096
	ds_write_b128 v23, v[144:147] offset:5120
	s_waitcnt lgkmcnt(0)
	s_barrier
	v_mov_b32_dpp v38, v20 wave_shr:1 row_mask:0xf bank_mask:0xf bound_ctrl:1
	v_mov_b32_dpp v39, v21 wave_shr:1 row_mask:0xf bank_mask:0xf bound_ctrl:1
	v_mov_b32_dpp v54, v20 wave_shl:1 row_mask:0xf bank_mask:0xf bound_ctrl:1
	v_mov_b32_dpp v55, v21 wave_shl:1 row_mask:0xf bank_mask:0xf bound_ctrl:1
	v_pk_mul_f32 v[80:81], v[20:21], v[32:33] op_sel_hi:[1,0]
	v_pk_mul_f32 v[92:93], v[20:21], v[32:33] op_sel:[0,1]
	v_pk_mul_f32 v[108:109], v[20:21], v[34:35] op_sel_hi:[1,0]
	v_pk_add_f32 v[120:121], v[20:21], v[38:39]
	v_pk_fma_f32 v[80:81], v[38:39], v[76:77], v[80:81] op_sel_hi:[1,0,1]
	v_pk_fma_f32 v[92:93], v[38:39], v[76:77], v[92:93] op_sel:[0,1,0]
	v_pk_fma_f32 v[108:109], v[38:39], v[78:79], v[108:109] op_sel_hi:[1,0,1]
	v_pk_add_f32 v[120:121], v[120:121], v[54:55]
	v_pk_fma_f32 v[80:81], v[54:55], v[104:105], v[80:81] op_sel_hi:[1,0,1]
	v_pk_fma_f32 v[92:93], v[54:55], v[104:105], v[92:93] op_sel:[0,1,0]
	v_pk_fma_f32 v[108:109], v[54:55], v[106:107], v[108:109] op_sel_hi:[1,0,1]
	v_pk_add_f32 v[38:39], v[50:51], v[120:121]
	v_pk_add_f32 v[50:51], v[118:119], v[80:81]
	v_pk_add_f32 v[54:55], v[64:65], v[92:93]
	v_pk_add_f32 v[64:65], v[90:91], v[108:109]
	v_pk_fma_f32 v[50:51], v[112:113], v[38:39], v[50:51] op_sel_hi:[0,1,1] neg_lo:[1,0,0] neg_hi:[1,0,0]
	v_pk_fma_f32 v[54:55], v[112:113], v[38:39], v[54:55] op_sel:[1,0,0] neg_lo:[1,0,0] neg_hi:[1,0,0]
	v_pk_fma_f32 v[64:65], v[114:115], v[38:39], v[64:65] op_sel_hi:[0,1,1] neg_lo:[1,0,0] neg_hi:[1,0,0]
	v_pk_mul_f32 v[90:91], v[114:115], v[50:51] op_sel:[1,0]
	v_pk_mul_f32 v[118:119], v[140:141], v[50:51] op_sel_hi:[0,1]
	v_pk_mul_f32 v[152:153], v[140:141], v[50:51] op_sel:[1,0]
	v_pk_fma_f32 v[90:91], v[140:141], v[54:55], v[90:91] op_sel_hi:[0,1,1]
	v_pk_fma_f32 v[118:119], v[142:143], v[54:55], v[118:119] op_sel_hi:[0,1,1]
	v_pk_fma_f32 v[152:153], v[142:143], v[54:55], v[152:153] op_sel:[1,0,0]
	v_pk_fma_f32 v[90:91], v[140:141], v[64:65], v[90:91] op_sel:[1,0,0]
	v_pk_fma_f32 v[118:119], v[142:143], v[64:65], v[118:119] op_sel:[1,0,0]
	v_pk_fma_f32 v[152:153], v[144:145], v[64:65], v[152:153] op_sel_hi:[0,1,1]
	v_pk_mul_f32 v[154:155], v[112:113], v[90:91] op_sel_hi:[0,1]
	v_pk_fma_f32 v[154:155], v[112:113], v[118:119], v[154:155] op_sel:[1,0,0]
	v_pk_fma_f32 v[154:155], v[114:115], v[152:153], v[154:155] op_sel_hi:[0,1,1]
	v_pk_fma_f32 v[154:155], v[144:145], v[38:39], v[154:155] op_sel:[1,0,0] neg_lo:[0,0,1] neg_hi:[0,0,1]
	v_cmp_eq_u32_e64 s[10:11], 6, v147
	v_cmp_eq_u32_e64 s[14:15], 7, v147
	v_pk_add_f32 v[38:39], v[60:61], v[90:91]
	v_pk_add_f32 v[50:51], v[58:59], v[118:119]
	v_pk_add_f32 v[54:55], v[82:83], v[152:153]
	v_pk_add_f32 v[58:59], v[122:123], v[154:155]
	v_pk_fma_f32 v[60:61], v[96:97], v[38:39], v[58:59] op_sel_hi:[0,1,1]
	v_pk_fma_f32 v[64:65], v[100:101], v[38:39], v[58:59] op_sel_hi:[0,1,1]
	v_pk_fma_f32 v[60:61], v[96:97], v[50:51], v[60:61] op_sel:[1,0,0]
	v_pk_fma_f32 v[64:65], v[100:101], v[50:51], v[64:65] op_sel:[1,0,0]
	v_pk_fma_f32 v[60:61], v[98:99], v[54:55], v[60:61] op_sel_hi:[0,1,1]
	v_pk_fma_f32 v[64:65], v[102:103], v[54:55], v[64:65] op_sel_hi:[0,1,1]
	v_pk_fma_f32 v[58:59], v[8:9], v[38:39], v[58:59] op_sel_hi:[0,1,1]
	v_pk_fma_f32 v[58:59], v[8:9], v[50:51], v[58:59] op_sel:[1,0,0]
	v_pk_fma_f32 v[58:59], v[10:11], v[54:55], v[58:59] op_sel_hi:[0,1,1]
	v_cndmask_b32_e64 v82, 0, v18, s[10:11]
	v_cndmask_b32_e64 v83, 0, v18, s[14:15]
	v_add_f32_dpp v58, v60, v58 wave_shl:1 row_mask:0xf bank_mask:0xf bound_ctrl:1
	v_add_f32_dpp v59, v61, v59 wave_shl:1 row_mask:0xf bank_mask:0xf bound_ctrl:1
	s_add_i32 s4, s34, 3
	s_cmpk_lt_i32 s4, 0x201
	s_cselect_b64 s[12:13], s[0:1], 0
	v_add_f32_dpp v58, v64, v58 wave_shr:1 row_mask:0xf bank_mask:0xf bound_ctrl:1
	v_add_f32_dpp v59, v65, v59 wave_shr:1 row_mask:0xf bank_mask:0xf bound_ctrl:1
	v_pk_fma_f32 v[58:59], v[4:5], v[146:147], v[58:59] op_sel_hi:[1,0,1] neg_lo:[0,0,1] neg_hi:[0,0,1]
	v_pk_add_f32 v[58:59], v[58:59], v[82:83] neg_lo:[0,1] neg_hi:[0,1]
	v_pk_mul_f32 v[122:123], v[58:59], v[58:59]
	v_add_f32_e32 v122, v122, v123
	v_cndmask_b32_e64 v123, 0, v122, s[12:13]
	v_add_f32_e32 v1, v1, v123
	s_add_i32 s5, s34, 8
	s_min_i32 s5, s5, 0x200
	s_mul_i32 s6, s5, 0x804
	s_add_i32 s6, s6, s35
	s_add_i32 s7, s6, 0x505014
	s_add_i32 s8, s6, 0x606018
	s_mul_i32 s9, s5, 0x180c
	s_add_i32 s9, s9, s33
	s_add_i32 s4, s34, 9
	s_min_i32 s4, s4, 0x200
	s_mul_i32 s4, s4, 0x804
	s_add_i32 s4, s4, s38
	buffer_load_dword v17, v28, s[20:23], s4 offen nt
	buffer_load_dwordx3 v[8:10], v27, s[24:27], s9 offen nt
	buffer_load_dword v4, v28, s[16:19], s7 offen nt
	buffer_load_dword v5, v28, s[16:19], s8 offen nt
	s_waitcnt vmcnt(8)
	v_mov_b32_dpp v96, v40 wave_shr:1 row_mask:0xf bank_mask:0xf bound_ctrl:1
	v_mov_b32_dpp v97, v41 wave_shr:1 row_mask:0xf bank_mask:0xf bound_ctrl:1
	v_mov_b32_dpp v98, v42 wave_shr:1 row_mask:0xf bank_mask:0xf bound_ctrl:1
	v_mov_b32_dpp v100, v40 wave_shl:1 row_mask:0xf bank_mask:0xf bound_ctrl:1
	v_mov_b32_dpp v101, v41 wave_shl:1 row_mask:0xf bank_mask:0xf bound_ctrl:1
	v_mov_b32_dpp v102, v42 wave_shl:1 row_mask:0xf bank_mask:0xf bound_ctrl:1
	s_add_i32 s4, s34, 7
	s_cmpk_lt_u32 s4, 0x201
	s_cselect_b64 s[12:13], s[40:41], 0
	v_cmp_eq_u32_e64 s[14:15], s37, v25
	s_and_b64 s[14:15], s[14:15], s[12:13]
	v_cndmask_b32_e64 v29, 0, 1, s[14:15]
	v_mul_f32_e64 v38, v40, v40
	v_mul_f32_e64 v39, v40, v41
	v_mul_f32_e64 v50, v40, v42
	v_mul_f32_e64 v51, v41, v41
	v_mul_f32_e64 v54, v41, v42
	v_mul_f32_e64 v55, v42, v42
	v_or_b32_dpp v31, v29, v29 wave_shr:1 row_mask:0xf bank_mask:0xf bound_ctrl:1
	s_nop 1
	v_or_b32_dpp v31, v29, v31 wave_shl:1 row_mask:0xf bank_mask:0xf bound_ctrl:1
	s_nop 1
	v_or_b32_dpp v53, v31, v31 wave_shr:1 row_mask:0xf bank_mask:0xf bound_ctrl:1
	s_nop 1
	v_or_b32_dpp v53, v31, v53 wave_shl:1 row_mask:0xf bank_mask:0xf bound_ctrl:1
	v_or3_b32 v29, v53, v84, v85
	v_or3_b32 v29, v29, v52, v30
	s_add_i32 s4, s34, 4
	s_cmpk_lt_u32 s4, 0x1ff
	s_cselect_b64 s[12:13], s[42:43], 0
	v_cmp_ne_u32_e64 s[30:31], 0, v29
	s_and_b64 s[30:31], s[30:31], s[12:13]
	v_cndmask_b32_e64 v29, 0, 1.0, s[30:31]
	v_add_f32_e64 v58, v40, v96
	v_add_f32_e64 v59, v41, v97
	v_add_f32_e64 v60, v42, v98
	v_fma_f32 v38, v96, v96, v38
	v_fma_f32 v39, v96, v97, v39
	v_fma_f32 v50, v96, v98, v50
	v_fma_f32 v51, v97, v97, v51
	v_fma_f32 v54, v97, v98, v54
	v_fma_f32 v55, v98, v98, v55
	v_add_f32_dpp v113, v29, v29 wave_shr:1 row_mask:0xf bank_mask:0xf bound_ctrl:1
	v_add_f32_e64 v58, v58, v100
	v_add_f32_e64 v59, v59, v101
	v_add_f32_e64 v60, v60, v102
	v_fma_f32 v61, v100, v100, v38
	v_fma_f32 v64, v100, v101, v39
	v_fma_f32 v65, v100, v102, v50
	v_fma_f32 v82, v101, v101, v51
	v_fma_f32 v83, v101, v102, v54
	v_fma_f32 v112, v102, v102, v55
	v_add_f32_dpp v113, v29, v113 wave_shl:1 row_mask:0xf bank_mask:0xf bound_ctrl:1
	v_pk_add_f32 v[38:39], v[124:125], v[58:59]
	v_pk_add_f32 v[50:51], v[56:57], v[38:39]
	v_pk_add_f32 v[54:55], v[126:127], v[60:61]
	v_pk_add_f32 v[56:57], v[62:63], v[54:55]
	v_pk_add_f32 v[62:63], v[130:131], v[64:65]
	v_pk_add_f32 v[114:115], v[66:67], v[62:63]
	v_pk_add_f32 v[66:67], v[136:137], v[82:83]
	v_pk_add_f32 v[122:123], v[86:87], v[66:67]
	v_pk_add_f32 v[86:87], v[138:139], v[112:113]
	v_pk_add_f32 v[124:125], v[88:89], v[86:87]
	v_mul_f32_e64 v136, v50, v22
	v_mul_f32_e64 v137, v51, v22
	v_mul_f32_e64 v138, v56, v22
	v_fma_f32 v29, v57, v22, v26
	v_mul_f32_e64 v31, v114, v22
	v_mul_f32_e64 v88, v115, v22
	v_fma_f32 v89, v122, v22, v26
	v_mul_f32_e64 v126, v123, v22
	v_fma_f32 v127, v124, v22, v26
	v_fma_f32 v29, -v136, v136, v29
	v_fma_f32 v31, -v136, v137, v31
	v_fma_f32 v88, -v136, v138, v88
	v_fma_f32 v89, -v137, v137, v89
	v_fma_f32 v126, -v137, v138, v126
	v_fma_f32 v127, -v138, v138, v127
	v_mul_f32_e64 v130, v126, v126
	v_mul_f32_e64 v131, v31, v127
	v_mul_f32_e64 v156, v88, v89
	v_mul_f32_e64 v157, v88, v88
	v_mul_f32_e64 v158, v29, v126
	v_mul_f32_e64 v159, v31, v31
	v_fma_f32 v130, v89, v127, -v130
	v_fma_f32 v131, v88, v126, -v131
	v_fma_f32 v156, v31, v126, -v156
	v_fma_f32 v157, v29, v127, -v157
	v_fma_f32 v158, v31, v88, -v158
	v_fma_f32 v159, v29, v89, -v159
	v_mul_f32_e64 v160, v29, v130
	v_fma_f32 v160, v31, v131, v160
	v_fma_f32 v160, v88, v156, v160
	v_rcp_f32_e32 v160, v160
	v_cmp_ne_u32_e64 vcc, s37, v2
	v_mul_f32_e64 v160, v160, v22
	v_cndmask_b32_e64 v160, 0, v160, s[30:31]
	v_cndmask_b32_e64 v29, 0, v18, vcc
	v_cndmask_b32_e64 v145, 0, v22, s[30:31]
	v_mul_f32_e64 v139, v130, v160
	v_mul_f32_e64 v140, v131, v160
	v_mul_f32_e64 v141, v156, v160
	v_mul_f32_e64 v142, v157, v160
	v_mul_f32_e64 v143, v158, v160
	v_mul_f32_e64 v144, v159, v160
	v_add_f32_e64 v146, v125, v29
	v_mov_b32_e32 v147, v2
	ds_write_b128 v23, v[136:139]
	ds_write_b128 v23, v[140:143] offset:1024
	ds_write_b128 v23, v[144:147] offset:2048
	s_waitcnt lgkmcnt(0)
	s_barrier
	v_mov_b32_dpp v30, v36 wave_shr:1 row_mask:0xf bank_mask:0xf bound_ctrl:1
	v_mov_b32_dpp v31, v37 wave_shr:1 row_mask:0xf bank_mask:0xf bound_ctrl:1
	v_mov_b32_dpp v50, v36 wave_shl:1 row_mask:0xf bank_mask:0xf bound_ctrl:1
	v_mov_b32_dpp v51, v37 wave_shl:1 row_mask:0xf bank_mask:0xf bound_ctrl:1
	v_pk_mul_f32 v[56:57], v[36:37], v[40:41] op_sel_hi:[1,0]
	v_pk_mul_f32 v[88:89], v[36:37], v[40:41] op_sel:[0,1]
	v_pk_mul_f32 v[114:115], v[36:37], v[42:43] op_sel_hi:[1,0]
	v_pk_add_f32 v[122:123], v[36:37], v[30:31]
	v_pk_fma_f32 v[56:57], v[30:31], v[96:97], v[56:57] op_sel_hi:[1,0,1]
	v_pk_fma_f32 v[88:89], v[30:31], v[96:97], v[88:89] op_sel:[0,1,0]
	v_pk_fma_f32 v[114:115], v[30:31], v[98:99], v[114:115] op_sel_hi:[1,0,1]
	v_pk_add_f32 v[122:123], v[122:123], v[50:51]
	v_pk_fma_f32 v[56:57], v[50:51], v[100:101], v[56:57] op_sel_hi:[1,0,1]
	v_pk_fma_f32 v[88:89], v[50:51], v[100:101], v[88:89] op_sel:[0,1,0]
	v_pk_fma_f32 v[114:115], v[50:51], v[102:103], v[114:115] op_sel_hi:[1,0,1]
	v_pk_add_f32 v[30:31], v[120:121], v[122:123]
	v_pk_add_f32 v[50:51], v[134:135], v[30:31]
	v_pk_add_f32 v[120:121], v[80:81], v[56:57]
	v_pk_add_f32 v[124:125], v[110:111], v[120:121]
	v_pk_add_f32 v[80:81], v[92:93], v[88:89]
	v_pk_add_f32 v[110:111], v[116:117], v[80:81]
	v_pk_add_f32 v[92:93], v[108:109], v[114:115]
	v_pk_add_f32 v[116:117], v[132:133], v[92:93]
	v_pk_fma_f32 v[124:125], v[136:137], v[50:51], v[124:125] op_sel_hi:[0,1,1] neg_lo:[1,0,0] neg_hi:[1,0,0]
	v_pk_fma_f32 v[110:111], v[136:137], v[50:51], v[110:111] op_sel:[1,0,0] neg_lo:[1,0,0] neg_hi:[1,0,0]
	v_pk_fma_f32 v[116:117], v[138:139], v[50:51], v[116:117] op_sel_hi:[0,1,1] neg_lo:[1,0,0] neg_hi:[1,0,0]
	v_pk_mul_f32 v[108:109], v[138:139], v[124:125] op_sel:[1,0]
	v_pk_mul_f32 v[126:127], v[140:141], v[124:125] op_sel_hi:[0,1]
	v_pk_mul_f32 v[130:131], v[140:141], v[124:125] op_sel:[1,0]
	v_pk_fma_f32 v[108:109], v[140:141], v[110:111], v[108:109] op_sel_hi:[0,1,1]
	v_pk_fma_f32 v[126:127], v[142:143], v[110:111], v[126:127] op_sel_hi:[0,1,1]
	v_pk_fma_f32 v[130:131], v[142:143], v[110:111], v[130:131] op_sel:[1,0,0]
	v_pk_fma_f32 v[108:109], v[140:141], v[116:117], v[108:109] op_sel:[1,0,0]
	v_pk_fma_f32 v[126:127], v[142:143], v[116:117], v[126:127] op_sel:[1,0,0]
	v_pk_fma_f32 v[130:131], v[144:145], v[116:117], v[130:131] op_sel_hi:[0,1,1]
	v_pk_mul_f32 v[132:133], v[136:137], v[108:109] op_sel_hi:[0,1]
	v_pk_fma_f32 v[132:133], v[136:137], v[126:127], v[132:133] op_sel:[1,0,0]
	v_pk_fma_f32 v[132:133], v[138:139], v[130:131], v[132:133] op_sel_hi:[0,1,1]
	v_pk_fma_f32 v[132:133], v[144:145], v[50:51], v[132:133] op_sel:[1,0,0] neg_lo:[0,0,1] neg_hi:[0,0,1]
	v_cmp_eq_u32_e64 s[10:11], 6, v147
	v_cmp_eq_u32_e64 s[14:15], 7, v147
	v_pk_add_f32 v[50:51], v[90:91], v[108:109]
	v_pk_add_f32 v[110:111], v[94:95], v[50:51]
	v_pk_add_f32 v[90:91], v[118:119], v[126:127]
	v_pk_add_f32 v[94:95], v[128:129], v[90:91]
	v_pk_add_f32 v[116:117], v[152:153], v[130:131]
	v_pk_add_f32 v[118:119], v[148:149], v[116:117]
	v_pk_add_f32 v[124:125], v[154:155], v[132:133]
	v_pk_add_f32 v[128:129], v[150:151], v[124:125]
	v_pk_fma_f32 v[134:135], v[44:45], v[110:111], v[128:129] op_sel_hi:[0,1,1]
	v_pk_fma_f32 v[148:149], v[68:69], v[110:111], v[128:129] op_sel_hi:[0,1,1]
	v_pk_fma_f32 v[134:135], v[44:45], v[94:95], v[134:135] op_sel:[1,0,0]
	v_pk_fma_f32 v[148:149], v[68:69], v[94:95], v[148:149] op_sel:[1,0,0]
	v_pk_fma_f32 v[134:135], v[46:47], v[118:119], v[134:135] op_sel_hi:[0,1,1]
	v_pk_fma_f32 v[148:149], v[70:71], v[118:119], v[148:149] op_sel_hi:[0,1,1]
	v_pk_fma_f32 v[128:129], v[12:13], v[110:111], v[128:129] op_sel_hi:[0,1,1]
	v_pk_fma_f32 v[128:129], v[12:13], v[94:95], v[128:129] op_sel:[1,0,0]
	v_pk_fma_f32 v[128:129], v[14:15], v[118:119], v[128:129] op_sel_hi:[0,1,1]
	v_cndmask_b32_e64 v150, 0, v18, s[10:11]
	v_cndmask_b32_e64 v151, 0, v18, s[14:15]
	v_add_f32_dpp v128, v134, v128 wave_shl:1 row_mask:0xf bank_mask:0xf bound_ctrl:1
	v_add_f32_dpp v129, v135, v129 wave_shl:1 row_mask:0xf bank_mask:0xf bound_ctrl:1
	s_add_i32 s4, s34, 4
	s_cmpk_lt_i32 s4, 0x201
	s_cselect_b64 s[12:13], s[0:1], 0
	v_add_f32_dpp v128, v148, v128 wave_shr:1 row_mask:0xf bank_mask:0xf bound_ctrl:1
	v_add_f32_dpp v129, v149, v129 wave_shr:1 row_mask:0xf bank_mask:0xf bound_ctrl:1
	v_pk_fma_f32 v[128:129], v[6:7], v[146:147], v[128:129] op_sel_hi:[1,0,1] neg_lo:[0,0,1] neg_hi:[0,0,1]
	v_pk_add_f32 v[128:129], v[128:129], v[150:151] neg_lo:[0,1] neg_hi:[0,1]
	v_pk_mul_f32 v[152:153], v[128:129], v[128:129]
	v_add_f32_e32 v152, v152, v153
	v_cndmask_b32_e64 v153, 0, v152, s[12:13]
	v_add_f32_e32 v1, v1, v153
	s_add_i32 s5, s34, 9
	s_min_i32 s5, s5, 0x200
	s_mul_i32 s6, s5, 0x804
	s_add_i32 s6, s6, s35
	s_add_i32 s7, s6, 0x505014
	s_add_i32 s8, s6, 0x606018
	s_mul_i32 s9, s5, 0x180c
	s_add_i32 s9, s9, s33
	s_add_i32 s4, s34, 10
	s_min_i32 s4, s4, 0x200
	s_mul_i32 s4, s4, 0x804
	s_add_i32 s4, s4, s38
	buffer_load_dword v2, v28, s[20:23], s4 offen nt
	buffer_load_dwordx3 v[12:14], v27, s[24:27], s9 offen nt
	buffer_load_dword v6, v28, s[16:19], s7 offen nt
	buffer_load_dword v7, v28, s[16:19], s8 offen nt
	s_waitcnt vmcnt(8)
	v_mov_b32_dpp v44, v72 wave_shr:1 row_mask:0xf bank_mask:0xf bound_ctrl:1
	v_mov_b32_dpp v45, v73 wave_shr:1 row_mask:0xf bank_mask:0xf bound_ctrl:1
	v_mov_b32_dpp v46, v74 wave_shr:1 row_mask:0xf bank_mask:0xf bound_ctrl:1
	v_mov_b32_dpp v68, v72 wave_shl:1 row_mask:0xf bank_mask:0xf bound_ctrl:1
	v_mov_b32_dpp v69, v73 wave_shl:1 row_mask:0xf bank_mask:0xf bound_ctrl:1
	v_mov_b32_dpp v70, v74 wave_shl:1 row_mask:0xf bank_mask:0xf bound_ctrl:1
	s_add_i32 s4, s34, 8
	s_cmpk_lt_u32 s4, 0x201
	s_cselect_b64 s[12:13], s[40:41], 0
	v_cmp_eq_u32_e64 s[14:15], s37, v24
	s_and_b64 s[14:15], s[14:15], s[12:13]
	v_cndmask_b32_e64 v29, 0, 1, s[14:15]
	v_mul_f32_e64 v94, v72, v72
	v_mul_f32_e64 v95, v72, v73
	v_mul_f32_e64 v110, v72, v74
	v_mul_f32_e64 v111, v73, v73
	v_mul_f32_e64 v118, v73, v74
	v_mul_f32_e64 v119, v74, v74
	v_or_b32_dpp v128, v29, v29 wave_shr:1 row_mask:0xf bank_mask:0xf bound_ctrl:1
	s_nop 1
	v_or_b32_dpp v128, v29, v128 wave_shl:1 row_mask:0xf bank_mask:0xf bound_ctrl:1
	s_nop 1
	v_or_b32_dpp v129, v128, v128 wave_shr:1 row_mask:0xf bank_mask:0xf bound_ctrl:1
	s_nop 1
	v_or_b32_dpp v129, v128, v129 wave_shl:1 row_mask:0xf bank_mask:0xf bound_ctrl:1
	v_or3_b32 v29, v129, v53, v84
	v_or3_b32 v29, v29, v85, v52
	s_add_i32 s4, s34, 5
	s_cmpk_lt_u32 s4, 0x1ff
	s_cselect_b64 s[12:13], s[42:43], 0
	v_cmp_ne_u32_e64 s[30:31], 0, v29
	s_and_b64 s[30:31], s[30:31], s[12:13]
	v_cndmask_b32_e64 v29, 0, 1.0, s[30:31]
	v_add_f32_e64 v134, v72, v44
	v_add_f32_e64 v135, v73, v45
	v_add_f32_e64 v136, v74, v46
	v_fma_f32 v94, v44, v44, v94
	v_fma_f32 v95, v44, v45, v95
	v_fma_f32 v110, v44, v46, v110
	v_fma_f32 v111, v45, v45, v111
	v_fma_f32 v118, v45, v46, v118
	v_fma_f32 v119, v46, v46, v119
	v_add_f32_dpp v143, v29, v29 wave_shr:1 row_mask:0xf bank_mask:0xf bound_ctrl:1
	v_add_f32_e64 v134, v134, v68
	v_add_f32_e64 v135, v135, v69
	v_add_f32_e64 v136, v136, v70
	v_fma_f32 v137, v68, v68, v94
	v_fma_f32 v138, v68, v69, v95
	v_fma_f32 v139, v68, v70, v110
	v_fma_f32 v140, v69, v69, v111
	v_fma_f32 v141, v69, v70, v118
	v_fma_f32 v142, v70, v70, v119
	v_add_f32_dpp v143, v29, v143 wave_shl:1 row_mask:0xf bank_mask:0xf bound_ctrl:1
	v_pk_add_f32 v[94:95], v[38:39], v[134:135]
	v_pk_add_f32 v[38:39], v[54:55], v[136:137]
	v_pk_add_f32 v[54:55], v[62:63], v[138:139]
	v_pk_add_f32 v[62:63], v[66:67], v[140:141]
	v_pk_add_f32 v[66:67], v[86:87], v[142:143]
	v_mul_f32_e64 v144, v94, v22
	v_mul_f32_e64 v145, v95, v22
	v_mul_f32_e64 v146, v38, v22
	v_fma_f32 v29, v39, v22, v26
	v_mul_f32_e64 v128, v54, v22
	v_mul_f32_e64 v86, v55, v22
	v_fma_f32 v87, v62, v22, v26
	v_mul_f32_e64 v110, v63, v22
	v_fma_f32 v111, v66, v22, v26
	v_fma_f32 v29, -v144, v144, v29
	v_fma_f32 v128, -v144, v145, v128
	v_fma_f32 v86, -v144, v146, v86
	v_fma_f32 v87, -v145, v145, v87
	v_fma_f32 v110, -v145, v146, v110
	v_fma_f32 v111, -v146, v146, v111
	v_mul_f32_e64 v118, v110, v110
	v_mul_f32_e64 v119, v128, v111
	v_mul_f32_e64 v156, v86, v87
	v_mul_f32_e64 v157, v86, v86
	v_mul_f32_e64 v158, v29, v110
	v_mul_f32_e64 v159, v128, v128
	v_fma_f32 v118, v87, v111, -v118
	v_fma_f32 v119, v86, v110, -v119
	v_fma_f32 v156, v128, v110, -v156
	v_fma_f32 v157, v29, v111, -v157
	v_fma_f32 v158, v128, v86, -v158
	v_fma_f32 v159, v29, v87, -v159
	v_mul_f32_e64 v160, v29, v118
	v_fma_f32 v160, v128, v119, v160
	v_fma_f32 v160, v86, v156, v160
	v_rcp_f32_e32 v160, v160
	v_cmp_ne_u32_e64 vcc, s37, v3
	v_mul_f32_e64 v160, v160, v22
	v_cndmask_b32_e64 v160, 0, v160, s[30:31]
	v_cndmask_b32_e64 v29, 0, v18, vcc
	v_cndmask_b32_e64 v153, 0, v22, s[30:31]
	v_mul_f32_e64 v147, v118, v160
	v_mul_f32_e64 v148, v119, v160
	v_mul_f32_e64 v149, v156, v160
	v_mul_f32_e64 v150, v157, v160
	v_mul_f32_e64 v151, v158, v160
	v_mul_f32_e64 v152, v159, v160
	v_add_f32_e64 v154, v67, v29
	v_mov_b32_e32 v155, v3
	ds_write_b128 v23, v[144:147] offset:3072
	ds_write_b128 v23, v[148:151] offset:4096
	ds_write_b128 v23, v[152:155] offset:5120
	s_waitcnt lgkmcnt(0)
	s_barrier
	v_mov_b32_dpp v38, v48 wave_shr:1 row_mask:0xf bank_mask:0xf bound_ctrl:1
	v_mov_b32_dpp v39, v49 wave_shr:1 row_mask:0xf bank_mask:0xf bound_ctrl:1
	v_mov_b32_dpp v54, v48 wave_shl:1 row_mask:0xf bank_mask:0xf bound_ctrl:1
	v_mov_b32_dpp v55, v49 wave_shl:1 row_mask:0xf bank_mask:0xf bound_ctrl:1
	v_pk_mul_f32 v[62:63], v[48:49], v[72:73] op_sel_hi:[1,0]
	v_pk_mul_f32 v[66:67], v[48:49], v[72:73] op_sel:[0,1]
	v_pk_mul_f32 v[86:87], v[48:49], v[74:75] op_sel_hi:[1,0]
	v_pk_add_f32 v[94:95], v[48:49], v[38:39]
	v_pk_fma_f32 v[62:63], v[38:39], v[44:45], v[62:63] op_sel_hi:[1,0,1]
	v_pk_fma_f32 v[66:67], v[38:39], v[44:45], v[66:67] op_sel:[0,1,0]
	v_pk_fma_f32 v[86:87], v[38:39], v[46:47], v[86:87] op_sel_hi:[1,0,1]
	v_pk_add_f32 v[94:95], v[94:95], v[54:55]
	v_pk_fma_f32 v[62:63], v[54:55], v[68:69], v[62:63] op_sel_hi:[1,0,1]
	v_pk_fma_f32 v[66:67], v[54:55], v[68:69], v[66:67] op_sel:[0,1,0]
	v_pk_fma_f32 v[86:87], v[54:55], v[70:71], v[86:87] op_sel_hi:[1,0,1]
	v_pk_add_f32 v[38:39], v[30:31], v[94:95]
	v_pk_add_f32 v[30:31], v[120:121], v[62:63]
	v_pk_add_f32 v[54:55], v[80:81], v[66:67]
	v_pk_add_f32 v[80:81], v[92:93], v[86:87]
	v_pk_fma_f32 v[30:31], v[144:145], v[38:39], v[30:31] op_sel_hi:[0,1,1] neg_lo:[1,0,0] neg_hi:[1,0,0]
	v_pk_fma_f32 v[54:55], v[144:145], v[38:39], v[54:55] op_sel:[1,0,0] neg_lo:[1,0,0] neg_hi:[1,0,0]
	v_pk_fma_f32 v[80:81], v[146:147], v[38:39], v[80:81] op_sel_hi:[0,1,1] neg_lo:[1,0,0] neg_hi:[1,0,0]
	v_pk_mul_f32 v[92:93], v[146:147], v[30:31] op_sel:[1,0]
	v_pk_mul_f32 v[110:111], v[148:149], v[30:31] op_sel_hi:[0,1]
	v_pk_mul_f32 v[118:119], v[148:149], v[30:31] op_sel:[1,0]
	v_pk_fma_f32 v[92:93], v[148:149], v[54:55], v[92:93] op_sel_hi:[0,1,1]
	v_pk_fma_f32 v[110:111], v[150:151], v[54:55], v[110:111] op_sel_hi:[0,1,1]
	v_pk_fma_f32 v[118:119], v[150:151], v[54:55], v[118:119] op_sel:[1,0,0]
	v_pk_fma_f32 v[92:93], v[148:149], v[80:81], v[92:93] op_sel:[1,0,0]
	v_pk_fma_f32 v[110:111], v[150:151], v[80:81], v[110:111] op_sel:[1,0,0]
	v_pk_fma_f32 v[118:119], v[152:153], v[80:81], v[118:119] op_sel_hi:[0,1,1]
	v_pk_mul_f32 v[120:121], v[144:145], v[92:93] op_sel_hi:[0,1]
	v_pk_fma_f32 v[120:121], v[144:145], v[110:111], v[120:121] op_sel:[1,0,0]
	v_pk_fma_f32 v[120:121], v[146:147], v[118:119], v[120:121] op_sel_hi:[0,1,1]
	v_pk_fma_f32 v[120:121], v[152:153], v[38:39], v[120:121] op_sel:[1,0,0] neg_lo:[0,0,1] neg_hi:[0,0,1]
	v_cmp_eq_u32_e64 s[10:11], 6, v155
	v_cmp_eq_u32_e64 s[14:15], 7, v155
	v_pk_add_f32 v[30:31], v[50:51], v[92:93]
	v_pk_add_f32 v[38:39], v[90:91], v[110:111]
	v_pk_add_f32 v[50:51], v[116:117], v[118:119]
	v_pk_add_f32 v[54:55], v[124:125], v[120:121]
	v_pk_fma_f32 v[80:81], v[76:77], v[30:31], v[54:55] op_sel_hi:[0,1,1]
	v_pk_fma_f32 v[90:91], v[104:105], v[30:31], v[54:55] op_sel_hi:[0,1,1]
	v_pk_fma_f32 v[80:81], v[76:77], v[38:39], v[80:81] op_sel:[1,0,0]
	v_pk_fma_f32 v[90:91], v[104:105], v[38:39], v[90:91] op_sel:[1,0,0]
	v_pk_fma_f32 v[80:81], v[78:79], v[50:51], v[80:81] op_sel_hi:[0,1,1]
	v_pk_fma_f32 v[90:91], v[106:107], v[50:51], v[90:91] op_sel_hi:[0,1,1]
	v_pk_fma_f32 v[54:55], v[32:33], v[30:31], v[54:55] op_sel_hi:[0,1,1]
	v_pk_fma_f32 v[54:55], v[32:33], v[38:39], v[54:55] op_sel:[1,0,0]
	v_pk_fma_f32 v[54:55], v[34:35], v[50:51], v[54:55] op_sel_hi:[0,1,1]
	v_cndmask_b32_e64 v116, 0, v18, s[10:11]
	v_cndmask_b32_e64 v117, 0, v18, s[14:15]
	v_add_f32_dpp v54, v80, v54 wave_shl:1 row_mask:0xf bank_mask:0xf bound_ctrl:1
	v_add_f32_dpp v55, v81, v55 wave_shl:1 row_mask:0xf bank_mask:0xf bound_ctrl:1
	s_add_i32 s4, s34, 5
	s_cmpk_lt_i32 s4, 0x201
	s_cselect_b64 s[12:13], s[0:1], 0
	v_add_f32_dpp v54, v90, v54 wave_shr:1 row_mask:0xf bank_mask:0xf bound_ctrl:1
	v_add_f32_dpp v55, v91, v55 wave_shr:1 row_mask:0xf bank_mask:0xf bound_ctrl:1
	v_pk_fma_f32 v[54:55], v[20:21], v[154:155], v[54:55] op_sel_hi:[1,0,1] neg_lo:[0,0,1] neg_hi:[0,0,1]
	v_pk_add_f32 v[54:55], v[54:55], v[116:117] neg_lo:[0,1] neg_hi:[0,1]
	v_pk_mul_f32 v[124:125], v[54:55], v[54:55]
	v_add_f32_e32 v124, v124, v125
	v_cndmask_b32_e64 v125, 0, v124, s[12:13]
	v_add_f32_e32 v1, v1, v125
	s_add_i32 s5, s34, 10
	s_min_i32 s5, s5, 0x200
	s_mul_i32 s6, s5, 0x804
	s_add_i32 s6, s6, s35
	s_add_i32 s7, s6, 0x505014
	s_add_i32 s8, s6, 0x606018
	s_mul_i32 s9, s5, 0x180c
	s_add_i32 s9, s9, s33
	s_add_i32 s4, s34, 11
	s_min_i32 s4, s4, 0x200
	s_mul_i32 s4, s4, 0x804
	s_add_i32 s4, s4, s38
	buffer_load_dword v3, v28, s[20:23], s4 offen nt
	buffer_load_dwordx3 v[32:34], v27, s[24:27], s9 offen nt
	buffer_load_dword v20, v28, s[16:19], s7 offen nt
	buffer_load_dword v21, v28, s[16:19], s8 offen nt
	s_waitcnt vmcnt(8)
	v_mov_b32_dpp v76, v8 wave_shr:1 row_mask:0xf bank_mask:0xf bound_ctrl:1
	v_mov_b32_dpp v77, v9 wave_shr:1 row_mask:0xf bank_mask:0xf bound_ctrl:1
	v_mov_b32_dpp v78, v10 wave_shr:1 row_mask:0xf bank_mask:0xf bound_ctrl:1
	v_mov_b32_dpp v104, v8 wave_shl:1 row_mask:0xf bank_mask:0xf bound_ctrl:1
	v_mov_b32_dpp v105, v9 wave_shl:1 row_mask:0xf bank_mask:0xf bound_ctrl:1
	v_mov_b32_dpp v106, v10 wave_shl:1 row_mask:0xf bank_mask:0xf bound_ctrl:1
	s_add_i32 s4, s34, 9
	s_cmpk_lt_u32 s4, 0x201
	s_cselect_b64 s[12:13], s[40:41], 0
	v_cmp_eq_u32_e64 s[14:15], s37, v17
	s_and_b64 s[14:15], s[14:15], s[12:13]
	v_cndmask_b32_e64 v29, 0, 1, s[14:15]
	v_mul_f32_e64 v30, v8, v8
	v_mul_f32_e64 v31, v8, v9
	v_mul_f32_e64 v38, v8, v10
	v_mul_f32_e64 v39, v9, v9
	v_mul_f32_e64 v50, v9, v10
	v_mul_f32_e64 v51, v10, v10
	v_or_b32_dpp v52, v29, v29 wave_shr:1 row_mask:0xf bank_mask:0xf bound_ctrl:1
	s_nop 1
	v_or_b32_dpp v52, v29, v52 wave_shl:1 row_mask:0xf bank_mask:0xf bound_ctrl:1
	s_nop 1
	v_or_b32_dpp v128, v52, v52 wave_shr:1 row_mask:0xf bank_mask:0xf bound_ctrl:1
	s_nop 1
	v_or_b32_dpp v128, v52, v128 wave_shl:1 row_mask:0xf bank_mask:0xf bound_ctrl:1
	v_or3_b32 v29, v128, v129, v53
	v_or3_b32 v29, v29, v84, v85
	s_add_i32 s4, s34, 6
	s_cmpk_lt_u32 s4, 0x1ff
	s_cselect_b64 s[12:13], s[42:43], 0
	v_cmp_ne_u32_e64 s[30:31], 0, v29
	s_and_b64 s[30:31], s[30:31], s[12:13]
	v_cndmask_b32_e64 v29, 0, 1.0, s[30:31]
	v_add_f32_e64 v54, v8, v76
	v_add_f32_e64 v55, v9, v77
	v_add_f32_e64 v80, v10, v78
	v_fma_f32 v30, v76, v76, v30
	v_fma_f32 v31, v76, v77, v31
	v_fma_f32 v38, v76, v78, v38
	v_fma_f32 v39, v77, v77, v39
	v_fma_f32 v50, v77, v78, v50
	v_fma_f32 v51, v78, v78, v51
	v_add_f32_dpp v125, v29, v29 wave_shr:1 row_mask:0xf bank_mask:0xf bound_ctrl:1
	v_add_f32_e64 v54, v54, v104
	v_add_f32_e64 v55, v55, v105
	v_add_f32_e64 v80, v80, v106
	v_fma_f32 v81, v104, v104, v30
	v_fma_f32 v90, v104, v105, v31
	v_fma_f32 v91, v104, v106, v38
	v_fma_f32 v116, v105, v105, v39
	v_fma_f32 v117, v105, v106, v50
	v_fma_f32 v124, v106, v106, v51
	v_add_f32_dpp v125, v29, v125 wave_shl:1 row_mask:0xf bank_mask:0xf bound_ctrl:1
	v_pk_add_f32 v[30:31], v[134:135], v[54:55]
	v_pk_add_f32 v[38:39], v[58:59], v[30:31]
	v_pk_add_f32 v[50:51], v[136:137], v[80:81]
	v_pk_add_f32 v[58:59], v[60:61], v[50:51]
	v_pk_add_f32 v[60:61], v[138:139], v[90:91]
	v_pk_add_f32 v[134:135], v[64:65], v[60:61]
	v_pk_add_f32 v[64:65], v[140:141], v[116:117]
	v_pk_add_f32 v[136:137], v[82:83], v[64:65]
	v_pk_add_f32 v[82:83], v[142:143], v[124:125]
	v_pk_add_f32 v[138:139], v[112:113], v[82:83]
	v_mul_f32_e64 v140, v38, v22
	v_mul_f32_e64 v141, v39, v22
	v_mul_f32_e64 v142, v58, v22
	v_fma_f32 v29, v59, v22, v26
	v_mul_f32_e64 v52, v134, v22
	v_mul_f32_e64 v112, v135, v22
	v_fma_f32 v113, v136, v22, v26
	v_mul_f32_e64 v152, v137, v22
	v_fma_f32 v153, v138, v22, v26
	v_fma_f32 v29, -v140, v140, v29
	v_fma_f32 v52, -v140, v141, v52
	v_fma_f32 v112, -v140, v142, v112
	v_fma_f32 v113, -v141, v141, v113
	v_fma_f32 v152, -v141, v142, v152
	v_fma_f32 v153, -v142, v142, v153
	v_mul_f32_e64 v154, v152, v152
	v_mul_f32_e64 v155, v52, v153
	v_mul_f32_e64 v156, v112, v113
	v_mul_f32_e64 v157, v112, v112
	v_mul_f32_e64 v158, v29, v152
	v_mul_f32_e64 v159, v52, v52
	v_fma_f32 v154, v113, v153, -v154
	v_fma_f32 v155, v112, v152, -v155
	v_fma_f32 v156, v52, v152, -v156
	v_fma_f32 v157, v29, v153, -v157
	v_fma_f32 v158, v52, v112, -v158
	v_fma_f32 v159, v29, v113, -v159
	v_mul_f32_e64 v160, v29, v154
	v_fma_f32 v160, v52, v155, v160
	v_fma_f32 v160, v112, v156, v160
	v_rcp_f32_e32 v160, v160
	v_cmp_ne_u32_e64 vcc, s37, v16
	v_mul_f32_e64 v160, v160, v22
	v_cndmask_b32_e64 v160, 0, v160, s[30:31]
	v_cndmask_b32_e64 v29, 0, v18, vcc
	v_cndmask_b32_e64 v149, 0, v22, s[30:31]
	v_mul_f32_e64 v143, v154, v160
	v_mul_f32_e64 v144, v155, v160
	v_mul_f32_e64 v145, v156, v160
	v_mul_f32_e64 v146, v157, v160
	v_mul_f32_e64 v147, v158, v160
	v_mul_f32_e64 v148, v159, v160
	v_add_f32_e64 v150, v139, v29
	v_mov_b32_e32 v151, v16
	ds_write_b128 v23, v[140:143]
	ds_write_b128 v23, v[144:147] offset:1024
	ds_write_b128 v23, v[148:151] offset:2048
	s_waitcnt lgkmcnt(0)
	s_barrier
	v_mov_b32_dpp v38, v4 wave_shr:1 row_mask:0xf bank_mask:0xf bound_ctrl:1
	v_mov_b32_dpp v39, v5 wave_shr:1 row_mask:0xf bank_mask:0xf bound_ctrl:1
	v_mov_b32_dpp v58, v4 wave_shl:1 row_mask:0xf bank_mask:0xf bound_ctrl:1
	v_mov_b32_dpp v59, v5 wave_shl:1 row_mask:0xf bank_mask:0xf bound_ctrl:1
	v_pk_mul_f32 v[112:113], v[4:5], v[8:9] op_sel_hi:[1,0]
	v_pk_mul_f32 v[134:135], v[4:5], v[8:9] op_sel:[0,1]
	v_pk_mul_f32 v[136:137], v[4:5], v[10:11] op_sel_hi:[1,0]
	v_pk_add_f32 v[138:139], v[4:5], v[38:39]
	v_pk_fma_f32 v[112:113], v[38:39], v[76:77], v[112:113] op_sel_hi:[1,0,1]
	v_pk_fma_f32 v[134:135], v[38:39], v[76:77], v[134:135] op_sel:[0,1,0]
	v_pk_fma_f32 v[136:137], v[38:39], v[78:79], v[136:137] op_sel_hi:[1,0,1]
	v_pk_add_f32 v[138:139], v[138:139], v[58:59]
	v_pk_fma_f32 v[112:113], v[58:59], v[104:105], v[112:113] op_sel_hi:[1,0,1]
	v_pk_fma_f32 v[134:135], v[58:59], v[104:105], v[134:135] op_sel:[0,1,0]
	v_pk_fma_f32 v[136:137], v[58:59], v[106:107], v[136:137] op_sel_hi:[1,0,1]
	v_pk_add_f32 v[38:39], v[94:95], v[138:139]
	v_pk_add_f32 v[58:59], v[122:123], v[38:39]
	v_pk_add_f32 v[94:95], v[62:63], v[112:113]
	v_pk_add_f32 v[122:123], v[56:57], v[94:95]
	v_pk_add_f32 v[56:57], v[66:67], v[134:135]
	v_pk_add_f32 v[62:63], v[88:89], v[56:57]
	v_pk_add_f32 v[66:67], v[86:87], v[136:137]
	v_pk_add_f32 v[88:89], v[114:115], v[66:67]
	v_pk_fma_f32 v[122:123], v[140:141], v[58:59], v[122:123] op_sel_hi:[0,1,1] neg_lo:[1,0,0] neg_hi:[1,0,0]
	v_pk_fma_f32 v[62:63], v[140:141], v[58:59], v[62:63] op_sel:[1,0,0] neg_lo:[1,0,0] neg_hi:[1,0,0]
	v_pk_fma_f32 v[88:89], v[142:143], v[58:59], v[88:89] op_sel_hi:[0,1,1] neg_lo:[1,0,0] neg_hi:[1,0,0]
	v_pk_mul_f32 v[86:87], v[142:143], v[122:123] op_sel:[1,0]
	v_pk_mul_f32 v[114:115], v[144:145], v[122:123] op_sel_hi:[0,1]
	v_pk_mul_f32 v[152:153], v[144:145], v[122:123] op_sel:[1,0]
	v_pk_fma_f32 v[86:87], v[144:145], v[62:63], v[86:87] op_sel_hi:[0,1,1]
	v_pk_fma_f32 v[114:115], v[146:147], v[62:63], v[114:115] op_sel_hi:[0,1,1]
	v_pk_fma_f32 v[152:153], v[146:147], v[62:63], v[152:153] op_sel:[1,0,0]
	v_pk_fma_f32 v[86:87], v[144:145], v[88:89], v[86:87] op_sel:[1,0,0]
	v_pk_fma_f32 v[114:115], v[146:147], v[88:89], v[114:115] op_sel:[1,0,0]
	v_pk_fma_f32 v[152:153], v[148:149], v[88:89], v[152:153] op_sel_hi:[0,1,1]
	v_pk_mul_f32 v[154:155], v[140:141], v[86:87] op_sel_hi:[0,1]
	v_pk_fma_f32 v[154:155], v[140:141], v[114:115], v[154:155] op_sel:[1,0,0]
	v_pk_fma_f32 v[154:155], v[142:143], v[152:153], v[154:155] op_sel_hi:[0,1,1]
	v_pk_fma_f32 v[154:155], v[148:149], v[58:59], v[154:155] op_sel:[1,0,0] neg_lo:[0,0,1] neg_hi:[0,0,1]
	v_cmp_eq_u32_e64 s[10:11], 6, v151
	v_cmp_eq_u32_e64 s[14:15], 7, v151
	v_pk_add_f32 v[58:59], v[92:93], v[86:87]
	v_pk_add_f32 v[62:63], v[108:109], v[58:59]
	v_pk_add_f32 v[88:89], v[110:111], v[114:115]
	v_pk_add_f32 v[92:93], v[126:127], v[88:89]
	v_pk_add_f32 v[108:109], v[118:119], v[152:153]
	v_pk_add_f32 v[110:111], v[130:131], v[108:109]
	v_pk_add_f32 v[118:119], v[120:121], v[154:155]
	v_pk_add_f32 v[122:123], v[132:133], v[118:119]
	v_pk_fma_f32 v[120:121], v[96:97], v[62:63], v[122:123] op_sel_hi:[0,1,1]
	v_pk_fma_f32 v[126:127], v[100:101], v[62:63], v[122:123] op_sel_hi:[0,1,1]
	v_pk_fma_f32 v[120:121], v[96:97], v[92:93], v[120:121] op_sel:[1,0,0]
	v_pk_fma_f32 v[126:127], v[100:101], v[92:93], v[126:127] op_sel:[1,0,0]
	v_pk_fma_f32 v[120:121], v[98:99], v[110:111], v[120:121] op_sel_hi:[0,1,1]
	v_pk_fma_f32 v[126:127], v[102:103], v[110:111], v[126:127] op_sel_hi:[0,1,1]
	v_pk_fma_f32 v[122:123], v[40:41], v[62:63], v[122:123] op_sel_hi:[0,1,1]
	v_pk_fma_f32 v[122:123], v[40:41], v[92:93], v[122:123] op_sel:[1,0,0]
	v_pk_fma_f32 v[122:123], v[42:43], v[110:111], v[122:123] op_sel_hi:[0,1,1]
	v_cndmask_b32_e64 v130, 0, v18, s[10:11]
	v_cndmask_b32_e64 v131, 0, v18, s[14:15]
	v_add_f32_dpp v122, v120, v122 wave_shl:1 row_mask:0xf bank_mask:0xf bound_ctrl:1
	v_add_f32_dpp v123, v121, v123 wave_shl:1 row_mask:0xf bank_mask:0xf bound_ctrl:1
	s_add_i32 s4, s34, 6
	s_cmpk_lt_i32 s4, 0x201
	s_cselect_b64 s[12:13], s[0:1], 0
	v_add_f32_dpp v122, v126, v122 wave_shr:1 row_mask:0xf bank_mask:0xf bound_ctrl:1
	v_add_f32_dpp v123, v127, v123 wave_shr:1 row_mask:0xf bank_mask:0xf bound_ctrl:1
	v_pk_fma_f32 v[122:123], v[36:37], v[150:151], v[122:123] op_sel_hi:[1,0,1] neg_lo:[0,0,1] neg_hi:[0,0,1]
	v_pk_add_f32 v[122:123], v[122:123], v[130:131] neg_lo:[0,1] neg_hi:[0,1]
	v_pk_mul_f32 v[132:133], v[122:123], v[122:123]
	v_add_f32_e32 v132, v132, v133
	v_cndmask_b32_e64 v133, 0, v132, s[12:13]
	v_add_f32_e32 v1, v1, v133
	s_add_i32 s5, s34, 11
	s_min_i32 s5, s5, 0x200
	s_mul_i32 s6, s5, 0x804
	s_add_i32 s6, s6, s35
	s_add_i32 s7, s6, 0x505014
	s_add_i32 s8, s6, 0x606018
	s_mul_i32 s9, s5, 0x180c
	s_add_i32 s9, s9, s33
	s_add_i32 s4, s34, 12
	s_min_i32 s4, s4, 0x200
	s_mul_i32 s4, s4, 0x804
	s_add_i32 s4, s4, s38
	buffer_load_dword v16, v28, s[20:23], s4 offen nt
	buffer_load_dwordx3 v[40:42], v27, s[24:27], s9 offen nt
	buffer_load_dword v36, v28, s[16:19], s7 offen nt
	buffer_load_dword v37, v28, s[16:19], s8 offen nt
	s_waitcnt vmcnt(8)
	v_mov_b32_dpp v96, v12 wave_shr:1 row_mask:0xf bank_mask:0xf bound_ctrl:1
	v_mov_b32_dpp v97, v13 wave_shr:1 row_mask:0xf bank_mask:0xf bound_ctrl:1
	v_mov_b32_dpp v98, v14 wave_shr:1 row_mask:0xf bank_mask:0xf bound_ctrl:1
	v_mov_b32_dpp v100, v12 wave_shl:1 row_mask:0xf bank_mask:0xf bound_ctrl:1
	v_mov_b32_dpp v101, v13 wave_shl:1 row_mask:0xf bank_mask:0xf bound_ctrl:1
	v_mov_b32_dpp v102, v14 wave_shl:1 row_mask:0xf bank_mask:0xf bound_ctrl:1
	s_add_i32 s4, s34, 10
	s_cmpk_lt_u32 s4, 0x201
	s_cselect_b64 s[12:13], s[40:41], 0
	v_cmp_eq_u32_e64 s[14:15], s37, v2
	s_and_b64 s[14:15], s[14:15], s[12:13]
	v_cndmask_b32_e64 v29, 0, 1, s[14:15]
	v_mul_f32_e64 v62, v12, v12
	v_mul_f32_e64 v63, v12, v13
	v_mul_f32_e64 v92, v12, v14
	v_mul_f32_e64 v93, v13, v13
	v_mul_f32_e64 v110, v13, v14
	v_mul_f32_e64 v111, v14, v14
	v_or_b32_dpp v52, v29, v29 wave_shr:1 row_mask:0xf bank_mask:0xf bound_ctrl:1
	s_nop 1
	v_or_b32_dpp v52, v29, v52 wave_shl:1 row_mask:0xf bank_mask:0xf bound_ctrl:1
	s_nop 1
	v_or_b32_dpp v85, v52, v52 wave_shr:1 row_mask:0xf bank_mask:0xf bound_ctrl:1
	s_nop 1
	v_or_b32_dpp v85, v52, v85 wave_shl:1 row_mask:0xf bank_mask:0xf bound_ctrl:1
	v_or3_b32 v29, v85, v128, v129
	v_or3_b32 v29, v29, v53, v84
	s_add_i32 s4, s34, 7
	s_cmpk_lt_u32 s4, 0x1ff
	s_cselect_b64 s[12:13], s[42:43], 0
	v_cmp_ne_u32_e64 s[30:31], 0, v29
	s_and_b64 s[30:31], s[30:31], s[12:13]
	v_cndmask_b32_e64 v29, 0, 1.0, s[30:31]
	v_add_f32_e64 v120, v12, v96
	v_add_f32_e64 v121, v13, v97
	v_add_f32_e64 v122, v14, v98
	v_fma_f32 v62, v96, v96, v62
	v_fma_f32 v63, v96, v97, v63
	v_fma_f32 v92, v96, v98, v92
	v_fma_f32 v93, v97, v97, v93
	v_fma_f32 v110, v97, v98, v110
	v_fma_f32 v111, v98, v98, v111
	v_add_f32_dpp v133, v29, v29 wave_shr:1 row_mask:0xf bank_mask:0xf bound_ctrl:1
	v_add_f32_e64 v120, v120, v100
	v_add_f32_e64 v121, v121, v101
	v_add_f32_e64 v122, v122, v102
	v_fma_f32 v123, v100, v100, v62
	v_fma_f32 v126, v100, v101, v63
	v_fma_f32 v127, v100, v102, v92
	v_fma_f32 v130, v101, v101, v93
	v_fma_f32 v131, v101, v102, v110
	v_fma_f32 v132, v102, v102, v111
	v_add_f32_dpp v133, v29, v133 wave_shl:1 row_mask:0xf bank_mask:0xf bound_ctrl:1
	v_pk_add_f32 v[62:63], v[30:31], v[120:121]
	v_pk_add_f32 v[30:31], v[50:51], v[122:123]
	v_pk_add_f32 v[50:51], v[60:61], v[126:127]
	v_pk_add_f32 v[60:61], v[64:65], v[130:131]
	v_pk_add_f32 v[64:65], v[82:83], v[132:133]
	v_mul_f32_e64 v140, v62, v22
	v_mul_f32_e64 v141, v63, v22
	v_mul_f32_e64 v142, v30, v22
	v_fma_f32 v29, v31, v22, v26
	v_mul_f32_e64 v52, v50, v22
	v_mul_f32_e64 v82, v51, v22
	v_fma_f32 v83, v60, v22, v26
	v_mul_f32_e64 v92, v61, v22
	v_fma_f32 v93, v64, v22, v26
	v_fma_f32 v29, -v140, v140, v29
	v_fma_f32 v52, -v140, v141, v52
	v_fma_f32 v82, -v140, v142, v82
	v_fma_f32 v83, -v141, v141, v83
	v_fma_f32 v92, -v141, v142, v92
	v_fma_f32 v93, -v142, v142, v93
	v_mul_f32_e64 v110, v92, v92
	v_mul_f32_e64 v111, v52, v93
	v_mul_f32_e64 v156, v82, v83
	v_mul_f32_e64 v157, v82, v82
	v_mul_f32_e64 v158, v29, v92
	v_mul_f32_e64 v159, v52, v52
	v_fma_f32 v110, v83, v93, -v110
	v_fma_f32 v111, v82, v92, -v111
	v_fma_f32 v156, v52, v92, -v156
	v_fma_f32 v157, v29, v93, -v157
	v_fma_f32 v158, v52, v82, -v158
	v_fma_f32 v159, v29, v83, -v159
	v_mul_f32_e64 v160, v29, v110
	v_fma_f32 v160, v52, v111, v160
	v_fma_f32 v160, v82, v156, v160
	v_rcp_f32_e32 v160, v160
	v_cmp_ne_u32_e64 vcc, s37, v25
	v_mul_f32_e64 v160, v160, v22
	v_cndmask_b32_e64 v160, 0, v160, s[30:31]
	v_cndmask_b32_e64 v29, 0, v18, vcc
	v_cndmask_b32_e64 v149, 0, v22, s[30:31]
	v_mul_f32_e64 v143, v110, v160
	v_mul_f32_e64 v144, v111, v160
	v_mul_f32_e64 v145, v156, v160
	v_mul_f32_e64 v146, v157, v160
	v_mul_f32_e64 v147, v158, v160
	v_mul_f32_e64 v148, v159, v160
	v_add_f32_e64 v150, v65, v29
	v_mov_b32_e32 v151, v25
	ds_write_b128 v23, v[140:143] offset:3072
	ds_write_b128 v23, v[144:147] offset:4096
	ds_write_b128 v23, v[148:151] offset:5120
	s_waitcnt lgkmcnt(0)
	s_barrier
	v_mov_b32_dpp v30, v6 wave_shr:1 row_mask:0xf bank_mask:0xf bound_ctrl:1
	v_mov_b32_dpp v31, v7 wave_shr:1 row_mask:0xf bank_mask:0xf bound_ctrl:1
	v_mov_b32_dpp v50, v6 wave_shl:1 row_mask:0xf bank_mask:0xf bound_ctrl:1
	v_mov_b32_dpp v51, v7 wave_shl:1 row_mask:0xf bank_mask:0xf bound_ctrl:1
	v_pk_mul_f32 v[60:61], v[6:7], v[12:13] op_sel_hi:[1,0]
	v_pk_mul_f32 v[62:63], v[6:7], v[12:13] op_sel:[0,1]
	v_pk_mul_f32 v[64:65], v[6:7], v[14:15] op_sel_hi:[1,0]
	v_pk_add_f32 v[82:83], v[6:7], v[30:31]
	v_pk_fma_f32 v[60:61], v[30:31], v[96:97], v[60:61] op_sel_hi:[1,0,1]
	v_pk_fma_f32 v[62:63], v[30:31], v[96:97], v[62:63] op_sel:[0,1,0]
	v_pk_fma_f32 v[64:65], v[30:31], v[98:99], v[64:65] op_sel_hi:[1,0,1]
	v_pk_add_f32 v[82:83], v[82:83], v[50:51]
	v_pk_fma_f32 v[60:61], v[50:51], v[100:101], v[60:61] op_sel_hi:[1,0,1]
	v_pk_fma_f32 v[62:63], v[50:51], v[100:101], v[62:63] op_sel:[0,1,0]
	v_pk_fma_f32 v[64:65], v[50:51], v[102:103], v[64:65] op_sel_hi:[1,0,1]
	v_pk_add_f32 v[30:31], v[38:39], v[82:83]
	v_pk_add_f32 v[38:39], v[94:95], v[60:61]
	v_pk_add_f32 v[50:51], v[56:57], v[62:63]
	v_pk_add_f32 v[56:57], v[66:67], v[64:65]
	v_pk_fma_f32 v[38:39], v[140:141], v[30:31], v[38:39] op_sel_hi:[0,1,1] neg_lo:[1,0,0] neg_hi:[1,0,0]
	v_pk_fma_f32 v[50:51], v[140:141], v[30:31], v[50:51] op_sel:[1,0,0] neg_lo:[1,0,0] neg_hi:[1,0,0]
	v_pk_fma_f32 v[56:57], v[142:143], v[30:31], v[56:57] op_sel_hi:[0,1,1] neg_lo:[1,0,0] neg_hi:[1,0,0]
	v_pk_mul_f32 v[66:67], v[142:143], v[38:39] op_sel:[1,0]
	v_pk_mul_f32 v[92:93], v[144:145], v[38:39] op_sel_hi:[0,1]
	v_pk_mul_f32 v[94:95], v[144:145], v[38:39] op_sel:[1,0]
	v_pk_fma_f32 v[66:67], v[144:145], v[50:51], v[66:67] op_sel_hi:[0,1,1]
	v_pk_fma_f32 v[92:93], v[146:147], v[50:51], v[92:93] op_sel_hi:[0,1,1]
	v_pk_fma_f32 v[94:95], v[146:147], v[50:51], v[94:95] op_sel:[1,0,0]
	v_pk_fma_f32 v[66:67], v[144:145], v[56:57], v[66:67] op_sel:[1,0,0]
	v_pk_fma_f32 v[92:93], v[146:147], v[56:57], v[92:93] op_sel:[1,0,0]
	v_pk_fma_f32 v[94:95], v[148:149], v[56:57], v[94:95] op_sel_hi:[0,1,1]
	v_pk_mul_f32 v[110:111], v[140:141], v[66:67] op_sel_hi:[0,1]
	v_pk_fma_f32 v[110:111], v[140:141], v[92:93], v[110:111] op_sel:[1,0,0]
	v_pk_fma_f32 v[110:111], v[142:143], v[94:95], v[110:111] op_sel_hi:[0,1,1]
	v_pk_fma_f32 v[110:111], v[148:149], v[30:31], v[110:111] op_sel:[1,0,0] neg_lo:[0,0,1] neg_hi:[0,0,1]
	v_cmp_eq_u32_e64 s[10:11], 6, v151
	v_cmp_eq_u32_e64 s[14:15], 7, v151
	v_pk_add_f32 v[30:31], v[58:59], v[66:67]
	v_pk_add_f32 v[38:39], v[88:89], v[92:93]
	v_pk_add_f32 v[50:51], v[108:109], v[94:95]
	v_pk_add_f32 v[56:57], v[118:119], v[110:111]
	v_pk_fma_f32 v[58:59], v[44:45], v[30:31], v[56:57] op_sel_hi:[0,1,1]
	v_pk_fma_f32 v[88:89], v[68:69], v[30:31], v[56:57] op_sel_hi:[0,1,1]
	v_pk_fma_f32 v[58:59], v[44:45], v[38:39], v[58:59] op_sel:[1,0,0]
	v_pk_fma_f32 v[88:89], v[68:69], v[38:39], v[88:89] op_sel:[1,0,0]
	v_pk_fma_f32 v[58:59], v[46:47], v[50:51], v[58:59] op_sel_hi:[0,1,1]
	v_pk_fma_f32 v[88:89], v[70:71], v[50:51], v[88:89] op_sel_hi:[0,1,1]
	v_pk_fma_f32 v[56:57], v[72:73], v[30:31], v[56:57] op_sel_hi:[0,1,1]
	v_pk_fma_f32 v[56:57], v[72:73], v[38:39], v[56:57] op_sel:[1,0,0]
	v_pk_fma_f32 v[56:57], v[74:75], v[50:51], v[56:57] op_sel_hi:[0,1,1]
	v_cndmask_b32_e64 v108, 0, v18, s[10:11]
	v_cndmask_b32_e64 v109, 0, v18, s[14:15]
	v_add_f32_dpp v56, v58, v56 wave_shl:1 row_mask:0xf bank_mask:0xf bound_ctrl:1
	v_add_f32_dpp v57, v59, v57 wave_shl:1 row_mask:0xf bank_mask:0xf bound_ctrl:1
	s_add_i32 s4, s34, 7
	s_cmpk_lt_i32 s4, 0x201
	s_cselect_b64 s[12:13], s[0:1], 0
	v_add_f32_dpp v56, v88, v56 wave_shr:1 row_mask:0xf bank_mask:0xf bound_ctrl:1
	v_add_f32_dpp v57, v89, v57 wave_shr:1 row_mask:0xf bank_mask:0xf bound_ctrl:1
	v_pk_fma_f32 v[56:57], v[48:49], v[150:151], v[56:57] op_sel_hi:[1,0,1] neg_lo:[0,0,1] neg_hi:[0,0,1]
	v_pk_add_f32 v[56:57], v[56:57], v[108:109] neg_lo:[0,1] neg_hi:[0,1]
	v_pk_mul_f32 v[118:119], v[56:57], v[56:57]
	v_add_f32_e32 v118, v118, v119
	v_cndmask_b32_e64 v119, 0, v118, s[12:13]
	v_add_f32_e32 v1, v1, v119
	s_waitcnt vmcnt(4)
	v_mov_b32_dpp v44, v32 wave_shr:1 row_mask:0xf bank_mask:0xf bound_ctrl:1
	v_mov_b32_dpp v45, v33 wave_shr:1 row_mask:0xf bank_mask:0xf bound_ctrl:1
	v_mov_b32_dpp v46, v34 wave_shr:1 row_mask:0xf bank_mask:0xf bound_ctrl:1
	v_mov_b32_dpp v48, v32 wave_shl:1 row_mask:0xf bank_mask:0xf bound_ctrl:1
	v_mov_b32_dpp v49, v33 wave_shl:1 row_mask:0xf bank_mask:0xf bound_ctrl:1
	v_mov_b32_dpp v50, v34 wave_shl:1 row_mask:0xf bank_mask:0xf bound_ctrl:1
	s_add_i32 s4, s34, 11
	s_cmpk_lt_u32 s4, 0x201
	s_cselect_b64 s[12:13], s[40:41], 0
	v_cmp_eq_u32_e64 s[14:15], s37, v3
	s_and_b64 s[14:15], s[14:15], s[12:13]
	v_cndmask_b32_e64 v25, 0, 1, s[14:15]
	v_mul_f32_e64 v30, v32, v32
	v_mul_f32_e64 v31, v32, v33
	v_mul_f32_e64 v38, v32, v34
	v_mul_f32_e64 v39, v33, v33
	v_mul_f32_e64 v56, v33, v34
	v_mul_f32_e64 v57, v34, v34
	v_or_b32_dpp v29, v25, v25 wave_shr:1 row_mask:0xf bank_mask:0xf bound_ctrl:1
	s_nop 1
	v_or_b32_dpp v29, v25, v29 wave_shl:1 row_mask:0xf bank_mask:0xf bound_ctrl:1
	s_nop 1
	v_or_b32_dpp v52, v29, v29 wave_shr:1 row_mask:0xf bank_mask:0xf bound_ctrl:1
	s_nop 1
	v_or_b32_dpp v52, v29, v52 wave_shl:1 row_mask:0xf bank_mask:0xf bound_ctrl:1
	v_or3_b32 v25, v52, v85, v128
	v_or3_b32 v25, v25, v129, v53
	s_add_i32 s4, s34, 8
	s_cmpk_lt_u32 s4, 0x1ff
	s_cselect_b64 s[12:13], s[42:43], 0
	v_cmp_ne_u32_e64 s[30:31], 0, v25
	s_and_b64 s[30:31], s[30:31], s[12:13]
	v_cndmask_b32_e64 v25, 0, 1.0, s[30:31]
	v_add_f32_e64 v58, v32, v44
	v_add_f32_e64 v59, v33, v45
	v_add_f32_e64 v68, v34, v46
	v_fma_f32 v30, v44, v44, v30
	v_fma_f32 v31, v44, v45, v31
	v_fma_f32 v38, v44, v46, v38
	v_fma_f32 v39, v45, v45, v39
	v_fma_f32 v56, v45, v46, v56
	v_fma_f32 v57, v46, v46, v57
	v_add_f32_dpp v75, v25, v25 wave_shr:1 row_mask:0xf bank_mask:0xf bound_ctrl:1
	v_add_f32_e64 v58, v58, v48
	v_add_f32_e64 v59, v59, v49
	v_add_f32_e64 v68, v68, v50
	v_fma_f32 v69, v48, v48, v30
	v_fma_f32 v70, v48, v49, v31
	v_fma_f32 v71, v48, v50, v38
	v_fma_f32 v72, v49, v49, v39
	v_fma_f32 v73, v49, v50, v56
	v_fma_f32 v74, v50, v50, v57
	v_add_f32_dpp v75, v25, v75 wave_shl:1 row_mask:0xf bank_mask:0xf bound_ctrl:1
	v_pk_add_f32 v[30:31], v[120:121], v[58:59]
	v_pk_add_f32 v[38:39], v[54:55], v[30:31]
	v_pk_add_f32 v[54:55], v[122:123], v[68:69]
	v_pk_add_f32 v[56:57], v[80:81], v[54:55]
	v_pk_add_f32 v[80:81], v[126:127], v[70:71]
	v_pk_add_f32 v[88:89], v[90:91], v[80:81]
	v_pk_add_f32 v[90:91], v[130:131], v[72:73]
	v_pk_add_f32 v[108:109], v[116:117], v[90:91]
	v_pk_add_f32 v[116:117], v[132:133], v[74:75]
	v_pk_add_f32 v[118:119], v[124:125], v[116:117]
	v_mul_f32_e64 v120, v38, v22
	v_mul_f32_e64 v121, v39, v22
	v_mul_f32_e64 v122, v56, v22
	v_fma_f32 v25, v57, v22, v26
	v_mul_f32_e64 v29, v88, v22
	v_mul_f32_e64 v84, v89, v22
	v_fma_f32 v130, v108, v22, v26
	v_mul_f32_e64 v131, v109, v22
	v_fma_f32 v132, v118, v22, v26
	v_fma_f32 v25, -v120, v120, v25
	v_fma_f32 v29, -v120, v121, v29
	v_fma_f32 v84, -v120, v122, v84
	v_fma_f32 v130, -v121, v121, v130
	v_fma_f32 v131, -v121, v122, v131
	v_fma_f32 v132, -v122, v122, v132
	v_mul_f32_e64 v133, v131, v131
	v_mul_f32_e64 v144, v29, v132
	v_mul_f32_e64 v145, v84, v130
	v_mul_f32_e64 v146, v84, v84
	v_mul_f32_e64 v147, v25, v131
	v_mul_f32_e64 v148, v29, v29
	v_fma_f32 v133, v130, v132, -v133
	v_fma_f32 v144, v84, v131, -v144
	v_fma_f32 v145, v29, v131, -v145
	v_fma_f32 v146, v25, v132, -v146
	v_fma_f32 v147, v29, v84, -v147
	v_fma_f32 v148, v25, v130, -v148
	v_mul_f32_e64 v149, v25, v133
	v_fma_f32 v149, v29, v144, v149
	v_fma_f32 v149, v84, v145, v149
	v_rcp_f32_e32 v149, v149
	v_cmp_ne_u32_e64 vcc, s37, v24
	v_mul_f32_e64 v149, v149, v22
	v_cndmask_b32_e64 v149, 0, v149, s[30:31]
	v_cndmask_b32_e64 v25, 0, v18, vcc
	v_cndmask_b32_e64 v141, 0, v22, s[30:31]
	v_mul_f32_e64 v123, v133, v149
	v_mul_f32_e64 v124, v144, v149
	v_mul_f32_e64 v125, v145, v149
	v_mul_f32_e64 v126, v146, v149
	v_mul_f32_e64 v127, v147, v149
	v_mul_f32_e64 v140, v148, v149
	v_add_f32_e64 v142, v119, v25
	v_mov_b32_e32 v143, v24
	ds_write_b128 v23, v[120:123]
	ds_write_b128 v23, v[124:127] offset:1024
	ds_write_b128 v23, v[140:143] offset:2048
	s_waitcnt lgkmcnt(0)
	s_barrier
	v_mov_b32_dpp v24, v20 wave_shr:1 row_mask:0xf bank_mask:0xf bound_ctrl:1
	v_mov_b32_dpp v25, v21 wave_shr:1 row_mask:0xf bank_mask:0xf bound_ctrl:1
	v_mov_b32_dpp v38, v20 wave_shl:1 row_mask:0xf bank_mask:0xf bound_ctrl:1
	v_mov_b32_dpp v39, v21 wave_shl:1 row_mask:0xf bank_mask:0xf bound_ctrl:1
	v_pk_mul_f32 v[56:57], v[20:21], v[32:33] op_sel_hi:[1,0]
	v_pk_mul_f32 v[88:89], v[20:21], v[32:33] op_sel:[0,1]
	v_pk_mul_f32 v[108:109], v[20:21], v[34:35] op_sel_hi:[1,0]
	v_pk_add_f32 v[118:119], v[20:21], v[24:25]
	v_pk_fma_f32 v[56:57], v[24:25], v[44:45], v[56:57] op_sel_hi:[1,0,1]
	v_pk_fma_f32 v[88:89], v[24:25], v[44:45], v[88:89] op_sel:[0,1,0]
	v_pk_fma_f32 v[108:109], v[24:25], v[46:47], v[108:109] op_sel_hi:[1,0,1]
	v_pk_add_f32 v[118:119], v[118:119], v[38:39]
	v_pk_fma_f32 v[56:57], v[38:39], v[48:49], v[56:57] op_sel_hi:[1,0,1]
	v_pk_fma_f32 v[88:89], v[38:39], v[48:49], v[88:89] op_sel:[0,1,0]
	v_pk_fma_f32 v[108:109], v[38:39], v[50:51], v[108:109] op_sel_hi:[1,0,1]
	v_pk_add_f32 v[24:25], v[82:83], v[118:119]
	v_pk_add_f32 v[38:39], v[138:139], v[24:25]
	v_pk_add_f32 v[82:83], v[60:61], v[56:57]
	v_pk_add_f32 v[130:131], v[112:113], v[82:83]
	v_pk_add_f32 v[60:61], v[62:63], v[88:89]
	v_pk_add_f32 v[112:113], v[134:135], v[60:61]
	v_pk_add_f32 v[62:63], v[64:65], v[108:109]
	v_pk_add_f32 v[132:133], v[136:137], v[62:63]
	v_pk_fma_f32 v[130:131], v[120:121], v[38:39], v[130:131] op_sel_hi:[0,1,1] neg_lo:[1,0,0] neg_hi:[1,0,0]
	v_pk_fma_f32 v[112:113], v[120:121], v[38:39], v[112:113] op_sel:[1,0,0] neg_lo:[1,0,0] neg_hi:[1,0,0]
	v_pk_fma_f32 v[132:133], v[122:123], v[38:39], v[132:133] op_sel_hi:[0,1,1] neg_lo:[1,0,0] neg_hi:[1,0,0]
	v_pk_mul_f32 v[64:65], v[122:123], v[130:131] op_sel:[1,0]
	v_pk_mul_f32 v[134:135], v[124:125], v[130:131] op_sel_hi:[0,1]
	v_pk_mul_f32 v[136:137], v[124:125], v[130:131] op_sel:[1,0]
	v_pk_fma_f32 v[64:65], v[124:125], v[112:113], v[64:65] op_sel_hi:[0,1,1]
	v_pk_fma_f32 v[134:135], v[126:127], v[112:113], v[134:135] op_sel_hi:[0,1,1]
	v_pk_fma_f32 v[136:137], v[126:127], v[112:113], v[136:137] op_sel:[1,0,0]
	v_pk_fma_f32 v[64:65], v[124:125], v[132:133], v[64:65] op_sel:[1,0,0]
	v_pk_fma_f32 v[134:135], v[126:127], v[132:133], v[134:135] op_sel:[1,0,0]
	v_pk_fma_f32 v[136:137], v[140:141], v[132:133], v[136:137] op_sel_hi:[0,1,1]
	v_pk_mul_f32 v[138:139], v[120:121], v[64:65] op_sel_hi:[0,1]
	v_pk_fma_f32 v[138:139], v[120:121], v[134:135], v[138:139] op_sel:[1,0,0]
	v_pk_fma_f32 v[138:139], v[122:123], v[136:137], v[138:139] op_sel_hi:[0,1,1]
	v_pk_fma_f32 v[138:139], v[140:141], v[38:39], v[138:139] op_sel:[1,0,0] neg_lo:[0,0,1] neg_hi:[0,0,1]
	v_cmp_eq_u32_e64 s[10:11], 6, v143
	v_cmp_eq_u32_e64 s[14:15], 7, v143
	v_pk_add_f32 v[38:39], v[66:67], v[64:65]
	v_pk_add_f32 v[112:113], v[86:87], v[38:39]
	v_pk_add_f32 v[66:67], v[92:93], v[134:135]
	v_pk_add_f32 v[86:87], v[114:115], v[66:67]
	v_pk_add_f32 v[92:93], v[94:95], v[136:137]
	v_pk_add_f32 v[114:115], v[152:153], v[92:93]
	v_pk_add_f32 v[94:95], v[110:111], v[138:139]
	v_pk_add_f32 v[130:131], v[154:155], v[94:95]
	v_pk_fma_f32 v[110:111], v[76:77], v[112:113], v[130:131] op_sel_hi:[0,1,1]
	v_pk_fma_f32 v[132:133], v[104:105], v[112:113], v[130:131] op_sel_hi:[0,1,1]
	v_pk_fma_f32 v[110:111], v[76:77], v[86:87], v[110:111] op_sel:[1,0,0]
	v_pk_fma_f32 v[132:133], v[104:105], v[86:87], v[132:133] op_sel:[1,0,0]
	v_pk_fma_f32 v[110:111], v[78:79], v[114:115], v[110:111] op_sel_hi:[0,1,1]
	v_pk_fma_f32 v[132:133], v[106:107], v[114:115], v[132:133] op_sel_hi:[0,1,1]
	v_pk_fma_f32 v[130:131], v[8:9], v[112:113], v[130:131] op_sel_hi:[0,1,1]
	v_pk_fma_f32 v[130:131], v[8:9], v[86:87], v[130:131] op_sel:[1,0,0]
	v_pk_fma_f32 v[130:131], v[10:11], v[114:115], v[130:131] op_sel_hi:[0,1,1]
	v_cndmask_b32_e64 v144, 0, v18, s[10:11]
	v_cndmask_b32_e64 v145, 0, v18, s[14:15]
	v_add_f32_dpp v130, v110, v130 wave_shl:1 row_mask:0xf bank_mask:0xf bound_ctrl:1
	v_add_f32_dpp v131, v111, v131 wave_shl:1 row_mask:0xf bank_mask:0xf bound_ctrl:1
	s_add_i32 s4, s34, 8
	s_cmpk_lt_i32 s4, 0x201
	s_cselect_b64 s[12:13], s[0:1], 0
	v_add_f32_dpp v130, v132, v130 wave_shr:1 row_mask:0xf bank_mask:0xf bound_ctrl:1
	v_add_f32_dpp v131, v133, v131 wave_shr:1 row_mask:0xf bank_mask:0xf bound_ctrl:1
	v_pk_fma_f32 v[130:131], v[4:5], v[142:143], v[130:131] op_sel_hi:[1,0,1] neg_lo:[0,0,1] neg_hi:[0,0,1]
	v_pk_add_f32 v[130:131], v[130:131], v[144:145] neg_lo:[0,1] neg_hi:[0,1]
	v_pk_mul_f32 v[146:147], v[130:131], v[130:131]
	v_add_f32_e32 v146, v146, v147
	v_cndmask_b32_e64 v147, 0, v146, s[12:13]
	v_add_f32_e32 v1, v1, v147
	s_waitcnt vmcnt(0)
	v_mov_b32_dpp v8, v40 wave_shr:1 row_mask:0xf bank_mask:0xf bound_ctrl:1
	v_mov_b32_dpp v9, v41 wave_shr:1 row_mask:0xf bank_mask:0xf bound_ctrl:1
	v_mov_b32_dpp v10, v42 wave_shr:1 row_mask:0xf bank_mask:0xf bound_ctrl:1
	v_mov_b32_dpp v76, v40 wave_shl:1 row_mask:0xf bank_mask:0xf bound_ctrl:1
	v_mov_b32_dpp v77, v41 wave_shl:1 row_mask:0xf bank_mask:0xf bound_ctrl:1
	v_mov_b32_dpp v78, v42 wave_shl:1 row_mask:0xf bank_mask:0xf bound_ctrl:1
	s_add_i32 s4, s34, 12
	s_cmpk_lt_u32 s4, 0x201
	s_cselect_b64 s[12:13], s[40:41], 0
	v_cmp_eq_u32_e64 s[14:15], s37, v16
	s_and_b64 s[14:15], s[14:15], s[12:13]
	v_cndmask_b32_e64 v29, 0, 1, s[14:15]
	v_mul_f32_e64 v4, v40, v40
	v_mul_f32_e64 v5, v40, v41
	v_mul_f32_e64 v86, v40, v42
	v_mul_f32_e64 v87, v41, v41
	v_mul_f32_e64 v104, v41, v42
	v_mul_f32_e64 v105, v42, v42
	v_or_b32_dpp v53, v29, v29 wave_shr:1 row_mask:0xf bank_mask:0xf bound_ctrl:1
	s_nop 1
	v_or_b32_dpp v53, v29, v53 wave_shl:1 row_mask:0xf bank_mask:0xf bound_ctrl:1
	s_nop 1
	v_or_b32_dpp v84, v53, v53 wave_shr:1 row_mask:0xf bank_mask:0xf bound_ctrl:1
	s_nop 1
	v_or_b32_dpp v84, v53, v84 wave_shl:1 row_mask:0xf bank_mask:0xf bound_ctrl:1
	v_or3_b32 v29, v84, v52, v85
	v_or3_b32 v29, v29, v128, v129
	s_add_i32 s4, s34, 9
	s_cmpk_lt_u32 s4, 0x1ff
	s_cselect_b64 s[12:13], s[42:43], 0
	v_cmp_ne_u32_e64 s[30:31], 0, v29
	s_and_b64 s[30:31], s[30:31], s[12:13]
	v_cndmask_b32_e64 v29, 0, 1.0, s[30:31]
	v_add_f32_e64 v106, v40, v8
	v_add_f32_e64 v107, v41, v9
	v_add_f32_e64 v110, v42, v10
	v_fma_f32 v4, v8, v8, v4
	v_fma_f32 v5, v8, v9, v5
	v_fma_f32 v86, v8, v10, v86
	v_fma_f32 v87, v9, v9, v87
	v_fma_f32 v104, v9, v10, v104
	v_fma_f32 v105, v10, v10, v105
	v_add_f32_dpp v121, v29, v29 wave_shr:1 row_mask:0xf bank_mask:0xf bound_ctrl:1
	v_add_f32_e64 v106, v106, v76
	v_add_f32_e64 v107, v107, v77
	v_add_f32_e64 v110, v110, v78
	v_fma_f32 v111, v76, v76, v4
	v_fma_f32 v112, v76, v77, v5
	v_fma_f32 v113, v76, v78, v86
	v_fma_f32 v114, v77, v77, v87
	v_fma_f32 v115, v77, v78, v104
	v_fma_f32 v120, v78, v78, v105
	v_add_f32_dpp v121, v29, v121 wave_shl:1 row_mask:0xf bank_mask:0xf bound_ctrl:1
	v_pk_add_f32 v[4:5], v[30:31], v[106:107]
	v_pk_add_f32 v[30:31], v[54:55], v[110:111]
	v_pk_add_f32 v[54:55], v[80:81], v[112:113]
	v_pk_add_f32 v[80:81], v[90:91], v[114:115]
	v_pk_add_f32 v[86:87], v[116:117], v[120:121]
	v_mul_f32_e64 v124, v4, v22
	v_mul_f32_e64 v125, v5, v22
	v_mul_f32_e64 v126, v30, v22
	v_fma_f32 v29, v31, v22, v26
	v_mul_f32_e64 v53, v54, v22
	v_mul_f32_e64 v90, v55, v22
	v_fma_f32 v91, v80, v22, v26
	v_mul_f32_e64 v104, v81, v22
	v_fma_f32 v105, v86, v22, v26
	v_fma_f32 v29, -v124, v124, v29
	v_fma_f32 v53, -v124, v125, v53
	v_fma_f32 v90, -v124, v126, v90
	v_fma_f32 v91, -v125, v125, v91
	v_fma_f32 v104, -v125, v126, v104
	v_fma_f32 v105, -v126, v126, v105
	v_mul_f32_e64 v116, v104, v104
	v_mul_f32_e64 v117, v53, v105
	v_mul_f32_e64 v122, v90, v91
	v_mul_f32_e64 v123, v90, v90
	v_mul_f32_e64 v130, v29, v104
	v_mul_f32_e64 v131, v53, v53
	v_fma_f32 v116, v91, v105, -v116
	v_fma_f32 v117, v90, v104, -v117
	v_fma_f32 v122, v53, v104, -v122
	v_fma_f32 v123, v29, v105, -v123
	v_fma_f32 v130, v53, v90, -v130
	v_fma_f32 v131, v29, v91, -v131
	v_mul_f32_e64 v132, v29, v116
	v_fma_f32 v132, v53, v117, v132
	v_fma_f32 v132, v90, v122, v132
	v_rcp_f32_e32 v132, v132
	v_cmp_ne_u32_e64 vcc, s37, v17
	v_mul_f32_e64 v132, v132, v22
	v_cndmask_b32_e64 v132, 0, v132, s[30:31]
	v_cndmask_b32_e64 v29, 0, v18, vcc
	v_cndmask_b32_e64 v145, 0, v22, s[30:31]
	v_mul_f32_e64 v127, v116, v132
	v_mul_f32_e64 v140, v117, v132
	v_mul_f32_e64 v141, v122, v132
	v_mul_f32_e64 v142, v123, v132
	v_mul_f32_e64 v143, v130, v132
	v_mul_f32_e64 v144, v131, v132
	v_add_f32_e64 v146, v87, v29
	v_mov_b32_e32 v147, v17
	ds_write_b128 v23, v[124:127] offset:3072
	ds_write_b128 v23, v[140:143] offset:4096
	ds_write_b128 v23, v[144:147] offset:5120
	s_waitcnt lgkmcnt(0)
	s_barrier
	v_mov_b32_dpp v4, v36 wave_shr:1 row_mask:0xf bank_mask:0xf bound_ctrl:1
	v_mov_b32_dpp v5, v37 wave_shr:1 row_mask:0xf bank_mask:0xf bound_ctrl:1
	v_mov_b32_dpp v30, v36 wave_shl:1 row_mask:0xf bank_mask:0xf bound_ctrl:1
	v_mov_b32_dpp v31, v37 wave_shl:1 row_mask:0xf bank_mask:0xf bound_ctrl:1
	v_pk_mul_f32 v[54:55], v[36:37], v[40:41] op_sel_hi:[1,0]
	v_pk_mul_f32 v[80:81], v[36:37], v[40:41] op_sel:[0,1]
	v_pk_mul_f32 v[86:87], v[36:37], v[42:43] op_sel_hi:[1,0]
	v_pk_add_f32 v[90:91], v[36:37], v[4:5]
	v_pk_fma_f32 v[54:55], v[4:5], v[8:9], v[54:55] op_sel_hi:[1,0,1]
	v_pk_fma_f32 v[80:81], v[4:5], v[8:9], v[80:81] op_sel:[0,1,0]
	v_pk_fma_f32 v[86:87], v[4:5], v[10:11], v[86:87] op_sel_hi:[1,0,1]
	v_pk_add_f32 v[90:91], v[90:91], v[30:31]
	v_pk_fma_f32 v[54:55], v[30:31], v[76:77], v[54:55] op_sel_hi:[1,0,1]
	v_pk_fma_f32 v[80:81], v[30:31], v[76:77], v[80:81] op_sel:[0,1,0]
	v_pk_fma_f32 v[86:87], v[30:31], v[78:79], v[86:87] op_sel_hi:[1,0,1]
	v_pk_add_f32 v[4:5], v[24:25], v[90:91]
	v_pk_add_f32 v[24:25], v[82:83], v[54:55]
	v_pk_add_f32 v[30:31], v[60:61], v[80:81]
	v_pk_add_f32 v[60:61], v[62:63], v[86:87]
	v_pk_fma_f32 v[24:25], v[124:125], v[4:5], v[24:25] op_sel_hi:[0,1,1] neg_lo:[1,0,0] neg_hi:[1,0,0]
	v_pk_fma_f32 v[30:31], v[124:125], v[4:5], v[30:31] op_sel:[1,0,0] neg_lo:[1,0,0] neg_hi:[1,0,0]
	v_pk_fma_f32 v[60:61], v[126:127], v[4:5], v[60:61] op_sel_hi:[0,1,1] neg_lo:[1,0,0] neg_hi:[1,0,0]
	v_pk_mul_f32 v[62:63], v[126:127], v[24:25] op_sel:[1,0]
	v_pk_mul_f32 v[82:83], v[140:141], v[24:25] op_sel_hi:[0,1]
	v_pk_mul_f32 v[104:105], v[140:141], v[24:25] op_sel:[1,0]
	v_pk_fma_f32 v[62:63], v[140:141], v[30:31], v[62:63] op_sel_hi:[0,1,1]
	v_pk_fma_f32 v[82:83], v[142:143], v[30:31], v[82:83] op_sel_hi:[0,1,1]
	v_pk_fma_f32 v[104:105], v[142:143], v[30:31], v[104:105] op_sel:[1,0,0]
	v_pk_fma_f32 v[62:63], v[140:141], v[60:61], v[62:63] op_sel:[1,0,0]
	v_pk_fma_f32 v[82:83], v[142:143], v[60:61], v[82:83] op_sel:[1,0,0]
	v_pk_fma_f32 v[104:105], v[144:145], v[60:61], v[104:105] op_sel_hi:[0,1,1]
	v_pk_mul_f32 v[116:117], v[124:125], v[62:63] op_sel_hi:[0,1]
	v_pk_fma_f32 v[116:117], v[124:125], v[82:83], v[116:117] op_sel:[1,0,0]
	v_pk_fma_f32 v[116:117], v[126:127], v[104:105], v[116:117] op_sel_hi:[0,1,1]
	v_pk_fma_f32 v[116:117], v[144:145], v[4:5], v[116:117] op_sel:[1,0,0] neg_lo:[0,0,1] neg_hi:[0,0,1]
	v_cmp_eq_u32_e64 s[10:11], 6, v147
	v_cmp_eq_u32_e64 s[14:15], 7, v147
	v_pk_add_f32 v[4:5], v[38:39], v[62:63]
	v_pk_add_f32 v[24:25], v[66:67], v[82:83]
	v_pk_add_f32 v[30:31], v[92:93], v[104:105]
	v_pk_add_f32 v[38:39], v[94:95], v[116:117]
	v_pk_fma_f32 v[60:61], v[96:97], v[4:5], v[38:39] op_sel_hi:[0,1,1]
	v_pk_fma_f32 v[66:67], v[100:101], v[4:5], v[38:39] op_sel_hi:[0,1,1]
	v_pk_fma_f32 v[60:61], v[96:97], v[24:25], v[60:61] op_sel:[1,0,0]
	v_pk_fma_f32 v[66:67], v[100:101], v[24:25], v[66:67] op_sel:[1,0,0]
	v_pk_fma_f32 v[60:61], v[98:99], v[30:31], v[60:61] op_sel_hi:[0,1,1]
	v_pk_fma_f32 v[66:67], v[102:103], v[30:31], v[66:67] op_sel_hi:[0,1,1]
	v_pk_fma_f32 v[38:39], v[12:13], v[4:5], v[38:39] op_sel_hi:[0,1,1]
	v_pk_fma_f32 v[38:39], v[12:13], v[24:25], v[38:39] op_sel:[1,0,0]
	v_pk_fma_f32 v[38:39], v[14:15], v[30:31], v[38:39] op_sel_hi:[0,1,1]
	v_cndmask_b32_e64 v92, 0, v18, s[10:11]
	v_cndmask_b32_e64 v93, 0, v18, s[14:15]
	v_add_f32_dpp v38, v60, v38 wave_shl:1 row_mask:0xf bank_mask:0xf bound_ctrl:1
	v_add_f32_dpp v39, v61, v39 wave_shl:1 row_mask:0xf bank_mask:0xf bound_ctrl:1
	s_add_i32 s4, s34, 9
	s_cmpk_lt_i32 s4, 0x201
	s_cselect_b64 s[12:13], s[0:1], 0
	v_add_f32_dpp v38, v66, v38 wave_shr:1 row_mask:0xf bank_mask:0xf bound_ctrl:1
	v_add_f32_dpp v39, v67, v39 wave_shr:1 row_mask:0xf bank_mask:0xf bound_ctrl:1
	v_pk_fma_f32 v[38:39], v[6:7], v[146:147], v[38:39] op_sel_hi:[1,0,1] neg_lo:[0,0,1] neg_hi:[0,0,1]
	v_pk_add_f32 v[38:39], v[38:39], v[92:93] neg_lo:[0,1] neg_hi:[0,1]
	v_pk_mul_f32 v[94:95], v[38:39], v[38:39]
	v_add_f32_e32 v94, v94, v95
	v_cndmask_b32_e64 v95, 0, v94, s[12:13]
	v_add_f32_e32 v1, v1, v95
	v_mov_b32_e32 v0, v1
	s_branch .LBB0_29
.LBB0_15:
.LBB0_16:
	s_mov_b32 s27, s19
	v_mov_b32_e32 v1, 0x42c80000
	v_mov_b32_e32 v0, 0
	s_add_i32 s4, s34, -2
	s_max_i32 s4, s4, 0
	s_mul_i32 s5, s4, 0x804
	s_add_i32 s5, s5, s35
	s_add_i32 s6, s5, 0x0
	s_add_i32 s7, s5, 0x101004
	s_add_i32 s8, s5, 0x202008
	s_add_i32 s11, s5, 0x30300c
	s_add_i32 s15, s5, 0x404010
	s_mul_i32 s9, s4, 0x180c
	s_add_i32 s9, s9, s33
	buffer_load_dword v2, v28, s[16:19], s6 offen nt
	buffer_load_dword v3, v28, s[16:19], s7 offen nt
	buffer_load_dword v4, v28, s[16:19], s8 offen nt
	buffer_load_dword v5, v28, s[16:19], s11 offen nt
	buffer_load_dword v6, v28, s[16:19], s15 offen nt
	buffer_load_dwordx3 v[8:10], v27, s[24:27], s9 offen nt
	s_add_i32 s4, s34, -1
	s_max_i32 s4, s4, 0
	s_mul_i32 s5, s4, 0x804
	s_add_i32 s5, s5, s35
	s_add_i32 s6, s5, 0x0
	s_add_i32 s7, s5, 0x101004
	s_add_i32 s8, s5, 0x202008
	s_add_i32 s11, s5, 0x30300c
	s_add_i32 s15, s5, 0x404010
	s_mul_i32 s9, s4, 0x180c
	s_add_i32 s9, s9, s33
	buffer_load_dword v12, v28, s[16:19], s6 offen nt
	buffer_load_dword v13, v28, s[16:19], s7 offen nt
	buffer_load_dword v14, v28, s[16:19], s8 offen nt
	buffer_load_dword v15, v28, s[16:19], s11 offen nt
	buffer_load_dword v16, v28, s[16:19], s15 offen nt
	buffer_load_dwordx3 v[32:34], v27, s[24:27], s9 offen nt
	s_add_i32 s4, s34, 0
	s_min_i32 s4, s4, 0x200
	s_mul_i32 s5, s4, 0x804
	s_add_i32 s5, s5, s35
	s_add_i32 s6, s5, 0x0
	s_add_i32 s7, s5, 0x101004
	s_add_i32 s8, s5, 0x202008
	s_add_i32 s11, s5, 0x30300c
	s_add_i32 s15, s5, 0x404010
	s_mul_i32 s9, s4, 0x180c
	s_add_i32 s9, s9, s33
	buffer_load_dword v20, v28, s[16:19], s6 offen nt
	buffer_load_dword v21, v28, s[16:19], s7 offen nt
	buffer_load_dword v24, v28, s[16:19], s8 offen nt
	buffer_load_dword v25, v28, s[16:19], s11 offen nt
	buffer_load_dword v30, v28, s[16:19], s15 offen nt
	buffer_load_dwordx3 v[36:38], v27, s[24:27], s9 offen nt
	s_waitcnt vmcnt(12)
	v_mov_b32_dpp v40, v8 wave_shr:1 row_mask:0xf bank_mask:0xf bound_ctrl:1
	v_mov_b32_dpp v41, v9 wave_shr:1 row_mask:0xf bank_mask:0xf bound_ctrl:1
	v_mov_b32_dpp v42, v10 wave_shr:1 row_mask:0xf bank_mask:0xf bound_ctrl:1
	v_mov_b32_dpp v44, v8 wave_shl:1 row_mask:0xf bank_mask:0xf bound_ctrl:1
	v_mov_b32_dpp v45, v9 wave_shl:1 row_mask:0xf bank_mask:0xf bound_ctrl:1
	v_mov_b32_dpp v46, v10 wave_shl:1 row_mask:0xf bank_mask:0xf bound_ctrl:1
	v_mov_b32_dpp v48, v2 wave_shr:1 row_mask:0xf bank_mask:0xf bound_ctrl:1
	v_mov_b32_dpp v49, v3 wave_shr:1 row_mask:0xf bank_mask:0xf bound_ctrl:1
	v_mov_b32_dpp v50, v4 wave_shr:1 row_mask:0xf bank_mask:0xf bound_ctrl:1
	v_mov_b32_dpp v51, v5 wave_shr:1 row_mask:0xf bank_mask:0xf bound_ctrl:1
	v_mov_b32_dpp v52, v6 wave_shr:1 row_mask:0xf bank_mask:0xf bound_ctrl:1
	v_mov_b32_dpp v54, v2 wave_shl:1 row_mask:0xf bank_mask:0xf bound_ctrl:1
	v_mov_b32_dpp v55, v3 wave_shl:1 row_mask:0xf bank_mask:0xf bound_ctrl:1
	v_mov_b32_dpp v56, v4 wave_shl:1 row_mask:0xf bank_mask:0xf bound_ctrl:1
	v_mov_b32_dpp v57, v5 wave_shl:1 row_mask:0xf bank_mask:0xf bound_ctrl:1
	v_mov_b32_dpp v58, v6 wave_shl:1 row_mask:0xf bank_mask:0xf bound_ctrl:1
	v_pk_mul_f32 v[60:61], v[2:3], v[8:9] op_sel_hi:[1,0]
	v_pk_mul_f32 v[62:63], v[4:5], v[8:9] op_sel_hi:[1,0]
	v_mul_f32_e64 v64, v6, v8
	v_pk_mul_f32 v[66:67], v[2:3], v[8:9] op_sel:[0,1]
	v_pk_mul_f32 v[68:69], v[4:5], v[8:9] op_sel:[0,1]
	v_mul_f32_e64 v70, v6, v9
	v_pk_mul_f32 v[72:73], v[2:3], v[10:11] op_sel_hi:[1,0]
	v_pk_mul_f32 v[74:75], v[4:5], v[10:11] op_sel_hi:[1,0]
	v_mul_f32_e64 v76, v6, v10
	v_pk_add_f32 v[78:79], v[2:3], v[48:49]
	v_pk_add_f32 v[80:81], v[4:5], v[50:51]
	v_add_f32_e64 v82, v6, v52
	v_pk_fma_f32 v[60:61], v[48:49], v[40:41], v[60:61] op_sel_hi:[1,0,1]
	v_pk_fma_f32 v[62:63], v[50:51], v[40:41], v[62:63] op_sel_hi:[1,0,1]
	v_fma_f32 v64, v52, v40, v64
	v_pk_fma_f32 v[66:67], v[48:49], v[40:41], v[66:67] op_sel:[0,1,0]
	v_pk_fma_f32 v[68:69], v[50:51], v[40:41], v[68:69] op_sel:[0,1,0]
	v_fma_f32 v70, v52, v41, v70
	v_pk_fma_f32 v[72:73], v[48:49], v[42:43], v[72:73] op_sel_hi:[1,0,1]
	v_pk_fma_f32 v[74:75], v[50:51], v[42:43], v[74:75] op_sel_hi:[1,0,1]
	v_fma_f32 v76, v52, v42, v76
	v_pk_add_f32 v[78:79], v[78:79], v[54:55]
	v_pk_add_f32 v[80:81], v[80:81], v[56:57]
	v_add_f32_e64 v82, v82, v58
	v_pk_fma_f32 v[60:61], v[54:55], v[44:45], v[60:61] op_sel_hi:[1,0,1]
	v_pk_fma_f32 v[62:63], v[56:57], v[44:45], v[62:63] op_sel_hi:[1,0,1]
	v_fma_f32 v64, v58, v44, v64
	v_pk_fma_f32 v[66:67], v[54:55], v[44:45], v[66:67] op_sel:[0,1,0]
	v_pk_fma_f32 v[68:69], v[56:57], v[44:45], v[68:69] op_sel:[0,1,0]
	v_fma_f32 v70, v58, v45, v70
	v_pk_fma_f32 v[72:73], v[54:55], v[46:47], v[72:73] op_sel_hi:[1,0,1]
	v_pk_fma_f32 v[74:75], v[56:57], v[46:47], v[74:75] op_sel_hi:[1,0,1]
	v_fma_f32 v76, v58, v46, v76
	s_barrier
	s_add_i32 s4, s34, 1
	s_min_i32 s4, s4, 0x200
	s_mul_i32 s5, s4, 0x804
	s_add_i32 s5, s5, s35
	s_add_i32 s6, s5, 0x0
	s_add_i32 s7, s5, 0x101004
	s_add_i32 s8, s5, 0x202008
	s_add_i32 s11, s5, 0x30300c
	s_add_i32 s15, s5, 0x404010
	s_mul_i32 s9, s4, 0x180c
	s_add_i32 s9, s9, s33
	buffer_load_dword v48, v28, s[16:19], s6 offen nt
	buffer_load_dword v49, v28, s[16:19], s7 offen nt
	buffer_load_dword v50, v28, s[16:19], s8 offen nt
	buffer_load_dword v51, v28, s[16:19], s11 offen nt
	buffer_load_dword v52, v28, s[16:19], s15 offen nt
	buffer_load_dwordx3 v[56:58], v27, s[24:27], s9 offen nt
	s_waitcnt vmcnt(12)
	v_mov_b32_dpp v84, v32 wave_shr:1 row_mask:0xf bank_mask:0xf bound_ctrl:1
	v_mov_b32_dpp v85, v33 wave_shr:1 row_mask:0xf bank_mask:0xf bound_ctrl:1
	v_mov_b32_dpp v86, v34 wave_shr:1 row_mask:0xf bank_mask:0xf bound_ctrl:1
	v_mov_b32_dpp v88, v32 wave_shl:1 row_mask:0xf bank_mask:0xf bound_ctrl:1
	v_mov_b32_dpp v89, v33 wave_shl:1 row_mask:0xf bank_mask:0xf bound_ctrl:1
	v_mov_b32_dpp v90, v34 wave_shl:1 row_mask:0xf bank_mask:0xf bound_ctrl:1
	v_mov_b32_dpp v54, v12 wave_shr:1 row_mask:0xf bank_mask:0xf bound_ctrl:1
	v_mov_b32_dpp v55, v13 wave_shr:1 row_mask:0xf bank_mask:0xf bound_ctrl:1
	v_mov_b32_dpp v92, v14 wave_shr:1 row_mask:0xf bank_mask:0xf bound_ctrl:1
	v_mov_b32_dpp v93, v15 wave_shr:1 row_mask:0xf bank_mask:0xf bound_ctrl:1
	v_mov_b32_dpp v94, v16 wave_shr:1 row_mask:0xf bank_mask:0xf bound_ctrl:1
	v_mov_b32_dpp v96, v12 wave_shl:1 row_mask:0xf bank_mask:0xf bound_ctrl:1
	v_mov_b32_dpp v97, v13 wave_shl:1 row_mask:0xf bank_mask:0xf bound_ctrl:1
	v_mov_b32_dpp v98, v14 wave_shl:1 row_mask:0xf bank_mask:0xf bound_ctrl:1
	v_mov_b32_dpp v99, v15 wave_shl:1 row_mask:0xf bank_mask:0xf bound_ctrl:1
	v_mov_b32_dpp v100, v16 wave_shl:1 row_mask:0xf bank_mask:0xf bound_ctrl:1
	v_pk_mul_f32 v[102:103], v[12:13], v[32:33] op_sel_hi:[1,0]
	v_pk_mul_f32 v[104:105], v[14:15], v[32:33] op_sel_hi:[1,0]
	v_mul_f32_e64 v106, v16, v32
	v_pk_mul_f32 v[108:109], v[12:13], v[32:33] op_sel:[0,1]
	v_pk_mul_f32 v[110:111], v[14:15], v[32:33] op_sel:[0,1]
	v_mul_f32_e64 v112, v16, v33
	v_pk_mul_f32 v[114:115], v[12:13], v[34:35] op_sel_hi:[1,0]
	v_pk_mul_f32 v[116:117], v[14:15], v[34:35] op_sel_hi:[1,0]
	v_mul_f32_e64 v118, v16, v34
	v_pk_add_f32 v[120:121], v[12:13], v[54:55]
	v_pk_add_f32 v[122:123], v[14:15], v[92:93]
	v_add_f32_e64 v124, v16, v94
	v_pk_fma_f32 v[102:103], v[54:55], v[84:85], v[102:103] op_sel_hi:[1,0,1]
	v_pk_fma_f32 v[104:105], v[92:93], v[84:85], v[104:105] op_sel_hi:[1,0,1]
	v_fma_f32 v106, v94, v84, v106
	v_pk_fma_f32 v[108:109], v[54:55], v[84:85], v[108:109] op_sel:[0,1,0]
	v_pk_fma_f32 v[110:111], v[92:93], v[84:85], v[110:111] op_sel:[0,1,0]
	v_fma_f32 v112, v94, v85, v112
	v_pk_fma_f32 v[114:115], v[54:55], v[86:87], v[114:115] op_sel_hi:[1,0,1]
	v_pk_fma_f32 v[116:117], v[92:93], v[86:87], v[116:117] op_sel_hi:[1,0,1]
	v_fma_f32 v118, v94, v86, v118
	v_pk_add_f32 v[120:121], v[120:121], v[96:97]
	v_pk_add_f32 v[122:123], v[122:123], v[98:99]
	v_add_f32_e64 v124, v124, v100
	v_pk_fma_f32 v[102:103], v[96:97], v[88:89], v[102:103] op_sel_hi:[1,0,1]
	v_pk_fma_f32 v[104:105], v[98:99], v[88:89], v[104:105] op_sel_hi:[1,0,1]
	v_fma_f32 v106, v100, v88, v106
	v_pk_fma_f32 v[108:109], v[96:97], v[88:89], v[108:109] op_sel:[0,1,0]
	v_pk_fma_f32 v[110:111], v[98:99], v[88:89], v[110:111] op_sel:[0,1,0]
	v_fma_f32 v112, v100, v89, v112
	v_pk_fma_f32 v[114:115], v[96:97], v[90:91], v[114:115] op_sel_hi:[1,0,1]
	v_pk_fma_f32 v[116:117], v[98:99], v[90:91], v[116:117] op_sel_hi:[1,0,1]
	v_fma_f32 v118, v100, v90, v118
	s_barrier
	s_add_i32 s4, s34, 2
	s_min_i32 s4, s4, 0x200
	s_mul_i32 s5, s4, 0x804
	s_add_i32 s5, s5, s35
	s_add_i32 s6, s5, 0x0
	s_add_i32 s7, s5, 0x101004
	s_add_i32 s8, s5, 0x202008
	s_add_i32 s11, s5, 0x30300c
	s_add_i32 s15, s5, 0x404010
	s_mul_i32 s9, s4, 0x180c
	s_add_i32 s9, s9, s33
	buffer_load_dword v54, v28, s[16:19], s6 offen nt
	buffer_load_dword v55, v28, s[16:19], s7 offen nt
	buffer_load_dword v92, v28, s[16:19], s8 offen nt
	buffer_load_dword v93, v28, s[16:19], s11 offen nt
	buffer_load_dword v94, v28, s[16:19], s15 offen nt
	buffer_load_dwordx3 v[96:98], v27, s[24:27], s9 offen nt
	s_waitcnt vmcnt(12)
	v_mov_b32_dpp v128, v36 wave_shr:1 row_mask:0xf bank_mask:0xf bound_ctrl:1
	v_mov_b32_dpp v129, v37 wave_shr:1 row_mask:0xf bank_mask:0xf bound_ctrl:1
	v_mov_b32_dpp v130, v38 wave_shr:1 row_mask:0xf bank_mask:0xf bound_ctrl:1
	v_mov_b32_dpp v132, v36 wave_shl:1 row_mask:0xf bank_mask:0xf bound_ctrl:1
	v_mov_b32_dpp v133, v37 wave_shl:1 row_mask:0xf bank_mask:0xf bound_ctrl:1
	v_mov_b32_dpp v134, v38 wave_shl:1 row_mask:0xf bank_mask:0xf bound_ctrl:1
	v_mov_b32_dpp v100, v20 wave_shr:1 row_mask:0xf bank_mask:0xf bound_ctrl:1
	v_mov_b32_dpp v101, v21 wave_shr:1 row_mask:0xf bank_mask:0xf bound_ctrl:1
	v_mov_b32_dpp v126, v24 wave_shr:1 row_mask:0xf bank_mask:0xf bound_ctrl:1
	v_mov_b32_dpp v127, v25 wave_shr:1 row_mask:0xf bank_mask:0xf bound_ctrl:1
	v_mov_b32_dpp v136, v30 wave_shr:1 row_mask:0xf bank_mask:0xf bound_ctrl:1
	v_mov_b32_dpp v138, v20 wave_shl:1 row_mask:0xf bank_mask:0xf bound_ctrl:1
	v_mov_b32_dpp v139, v21 wave_shl:1 row_mask:0xf bank_mask:0xf bound_ctrl:1
	v_mov_b32_dpp v140, v24 wave_shl:1 row_mask:0xf bank_mask:0xf bound_ctrl:1
	v_mov_b32_dpp v141, v25 wave_shl:1 row_mask:0xf bank_mask:0xf bound_ctrl:1
	v_mov_b32_dpp v142, v30 wave_shl:1 row_mask:0xf bank_mask:0xf bound_ctrl:1
	v_pk_mul_f32 v[144:145], v[20:21], v[36:37] op_sel_hi:[1,0]
	v_pk_mul_f32 v[146:147], v[24:25], v[36:37] op_sel_hi:[1,0]
	v_mul_f32_e64 v148, v30, v36
	v_pk_mul_f32 v[150:151], v[20:21], v[36:37] op_sel:[0,1]
	v_pk_mul_f32 v[152:153], v[24:25], v[36:37] op_sel:[0,1]
	v_mul_f32_e64 v154, v30, v37
	v_pk_mul_f32 v[156:157], v[20:21], v[38:39] op_sel_hi:[1,0]
	v_pk_mul_f32 v[158:159], v[24:25], v[38:39] op_sel_hi:[1,0]
	v_mul_f32_e64 v160, v30, v38
	v_pk_add_f32 v[162:163], v[20:21], v[100:101]
	v_pk_add_f32 v[164:165], v[24:25], v[126:127]
	v_add_f32_e64 v166, v30, v136
	v_pk_fma_f32 v[144:145], v[100:101], v[128:129], v[144:145] op_sel_hi:[1,0,1]
	v_pk_fma_f32 v[146:147], v[126:127], v[128:129], v[146:147] op_sel_hi:[1,0,1]
	v_fma_f32 v148, v136, v128, v148
	v_pk_fma_f32 v[150:151], v[100:101], v[128:129], v[150:151] op_sel:[0,1,0]
	v_pk_fma_f32 v[152:153], v[126:127], v[128:129], v[152:153] op_sel:[0,1,0]
	v_fma_f32 v154, v136, v129, v154
	v_pk_fma_f32 v[156:157], v[100:101], v[130:131], v[156:157] op_sel_hi:[1,0,1]
	v_pk_fma_f32 v[158:159], v[126:127], v[130:131], v[158:159] op_sel_hi:[1,0,1]
	v_fma_f32 v160, v136, v130, v160
	v_pk_add_f32 v[162:163], v[162:163], v[138:139]
	v_pk_add_f32 v[164:165], v[164:165], v[140:141]
	v_add_f32_e64 v166, v166, v142
	v_pk_fma_f32 v[144:145], v[138:139], v[132:133], v[144:145] op_sel_hi:[1,0,1]
	v_pk_fma_f32 v[146:147], v[140:141], v[132:133], v[146:147] op_sel_hi:[1,0,1]
	v_fma_f32 v148, v142, v132, v148
	v_pk_fma_f32 v[150:151], v[138:139], v[132:133], v[150:151] op_sel:[0,1,0]
	v_pk_fma_f32 v[152:153], v[140:141], v[132:133], v[152:153] op_sel:[0,1,0]
	v_fma_f32 v154, v142, v133, v154
	v_pk_fma_f32 v[156:157], v[138:139], v[134:135], v[156:157] op_sel_hi:[1,0,1]
	v_pk_fma_f32 v[158:159], v[140:141], v[134:135], v[158:159] op_sel_hi:[1,0,1]
	v_fma_f32 v160, v142, v134, v160
	s_barrier
	ds_read_b128 v[136:139], v23 offset:0
	ds_read_b128 v[140:143], v23 offset:1024
	ds_read_b128 v[168:171], v23 offset:2048
	v_pk_add_f32 v[100:101], v[120:121], v[162:163]
	v_pk_add_f32 v[126:127], v[78:79], v[100:101]
	v_pk_add_f32 v[78:79], v[122:123], v[164:165]
	v_pk_add_f32 v[120:121], v[80:81], v[78:79]
	v_add_f32_e64 v80, v124, v166
	v_add_f32_e64 v122, v82, v80
	v_pk_add_f32 v[82:83], v[102:103], v[144:145]
	v_pk_add_f32 v[124:125], v[60:61], v[82:83]
	v_pk_add_f32 v[60:61], v[104:105], v[146:147]
	v_pk_add_f32 v[102:103], v[62:63], v[60:61]
	v_add_f32_e64 v62, v106, v148
	v_add_f32_e64 v104, v64, v62
	v_pk_add_f32 v[64:65], v[108:109], v[150:151]
	v_pk_add_f32 v[106:107], v[66:67], v[64:65]
	v_pk_add_f32 v[66:67], v[110:111], v[152:153]
	v_pk_add_f32 v[108:109], v[68:69], v[66:67]
	v_add_f32_e64 v68, v112, v154
	v_add_f32_e64 v110, v70, v68
	v_pk_add_f32 v[70:71], v[114:115], v[156:157]
	v_pk_add_f32 v[112:113], v[72:73], v[70:71]
	v_pk_add_f32 v[72:73], v[116:117], v[158:159]
	v_pk_add_f32 v[114:115], v[74:75], v[72:73]
	v_add_f32_e64 v74, v118, v160
	v_add_f32_e64 v116, v76, v74
	s_waitcnt lgkmcnt(2)
	v_pk_fma_f32 v[124:125], v[136:137], v[126:127], v[124:125] op_sel_hi:[0,1,1] neg_lo:[1,0,0] neg_hi:[1,0,0]
	v_pk_fma_f32 v[102:103], v[136:137], v[120:121], v[102:103] op_sel_hi:[0,1,1] neg_lo:[1,0,0] neg_hi:[1,0,0]
	v_fma_f32 v104, -v136, v122, v104
	v_pk_fma_f32 v[106:107], v[136:137], v[126:127], v[106:107] op_sel:[1,0,0] neg_lo:[1,0,0] neg_hi:[1,0,0]
	v_pk_fma_f32 v[108:109], v[136:137], v[120:121], v[108:109] op_sel:[1,0,0] neg_lo:[1,0,0] neg_hi:[1,0,0]
	v_fma_f32 v110, -v137, v122, v110
	v_pk_fma_f32 v[112:113], v[138:139], v[126:127], v[112:113] op_sel_hi:[0,1,1] neg_lo:[1,0,0] neg_hi:[1,0,0]
	v_pk_fma_f32 v[114:115], v[138:139], v[120:121], v[114:115] op_sel_hi:[0,1,1] neg_lo:[1,0,0] neg_hi:[1,0,0]
	v_fma_f32 v116, -v138, v122, v116
	v_pk_mul_f32 v[76:77], v[138:139], v[124:125] op_sel:[1,0]
	v_pk_mul_f32 v[174:175], v[138:139], v[102:103] op_sel:[1,0]
	v_mul_f32_e64 v180, v139, v104
	s_waitcnt lgkmcnt(1)
	v_pk_mul_f32 v[118:119], v[140:141], v[124:125] op_sel_hi:[0,1]
	v_pk_mul_f32 v[176:177], v[140:141], v[102:103] op_sel_hi:[0,1]
	v_mul_f32_e64 v182, v140, v104
	v_pk_mul_f32 v[172:173], v[140:141], v[124:125] op_sel:[1,0]
	v_pk_mul_f32 v[178:179], v[140:141], v[102:103] op_sel:[1,0]
	v_mul_f32_e64 v184, v141, v104
	v_pk_fma_f32 v[76:77], v[140:141], v[106:107], v[76:77] op_sel_hi:[0,1,1]
	v_pk_fma_f32 v[174:175], v[140:141], v[108:109], v[174:175] op_sel_hi:[0,1,1]
	v_fma_f32 v180, v140, v110, v180
	v_pk_fma_f32 v[118:119], v[142:143], v[106:107], v[118:119] op_sel_hi:[0,1,1]
	v_pk_fma_f32 v[176:177], v[142:143], v[108:109], v[176:177] op_sel_hi:[0,1,1]
	v_fma_f32 v182, v142, v110, v182
	v_pk_fma_f32 v[172:173], v[142:143], v[106:107], v[172:173] op_sel:[1,0,0]
	v_pk_fma_f32 v[178:179], v[142:143], v[108:109], v[178:179] op_sel:[1,0,0]
	v_fma_f32 v184, v143, v110, v184
	v_pk_fma_f32 v[76:77], v[140:141], v[112:113], v[76:77] op_sel:[1,0,0]
	v_pk_fma_f32 v[174:175], v[140:141], v[114:115], v[174:175] op_sel:[1,0,0]
	v_fma_f32 v180, v141, v116, v180
	v_pk_fma_f32 v[118:119], v[142:143], v[112:113], v[118:119] op_sel:[1,0,0]
	v_pk_fma_f32 v[176:177], v[142:143], v[114:115], v[176:177] op_sel:[1,0,0]
	v_fma_f32 v182, v143, v116, v182
	s_waitcnt lgkmcnt(0)
	v_pk_fma_f32 v[172:173], v[168:169], v[112:113], v[172:173] op_sel_hi:[0,1,1]
	v_pk_fma_f32 v[178:179], v[168:169], v[114:115], v[178:179] op_sel_hi:[0,1,1]
	v_fma_f32 v184, v168, v116, v184
	v_pk_mul_f32 v[186:187], v[136:137], v[76:77] op_sel_hi:[0,1]
	v_pk_mul_f32 v[188:189], v[136:137], v[174:175] op_sel_hi:[0,1]
	v_mul_f32_e64 v190, v136, v180
	v_pk_fma_f32 v[186:187], v[136:137], v[118:119], v[186:187] op_sel:[1,0,0]
	v_pk_fma_f32 v[188:189], v[136:137], v[176:177], v[188:189] op_sel:[1,0,0]
	v_fma_f32 v190, v137, v182, v190
	v_pk_fma_f32 v[186:187], v[138:139], v[172:173], v[186:187] op_sel_hi:[0,1,1]
	v_pk_fma_f32 v[188:189], v[138:139], v[178:179], v[188:189] op_sel_hi:[0,1,1]
	v_fma_f32 v190, v138, v184, v190
	v_pk_fma_f32 v[186:187], v[168:169], v[126:127], v[186:187] op_sel:[1,0,0] neg_lo:[0,0,1] neg_hi:[0,0,1]
	v_pk_fma_f32 v[188:189], v[168:169], v[120:121], v[188:189] op_sel:[1,0,0] neg_lo:[0,0,1] neg_hi:[0,0,1]
	v_fma_f32 v190, v169, v122, -v190
	s_add_i32 s4, s34, 3
	s_min_i32 s4, s4, 0x200
	s_mul_i32 s5, s4, 0x804
	s_add_i32 s5, s5, s35
	s_add_i32 s6, s5, 0x0
	s_add_i32 s7, s5, 0x101004
	s_add_i32 s8, s5, 0x202008
	s_add_i32 s11, s5, 0x30300c
	s_add_i32 s15, s5, 0x404010
	s_mul_i32 s9, s4, 0x180c
	s_add_i32 s9, s9, s33
	buffer_load_dword v2, v28, s[16:19], s6 offen nt
	buffer_load_dword v3, v28, s[16:19], s7 offen nt
	buffer_load_dword v4, v28, s[16:19], s8 offen nt
	buffer_load_dword v5, v28, s[16:19], s11 offen nt
	buffer_load_dword v6, v28, s[16:19], s15 offen nt
	buffer_load_dwordx3 v[8:10], v27, s[24:27], s9 offen nt
	s_waitcnt vmcnt(12)
	v_mov_b32_dpp v40, v56 wave_shr:1 row_mask:0xf bank_mask:0xf bound_ctrl:1
	v_mov_b32_dpp v41, v57 wave_shr:1 row_mask:0xf bank_mask:0xf bound_ctrl:1
	v_mov_b32_dpp v42, v58 wave_shr:1 row_mask:0xf bank_mask:0xf bound_ctrl:1
	v_mov_b32_dpp v44, v56 wave_shl:1 row_mask:0xf bank_mask:0xf bound_ctrl:1
	v_mov_b32_dpp v45, v57 wave_shl:1 row_mask:0xf bank_mask:0xf bound_ctrl:1
	v_mov_b32_dpp v46, v58 wave_shl:1 row_mask:0xf bank_mask:0xf bound_ctrl:1
	v_mov_b32_dpp v102, v48 wave_shr:1 row_mask:0xf bank_mask:0xf bound_ctrl:1
	v_mov_b32_dpp v103, v49 wave_shr:1 row_mask:0xf bank_mask:0xf bound_ctrl:1
	v_mov_b32_dpp v104, v50 wave_shr:1 row_mask:0xf bank_mask:0xf bound_ctrl:1
	v_mov_b32_dpp v105, v51 wave_shr:1 row_mask:0xf bank_mask:0xf bound_ctrl:1
	v_mov_b32_dpp v106, v52 wave_shr:1 row_mask:0xf bank_mask:0xf bound_ctrl:1
	v_mov_b32_dpp v108, v48 wave_shl:1 row_mask:0xf bank_mask:0xf bound_ctrl:1
	v_mov_b32_dpp v109, v49 wave_shl:1 row_mask:0xf bank_mask:0xf bound_ctrl:1
	v_mov_b32_dpp v110, v50 wave_shl:1 row_mask:0xf bank_mask:0xf bound_ctrl:1
	v_mov_b32_dpp v111, v51 wave_shl:1 row_mask:0xf bank_mask:0xf bound_ctrl:1
	v_mov_b32_dpp v112, v52 wave_shl:1 row_mask:0xf bank_mask:0xf bound_ctrl:1
	v_pk_mul_f32 v[114:115], v[48:49], v[56:57] op_sel_hi:[1,0]
	v_pk_mul_f32 v[116:117], v[50:51], v[56:57] op_sel_hi:[1,0]
	v_mul_f32_e64 v120, v52, v56
	v_pk_mul_f32 v[122:123], v[48:49], v[56:57] op_sel:[0,1]
	v_pk_mul_f32 v[124:125], v[50:51], v[56:57] op_sel:[0,1]
	v_mul_f32_e64 v126, v52, v57
	v_pk_mul_f32 v[136:137], v[48:49], v[58:59] op_sel_hi:[1,0]
	v_pk_mul_f32 v[138:139], v[50:51], v[58:59] op_sel_hi:[1,0]
	v_mul_f32_e64 v140, v52, v58
	v_pk_add_f32 v[142:143], v[48:49], v[102:103]
	v_pk_add_f32 v[168:169], v[50:51], v[104:105]
	v_add_f32_e64 v170, v52, v106
	v_pk_fma_f32 v[114:115], v[102:103], v[40:41], v[114:115] op_sel_hi:[1,0,1]
	v_pk_fma_f32 v[116:117], v[104:105], v[40:41], v[116:117] op_sel_hi:[1,0,1]
	v_fma_f32 v120, v106, v40, v120
	v_pk_fma_f32 v[122:123], v[102:103], v[40:41], v[122:123] op_sel:[0,1,0]
	v_pk_fma_f32 v[124:125], v[104:105], v[40:41], v[124:125] op_sel:[0,1,0]
	v_fma_f32 v126, v106, v41, v126
	v_pk_fma_f32 v[136:137], v[102:103], v[42:43], v[136:137] op_sel_hi:[1,0,1]
	v_pk_fma_f32 v[138:139], v[104:105], v[42:43], v[138:139] op_sel_hi:[1,0,1]
	v_fma_f32 v140, v106, v42, v140
	v_pk_add_f32 v[142:143], v[142:143], v[108:109]
	v_pk_add_f32 v[168:169], v[168:169], v[110:111]
	v_add_f32_e64 v170, v170, v112
	v_pk_fma_f32 v[114:115], v[108:109], v[44:45], v[114:115] op_sel_hi:[1,0,1]
	v_pk_fma_f32 v[116:117], v[110:111], v[44:45], v[116:117] op_sel_hi:[1,0,1]
	v_fma_f32 v120, v112, v44, v120
	v_pk_fma_f32 v[122:123], v[108:109], v[44:45], v[122:123] op_sel:[0,1,0]
	v_pk_fma_f32 v[124:125], v[110:111], v[44:45], v[124:125] op_sel:[0,1,0]
	v_fma_f32 v126, v112, v45, v126
	v_pk_fma_f32 v[136:137], v[108:109], v[46:47], v[136:137] op_sel_hi:[1,0,1]
	v_pk_fma_f32 v[138:139], v[110:111], v[46:47], v[138:139] op_sel_hi:[1,0,1]
	v_fma_f32 v140, v112, v46, v140
	s_barrier
	ds_read_b128 v[104:107], v23 offset:3072
	ds_read_b128 v[108:111], v23 offset:4096
	ds_read_b128 v[192:195], v23 offset:5120
	v_pk_add_f32 v[102:103], v[100:101], v[142:143]
	v_pk_add_f32 v[100:101], v[78:79], v[168:169]
	v_add_f32_e64 v78, v80, v170
	v_pk_add_f32 v[80:81], v[82:83], v[114:115]
	v_pk_add_f32 v[82:83], v[60:61], v[116:117]
	v_add_f32_e64 v60, v62, v120
	v_pk_add_f32 v[62:63], v[64:65], v[122:123]
	v_pk_add_f32 v[64:65], v[66:67], v[124:125]
	v_add_f32_e64 v66, v68, v126
	v_pk_add_f32 v[68:69], v[70:71], v[136:137]
	v_pk_add_f32 v[70:71], v[72:73], v[138:139]
	v_add_f32_e64 v72, v74, v140
	s_waitcnt lgkmcnt(2)
	v_pk_fma_f32 v[80:81], v[104:105], v[102:103], v[80:81] op_sel_hi:[0,1,1] neg_lo:[1,0,0] neg_hi:[1,0,0]
	v_pk_fma_f32 v[82:83], v[104:105], v[100:101], v[82:83] op_sel_hi:[0,1,1] neg_lo:[1,0,0] neg_hi:[1,0,0]
	v_fma_f32 v60, -v104, v78, v60
	v_pk_fma_f32 v[62:63], v[104:105], v[102:103], v[62:63] op_sel:[1,0,0] neg_lo:[1,0,0] neg_hi:[1,0,0]
	v_pk_fma_f32 v[64:65], v[104:105], v[100:101], v[64:65] op_sel:[1,0,0] neg_lo:[1,0,0] neg_hi:[1,0,0]
	v_fma_f32 v66, -v105, v78, v66
	v_pk_fma_f32 v[68:69], v[106:107], v[102:103], v[68:69] op_sel_hi:[0,1,1] neg_lo:[1,0,0] neg_hi:[1,0,0]
	v_pk_fma_f32 v[70:71], v[106:107], v[100:101], v[70:71] op_sel_hi:[0,1,1] neg_lo:[1,0,0] neg_hi:[1,0,0]
	v_fma_f32 v72, -v106, v78, v72
	v_pk_mul_f32 v[74:75], v[106:107], v[80:81] op_sel:[1,0]
	v_pk_mul_f32 v[198:199], v[106:107], v[82:83] op_sel:[1,0]
	v_mul_f32_e64 v204, v107, v60
	s_waitcnt lgkmcnt(1)
	v_pk_mul_f32 v[112:113], v[108:109], v[80:81] op_sel_hi:[0,1]
	v_pk_mul_f32 v[200:201], v[108:109], v[82:83] op_sel_hi:[0,1]
	v_mul_f32_e64 v206, v108, v60
	v_pk_mul_f32 v[196:197], v[108:109], v[80:81] op_sel:[1,0]
	v_pk_mul_f32 v[202:203], v[108:109], v[82:83] op_sel:[1,0]
	v_mul_f32_e64 v208, v109, v60
	v_pk_fma_f32 v[74:75], v[108:109], v[62:63], v[74:75] op_sel_hi:[0,1,1]
	v_pk_fma_f32 v[198:199], v[108:109], v[64:65], v[198:199] op_sel_hi:[0,1,1]
	v_fma_f32 v204, v108, v66, v204
	v_pk_fma_f32 v[112:113], v[110:111], v[62:63], v[112:113] op_sel_hi:[0,1,1]
	v_pk_fma_f32 v[200:201], v[110:111], v[64:65], v[200:201] op_sel_hi:[0,1,1]
	v_fma_f32 v206, v110, v66, v206
	v_pk_fma_f32 v[196:197], v[110:111], v[62:63], v[196:197] op_sel:[1,0,0]
	v_pk_fma_f32 v[202:203], v[110:111], v[64:65], v[202:203] op_sel:[1,0,0]
	v_fma_f32 v208, v111, v66, v208
	v_pk_fma_f32 v[74:75], v[108:109], v[68:69], v[74:75] op_sel:[1,0,0]
	v_pk_fma_f32 v[198:199], v[108:109], v[70:71], v[198:199] op_sel:[1,0,0]
	v_fma_f32 v204, v109, v72, v204
	v_pk_fma_f32 v[112:113], v[110:111], v[68:69], v[112:113] op_sel:[1,0,0]
	v_pk_fma_f32 v[200:201], v[110:111], v[70:71], v[200:201] op_sel:[1,0,0]
	v_fma_f32 v206, v111, v72, v206
	s_waitcnt lgkmcnt(0)
	v_pk_fma_f32 v[196:197], v[192:193], v[68:69], v[196:197] op_sel_hi:[0,1,1]
	v_pk_fma_f32 v[202:203], v[192:193], v[70:71], v[202:203] op_sel_hi:[0,1,1]
	v_fma_f32 v208, v192, v72, v208
	v_pk_mul_f32 v[210:211], v[104:105], v[74:75] op_sel_hi:[0,1]
	v_pk_mul_f32 v[212:213], v[104:105], v[198:199] op_sel_hi:[0,1]
	v_mul_f32_e64 v214, v104, v204
	v_pk_fma_f32 v[210:211], v[104:105], v[112:113], v[210:211] op_sel:[1,0,0]
	v_pk_fma_f32 v[212:213], v[104:105], v[200:201], v[212:213] op_sel:[1,0,0]
	v_fma_f32 v214, v105, v206, v214
	v_pk_fma_f32 v[210:211], v[106:107], v[196:197], v[210:211] op_sel_hi:[0,1,1]
	v_pk_fma_f32 v[212:213], v[106:107], v[202:203], v[212:213] op_sel_hi:[0,1,1]
	v_fma_f32 v214, v106, v208, v214
	v_pk_fma_f32 v[210:211], v[192:193], v[102:103], v[210:211] op_sel:[1,0,0] neg_lo:[0,0,1] neg_hi:[0,0,1]
	v_pk_fma_f32 v[212:213], v[192:193], v[100:101], v[212:213] op_sel:[1,0,0] neg_lo:[0,0,1] neg_hi:[0,0,1]
	v_fma_f32 v214, v193, v78, -v214
	s_add_i32 s4, s34, 4
	s_min_i32 s4, s4, 0x200
	s_mul_i32 s5, s4, 0x804
	s_add_i32 s5, s5, s35
	s_add_i32 s6, s5, 0x0
	s_add_i32 s7, s5, 0x101004
	s_add_i32 s8, s5, 0x202008
	s_add_i32 s11, s5, 0x30300c
	s_add_i32 s15, s5, 0x404010
	s_mul_i32 s9, s4, 0x180c
	s_add_i32 s9, s9, s33
	buffer_load_dword v12, v28, s[16:19], s6 offen nt
	buffer_load_dword v13, v28, s[16:19], s7 offen nt
	buffer_load_dword v14, v28, s[16:19], s8 offen nt
	buffer_load_dword v15, v28, s[16:19], s11 offen nt
	buffer_load_dword v16, v28, s[16:19], s15 offen nt
	buffer_load_dwordx3 v[32:34], v27, s[24:27], s9 offen nt
	s_waitcnt vmcnt(12)
	v_mov_b32_dpp v60, v96 wave_shr:1 row_mask:0xf bank_mask:0xf bound_ctrl:1
	v_mov_b32_dpp v61, v97 wave_shr:1 row_mask:0xf bank_mask:0xf bound_ctrl:1
	v_mov_b32_dpp v62, v98 wave_shr:1 row_mask:0xf bank_mask:0xf bound_ctrl:1
	v_mov_b32_dpp v64, v96 wave_shl:1 row_mask:0xf bank_mask:0xf bound_ctrl:1
	v_mov_b32_dpp v65, v97 wave_shl:1 row_mask:0xf bank_mask:0xf bound_ctrl:1
	v_mov_b32_dpp v66, v98 wave_shl:1 row_mask:0xf bank_mask:0xf bound_ctrl:1
	v_mov_b32_dpp v68, v54 wave_shr:1 row_mask:0xf bank_mask:0xf bound_ctrl:1
	v_mov_b32_dpp v69, v55 wave_shr:1 row_mask:0xf bank_mask:0xf bound_ctrl:1
	v_mov_b32_dpp v70, v92 wave_shr:1 row_mask:0xf bank_mask:0xf bound_ctrl:1
	v_mov_b32_dpp v71, v93 wave_shr:1 row_mask:0xf bank_mask:0xf bound_ctrl:1
	v_mov_b32_dpp v72, v94 wave_shr:1 row_mask:0xf bank_mask:0xf bound_ctrl:1
	v_mov_b32_dpp v78, v54 wave_shl:1 row_mask:0xf bank_mask:0xf bound_ctrl:1
	v_mov_b32_dpp v79, v55 wave_shl:1 row_mask:0xf bank_mask:0xf bound_ctrl:1
	v_mov_b32_dpp v80, v92 wave_shl:1 row_mask:0xf bank_mask:0xf bound_ctrl:1
	v_mov_b32_dpp v81, v93 wave_shl:1 row_mask:0xf bank_mask:0xf bound_ctrl:1
	v_mov_b32_dpp v82, v94 wave_shl:1 row_mask:0xf bank_mask:0xf bound_ctrl:1
	v_pk_mul_f32 v[84:85], v[54:55], v[96:97] op_sel_hi:[1,0]
	v_pk_mul_f32 v[86:87], v[92:93], v[96:97] op_sel_hi:[1,0]
	v_mul_f32_e64 v88, v94, v96
	v_pk_mul_f32 v[90:91], v[54:55], v[96:97] op_sel:[0,1]
	v_pk_mul_f32 v[100:101], v[92:93], v[96:97] op_sel:[0,1]
	v_mul_f32_e64 v102, v94, v97
	v_pk_mul_f32 v[104:105], v[54:55], v[98:99] op_sel_hi:[1,0]
	v_pk_mul_f32 v[106:107], v[92:93], v[98:99] op_sel_hi:[1,0]
	v_mul_f32_e64 v108, v94, v98
	v_pk_add_f32 v[110:111], v[54:55], v[68:69]
	v_pk_add_f32 v[192:193], v[92:93], v[70:71]
	v_add_f32_e64 v194, v94, v72
	v_pk_fma_f32 v[84:85], v[68:69], v[60:61], v[84:85] op_sel_hi:[1,0,1]
	v_pk_fma_f32 v[86:87], v[70:71], v[60:61], v[86:87] op_sel_hi:[1,0,1]
	v_fma_f32 v88, v72, v60, v88
	v_pk_fma_f32 v[90:91], v[68:69], v[60:61], v[90:91] op_sel:[0,1,0]
	v_pk_fma_f32 v[100:101], v[70:71], v[60:61], v[100:101] op_sel:[0,1,0]
	v_fma_f32 v102, v72, v61, v102
	v_pk_fma_f32 v[104:105], v[68:69], v[62:63], v[104:105] op_sel_hi:[1,0,1]
	v_pk_fma_f32 v[106:107], v[70:71], v[62:63], v[106:107] op_sel_hi:[1,0,1]
	v_fma_f32 v108, v72, v62, v108
	v_pk_add_f32 v[110:111], v[110:111], v[78:79]
	v_pk_add_f32 v[192:193], v[192:193], v[80:81]
	v_add_f32_e64 v194, v194, v82
	v_pk_fma_f32 v[84:85], v[78:79], v[64:65], v[84:85] op_sel_hi:[1,0,1]
	v_pk_fma_f32 v[86:87], v[80:81], v[64:65], v[86:87] op_sel_hi:[1,0,1]
	v_fma_f32 v88, v82, v64, v88
	v_pk_fma_f32 v[90:91], v[78:79], v[64:65], v[90:91] op_sel:[0,1,0]
	v_pk_fma_f32 v[100:101], v[80:81], v[64:65], v[100:101] op_sel:[0,1,0]
	v_fma_f32 v102, v82, v65, v102
	v_pk_fma_f32 v[104:105], v[78:79], v[66:67], v[104:105] op_sel_hi:[1,0,1]
	v_pk_fma_f32 v[106:107], v[80:81], v[66:67], v[106:107] op_sel_hi:[1,0,1]
	v_fma_f32 v108, v82, v66, v108
	s_barrier
	ds_read_b128 v[68:71], v23 offset:0
	ds_read_b128 v[80:83], v23 offset:1024
	ds_read_b128 v[216:219], v23 offset:2048
	v_pk_add_f32 v[72:73], v[142:143], v[110:111]
	v_pk_add_f32 v[78:79], v[162:163], v[72:73]
	v_pk_add_f32 v[142:143], v[168:169], v[192:193]
	v_pk_add_f32 v[162:163], v[164:165], v[142:143]
	v_add_f32_e64 v164, v170, v194
	v_add_f32_e64 v168, v166, v164
	v_pk_add_f32 v[166:167], v[114:115], v[84:85]
	v_pk_add_f32 v[170:171], v[144:145], v[166:167]
	v_pk_add_f32 v[114:115], v[116:117], v[86:87]
	v_pk_add_f32 v[144:145], v[146:147], v[114:115]
	v_add_f32_e64 v116, v120, v88
	v_add_f32_e64 v146, v148, v116
	v_pk_add_f32 v[120:121], v[122:123], v[90:91]
	v_pk_add_f32 v[148:149], v[150:151], v[120:121]
	v_pk_add_f32 v[122:123], v[124:125], v[100:101]
	v_pk_add_f32 v[150:151], v[152:153], v[122:123]
	v_add_f32_e64 v124, v126, v102
	v_add_f32_e64 v152, v154, v124
	v_pk_add_f32 v[126:127], v[136:137], v[104:105]
	v_pk_add_f32 v[154:155], v[156:157], v[126:127]
	v_pk_add_f32 v[136:137], v[138:139], v[106:107]
	v_pk_add_f32 v[156:157], v[158:159], v[136:137]
	v_add_f32_e64 v138, v140, v108
	v_add_f32_e64 v158, v160, v138
	s_waitcnt lgkmcnt(2)
	v_pk_fma_f32 v[170:171], v[68:69], v[78:79], v[170:171] op_sel_hi:[0,1,1] neg_lo:[1,0,0] neg_hi:[1,0,0]
	v_pk_fma_f32 v[144:145], v[68:69], v[162:163], v[144:145] op_sel_hi:[0,1,1] neg_lo:[1,0,0] neg_hi:[1,0,0]
	v_fma_f32 v146, -v68, v168, v146
	v_pk_fma_f32 v[148:149], v[68:69], v[78:79], v[148:149] op_sel:[1,0,0] neg_lo:[1,0,0] neg_hi:[1,0,0]
	v_pk_fma_f32 v[150:151], v[68:69], v[162:163], v[150:151] op_sel:[1,0,0] neg_lo:[1,0,0] neg_hi:[1,0,0]
	v_fma_f32 v152, -v69, v168, v152
	v_pk_fma_f32 v[154:155], v[70:71], v[78:79], v[154:155] op_sel_hi:[0,1,1] neg_lo:[1,0,0] neg_hi:[1,0,0]
	v_pk_fma_f32 v[156:157], v[70:71], v[162:163], v[156:157] op_sel_hi:[0,1,1] neg_lo:[1,0,0] neg_hi:[1,0,0]
	v_fma_f32 v158, -v70, v168, v158
	v_pk_mul_f32 v[140:141], v[70:71], v[170:171] op_sel:[1,0]
	v_pk_mul_f32 v[222:223], v[70:71], v[144:145] op_sel:[1,0]
	v_mul_f32_e64 v228, v71, v146
	s_waitcnt lgkmcnt(1)
	v_pk_mul_f32 v[160:161], v[80:81], v[170:171] op_sel_hi:[0,1]
	v_pk_mul_f32 v[224:225], v[80:81], v[144:145] op_sel_hi:[0,1]
	v_mul_f32_e64 v230, v80, v146
	v_pk_mul_f32 v[220:221], v[80:81], v[170:171] op_sel:[1,0]
	v_pk_mul_f32 v[226:227], v[80:81], v[144:145] op_sel:[1,0]
	v_mul_f32_e64 v232, v81, v146
	v_pk_fma_f32 v[140:141], v[80:81], v[148:149], v[140:141] op_sel_hi:[0,1,1]
	v_pk_fma_f32 v[222:223], v[80:81], v[150:151], v[222:223] op_sel_hi:[0,1,1]
	v_fma_f32 v228, v80, v152, v228
	v_pk_fma_f32 v[160:161], v[82:83], v[148:149], v[160:161] op_sel_hi:[0,1,1]
	v_pk_fma_f32 v[224:225], v[82:83], v[150:151], v[224:225] op_sel_hi:[0,1,1]
	v_fma_f32 v230, v82, v152, v230
	v_pk_fma_f32 v[220:221], v[82:83], v[148:149], v[220:221] op_sel:[1,0,0]
	v_pk_fma_f32 v[226:227], v[82:83], v[150:151], v[226:227] op_sel:[1,0,0]
	v_fma_f32 v232, v83, v152, v232
	v_pk_fma_f32 v[140:141], v[80:81], v[154:155], v[140:141] op_sel:[1,0,0]
	v_pk_fma_f32 v[222:223], v[80:81], v[156:157], v[222:223] op_sel:[1,0,0]
	v_fma_f32 v228, v81, v158, v228
	v_pk_fma_f32 v[160:161], v[82:83], v[154:155], v[160:161] op_sel:[1,0,0]
	v_pk_fma_f32 v[224:225], v[82:83], v[156:157], v[224:225] op_sel:[1,0,0]
	v_fma_f32 v230, v83, v158, v230
	s_waitcnt lgkmcnt(0)
	v_pk_fma_f32 v[220:221], v[216:217], v[154:155], v[220:221] op_sel_hi:[0,1,1]
	v_pk_fma_f32 v[226:227], v[216:217], v[156:157], v[226:227] op_sel_hi:[0,1,1]
	v_fma_f32 v232, v216, v158, v232
	v_pk_mul_f32 v[234:235], v[68:69], v[140:141] op_sel_hi:[0,1]
	v_pk_mul_f32 v[236:237], v[68:69], v[222:223] op_sel_hi:[0,1]
	v_mul_f32_e64 v238, v68, v228
	v_pk_fma_f32 v[234:235], v[68:69], v[160:161], v[234:235] op_sel:[1,0,0]
	v_pk_fma_f32 v[236:237], v[68:69], v[224:225], v[236:237] op_sel:[1,0,0]
	v_fma_f32 v238, v69, v230, v238
	v_pk_fma_f32 v[234:235], v[70:71], v[220:221], v[234:235] op_sel_hi:[0,1,1]
	v_pk_fma_f32 v[236:237], v[70:71], v[226:227], v[236:237] op_sel_hi:[0,1,1]
	v_fma_f32 v238, v70, v232, v238
	v_pk_fma_f32 v[234:235], v[216:217], v[78:79], v[234:235] op_sel:[1,0,0] neg_lo:[0,0,1] neg_hi:[0,0,1]
	v_pk_fma_f32 v[236:237], v[216:217], v[162:163], v[236:237] op_sel:[1,0,0] neg_lo:[0,0,1] neg_hi:[0,0,1]
	v_fma_f32 v238, v217, v168, -v238
	v_cmp_eq_u32_e64 s[10:11], 1, v219
	v_cmp_eq_u32_e64 s[14:15], 2, v219
	v_cmp_eq_u32_e64 s[20:21], 3, v219
	v_cmp_eq_u32_e64 s[22:23], 4, v219
	v_cmp_eq_u32_e64 s[30:31], 5, v219
	v_pk_add_f32 v[78:79], v[74:75], v[140:141]
	v_pk_add_f32 v[144:145], v[76:77], v[78:79]
	v_pk_add_f32 v[74:75], v[198:199], v[222:223]
	v_pk_add_f32 v[76:77], v[174:175], v[74:75]
	v_add_f32_e64 v146, v204, v228
	v_add_f32_e64 v148, v180, v146
	v_pk_add_f32 v[150:151], v[112:113], v[160:161]
	v_pk_add_f32 v[152:153], v[118:119], v[150:151]
	v_pk_add_f32 v[112:113], v[200:201], v[224:225]
	v_pk_add_f32 v[118:119], v[176:177], v[112:113]
	v_add_f32_e64 v154, v206, v230
	v_add_f32_e64 v156, v182, v154
	v_pk_add_f32 v[158:159], v[196:197], v[220:221]
	v_pk_add_f32 v[162:163], v[172:173], v[158:159]
	v_pk_add_f32 v[168:169], v[202:203], v[226:227]
	v_pk_add_f32 v[170:171], v[178:179], v[168:169]
	v_add_f32_e64 v172, v208, v232
	v_add_f32_e64 v174, v184, v172
	v_pk_add_f32 v[176:177], v[210:211], v[234:235]
	v_pk_add_f32 v[178:179], v[186:187], v[176:177]
	v_pk_add_f32 v[180:181], v[212:213], v[236:237]
	v_pk_add_f32 v[182:183], v[188:189], v[180:181]
	v_add_f32_e64 v184, v214, v238
	v_add_f32_e64 v186, v190, v184
	v_pk_fma_f32 v[188:189], v[128:129], v[144:145], v[178:179] op_sel_hi:[0,1,1]
	v_pk_fma_f32 v[190:191], v[128:129], v[76:77], v[182:183] op_sel_hi:[0,1,1]
	v_fma_f32 v196, v128, v148, v186
	v_pk_fma_f32 v[198:199], v[132:133], v[144:145], v[178:179] op_sel_hi:[0,1,1]
	v_pk_fma_f32 v[200:201], v[132:133], v[76:77], v[182:183] op_sel_hi:[0,1,1]
	v_fma_f32 v202, v132, v148, v186
	v_pk_fma_f32 v[188:189], v[128:129], v[152:153], v[188:189] op_sel:[1,0,0]
	v_pk_fma_f32 v[190:191], v[128:129], v[118:119], v[190:191] op_sel:[1,0,0]
	v_fma_f32 v196, v129, v156, v196
	v_pk_fma_f32 v[198:199], v[132:133], v[152:153], v[198:199] op_sel:[1,0,0]
	v_pk_fma_f32 v[200:201], v[132:133], v[118:119], v[200:201] op_sel:[1,0,0]
	v_fma_f32 v202, v133, v156, v202
	v_pk_fma_f32 v[188:189], v[130:131], v[162:163], v[188:189] op_sel_hi:[0,1,1]
	v_pk_fma_f32 v[190:191], v[130:131], v[170:171], v[190:191] op_sel_hi:[0,1,1]
	v_fma_f32 v196, v130, v174, v196
	v_pk_fma_f32 v[198:199], v[134:135], v[162:163], v[198:199] op_sel_hi:[0,1,1]
	v_pk_fma_f32 v[200:201], v[134:135], v[170:171], v[200:201] op_sel_hi:[0,1,1]
	v_fma_f32 v202, v134, v174, v202
	v_pk_fma_f32 v[178:179], v[36:37], v[144:145], v[178:179] op_sel_hi:[0,1,1]
	v_pk_fma_f32 v[182:183], v[36:37], v[76:77], v[182:183] op_sel_hi:[0,1,1]
	v_fma_f32 v186, v36, v148, v186
	v_pk_fma_f32 v[178:179], v[36:37], v[152:153], v[178:179] op_sel:[1,0,0]
	v_pk_fma_f32 v[182:183], v[36:37], v[118:119], v[182:183] op_sel:[1,0,0]
	v_fma_f32 v186, v37, v156, v186
	v_pk_fma_f32 v[178:179], v[38:39], v[162:163], v[178:179] op_sel_hi:[0,1,1]
	v_pk_fma_f32 v[182:183], v[38:39], v[170:171], v[182:183] op_sel_hi:[0,1,1]
	v_fma_f32 v186, v38, v174, v186
	v_cndmask_b32_e64 v204, 0, v1, s[10:11]
	v_cndmask_b32_e64 v205, 0, v1, s[14:15]
	v_cndmask_b32_e64 v206, 0, v1, s[20:21]
	v_cndmask_b32_e64 v207, 0, v1, s[22:23]
	v_cndmask_b32_e64 v208, 0, v1, s[30:31]
	v_add_f32_dpp v178, v188, v178 wave_shl:1 row_mask:0xf bank_mask:0xf bound_ctrl:1
	v_add_f32_dpp v179, v189, v179 wave_shl:1 row_mask:0xf bank_mask:0xf bound_ctrl:1
	v_add_f32_dpp v182, v190, v182 wave_shl:1 row_mask:0xf bank_mask:0xf bound_ctrl:1
	v_add_f32_dpp v183, v191, v183 wave_shl:1 row_mask:0xf bank_mask:0xf bound_ctrl:1
	v_add_f32_dpp v186, v196, v186 wave_shl:1 row_mask:0xf bank_mask:0xf bound_ctrl:1
	s_add_i32 s4, s34, 0
	s_cmpk_lt_i32 s4, 0x201
	s_cselect_b64 s[12:13], s[0:1], 0
	v_add_f32_dpp v178, v198, v178 wave_shr:1 row_mask:0xf bank_mask:0xf bound_ctrl:1
	v_add_f32_dpp v179, v199, v179 wave_shr:1 row_mask:0xf bank_mask:0xf bound_ctrl:1
	v_add_f32_dpp v182, v200, v182 wave_shr:1 row_mask:0xf bank_mask:0xf bound_ctrl:1
	v_add_f32_dpp v183, v201, v183 wave_shr:1 row_mask:0xf bank_mask:0xf bound_ctrl:1
	v_add_f32_dpp v186, v202, v186 wave_shr:1 row_mask:0xf bank_mask:0xf bound_ctrl:1
	v_pk_fma_f32 v[178:179], v[20:21], v[218:219], v[178:179] op_sel_hi:[1,0,1] neg_lo:[0,0,1] neg_hi:[0,0,1]
	v_pk_fma_f32 v[182:183], v[24:25], v[218:219], v[182:183] op_sel_hi:[1,0,1] neg_lo:[0,0,1] neg_hi:[0,0,1]
	v_fma_f32 v186, v30, v218, -v186
	v_pk_add_f32 v[178:179], v[178:179], v[204:205] neg_lo:[0,1] neg_hi:[0,1]
	v_pk_add_f32 v[182:183], v[182:183], v[206:207] neg_lo:[0,1] neg_hi:[0,1]
	v_add_f32_e64 v186, v186, -v208
	v_pk_mul_f32 v[210:211], v[178:179], v[178:179]
	v_pk_fma_f32 v[210:211], v[182:183], v[182:183], v[210:211]
	v_add_f32_e32 v210, v210, v211
	v_fma_f32 v210, v186, v186, v210
	v_cndmask_b32_e64 v211, 0, v210, s[12:13]
	v_add_f32_e32 v0, v0, v211
	s_add_i32 s4, s34, 5
	s_min_i32 s4, s4, 0x200
	s_mul_i32 s5, s4, 0x804
	s_add_i32 s5, s5, s35
	s_add_i32 s6, s5, 0x0
	s_add_i32 s7, s5, 0x101004
	s_add_i32 s8, s5, 0x202008
	s_add_i32 s11, s5, 0x30300c
	s_add_i32 s15, s5, 0x404010
	s_mul_i32 s9, s4, 0x180c
	s_add_i32 s9, s9, s33
	buffer_load_dword v20, v28, s[16:19], s6 offen nt
	buffer_load_dword v21, v28, s[16:19], s7 offen nt
	buffer_load_dword v24, v28, s[16:19], s8 offen nt
	buffer_load_dword v25, v28, s[16:19], s11 offen nt
	buffer_load_dword v30, v28, s[16:19], s15 offen nt
	buffer_load_dwordx3 v[36:38], v27, s[24:27], s9 offen nt
	s_waitcnt vmcnt(12)
	v_mov_b32_dpp v68, v8 wave_shr:1 row_mask:0xf bank_mask:0xf bound_ctrl:1
	v_mov_b32_dpp v69, v9 wave_shr:1 row_mask:0xf bank_mask:0xf bound_ctrl:1
	v_mov_b32_dpp v70, v10 wave_shr:1 row_mask:0xf bank_mask:0xf bound_ctrl:1
	v_mov_b32_dpp v80, v8 wave_shl:1 row_mask:0xf bank_mask:0xf bound_ctrl:1
	v_mov_b32_dpp v81, v9 wave_shl:1 row_mask:0xf bank_mask:0xf bound_ctrl:1
	v_mov_b32_dpp v82, v10 wave_shl:1 row_mask:0xf bank_mask:0xf bound_ctrl:1
	v_mov_b32_dpp v76, v2 wave_shr:1 row_mask:0xf bank_mask:0xf bound_ctrl:1
	v_mov_b32_dpp v77, v3 wave_shr:1 row_mask:0xf bank_mask:0xf bound_ctrl:1
	v_mov_b32_dpp v118, v4 wave_shr:1 row_mask:0xf bank_mask:0xf bound_ctrl:1
	v_mov_b32_dpp v119, v5 wave_shr:1 row_mask:0xf bank_mask:0xf bound_ctrl:1
	v_mov_b32_dpp v128, v6 wave_shr:1 row_mask:0xf bank_mask:0xf bound_ctrl:1
	v_mov_b32_dpp v130, v2 wave_shl:1 row_mask:0xf bank_mask:0xf bound_ctrl:1
	v_mov_b32_dpp v131, v3 wave_shl:1 row_mask:0xf bank_mask:0xf bound_ctrl:1
	v_mov_b32_dpp v132, v4 wave_shl:1 row_mask:0xf bank_mask:0xf bound_ctrl:1
	v_mov_b32_dpp v133, v5 wave_shl:1 row_mask:0xf bank_mask:0xf bound_ctrl:1
	v_mov_b32_dpp v134, v6 wave_shl:1 row_mask:0xf bank_mask:0xf bound_ctrl:1
	v_pk_mul_f32 v[144:145], v[2:3], v[8:9] op_sel_hi:[1,0]
	v_pk_mul_f32 v[148:149], v[4:5], v[8:9] op_sel_hi:[1,0]
	v_mul_f32_e64 v152, v6, v8
	v_pk_mul_f32 v[156:157], v[2:3], v[8:9] op_sel:[0,1]
	v_pk_mul_f32 v[162:163], v[4:5], v[8:9] op_sel:[0,1]
	v_mul_f32_e64 v170, v6, v9
	v_pk_mul_f32 v[174:175], v[2:3], v[10:11] op_sel_hi:[1,0]
	v_pk_mul_f32 v[178:179], v[4:5], v[10:11] op_sel_hi:[1,0]
	v_mul_f32_e64 v182, v6, v10
	v_pk_add_f32 v[186:187], v[2:3], v[76:77]
	v_pk_add_f32 v[188:189], v[4:5], v[118:119]
	v_add_f32_e64 v190, v6, v128
	v_pk_fma_f32 v[144:145], v[76:77], v[68:69], v[144:145] op_sel_hi:[1,0,1]
	v_pk_fma_f32 v[148:149], v[118:119], v[68:69], v[148:149] op_sel_hi:[1,0,1]
	v_fma_f32 v152, v128, v68, v152
	v_pk_fma_f32 v[156:157], v[76:77], v[68:69], v[156:157] op_sel:[0,1,0]
	v_pk_fma_f32 v[162:163], v[118:119], v[68:69], v[162:163] op_sel:[0,1,0]
	v_fma_f32 v170, v128, v69, v170
	v_pk_fma_f32 v[174:175], v[76:77], v[70:71], v[174:175] op_sel_hi:[1,0,1]
	v_pk_fma_f32 v[178:179], v[118:119], v[70:71], v[178:179] op_sel_hi:[1,0,1]
	v_fma_f32 v182, v128, v70, v182
	v_pk_add_f32 v[186:187], v[186:187], v[130:131]
	v_pk_add_f32 v[188:189], v[188:189], v[132:133]
	v_add_f32_e64 v190, v190, v134
	v_pk_fma_f32 v[144:145], v[130:131], v[80:81], v[144:145] op_sel_hi:[1,0,1]
	v_pk_fma_f32 v[148:149], v[132:133], v[80:81], v[148:149] op_sel_hi:[1,0,1]
	v_fma_f32 v152, v134, v80, v152
	v_pk_fma_f32 v[156:157], v[130:131], v[80:81], v[156:157] op_sel:[0,1,0]
	v_pk_fma_f32 v[162:163], v[132:133], v[80:81], v[162:163] op_sel:[0,1,0]
	v_fma_f32 v170, v134, v81, v170
	v_pk_fma_f32 v[174:175], v[130:131], v[82:83], v[174:175] op_sel_hi:[1,0,1]
	v_pk_fma_f32 v[178:179], v[132:133], v[82:83], v[178:179] op_sel_hi:[1,0,1]
	v_fma_f32 v182, v134, v82, v182
	s_barrier
	ds_read_b128 v[128:131], v23 offset:3072
	ds_read_b128 v[132:135], v23 offset:4096
	ds_read_b128 v[196:199], v23 offset:5120
	v_pk_add_f32 v[76:77], v[72:73], v[186:187]
	v_pk_add_f32 v[72:73], v[142:143], v[188:189]
	v_add_f32_e64 v118, v164, v190
	v_pk_add_f32 v[142:143], v[166:167], v[144:145]
	v_pk_add_f32 v[164:165], v[114:115], v[148:149]
	v_add_f32_e64 v114, v116, v152
	v_pk_add_f32 v[116:117], v[120:121], v[156:157]
	v_pk_add_f32 v[120:121], v[122:123], v[162:163]
	v_add_f32_e64 v122, v124, v170
	v_pk_add_f32 v[124:125], v[126:127], v[174:175]
	v_pk_add_f32 v[126:127], v[136:137], v[178:179]
	v_add_f32_e64 v136, v138, v182
	s_waitcnt lgkmcnt(2)
	v_pk_fma_f32 v[142:143], v[128:129], v[76:77], v[142:143] op_sel_hi:[0,1,1] neg_lo:[1,0,0] neg_hi:[1,0,0]
	v_pk_fma_f32 v[164:165], v[128:129], v[72:73], v[164:165] op_sel_hi:[0,1,1] neg_lo:[1,0,0] neg_hi:[1,0,0]
	v_fma_f32 v114, -v128, v118, v114
	v_pk_fma_f32 v[116:117], v[128:129], v[76:77], v[116:117] op_sel:[1,0,0] neg_lo:[1,0,0] neg_hi:[1,0,0]
	v_pk_fma_f32 v[120:121], v[128:129], v[72:73], v[120:121] op_sel:[1,0,0] neg_lo:[1,0,0] neg_hi:[1,0,0]
	v_fma_f32 v122, -v129, v118, v122
	v_pk_fma_f32 v[124:125], v[130:131], v[76:77], v[124:125] op_sel_hi:[0,1,1] neg_lo:[1,0,0] neg_hi:[1,0,0]
	v_pk_fma_f32 v[126:127], v[130:131], v[72:73], v[126:127] op_sel_hi:[0,1,1] neg_lo:[1,0,0] neg_hi:[1,0,0]
	v_fma_f32 v136, -v130, v118, v136
	v_pk_mul_f32 v[138:139], v[130:131], v[142:143] op_sel:[1,0]
	v_pk_mul_f32 v[202:203], v[130:131], v[164:165] op_sel:[1,0]
	v_mul_f32_e64 v208, v131, v114
	s_waitcnt lgkmcnt(1)
	v_pk_mul_f32 v[166:167], v[132:133], v[142:143] op_sel_hi:[0,1]
	v_pk_mul_f32 v[204:205], v[132:133], v[164:165] op_sel_hi:[0,1]
	v_mul_f32_e64 v210, v132, v114
	v_pk_mul_f32 v[200:201], v[132:133], v[142:143] op_sel:[1,0]
	v_pk_mul_f32 v[206:207], v[132:133], v[164:165] op_sel:[1,0]
	v_mul_f32_e64 v212, v133, v114
	v_pk_fma_f32 v[138:139], v[132:133], v[116:117], v[138:139] op_sel_hi:[0,1,1]
	v_pk_fma_f32 v[202:203], v[132:133], v[120:121], v[202:203] op_sel_hi:[0,1,1]
	v_fma_f32 v208, v132, v122, v208
	v_pk_fma_f32 v[166:167], v[134:135], v[116:117], v[166:167] op_sel_hi:[0,1,1]
	v_pk_fma_f32 v[204:205], v[134:135], v[120:121], v[204:205] op_sel_hi:[0,1,1]
	v_fma_f32 v210, v134, v122, v210
	v_pk_fma_f32 v[200:201], v[134:135], v[116:117], v[200:201] op_sel:[1,0,0]
	v_pk_fma_f32 v[206:207], v[134:135], v[120:121], v[206:207] op_sel:[1,0,0]
	v_fma_f32 v212, v135, v122, v212
	v_pk_fma_f32 v[138:139], v[132:133], v[124:125], v[138:139] op_sel:[1,0,0]
	v_pk_fma_f32 v[202:203], v[132:133], v[126:127], v[202:203] op_sel:[1,0,0]
	v_fma_f32 v208, v133, v136, v208
	v_pk_fma_f32 v[166:167], v[134:135], v[124:125], v[166:167] op_sel:[1,0,0]
	v_pk_fma_f32 v[204:205], v[134:135], v[126:127], v[204:205] op_sel:[1,0,0]
	v_fma_f32 v210, v135, v136, v210
	s_waitcnt lgkmcnt(0)
	v_pk_fma_f32 v[200:201], v[196:197], v[124:125], v[200:201] op_sel_hi:[0,1,1]
	v_pk_fma_f32 v[206:207], v[196:197], v[126:127], v[206:207] op_sel_hi:[0,1,1]
	v_fma_f32 v212, v196, v136, v212
	v_pk_mul_f32 v[214:215], v[128:129], v[138:139] op_sel_hi:[0,1]
	v_pk_mul_f32 v[216:217], v[128:129], v[202:203] op_sel_hi:[0,1]
	v_mul_f32_e64 v218, v128, v208
	v_pk_fma_f32 v[214:215], v[128:129], v[166:167], v[214:215] op_sel:[1,0,0]
	v_pk_fma_f32 v[216:217], v[128:129], v[204:205], v[216:217] op_sel:[1,0,0]
	v_fma_f32 v218, v129, v210, v218
	v_pk_fma_f32 v[214:215], v[130:131], v[200:201], v[214:215] op_sel_hi:[0,1,1]
	v_pk_fma_f32 v[216:217], v[130:131], v[206:207], v[216:217] op_sel_hi:[0,1,1]
	v_fma_f32 v218, v130, v212, v218
	v_pk_fma_f32 v[214:215], v[196:197], v[76:77], v[214:215] op_sel:[1,0,0] neg_lo:[0,0,1] neg_hi:[0,0,1]
	v_pk_fma_f32 v[216:217], v[196:197], v[72:73], v[216:217] op_sel:[1,0,0] neg_lo:[0,0,1] neg_hi:[0,0,1]
	v_fma_f32 v218, v197, v118, -v218
	v_cmp_eq_u32_e64 s[10:11], 1, v199
	v_cmp_eq_u32_e64 s[14:15], 2, v199
	v_cmp_eq_u32_e64 s[20:21], 3, v199
	v_cmp_eq_u32_e64 s[22:23], 4, v199
	v_cmp_eq_u32_e64 s[30:31], 5, v199
	v_pk_add_f32 v[72:73], v[78:79], v[138:139]
	v_pk_add_f32 v[76:77], v[74:75], v[202:203]
	v_add_f32_e64 v74, v146, v208
	v_pk_add_f32 v[78:79], v[150:151], v[166:167]
	v_pk_add_f32 v[114:115], v[112:113], v[204:205]
	v_add_f32_e64 v112, v154, v210
	v_pk_add_f32 v[116:117], v[158:159], v[200:201]
	v_pk_add_f32 v[118:119], v[168:169], v[206:207]
	v_add_f32_e64 v120, v172, v212
	v_pk_add_f32 v[122:123], v[176:177], v[214:215]
	v_pk_add_f32 v[124:125], v[180:181], v[216:217]
	v_add_f32_e64 v126, v184, v218
	v_pk_fma_f32 v[136:137], v[40:41], v[72:73], v[122:123] op_sel_hi:[0,1,1]
	v_pk_fma_f32 v[142:143], v[40:41], v[76:77], v[124:125] op_sel_hi:[0,1,1]
	v_fma_f32 v146, v40, v74, v126
	v_pk_fma_f32 v[150:151], v[44:45], v[72:73], v[122:123] op_sel_hi:[0,1,1]
	v_pk_fma_f32 v[154:155], v[44:45], v[76:77], v[124:125] op_sel_hi:[0,1,1]
	v_fma_f32 v158, v44, v74, v126
	v_pk_fma_f32 v[136:137], v[40:41], v[78:79], v[136:137] op_sel:[1,0,0]
	v_pk_fma_f32 v[142:143], v[40:41], v[114:115], v[142:143] op_sel:[1,0,0]
	v_fma_f32 v146, v41, v112, v146
	v_pk_fma_f32 v[150:151], v[44:45], v[78:79], v[150:151] op_sel:[1,0,0]
	v_pk_fma_f32 v[154:155], v[44:45], v[114:115], v[154:155] op_sel:[1,0,0]
	v_fma_f32 v158, v45, v112, v158
	v_pk_fma_f32 v[136:137], v[42:43], v[116:117], v[136:137] op_sel_hi:[0,1,1]
	v_pk_fma_f32 v[142:143], v[42:43], v[118:119], v[142:143] op_sel_hi:[0,1,1]
	v_fma_f32 v146, v42, v120, v146
	v_pk_fma_f32 v[150:151], v[46:47], v[116:117], v[150:151] op_sel_hi:[0,1,1]
	v_pk_fma_f32 v[154:155], v[46:47], v[118:119], v[154:155] op_sel_hi:[0,1,1]
	v_fma_f32 v158, v46, v120, v158
	v_pk_fma_f32 v[122:123], v[56:57], v[72:73], v[122:123] op_sel_hi:[0,1,1]
	v_pk_fma_f32 v[124:125], v[56:57], v[76:77], v[124:125] op_sel_hi:[0,1,1]
	v_fma_f32 v126, v56, v74, v126
	v_pk_fma_f32 v[122:123], v[56:57], v[78:79], v[122:123] op_sel:[1,0,0]
	v_pk_fma_f32 v[124:125], v[56:57], v[114:115], v[124:125] op_sel:[1,0,0]
	v_fma_f32 v126, v57, v112, v126
	v_pk_fma_f32 v[122:123], v[58:59], v[116:117], v[122:123] op_sel_hi:[0,1,1]
	v_pk_fma_f32 v[124:125], v[58:59], v[118:119], v[124:125] op_sel_hi:[0,1,1]
	v_fma_f32 v126, v58, v120, v126
	v_cndmask_b32_e64 v164, 0, v1, s[10:11]
	v_cndmask_b32_e64 v165, 0, v1, s[14:15]
	v_cndmask_b32_e64 v168, 0, v1, s[20:21]
	v_cndmask_b32_e64 v169, 0, v1, s[22:23]
	v_cndmask_b32_e64 v172, 0, v1, s[30:31]
	v_add_f32_dpp v122, v136, v122 wave_shl:1 row_mask:0xf bank_mask:0xf bound_ctrl:1
	v_add_f32_dpp v123, v137, v123 wave_shl:1 row_mask:0xf bank_mask:0xf bound_ctrl:1
	v_add_f32_dpp v124, v142, v124 wave_shl:1 row_mask:0xf bank_mask:0xf bound_ctrl:1
	v_add_f32_dpp v125, v143, v125 wave_shl:1 row_mask:0xf bank_mask:0xf bound_ctrl:1
	v_add_f32_dpp v126, v146, v126 wave_shl:1 row_mask:0xf bank_mask:0xf bound_ctrl:1
	s_add_i32 s4, s34, 1
	s_cmpk_lt_i32 s4, 0x201
	s_cselect_b64 s[12:13], s[0:1], 0
	v_add_f32_dpp v122, v150, v122 wave_shr:1 row_mask:0xf bank_mask:0xf bound_ctrl:1
	v_add_f32_dpp v123, v151, v123 wave_shr:1 row_mask:0xf bank_mask:0xf bound_ctrl:1
	v_add_f32_dpp v124, v154, v124 wave_shr:1 row_mask:0xf bank_mask:0xf bound_ctrl:1
	v_add_f32_dpp v125, v155, v125 wave_shr:1 row_mask:0xf bank_mask:0xf bound_ctrl:1
	v_add_f32_dpp v126, v158, v126 wave_shr:1 row_mask:0xf bank_mask:0xf bound_ctrl:1
	v_pk_fma_f32 v[122:123], v[48:49], v[198:199], v[122:123] op_sel_hi:[1,0,1] neg_lo:[0,0,1] neg_hi:[0,0,1]
	v_pk_fma_f32 v[124:125], v[50:51], v[198:199], v[124:125] op_sel_hi:[1,0,1] neg_lo:[0,0,1] neg_hi:[0,0,1]
	v_fma_f32 v126, v52, v198, -v126
	v_pk_add_f32 v[122:123], v[122:123], v[164:165] neg_lo:[0,1] neg_hi:[0,1]
	v_pk_add_f32 v[124:125], v[124:125], v[168:169] neg_lo:[0,1] neg_hi:[0,1]
	v_add_f32_e64 v126, v126, -v172
	v_pk_mul_f32 v[176:177], v[122:123], v[122:123]
	v_pk_fma_f32 v[176:177], v[124:125], v[124:125], v[176:177]
	v_add_f32_e32 v176, v176, v177
	v_fma_f32 v176, v126, v126, v176
	v_cndmask_b32_e64 v177, 0, v176, s[12:13]
	v_add_f32_e32 v0, v0, v177
	s_add_i32 s4, s34, 6
	s_min_i32 s4, s4, 0x200
	s_mul_i32 s5, s4, 0x804
	s_add_i32 s5, s5, s35
	s_add_i32 s6, s5, 0x0
	s_add_i32 s7, s5, 0x101004
	s_add_i32 s8, s5, 0x202008
	s_add_i32 s11, s5, 0x30300c
	s_add_i32 s15, s5, 0x404010
	s_mul_i32 s9, s4, 0x180c
	s_add_i32 s9, s9, s33
	buffer_load_dword v40, v28, s[16:19], s6 offen nt
	buffer_load_dword v41, v28, s[16:19], s7 offen nt
	buffer_load_dword v42, v28, s[16:19], s8 offen nt
	buffer_load_dword v43, v28, s[16:19], s11 offen nt
	buffer_load_dword v44, v28, s[16:19], s15 offen nt
	buffer_load_dwordx3 v[48:50], v27, s[24:27], s9 offen nt
	s_waitcnt vmcnt(12)
	v_mov_b32_dpp v56, v32 wave_shr:1 row_mask:0xf bank_mask:0xf bound_ctrl:1
	v_mov_b32_dpp v57, v33 wave_shr:1 row_mask:0xf bank_mask:0xf bound_ctrl:1
	v_mov_b32_dpp v58, v34 wave_shr:1 row_mask:0xf bank_mask:0xf bound_ctrl:1
	v_mov_b32_dpp v72, v32 wave_shl:1 row_mask:0xf bank_mask:0xf bound_ctrl:1
	v_mov_b32_dpp v73, v33 wave_shl:1 row_mask:0xf bank_mask:0xf bound_ctrl:1
	v_mov_b32_dpp v74, v34 wave_shl:1 row_mask:0xf bank_mask:0xf bound_ctrl:1
	v_mov_b32_dpp v46, v12 wave_shr:1 row_mask:0xf bank_mask:0xf bound_ctrl:1
	v_mov_b32_dpp v47, v13 wave_shr:1 row_mask:0xf bank_mask:0xf bound_ctrl:1
	v_mov_b32_dpp v52, v14 wave_shr:1 row_mask:0xf bank_mask:0xf bound_ctrl:1
	v_mov_b32_dpp v53, v15 wave_shr:1 row_mask:0xf bank_mask:0xf bound_ctrl:1
	v_mov_b32_dpp v76, v16 wave_shr:1 row_mask:0xf bank_mask:0xf bound_ctrl:1
	v_mov_b32_dpp v78, v12 wave_shl:1 row_mask:0xf bank_mask:0xf bound_ctrl:1
	v_mov_b32_dpp v79, v13 wave_shl:1 row_mask:0xf bank_mask:0xf bound_ctrl:1
	v_mov_b32_dpp v112, v14 wave_shl:1 row_mask:0xf bank_mask:0xf bound_ctrl:1
	v_mov_b32_dpp v113, v15 wave_shl:1 row_mask:0xf bank_mask:0xf bound_ctrl:1
	v_mov_b32_dpp v114, v16 wave_shl:1 row_mask:0xf bank_mask:0xf bound_ctrl:1
	v_pk_mul_f32 v[116:117], v[12:13], v[32:33] op_sel_hi:[1,0]
	v_pk_mul_f32 v[118:119], v[14:15], v[32:33] op_sel_hi:[1,0]
	v_mul_f32_e64 v120, v16, v32
	v_pk_mul_f32 v[122:123], v[12:13], v[32:33] op_sel:[0,1]
	v_pk_mul_f32 v[124:125], v[14:15], v[32:33] op_sel:[0,1]
	v_mul_f32_e64 v126, v16, v33
	v_pk_mul_f32 v[128:129], v[12:13], v[34:35] op_sel_hi:[1,0]
	v_pk_mul_f32 v[130:131], v[14:15], v[34:35] op_sel_hi:[1,0]
	v_mul_f32_e64 v132, v16, v34
	v_pk_add_f32 v[134:135], v[12:13], v[46:47]
	v_pk_add_f32 v[136:137], v[14:15], v[52:53]
	v_add_f32_e64 v142, v16, v76
	v_pk_fma_f32 v[116:117], v[46:47], v[56:57], v[116:117] op_sel_hi:[1,0,1]
	v_pk_fma_f32 v[118:119], v[52:53], v[56:57], v[118:119] op_sel_hi:[1,0,1]
	v_fma_f32 v120, v76, v56, v120
	v_pk_fma_f32 v[122:123], v[46:47], v[56:57], v[122:123] op_sel:[0,1,0]
	v_pk_fma_f32 v[124:125], v[52:53], v[56:57], v[124:125] op_sel:[0,1,0]
	v_fma_f32 v126, v76, v57, v126
	v_pk_fma_f32 v[128:129], v[46:47], v[58:59], v[128:129] op_sel_hi:[1,0,1]
	v_pk_fma_f32 v[130:131], v[52:53], v[58:59], v[130:131] op_sel_hi:[1,0,1]
	v_fma_f32 v132, v76, v58, v132
	v_pk_add_f32 v[134:135], v[134:135], v[78:79]
	v_pk_add_f32 v[136:137], v[136:137], v[112:113]
	v_add_f32_e64 v142, v142, v114
	v_pk_fma_f32 v[116:117], v[78:79], v[72:73], v[116:117] op_sel_hi:[1,0,1]
	v_pk_fma_f32 v[118:119], v[112:113], v[72:73], v[118:119] op_sel_hi:[1,0,1]
	v_fma_f32 v120, v114, v72, v120
	v_pk_fma_f32 v[122:123], v[78:79], v[72:73], v[122:123] op_sel:[0,1,0]
	v_pk_fma_f32 v[124:125], v[112:113], v[72:73], v[124:125] op_sel:[0,1,0]
	v_fma_f32 v126, v114, v73, v126
	v_pk_fma_f32 v[128:129], v[78:79], v[74:75], v[128:129] op_sel_hi:[1,0,1]
	v_pk_fma_f32 v[130:131], v[112:113], v[74:75], v[130:131] op_sel_hi:[1,0,1]
	v_fma_f32 v132, v114, v74, v132
	s_barrier
	ds_read_b128 v[76:79], v23 offset:0
	ds_read_b128 v[112:115], v23 offset:1024
	ds_read_b128 v[196:199], v23 offset:2048
	v_pk_add_f32 v[46:47], v[186:187], v[134:135]
	v_pk_add_f32 v[52:53], v[110:111], v[46:47]
	v_pk_add_f32 v[110:111], v[188:189], v[136:137]
	v_pk_add_f32 v[146:147], v[192:193], v[110:111]
	v_add_f32_e64 v150, v190, v142
	v_add_f32_e64 v154, v194, v150
	v_pk_add_f32 v[158:159], v[144:145], v[116:117]
	v_pk_add_f32 v[164:165], v[84:85], v[158:159]
	v_pk_add_f32 v[84:85], v[148:149], v[118:119]
	v_pk_add_f32 v[144:145], v[86:87], v[84:85]
	v_add_f32_e64 v86, v152, v120
	v_add_f32_e64 v148, v88, v86
	v_pk_add_f32 v[88:89], v[156:157], v[122:123]
	v_pk_add_f32 v[152:153], v[90:91], v[88:89]
	v_pk_add_f32 v[90:91], v[162:163], v[124:125]
	v_pk_add_f32 v[156:157], v[100:101], v[90:91]
	v_add_f32_e64 v100, v170, v126
	v_add_f32_e64 v162, v102, v100
	v_pk_add_f32 v[102:103], v[174:175], v[128:129]
	v_pk_add_f32 v[168:169], v[104:105], v[102:103]
	v_pk_add_f32 v[104:105], v[178:179], v[130:131]
	v_pk_add_f32 v[170:171], v[106:107], v[104:105]
	v_add_f32_e64 v106, v182, v132
	v_add_f32_e64 v172, v108, v106
	s_waitcnt lgkmcnt(2)
	v_pk_fma_f32 v[164:165], v[76:77], v[52:53], v[164:165] op_sel_hi:[0,1,1] neg_lo:[1,0,0] neg_hi:[1,0,0]
	v_pk_fma_f32 v[144:145], v[76:77], v[146:147], v[144:145] op_sel_hi:[0,1,1] neg_lo:[1,0,0] neg_hi:[1,0,0]
	v_fma_f32 v148, -v76, v154, v148
	v_pk_fma_f32 v[152:153], v[76:77], v[52:53], v[152:153] op_sel:[1,0,0] neg_lo:[1,0,0] neg_hi:[1,0,0]
	v_pk_fma_f32 v[156:157], v[76:77], v[146:147], v[156:157] op_sel:[1,0,0] neg_lo:[1,0,0] neg_hi:[1,0,0]
	v_fma_f32 v162, -v77, v154, v162
	v_pk_fma_f32 v[168:169], v[78:79], v[52:53], v[168:169] op_sel_hi:[0,1,1] neg_lo:[1,0,0] neg_hi:[1,0,0]
	v_pk_fma_f32 v[170:171], v[78:79], v[146:147], v[170:171] op_sel_hi:[0,1,1] neg_lo:[1,0,0] neg_hi:[1,0,0]
	v_fma_f32 v172, -v78, v154, v172
	v_pk_mul_f32 v[108:109], v[78:79], v[164:165] op_sel:[1,0]
	v_pk_mul_f32 v[178:179], v[78:79], v[144:145] op_sel:[1,0]
	v_mul_f32_e64 v184, v79, v148
	s_waitcnt lgkmcnt(1)
	v_pk_mul_f32 v[174:175], v[112:113], v[164:165] op_sel_hi:[0,1]
	v_pk_mul_f32 v[180:181], v[112:113], v[144:145] op_sel_hi:[0,1]
	v_mul_f32_e64 v186, v112, v148
	v_pk_mul_f32 v[176:177], v[112:113], v[164:165] op_sel:[1,0]
	v_pk_mul_f32 v[182:183], v[112:113], v[144:145] op_sel:[1,0]
	v_mul_f32_e64 v188, v113, v148
	v_pk_fma_f32 v[108:109], v[112:113], v[152:153], v[108:109] op_sel_hi:[0,1,1]
	v_pk_fma_f32 v[178:179], v[112:113], v[156:157], v[178:179] op_sel_hi:[0,1,1]
	v_fma_f32 v184, v112, v162, v184
	v_pk_fma_f32 v[174:175], v[114:115], v[152:153], v[174:175] op_sel_hi:[0,1,1]
	v_pk_fma_f32 v[180:181], v[114:115], v[156:157], v[180:181] op_sel_hi:[0,1,1]
	v_fma_f32 v186, v114, v162, v186
	v_pk_fma_f32 v[176:177], v[114:115], v[152:153], v[176:177] op_sel:[1,0,0]
	v_pk_fma_f32 v[182:183], v[114:115], v[156:157], v[182:183] op_sel:[1,0,0]
	v_fma_f32 v188, v115, v162, v188
	v_pk_fma_f32 v[108:109], v[112:113], v[168:169], v[108:109] op_sel:[1,0,0]
	v_pk_fma_f32 v[178:179], v[112:113], v[170:171], v[178:179] op_sel:[1,0,0]
	v_fma_f32 v184, v113, v172, v184
	v_pk_fma_f32 v[174:175], v[114:115], v[168:169], v[174:175] op_sel:[1,0,0]
	v_pk_fma_f32 v[180:181], v[114:115], v[170:171], v[180:181] op_sel:[1,0,0]
	v_fma_f32 v186, v115, v172, v186
	s_waitcnt lgkmcnt(0)
	v_pk_fma_f32 v[176:177], v[196:197], v[168:169], v[176:177] op_sel_hi:[0,1,1]
	v_pk_fma_f32 v[182:183], v[196:197], v[170:171], v[182:183] op_sel_hi:[0,1,1]
	v_fma_f32 v188, v196, v172, v188
	v_pk_mul_f32 v[190:191], v[76:77], v[108:109] op_sel_hi:[0,1]
	v_pk_mul_f32 v[192:193], v[76:77], v[178:179] op_sel_hi:[0,1]
	v_mul_f32_e64 v194, v76, v184
	v_pk_fma_f32 v[190:191], v[76:77], v[174:175], v[190:191] op_sel:[1,0,0]
	v_pk_fma_f32 v[192:193], v[76:77], v[180:181], v[192:193] op_sel:[1,0,0]
	v_fma_f32 v194, v77, v186, v194
	v_pk_fma_f32 v[190:191], v[78:79], v[176:177], v[190:191] op_sel_hi:[0,1,1]
	v_pk_fma_f32 v[192:193], v[78:79], v[182:183], v[192:193] op_sel_hi:[0,1,1]
	v_fma_f32 v194, v78, v188, v194
	v_pk_fma_f32 v[190:191], v[196:197], v[52:53], v[190:191] op_sel:[1,0,0] neg_lo:[0,0,1] neg_hi:[0,0,1]
	v_pk_fma_f32 v[192:193], v[196:197], v[146:147], v[192:193] op_sel:[1,0,0] neg_lo:[0,0,1] neg_hi:[0,0,1]
	v_fma_f32 v194, v197, v154, -v194
	v_cmp_eq_u32_e64 s[10:11], 1, v199
	v_cmp_eq_u32_e64 s[14:15], 2, v199
	v_cmp_eq_u32_e64 s[20:21], 3, v199
	v_cmp_eq_u32_e64 s[22:23], 4, v199
	v_cmp_eq_u32_e64 s[30:31], 5, v199
	v_pk_add_f32 v[52:53], v[138:139], v[108:109]
	v_pk_add_f32 v[144:145], v[140:141], v[52:53]
	v_pk_add_f32 v[138:139], v[202:203], v[178:179]
	v_pk_add_f32 v[140:141], v[222:223], v[138:139]
	v_add_f32_e64 v146, v208, v184
	v_add_f32_e64 v148, v228, v146
	v_pk_add_f32 v[152:153], v[166:167], v[174:175]
	v_pk_add_f32 v[154:155], v[160:161], v[152:153]
	v_pk_add_f32 v[156:157], v[204:205], v[180:181]
	v_pk_add_f32 v[160:161], v[224:225], v[156:157]
	v_add_f32_e64 v162, v210, v186
	v_add_f32_e64 v164, v230, v162
	v_pk_add_f32 v[166:167], v[200:201], v[176:177]
	v_pk_add_f32 v[168:169], v[220:221], v[166:167]
	v_pk_add_f32 v[170:171], v[206:207], v[182:183]
	v_pk_add_f32 v[172:173], v[226:227], v[170:171]
	v_add_f32_e64 v200, v212, v188
	v_add_f32_e64 v202, v232, v200
	v_pk_add_f32 v[204:205], v[214:215], v[190:191]
	v_pk_add_f32 v[206:207], v[234:235], v[204:205]
	v_pk_add_f32 v[208:209], v[216:217], v[192:193]
	v_pk_add_f32 v[210:211], v[236:237], v[208:209]
	v_add_f32_e64 v212, v218, v194
	v_add_f32_e64 v214, v238, v212
	v_pk_fma_f32 v[216:217], v[60:61], v[144:145], v[206:207] op_sel_hi:[0,1,1]
	v_pk_fma_f32 v[218:219], v[60:61], v[140:141], v[210:211] op_sel_hi:[0,1,1]
	v_fma_f32 v220, v60, v148, v214
	v_pk_fma_f32 v[222:223], v[64:65], v[144:145], v[206:207] op_sel_hi:[0,1,1]
	v_pk_fma_f32 v[224:225], v[64:65], v[140:141], v[210:211] op_sel_hi:[0,1,1]
	v_fma_f32 v226, v64, v148, v214
	v_pk_fma_f32 v[216:217], v[60:61], v[154:155], v[216:217] op_sel:[1,0,0]
	v_pk_fma_f32 v[218:219], v[60:61], v[160:161], v[218:219] op_sel:[1,0,0]
	v_fma_f32 v220, v61, v164, v220
	v_pk_fma_f32 v[222:223], v[64:65], v[154:155], v[222:223] op_sel:[1,0,0]
	v_pk_fma_f32 v[224:225], v[64:65], v[160:161], v[224:225] op_sel:[1,0,0]
	v_fma_f32 v226, v65, v164, v226
	v_pk_fma_f32 v[216:217], v[62:63], v[168:169], v[216:217] op_sel_hi:[0,1,1]
	v_pk_fma_f32 v[218:219], v[62:63], v[172:173], v[218:219] op_sel_hi:[0,1,1]
	v_fma_f32 v220, v62, v202, v220
	v_pk_fma_f32 v[222:223], v[66:67], v[168:169], v[222:223] op_sel_hi:[0,1,1]
	v_pk_fma_f32 v[224:225], v[66:67], v[172:173], v[224:225] op_sel_hi:[0,1,1]
	v_fma_f32 v226, v66, v202, v226
	v_pk_fma_f32 v[206:207], v[96:97], v[144:145], v[206:207] op_sel_hi:[0,1,1]
	v_pk_fma_f32 v[210:211], v[96:97], v[140:141], v[210:211] op_sel_hi:[0,1,1]
	v_fma_f32 v214, v96, v148, v214
	v_pk_fma_f32 v[206:207], v[96:97], v[154:155], v[206:207] op_sel:[1,0,0]
	v_pk_fma_f32 v[210:211], v[96:97], v[160:161], v[210:211] op_sel:[1,0,0]
	v_fma_f32 v214, v97, v164, v214
	v_pk_fma_f32 v[206:207], v[98:99], v[168:169], v[206:207] op_sel_hi:[0,1,1]
	v_pk_fma_f32 v[210:211], v[98:99], v[172:173], v[210:211] op_sel_hi:[0,1,1]
	v_fma_f32 v214, v98, v202, v214
	v_cndmask_b32_e64 v228, 0, v1, s[10:11]
	v_cndmask_b32_e64 v229, 0, v1, s[14:15]
	v_cndmask_b32_e64 v230, 0, v1, s[20:21]
	v_cndmask_b32_e64 v231, 0, v1, s[22:23]
	v_cndmask_b32_e64 v232, 0, v1, s[30:31]
	v_add_f32_dpp v206, v216, v206 wave_shl:1 row_mask:0xf bank_mask:0xf bound_ctrl:1
	v_add_f32_dpp v207, v217, v207 wave_shl:1 row_mask:0xf bank_mask:0xf bound_ctrl:1
	v_add_f32_dpp v210, v218, v210 wave_shl:1 row_mask:0xf bank_mask:0xf bound_ctrl:1
	v_add_f32_dpp v211, v219, v211 wave_shl:1 row_mask:0xf bank_mask:0xf bound_ctrl:1
	v_add_f32_dpp v214, v220, v214 wave_shl:1 row_mask:0xf bank_mask:0xf bound_ctrl:1
	s_add_i32 s4, s34, 2
	s_cmpk_lt_i32 s4, 0x201
	s_cselect_b64 s[12:13], s[0:1], 0
	v_add_f32_dpp v206, v222, v206 wave_shr:1 row_mask:0xf bank_mask:0xf bound_ctrl:1
	v_add_f32_dpp v207, v223, v207 wave_shr:1 row_mask:0xf bank_mask:0xf bound_ctrl:1
	v_add_f32_dpp v210, v224, v210 wave_shr:1 row_mask:0xf bank_mask:0xf bound_ctrl:1
	v_add_f32_dpp v211, v225, v211 wave_shr:1 row_mask:0xf bank_mask:0xf bound_ctrl:1
	v_add_f32_dpp v214, v226, v214 wave_shr:1 row_mask:0xf bank_mask:0xf bound_ctrl:1
	v_pk_fma_f32 v[206:207], v[54:55], v[198:199], v[206:207] op_sel_hi:[1,0,1] neg_lo:[0,0,1] neg_hi:[0,0,1]
	v_pk_fma_f32 v[210:211], v[92:93], v[198:199], v[210:211] op_sel_hi:[1,0,1] neg_lo:[0,0,1] neg_hi:[0,0,1]
	v_fma_f32 v214, v94, v198, -v214
	v_pk_add_f32 v[206:207], v[206:207], v[228:229] neg_lo:[0,1] neg_hi:[0,1]
	v_pk_add_f32 v[210:211], v[210:211], v[230:231] neg_lo:[0,1] neg_hi:[0,1]
	v_add_f32_e64 v214, v214, -v232
	v_pk_mul_f32 v[234:235], v[206:207], v[206:207]
	v_pk_fma_f32 v[234:235], v[210:211], v[210:211], v[234:235]
	v_add_f32_e32 v234, v234, v235
	v_fma_f32 v234, v214, v214, v234
	v_cndmask_b32_e64 v235, 0, v234, s[12:13]
	v_add_f32_e32 v0, v0, v235
	s_add_i32 s4, s34, 7
	s_min_i32 s4, s4, 0x200
	s_mul_i32 s5, s4, 0x804
	s_add_i32 s5, s5, s35
	s_add_i32 s6, s5, 0x0
	s_add_i32 s7, s5, 0x101004
	s_add_i32 s8, s5, 0x202008
	s_add_i32 s11, s5, 0x30300c
	s_add_i32 s15, s5, 0x404010
	s_mul_i32 s9, s4, 0x180c
	s_add_i32 s9, s9, s33
	buffer_load_dword v54, v28, s[16:19], s6 offen nt
	buffer_load_dword v55, v28, s[16:19], s7 offen nt
	buffer_load_dword v60, v28, s[16:19], s8 offen nt
	buffer_load_dword v61, v28, s[16:19], s11 offen nt
	buffer_load_dword v62, v28, s[16:19], s15 offen nt
	buffer_load_dwordx3 v[64:66], v27, s[24:27], s9 offen nt
	s_waitcnt vmcnt(12)
	v_mov_b32_dpp v76, v36 wave_shr:1 row_mask:0xf bank_mask:0xf bound_ctrl:1
	v_mov_b32_dpp v77, v37 wave_shr:1 row_mask:0xf bank_mask:0xf bound_ctrl:1
	v_mov_b32_dpp v78, v38 wave_shr:1 row_mask:0xf bank_mask:0xf bound_ctrl:1
	v_mov_b32_dpp v92, v36 wave_shl:1 row_mask:0xf bank_mask:0xf bound_ctrl:1
	v_mov_b32_dpp v93, v37 wave_shl:1 row_mask:0xf bank_mask:0xf bound_ctrl:1
	v_mov_b32_dpp v94, v38 wave_shl:1 row_mask:0xf bank_mask:0xf bound_ctrl:1
	v_mov_b32_dpp v96, v20 wave_shr:1 row_mask:0xf bank_mask:0xf bound_ctrl:1
	v_mov_b32_dpp v97, v21 wave_shr:1 row_mask:0xf bank_mask:0xf bound_ctrl:1
	v_mov_b32_dpp v98, v24 wave_shr:1 row_mask:0xf bank_mask:0xf bound_ctrl:1
	v_mov_b32_dpp v99, v25 wave_shr:1 row_mask:0xf bank_mask:0xf bound_ctrl:1
	v_mov_b32_dpp v112, v30 wave_shr:1 row_mask:0xf bank_mask:0xf bound_ctrl:1
	v_mov_b32_dpp v114, v20 wave_shl:1 row_mask:0xf bank_mask:0xf bound_ctrl:1
	v_mov_b32_dpp v115, v21 wave_shl:1 row_mask:0xf bank_mask:0xf bound_ctrl:1
	v_mov_b32_dpp v140, v24 wave_shl:1 row_mask:0xf bank_mask:0xf bound_ctrl:1
	v_mov_b32_dpp v141, v25 wave_shl:1 row_mask:0xf bank_mask:0xf bound_ctrl:1
	v_mov_b32_dpp v144, v30 wave_shl:1 row_mask:0xf bank_mask:0xf bound_ctrl:1
	v_pk_mul_f32 v[148:149], v[20:21], v[36:37] op_sel_hi:[1,0]
	v_pk_mul_f32 v[154:155], v[24:25], v[36:37] op_sel_hi:[1,0]
	v_mul_f32_e64 v160, v30, v36
	v_pk_mul_f32 v[164:165], v[20:21], v[36:37] op_sel:[0,1]
	v_pk_mul_f32 v[168:169], v[24:25], v[36:37] op_sel:[0,1]
	v_mul_f32_e64 v172, v30, v37
	v_pk_mul_f32 v[196:197], v[20:21], v[38:39] op_sel_hi:[1,0]
	v_pk_mul_f32 v[198:199], v[24:25], v[38:39] op_sel_hi:[1,0]
	v_mul_f32_e64 v202, v30, v38
	v_pk_add_f32 v[206:207], v[20:21], v[96:97]
	v_pk_add_f32 v[210:211], v[24:25], v[98:99]
	v_add_f32_e64 v214, v30, v112
	v_pk_fma_f32 v[148:149], v[96:97], v[76:77], v[148:149] op_sel_hi:[1,0,1]
	v_pk_fma_f32 v[154:155], v[98:99], v[76:77], v[154:155] op_sel_hi:[1,0,1]
	v_fma_f32 v160, v112, v76, v160
	v_pk_fma_f32 v[164:165], v[96:97], v[76:77], v[164:165] op_sel:[0,1,0]
	v_pk_fma_f32 v[168:169], v[98:99], v[76:77], v[168:169] op_sel:[0,1,0]
	v_fma_f32 v172, v112, v77, v172
	v_pk_fma_f32 v[196:197], v[96:97], v[78:79], v[196:197] op_sel_hi:[1,0,1]
	v_pk_fma_f32 v[198:199], v[98:99], v[78:79], v[198:199] op_sel_hi:[1,0,1]
	v_fma_f32 v202, v112, v78, v202
	v_pk_add_f32 v[206:207], v[206:207], v[114:115]
	v_pk_add_f32 v[210:211], v[210:211], v[140:141]
	v_add_f32_e64 v214, v214, v144
	v_pk_fma_f32 v[148:149], v[114:115], v[92:93], v[148:149] op_sel_hi:[1,0,1]
	v_pk_fma_f32 v[154:155], v[140:141], v[92:93], v[154:155] op_sel_hi:[1,0,1]
	v_fma_f32 v160, v144, v92, v160
	v_pk_fma_f32 v[164:165], v[114:115], v[92:93], v[164:165] op_sel:[0,1,0]
	v_pk_fma_f32 v[168:169], v[140:141], v[92:93], v[168:169] op_sel:[0,1,0]
	v_fma_f32 v172, v144, v93, v172
	v_pk_fma_f32 v[196:197], v[114:115], v[94:95], v[196:197] op_sel_hi:[1,0,1]
	v_pk_fma_f32 v[198:199], v[140:141], v[94:95], v[198:199] op_sel_hi:[1,0,1]
	v_fma_f32 v202, v144, v94, v202
	s_barrier
	ds_read_b128 v[96:99], v23 offset:3072
	ds_read_b128 v[112:115], v23 offset:4096
	ds_read_b128 v[216:219], v23 offset:5120
	v_pk_add_f32 v[140:141], v[46:47], v[206:207]
	v_pk_add_f32 v[46:47], v[110:111], v[210:211]
	v_add_f32_e64 v110, v150, v214
	v_pk_add_f32 v[144:145], v[158:159], v[148:149]
	v_pk_add_f32 v[150:151], v[84:85], v[154:155]
	v_add_f32_e64 v84, v86, v160
	v_pk_add_f32 v[86:87], v[88:89], v[164:165]
	v_pk_add_f32 v[88:89], v[90:91], v[168:169]
	v_add_f32_e64 v90, v100, v172
	v_pk_add_f32 v[100:101], v[102:103], v[196:197]
	v_pk_add_f32 v[102:103], v[104:105], v[198:199]
	v_add_f32_e64 v104, v106, v202
	s_waitcnt lgkmcnt(2)
	v_pk_fma_f32 v[144:145], v[96:97], v[140:141], v[144:145] op_sel_hi:[0,1,1] neg_lo:[1,0,0] neg_hi:[1,0,0]
	v_pk_fma_f32 v[150:151], v[96:97], v[46:47], v[150:151] op_sel_hi:[0,1,1] neg_lo:[1,0,0] neg_hi:[1,0,0]
	v_fma_f32 v84, -v96, v110, v84
	v_pk_fma_f32 v[86:87], v[96:97], v[140:141], v[86:87] op_sel:[1,0,0] neg_lo:[1,0,0] neg_hi:[1,0,0]
	v_pk_fma_f32 v[88:89], v[96:97], v[46:47], v[88:89] op_sel:[1,0,0] neg_lo:[1,0,0] neg_hi:[1,0,0]
	v_fma_f32 v90, -v97, v110, v90
	v_pk_fma_f32 v[100:101], v[98:99], v[140:141], v[100:101] op_sel_hi:[0,1,1] neg_lo:[1,0,0] neg_hi:[1,0,0]
	v_pk_fma_f32 v[102:103], v[98:99], v[46:47], v[102:103] op_sel_hi:[0,1,1] neg_lo:[1,0,0] neg_hi:[1,0,0]
	v_fma_f32 v104, -v98, v110, v104
	v_pk_mul_f32 v[106:107], v[98:99], v[144:145] op_sel:[1,0]
	v_pk_mul_f32 v[222:223], v[98:99], v[150:151] op_sel:[1,0]
	v_mul_f32_e64 v228, v99, v84
	s_waitcnt lgkmcnt(1)
	v_pk_mul_f32 v[158:159], v[112:113], v[144:145] op_sel_hi:[0,1]
	v_pk_mul_f32 v[224:225], v[112:113], v[150:151] op_sel_hi:[0,1]
	v_mul_f32_e64 v230, v112, v84
	v_pk_mul_f32 v[220:221], v[112:113], v[144:145] op_sel:[1,0]
	v_pk_mul_f32 v[226:227], v[112:113], v[150:151] op_sel:[1,0]
	v_mul_f32_e64 v232, v113, v84
	v_pk_fma_f32 v[106:107], v[112:113], v[86:87], v[106:107] op_sel_hi:[0,1,1]
	v_pk_fma_f32 v[222:223], v[112:113], v[88:89], v[222:223] op_sel_hi:[0,1,1]
	v_fma_f32 v228, v112, v90, v228
	v_pk_fma_f32 v[158:159], v[114:115], v[86:87], v[158:159] op_sel_hi:[0,1,1]
	v_pk_fma_f32 v[224:225], v[114:115], v[88:89], v[224:225] op_sel_hi:[0,1,1]
	v_fma_f32 v230, v114, v90, v230
	v_pk_fma_f32 v[220:221], v[114:115], v[86:87], v[220:221] op_sel:[1,0,0]
	v_pk_fma_f32 v[226:227], v[114:115], v[88:89], v[226:227] op_sel:[1,0,0]
	v_fma_f32 v232, v115, v90, v232
	v_pk_fma_f32 v[106:107], v[112:113], v[100:101], v[106:107] op_sel:[1,0,0]
	v_pk_fma_f32 v[222:223], v[112:113], v[102:103], v[222:223] op_sel:[1,0,0]
	v_fma_f32 v228, v113, v104, v228
	v_pk_fma_f32 v[158:159], v[114:115], v[100:101], v[158:159] op_sel:[1,0,0]
	v_pk_fma_f32 v[224:225], v[114:115], v[102:103], v[224:225] op_sel:[1,0,0]
	v_fma_f32 v230, v115, v104, v230
	s_waitcnt lgkmcnt(0)
	v_pk_fma_f32 v[220:221], v[216:217], v[100:101], v[220:221] op_sel_hi:[0,1,1]
	v_pk_fma_f32 v[226:227], v[216:217], v[102:103], v[226:227] op_sel_hi:[0,1,1]
	v_fma_f32 v232, v216, v104, v232
	v_pk_mul_f32 v[234:235], v[96:97], v[106:107] op_sel_hi:[0,1]
	v_pk_mul_f32 v[236:237], v[96:97], v[222:223] op_sel_hi:[0,1]
	v_mul_f32_e64 v238, v96, v228
	v_pk_fma_f32 v[234:235], v[96:97], v[158:159], v[234:235] op_sel:[1,0,0]
	v_pk_fma_f32 v[236:237], v[96:97], v[224:225], v[236:237] op_sel:[1,0,0]
	v_fma_f32 v238, v97, v230, v238
	v_pk_fma_f32 v[234:235], v[98:99], v[220:221], v[234:235] op_sel_hi:[0,1,1]
	v_pk_fma_f32 v[236:237], v[98:99], v[226:227], v[236:237] op_sel_hi:[0,1,1]
	v_fma_f32 v238, v98, v232, v238
	v_pk_fma_f32 v[234:235], v[216:217], v[140:141], v[234:235] op_sel:[1,0,0] neg_lo:[0,0,1] neg_hi:[0,0,1]
	v_pk_fma_f32 v[236:237], v[216:217], v[46:47], v[236:237] op_sel:[1,0,0] neg_lo:[0,0,1] neg_hi:[0,0,1]
	v_fma_f32 v238, v217, v110, -v238
	v_cmp_eq_u32_e64 s[10:11], 1, v219
	v_cmp_eq_u32_e64 s[14:15], 2, v219
	v_cmp_eq_u32_e64 s[20:21], 3, v219
	v_cmp_eq_u32_e64 s[22:23], 4, v219
	v_cmp_eq_u32_e64 s[30:31], 5, v219
	v_pk_add_f32 v[46:47], v[52:53], v[106:107]
	v_pk_add_f32 v[52:53], v[138:139], v[222:223]
	v_add_f32_e64 v84, v146, v228
	v_pk_add_f32 v[86:87], v[152:153], v[158:159]
	v_pk_add_f32 v[88:89], v[156:157], v[224:225]
	v_add_f32_e64 v90, v162, v230
	v_pk_add_f32 v[100:101], v[166:167], v[220:221]
	v_pk_add_f32 v[102:103], v[170:171], v[226:227]
	v_add_f32_e64 v104, v200, v232
	v_pk_add_f32 v[110:111], v[204:205], v[234:235]
	v_pk_add_f32 v[138:139], v[208:209], v[236:237]
	v_add_f32_e64 v140, v212, v238
	v_pk_fma_f32 v[144:145], v[68:69], v[46:47], v[110:111] op_sel_hi:[0,1,1]
	v_pk_fma_f32 v[146:147], v[68:69], v[52:53], v[138:139] op_sel_hi:[0,1,1]
	v_fma_f32 v150, v68, v84, v140
	v_pk_fma_f32 v[152:153], v[80:81], v[46:47], v[110:111] op_sel_hi:[0,1,1]
	v_pk_fma_f32 v[156:157], v[80:81], v[52:53], v[138:139] op_sel_hi:[0,1,1]
	v_fma_f32 v162, v80, v84, v140
	v_pk_fma_f32 v[144:145], v[68:69], v[86:87], v[144:145] op_sel:[1,0,0]
	v_pk_fma_f32 v[146:147], v[68:69], v[88:89], v[146:147] op_sel:[1,0,0]
	v_fma_f32 v150, v69, v90, v150
	v_pk_fma_f32 v[152:153], v[80:81], v[86:87], v[152:153] op_sel:[1,0,0]
	v_pk_fma_f32 v[156:157], v[80:81], v[88:89], v[156:157] op_sel:[1,0,0]
	v_fma_f32 v162, v81, v90, v162
	v_pk_fma_f32 v[144:145], v[70:71], v[100:101], v[144:145] op_sel_hi:[0,1,1]
	v_pk_fma_f32 v[146:147], v[70:71], v[102:103], v[146:147] op_sel_hi:[0,1,1]
	v_fma_f32 v150, v70, v104, v150
	v_pk_fma_f32 v[152:153], v[82:83], v[100:101], v[152:153] op_sel_hi:[0,1,1]
	v_pk_fma_f32 v[156:157], v[82:83], v[102:103], v[156:157] op_sel_hi:[0,1,1]
	v_fma_f32 v162, v82, v104, v162
	v_pk_fma_f32 v[110:111], v[8:9], v[46:47], v[110:111] op_sel_hi:[0,1,1]
	v_pk_fma_f32 v[138:139], v[8:9], v[52:53], v[138:139] op_sel_hi:[0,1,1]
	v_fma_f32 v140, v8, v84, v140
	v_pk_fma_f32 v[110:111], v[8:9], v[86:87], v[110:111] op_sel:[1,0,0]
	v_pk_fma_f32 v[138:139], v[8:9], v[88:89], v[138:139] op_sel:[1,0,0]
	v_fma_f32 v140, v9, v90, v140
	v_pk_fma_f32 v[110:111], v[10:11], v[100:101], v[110:111] op_sel_hi:[0,1,1]
	v_pk_fma_f32 v[138:139], v[10:11], v[102:103], v[138:139] op_sel_hi:[0,1,1]
	v_fma_f32 v140, v10, v104, v140
	v_cndmask_b32_e64 v166, 0, v1, s[10:11]
	v_cndmask_b32_e64 v167, 0, v1, s[14:15]
	v_cndmask_b32_e64 v170, 0, v1, s[20:21]
	v_cndmask_b32_e64 v171, 0, v1, s[22:23]
	v_cndmask_b32_e64 v200, 0, v1, s[30:31]
	v_add_f32_dpp v110, v144, v110 wave_shl:1 row_mask:0xf bank_mask:0xf bound_ctrl:1
	v_add_f32_dpp v111, v145, v111 wave_shl:1 row_mask:0xf bank_mask:0xf bound_ctrl:1
	v_add_f32_dpp v138, v146, v138 wave_shl:1 row_mask:0xf bank_mask:0xf bound_ctrl:1
	v_add_f32_dpp v139, v147, v139 wave_shl:1 row_mask:0xf bank_mask:0xf bound_ctrl:1
	v_add_f32_dpp v140, v150, v140 wave_shl:1 row_mask:0xf bank_mask:0xf bound_ctrl:1
	s_add_i32 s4, s34, 3
	s_cmpk_lt_i32 s4, 0x201
	s_cselect_b64 s[12:13], s[0:1], 0
	v_add_f32_dpp v110, v152, v110 wave_shr:1 row_mask:0xf bank_mask:0xf bound_ctrl:1
	v_add_f32_dpp v111, v153, v111 wave_shr:1 row_mask:0xf bank_mask:0xf bound_ctrl:1
	v_add_f32_dpp v138, v156, v138 wave_shr:1 row_mask:0xf bank_mask:0xf bound_ctrl:1
	v_add_f32_dpp v139, v157, v139 wave_shr:1 row_mask:0xf bank_mask:0xf bound_ctrl:1
	v_add_f32_dpp v140, v162, v140 wave_shr:1 row_mask:0xf bank_mask:0xf bound_ctrl:1
	v_pk_fma_f32 v[110:111], v[2:3], v[218:219], v[110:111] op_sel_hi:[1,0,1] neg_lo:[0,0,1] neg_hi:[0,0,1]
	v_pk_fma_f32 v[138:139], v[4:5], v[218:219], v[138:139] op_sel_hi:[1,0,1] neg_lo:[0,0,1] neg_hi:[0,0,1]
	v_fma_f32 v140, v6, v218, -v140
	v_pk_add_f32 v[110:111], v[110:111], v[166:167] neg_lo:[0,1] neg_hi:[0,1]
	v_pk_add_f32 v[138:139], v[138:139], v[170:171] neg_lo:[0,1] neg_hi:[0,1]
	v_add_f32_e64 v140, v140, -v200
	v_pk_mul_f32 v[204:205], v[110:111], v[110:111]
	v_pk_fma_f32 v[204:205], v[138:139], v[138:139], v[204:205]
	v_add_f32_e32 v204, v204, v205
	v_fma_f32 v204, v140, v140, v204
	v_cndmask_b32_e64 v205, 0, v204, s[12:13]
	v_add_f32_e32 v0, v0, v205
	s_add_i32 s4, s34, 8
	s_min_i32 s4, s4, 0x200
	s_mul_i32 s5, s4, 0x804
	s_add_i32 s5, s5, s35
	s_add_i32 s6, s5, 0x0
	s_add_i32 s7, s5, 0x101004
	s_add_i32 s8, s5, 0x202008
	s_add_i32 s11, s5, 0x30300c
	s_add_i32 s15, s5, 0x404010
	s_mul_i32 s9, s4, 0x180c
	s_add_i32 s9, s9, s33
	buffer_load_dword v2, v28, s[16:19], s6 offen nt
	buffer_load_dword v3, v28, s[16:19], s7 offen nt
	buffer_load_dword v4, v28, s[16:19], s8 offen nt
	buffer_load_dword v5, v28, s[16:19], s11 offen nt
	buffer_load_dword v6, v28, s[16:19], s15 offen nt
	buffer_load_dwordx3 v[8:10], v27, s[24:27], s9 offen nt
	s_waitcnt vmcnt(12)
	v_mov_b32_dpp v68, v48 wave_shr:1 row_mask:0xf bank_mask:0xf bound_ctrl:1
	v_mov_b32_dpp v69, v49 wave_shr:1 row_mask:0xf bank_mask:0xf bound_ctrl:1
	v_mov_b32_dpp v70, v50 wave_shr:1 row_mask:0xf bank_mask:0xf bound_ctrl:1
	v_mov_b32_dpp v80, v48 wave_shl:1 row_mask:0xf bank_mask:0xf bound_ctrl:1
	v_mov_b32_dpp v81, v49 wave_shl:1 row_mask:0xf bank_mask:0xf bound_ctrl:1
	v_mov_b32_dpp v82, v50 wave_shl:1 row_mask:0xf bank_mask:0xf bound_ctrl:1
	v_mov_b32_dpp v46, v40 wave_shr:1 row_mask:0xf bank_mask:0xf bound_ctrl:1
	v_mov_b32_dpp v47, v41 wave_shr:1 row_mask:0xf bank_mask:0xf bound_ctrl:1
	v_mov_b32_dpp v52, v42 wave_shr:1 row_mask:0xf bank_mask:0xf bound_ctrl:1
	v_mov_b32_dpp v53, v43 wave_shr:1 row_mask:0xf bank_mask:0xf bound_ctrl:1
	v_mov_b32_dpp v84, v44 wave_shr:1 row_mask:0xf bank_mask:0xf bound_ctrl:1
	v_mov_b32_dpp v86, v40 wave_shl:1 row_mask:0xf bank_mask:0xf bound_ctrl:1
	v_mov_b32_dpp v87, v41 wave_shl:1 row_mask:0xf bank_mask:0xf bound_ctrl:1
	v_mov_b32_dpp v88, v42 wave_shl:1 row_mask:0xf bank_mask:0xf bound_ctrl:1
	v_mov_b32_dpp v89, v43 wave_shl:1 row_mask:0xf bank_mask:0xf bound_ctrl:1
	v_mov_b32_dpp v90, v44 wave_shl:1 row_mask:0xf bank_mask:0xf bound_ctrl:1
	v_pk_mul_f32 v[96:97], v[40:41], v[48:49] op_sel_hi:[1,0]
	v_pk_mul_f32 v[98:99], v[42:43], v[48:49] op_sel_hi:[1,0]
	v_mul_f32_e64 v100, v44, v48
	v_pk_mul_f32 v[102:103], v[40:41], v[48:49] op_sel:[0,1]
	v_pk_mul_f32 v[104:105], v[42:43], v[48:49] op_sel:[0,1]
	v_mul_f32_e64 v110, v44, v49
	v_pk_mul_f32 v[112:113], v[40:41], v[50:51] op_sel_hi:[1,0]
	v_pk_mul_f32 v[114:115], v[42:43], v[50:51] op_sel_hi:[1,0]
	v_mul_f32_e64 v138, v44, v50
	v_pk_add_f32 v[140:141], v[40:41], v[46:47]
	v_pk_add_f32 v[144:145], v[42:43], v[52:53]
	v_add_f32_e64 v146, v44, v84
	v_pk_fma_f32 v[96:97], v[46:47], v[68:69], v[96:97] op_sel_hi:[1,0,1]
	v_pk_fma_f32 v[98:99], v[52:53], v[68:69], v[98:99] op_sel_hi:[1,0,1]
	v_fma_f32 v100, v84, v68, v100
	v_pk_fma_f32 v[102:103], v[46:47], v[68:69], v[102:103] op_sel:[0,1,0]
	v_pk_fma_f32 v[104:105], v[52:53], v[68:69], v[104:105] op_sel:[0,1,0]
	v_fma_f32 v110, v84, v69, v110
	v_pk_fma_f32 v[112:113], v[46:47], v[70:71], v[112:113] op_sel_hi:[1,0,1]
	v_pk_fma_f32 v[114:115], v[52:53], v[70:71], v[114:115] op_sel_hi:[1,0,1]
	v_fma_f32 v138, v84, v70, v138
	v_pk_add_f32 v[140:141], v[140:141], v[86:87]
	v_pk_add_f32 v[144:145], v[144:145], v[88:89]
	v_add_f32_e64 v146, v146, v90
	v_pk_fma_f32 v[96:97], v[86:87], v[80:81], v[96:97] op_sel_hi:[1,0,1]
	v_pk_fma_f32 v[98:99], v[88:89], v[80:81], v[98:99] op_sel_hi:[1,0,1]
	v_fma_f32 v100, v90, v80, v100
	v_pk_fma_f32 v[102:103], v[86:87], v[80:81], v[102:103] op_sel:[0,1,0]
	v_pk_fma_f32 v[104:105], v[88:89], v[80:81], v[104:105] op_sel:[0,1,0]
	v_fma_f32 v110, v90, v81, v110
	v_pk_fma_f32 v[112:113], v[86:87], v[82:83], v[112:113] op_sel_hi:[1,0,1]
	v_pk_fma_f32 v[114:115], v[88:89], v[82:83], v[114:115] op_sel_hi:[1,0,1]
	v_fma_f32 v138, v90, v82, v138
	s_barrier
	ds_read_b128 v[84:87], v23 offset:0
	ds_read_b128 v[88:91], v23 offset:1024
	ds_read_b128 v[216:219], v23 offset:2048
	v_pk_add_f32 v[46:47], v[206:207], v[140:141]
	v_pk_add_f32 v[52:53], v[134:135], v[46:47]
	v_pk_add_f32 v[134:135], v[210:211], v[144:145]
	v_pk_add_f32 v[150:151], v[136:137], v[134:135]
	v_add_f32_e64 v136, v214, v146
	v_add_f32_e64 v152, v142, v136
	v_pk_add_f32 v[142:143], v[148:149], v[96:97]
	v_pk_add_f32 v[156:157], v[116:117], v[142:143]
	v_pk_add_f32 v[116:117], v[154:155], v[98:99]
	v_pk_add_f32 v[148:149], v[118:119], v[116:117]
	v_add_f32_e64 v118, v160, v100
	v_add_f32_e64 v154, v120, v118
	v_pk_add_f32 v[120:121], v[164:165], v[102:103]
	v_pk_add_f32 v[160:161], v[122:123], v[120:121]
	v_pk_add_f32 v[122:123], v[168:169], v[104:105]
	v_pk_add_f32 v[162:163], v[124:125], v[122:123]
	v_add_f32_e64 v124, v172, v110
	v_add_f32_e64 v164, v126, v124
	v_pk_add_f32 v[126:127], v[196:197], v[112:113]
	v_pk_add_f32 v[166:167], v[128:129], v[126:127]
	v_pk_add_f32 v[128:129], v[198:199], v[114:115]
	v_pk_add_f32 v[168:169], v[130:131], v[128:129]
	v_add_f32_e64 v130, v202, v138
	v_add_f32_e64 v170, v132, v130
	s_waitcnt lgkmcnt(2)
	v_pk_fma_f32 v[156:157], v[84:85], v[52:53], v[156:157] op_sel_hi:[0,1,1] neg_lo:[1,0,0] neg_hi:[1,0,0]
	v_pk_fma_f32 v[148:149], v[84:85], v[150:151], v[148:149] op_sel_hi:[0,1,1] neg_lo:[1,0,0] neg_hi:[1,0,0]
	v_fma_f32 v154, -v84, v152, v154
	v_pk_fma_f32 v[160:161], v[84:85], v[52:53], v[160:161] op_sel:[1,0,0] neg_lo:[1,0,0] neg_hi:[1,0,0]
	v_pk_fma_f32 v[162:163], v[84:85], v[150:151], v[162:163] op_sel:[1,0,0] neg_lo:[1,0,0] neg_hi:[1,0,0]
	v_fma_f32 v164, -v85, v152, v164
	v_pk_fma_f32 v[166:167], v[86:87], v[52:53], v[166:167] op_sel_hi:[0,1,1] neg_lo:[1,0,0] neg_hi:[1,0,0]
	v_pk_fma_f32 v[168:169], v[86:87], v[150:151], v[168:169] op_sel_hi:[0,1,1] neg_lo:[1,0,0] neg_hi:[1,0,0]
	v_fma_f32 v170, -v86, v152, v170
	v_pk_mul_f32 v[132:133], v[86:87], v[156:157] op_sel:[1,0]
	v_pk_mul_f32 v[198:199], v[86:87], v[148:149] op_sel:[1,0]
	v_mul_f32_e64 v204, v87, v154
	s_waitcnt lgkmcnt(1)
	v_pk_mul_f32 v[172:173], v[88:89], v[156:157] op_sel_hi:[0,1]
	v_pk_mul_f32 v[200:201], v[88:89], v[148:149] op_sel_hi:[0,1]
	v_mul_f32_e64 v206, v88, v154
	v_pk_mul_f32 v[196:197], v[88:89], v[156:157] op_sel:[1,0]
	v_pk_mul_f32 v[202:203], v[88:89], v[148:149] op_sel:[1,0]
	v_mul_f32_e64 v208, v89, v154
	v_pk_fma_f32 v[132:133], v[88:89], v[160:161], v[132:133] op_sel_hi:[0,1,1]
	v_pk_fma_f32 v[198:199], v[88:89], v[162:163], v[198:199] op_sel_hi:[0,1,1]
	v_fma_f32 v204, v88, v164, v204
	v_pk_fma_f32 v[172:173], v[90:91], v[160:161], v[172:173] op_sel_hi:[0,1,1]
	v_pk_fma_f32 v[200:201], v[90:91], v[162:163], v[200:201] op_sel_hi:[0,1,1]
	v_fma_f32 v206, v90, v164, v206
	v_pk_fma_f32 v[196:197], v[90:91], v[160:161], v[196:197] op_sel:[1,0,0]
	v_pk_fma_f32 v[202:203], v[90:91], v[162:163], v[202:203] op_sel:[1,0,0]
	v_fma_f32 v208, v91, v164, v208
	v_pk_fma_f32 v[132:133], v[88:89], v[166:167], v[132:133] op_sel:[1,0,0]
	v_pk_fma_f32 v[198:199], v[88:89], v[168:169], v[198:199] op_sel:[1,0,0]
	v_fma_f32 v204, v89, v170, v204
	v_pk_fma_f32 v[172:173], v[90:91], v[166:167], v[172:173] op_sel:[1,0,0]
	v_pk_fma_f32 v[200:201], v[90:91], v[168:169], v[200:201] op_sel:[1,0,0]
	v_fma_f32 v206, v91, v170, v206
	s_waitcnt lgkmcnt(0)
	v_pk_fma_f32 v[196:197], v[216:217], v[166:167], v[196:197] op_sel_hi:[0,1,1]
	v_pk_fma_f32 v[202:203], v[216:217], v[168:169], v[202:203] op_sel_hi:[0,1,1]
	v_fma_f32 v208, v216, v170, v208
	v_pk_mul_f32 v[210:211], v[84:85], v[132:133] op_sel_hi:[0,1]
	v_pk_mul_f32 v[212:213], v[84:85], v[198:199] op_sel_hi:[0,1]
	v_mul_f32_e64 v214, v84, v204
	v_pk_fma_f32 v[210:211], v[84:85], v[172:173], v[210:211] op_sel:[1,0,0]
	v_pk_fma_f32 v[212:213], v[84:85], v[200:201], v[212:213] op_sel:[1,0,0]
	v_fma_f32 v214, v85, v206, v214
	v_pk_fma_f32 v[210:211], v[86:87], v[196:197], v[210:211] op_sel_hi:[0,1,1]
	v_pk_fma_f32 v[212:213], v[86:87], v[202:203], v[212:213] op_sel_hi:[0,1,1]
	v_fma_f32 v214, v86, v208, v214
	v_pk_fma_f32 v[210:211], v[216:217], v[52:53], v[210:211] op_sel:[1,0,0] neg_lo:[0,0,1] neg_hi:[0,0,1]
	v_pk_fma_f32 v[212:213], v[216:217], v[150:151], v[212:213] op_sel:[1,0,0] neg_lo:[0,0,1] neg_hi:[0,0,1]
	v_fma_f32 v214, v217, v152, -v214
	v_cmp_eq_u32_e64 s[10:11], 1, v219
	v_cmp_eq_u32_e64 s[14:15], 2, v219
	v_cmp_eq_u32_e64 s[20:21], 3, v219
	v_cmp_eq_u32_e64 s[22:23], 4, v219
	v_cmp_eq_u32_e64 s[30:31], 5, v219
	v_pk_add_f32 v[52:53], v[106:107], v[132:133]
	v_pk_add_f32 v[148:149], v[108:109], v[52:53]
	v_pk_add_f32 v[106:107], v[222:223], v[198:199]
	v_pk_add_f32 v[108:109], v[178:179], v[106:107]
	v_add_f32_e64 v150, v228, v204
	v_add_f32_e64 v152, v184, v150
	v_pk_add_f32 v[154:155], v[158:159], v[172:173]
	v_pk_add_f32 v[156:157], v[174:175], v[154:155]
	v_pk_add_f32 v[158:159], v[224:225], v[200:201]
	v_pk_add_f32 v[160:161], v[180:181], v[158:159]
	v_add_f32_e64 v162, v230, v206
	v_add_f32_e64 v164, v186, v162
	v_pk_add_f32 v[166:167], v[220:221], v[196:197]
	v_pk_add_f32 v[168:169], v[176:177], v[166:167]
	v_pk_add_f32 v[170:171], v[226:227], v[202:203]
	v_pk_add_f32 v[174:175], v[182:183], v[170:171]
	v_add_f32_e64 v176, v232, v208
	v_add_f32_e64 v178, v188, v176
	v_pk_add_f32 v[180:181], v[234:235], v[210:211]
	v_pk_add_f32 v[182:183], v[190:191], v[180:181]
	v_pk_add_f32 v[184:185], v[236:237], v[212:213]
	v_pk_add_f32 v[186:187], v[192:193], v[184:185]
	v_add_f32_e64 v188, v238, v214
	v_add_f32_e64 v190, v194, v188
	v_pk_fma_f32 v[192:193], v[56:57], v[148:149], v[182:183] op_sel_hi:[0,1,1]
	v_pk_fma_f32 v[194:195], v[56:57], v[108:109], v[186:187] op_sel_hi:[0,1,1]
	v_fma_f32 v220, v56, v152, v190
	v_pk_fma_f32 v[222:223], v[72:73], v[148:149], v[182:183] op_sel_hi:[0,1,1]
	v_pk_fma_f32 v[224:225], v[72:73], v[108:109], v[186:187] op_sel_hi:[0,1,1]
	v_fma_f32 v226, v72, v152, v190
	v_pk_fma_f32 v[192:193], v[56:57], v[156:157], v[192:193] op_sel:[1,0,0]
	v_pk_fma_f32 v[194:195], v[56:57], v[160:161], v[194:195] op_sel:[1,0,0]
	v_fma_f32 v220, v57, v164, v220
	v_pk_fma_f32 v[222:223], v[72:73], v[156:157], v[222:223] op_sel:[1,0,0]
	v_pk_fma_f32 v[224:225], v[72:73], v[160:161], v[224:225] op_sel:[1,0,0]
	v_fma_f32 v226, v73, v164, v226
	v_pk_fma_f32 v[192:193], v[58:59], v[168:169], v[192:193] op_sel_hi:[0,1,1]
	v_pk_fma_f32 v[194:195], v[58:59], v[174:175], v[194:195] op_sel_hi:[0,1,1]
	v_fma_f32 v220, v58, v178, v220
	v_pk_fma_f32 v[222:223], v[74:75], v[168:169], v[222:223] op_sel_hi:[0,1,1]
	v_pk_fma_f32 v[224:225], v[74:75], v[174:175], v[224:225] op_sel_hi:[0,1,1]
	v_fma_f32 v226, v74, v178, v226
	v_pk_fma_f32 v[182:183], v[32:33], v[148:149], v[182:183] op_sel_hi:[0,1,1]
	v_pk_fma_f32 v[186:187], v[32:33], v[108:109], v[186:187] op_sel_hi:[0,1,1]
	v_fma_f32 v190, v32, v152, v190
	v_pk_fma_f32 v[182:183], v[32:33], v[156:157], v[182:183] op_sel:[1,0,0]
	v_pk_fma_f32 v[186:187], v[32:33], v[160:161], v[186:187] op_sel:[1,0,0]
	v_fma_f32 v190, v33, v164, v190
	v_pk_fma_f32 v[182:183], v[34:35], v[168:169], v[182:183] op_sel_hi:[0,1,1]
	v_pk_fma_f32 v[186:187], v[34:35], v[174:175], v[186:187] op_sel_hi:[0,1,1]
	v_fma_f32 v190, v34, v178, v190
	v_cndmask_b32_e64 v228, 0, v1, s[10:11]
	v_cndmask_b32_e64 v229, 0, v1, s[14:15]
	v_cndmask_b32_e64 v230, 0, v1, s[20:21]
	v_cndmask_b32_e64 v231, 0, v1, s[22:23]
	v_cndmask_b32_e64 v232, 0, v1, s[30:31]
	v_add_f32_dpp v182, v192, v182 wave_shl:1 row_mask:0xf bank_mask:0xf bound_ctrl:1
	v_add_f32_dpp v183, v193, v183 wave_shl:1 row_mask:0xf bank_mask:0xf bound_ctrl:1
	v_add_f32_dpp v186, v194, v186 wave_shl:1 row_mask:0xf bank_mask:0xf bound_ctrl:1
	v_add_f32_dpp v187, v195, v187 wave_shl:1 row_mask:0xf bank_mask:0xf bound_ctrl:1
	v_add_f32_dpp v190, v220, v190 wave_shl:1 row_mask:0xf bank_mask:0xf bound_ctrl:1
	s_add_i32 s4, s34, 4
	s_cmpk_lt_i32 s4, 0x201
	s_cselect_b64 s[12:13], s[0:1], 0
	v_add_f32_dpp v182, v222, v182 wave_shr:1 row_mask:0xf bank_mask:0xf bound_ctrl:1
	v_add_f32_dpp v183, v223, v183 wave_shr:1 row_mask:0xf bank_mask:0xf bound_ctrl:1
	v_add_f32_dpp v186, v224, v186 wave_shr:1 row_mask:0xf bank_mask:0xf bound_ctrl:1
	v_add_f32_dpp v187, v225, v187 wave_shr:1 row_mask:0xf bank_mask:0xf bound_ctrl:1
	v_add_f32_dpp v190, v226, v190 wave_shr:1 row_mask:0xf bank_mask:0xf bound_ctrl:1
	v_pk_fma_f32 v[182:183], v[12:13], v[218:219], v[182:183] op_sel_hi:[1,0,1] neg_lo:[0,0,1] neg_hi:[0,0,1]
	v_pk_fma_f32 v[186:187], v[14:15], v[218:219], v[186:187] op_sel_hi:[1,0,1] neg_lo:[0,0,1] neg_hi:[0,0,1]
	v_fma_f32 v190, v16, v218, -v190
	v_pk_add_f32 v[182:183], v[182:183], v[228:229] neg_lo:[0,1] neg_hi:[0,1]
	v_pk_add_f32 v[186:187], v[186:187], v[230:231] neg_lo:[0,1] neg_hi:[0,1]
	v_add_f32_e64 v190, v190, -v232
	v_pk_mul_f32 v[234:235], v[182:183], v[182:183]
	v_pk_fma_f32 v[234:235], v[186:187], v[186:187], v[234:235]
	v_add_f32_e32 v234, v234, v235
	v_fma_f32 v234, v190, v190, v234
	v_cndmask_b32_e64 v235, 0, v234, s[12:13]
	v_add_f32_e32 v0, v0, v235
	s_add_i32 s4, s34, 9
	s_min_i32 s4, s4, 0x200
	s_mul_i32 s5, s4, 0x804
	s_add_i32 s5, s5, s35
	s_add_i32 s6, s5, 0x0
	s_add_i32 s7, s5, 0x101004
	s_add_i32 s8, s5, 0x202008
	s_add_i32 s11, s5, 0x30300c
	s_add_i32 s15, s5, 0x404010
	s_mul_i32 s9, s4, 0x180c
	s_add_i32 s9, s9, s33
	buffer_load_dword v12, v28, s[16:19], s6 offen nt
	buffer_load_dword v13, v28, s[16:19], s7 offen nt
	buffer_load_dword v14, v28, s[16:19], s8 offen nt
	buffer_load_dword v15, v28, s[16:19], s11 offen nt
	buffer_load_dword v16, v28, s[16:19], s15 offen nt
	buffer_load_dwordx3 v[32:34], v27, s[24:27], s9 offen nt
	s_waitcnt vmcnt(12)
	v_mov_b32_dpp v56, v64 wave_shr:1 row_mask:0xf bank_mask:0xf bound_ctrl:1
	v_mov_b32_dpp v57, v65 wave_shr:1 row_mask:0xf bank_mask:0xf bound_ctrl:1
	v_mov_b32_dpp v58, v66 wave_shr:1 row_mask:0xf bank_mask:0xf bound_ctrl:1
	v_mov_b32_dpp v72, v64 wave_shl:1 row_mask:0xf bank_mask:0xf bound_ctrl:1
	v_mov_b32_dpp v73, v65 wave_shl:1 row_mask:0xf bank_mask:0xf bound_ctrl:1
	v_mov_b32_dpp v74, v66 wave_shl:1 row_mask:0xf bank_mask:0xf bound_ctrl:1
	v_mov_b32_dpp v84, v54 wave_shr:1 row_mask:0xf bank_mask:0xf bound_ctrl:1
	v_mov_b32_dpp v85, v55 wave_shr:1 row_mask:0xf bank_mask:0xf bound_ctrl:1
	v_mov_b32_dpp v86, v60 wave_shr:1 row_mask:0xf bank_mask:0xf bound_ctrl:1
	v_mov_b32_dpp v87, v61 wave_shr:1 row_mask:0xf bank_mask:0xf bound_ctrl:1
	v_mov_b32_dpp v88, v62 wave_shr:1 row_mask:0xf bank_mask:0xf bound_ctrl:1
	v_mov_b32_dpp v90, v54 wave_shl:1 row_mask:0xf bank_mask:0xf bound_ctrl:1
	v_mov_b32_dpp v91, v55 wave_shl:1 row_mask:0xf bank_mask:0xf bound_ctrl:1
	v_mov_b32_dpp v108, v60 wave_shl:1 row_mask:0xf bank_mask:0xf bound_ctrl:1
	v_mov_b32_dpp v109, v61 wave_shl:1 row_mask:0xf bank_mask:0xf bound_ctrl:1
	v_mov_b32_dpp v148, v62 wave_shl:1 row_mask:0xf bank_mask:0xf bound_ctrl:1
	v_pk_mul_f32 v[152:153], v[54:55], v[64:65] op_sel_hi:[1,0]
	v_pk_mul_f32 v[156:157], v[60:61], v[64:65] op_sel_hi:[1,0]
	v_mul_f32_e64 v160, v62, v64
	v_pk_mul_f32 v[164:165], v[54:55], v[64:65] op_sel:[0,1]
	v_pk_mul_f32 v[168:169], v[60:61], v[64:65] op_sel:[0,1]
	v_mul_f32_e64 v174, v62, v65
	v_pk_mul_f32 v[178:179], v[54:55], v[66:67] op_sel_hi:[1,0]
	v_pk_mul_f32 v[182:183], v[60:61], v[66:67] op_sel_hi:[1,0]
	v_mul_f32_e64 v186, v62, v66
	v_pk_add_f32 v[190:191], v[54:55], v[84:85]
	v_pk_add_f32 v[192:193], v[60:61], v[86:87]
	v_add_f32_e64 v194, v62, v88
	v_pk_fma_f32 v[152:153], v[84:85], v[56:57], v[152:153] op_sel_hi:[1,0,1]
	v_pk_fma_f32 v[156:157], v[86:87], v[56:57], v[156:157] op_sel_hi:[1,0,1]
	v_fma_f32 v160, v88, v56, v160
	v_pk_fma_f32 v[164:165], v[84:85], v[56:57], v[164:165] op_sel:[0,1,0]
	v_pk_fma_f32 v[168:169], v[86:87], v[56:57], v[168:169] op_sel:[0,1,0]
	v_fma_f32 v174, v88, v57, v174
	v_pk_fma_f32 v[178:179], v[84:85], v[58:59], v[178:179] op_sel_hi:[1,0,1]
	v_pk_fma_f32 v[182:183], v[86:87], v[58:59], v[182:183] op_sel_hi:[1,0,1]
	v_fma_f32 v186, v88, v58, v186
	v_pk_add_f32 v[190:191], v[190:191], v[90:91]
	v_pk_add_f32 v[192:193], v[192:193], v[108:109]
	v_add_f32_e64 v194, v194, v148
	v_pk_fma_f32 v[152:153], v[90:91], v[72:73], v[152:153] op_sel_hi:[1,0,1]
	v_pk_fma_f32 v[156:157], v[108:109], v[72:73], v[156:157] op_sel_hi:[1,0,1]
	v_fma_f32 v160, v148, v72, v160
	v_pk_fma_f32 v[164:165], v[90:91], v[72:73], v[164:165] op_sel:[0,1,0]
	v_pk_fma_f32 v[168:169], v[108:109], v[72:73], v[168:169] op_sel:[0,1,0]
	v_fma_f32 v174, v148, v73, v174
	v_pk_fma_f32 v[178:179], v[90:91], v[74:75], v[178:179] op_sel_hi:[1,0,1]
	v_pk_fma_f32 v[182:183], v[108:109], v[74:75], v[182:183] op_sel_hi:[1,0,1]
	v_fma_f32 v186, v148, v74, v186
	s_barrier
	ds_read_b128 v[84:87], v23 offset:3072
	ds_read_b128 v[88:91], v23 offset:4096
	ds_read_b128 v[216:219], v23 offset:5120
	v_pk_add_f32 v[108:109], v[46:47], v[190:191]
	v_pk_add_f32 v[46:47], v[134:135], v[192:193]
	v_add_f32_e64 v134, v136, v194
	v_pk_add_f32 v[136:137], v[142:143], v[152:153]
	v_pk_add_f32 v[142:143], v[116:117], v[156:157]
	v_add_f32_e64 v116, v118, v160
	v_pk_add_f32 v[118:119], v[120:121], v[164:165]
	v_pk_add_f32 v[120:121], v[122:123], v[168:169]
	v_add_f32_e64 v122, v124, v174
	v_pk_add_f32 v[124:125], v[126:127], v[178:179]
	v_pk_add_f32 v[126:127], v[128:129], v[182:183]
	v_add_f32_e64 v128, v130, v186
	s_waitcnt lgkmcnt(2)
	v_pk_fma_f32 v[136:137], v[84:85], v[108:109], v[136:137] op_sel_hi:[0,1,1] neg_lo:[1,0,0] neg_hi:[1,0,0]
	v_pk_fma_f32 v[142:143], v[84:85], v[46:47], v[142:143] op_sel_hi:[0,1,1] neg_lo:[1,0,0] neg_hi:[1,0,0]
	v_fma_f32 v116, -v84, v134, v116
	v_pk_fma_f32 v[118:119], v[84:85], v[108:109], v[118:119] op_sel:[1,0,0] neg_lo:[1,0,0] neg_hi:[1,0,0]
	v_pk_fma_f32 v[120:121], v[84:85], v[46:47], v[120:121] op_sel:[1,0,0] neg_lo:[1,0,0] neg_hi:[1,0,0]
	v_fma_f32 v122, -v85, v134, v122
	v_pk_fma_f32 v[124:125], v[86:87], v[108:109], v[124:125] op_sel_hi:[0,1,1] neg_lo:[1,0,0] neg_hi:[1,0,0]
	v_pk_fma_f32 v[126:127], v[86:87], v[46:47], v[126:127] op_sel_hi:[0,1,1] neg_lo:[1,0,0] neg_hi:[1,0,0]
	v_fma_f32 v128, -v86, v134, v128
	v_pk_mul_f32 v[130:131], v[86:87], v[136:137] op_sel:[1,0]
	v_pk_mul_f32 v[222:223], v[86:87], v[142:143] op_sel:[1,0]
	v_mul_f32_e64 v228, v87, v116
	s_waitcnt lgkmcnt(1)
	v_pk_mul_f32 v[148:149], v[88:89], v[136:137] op_sel_hi:[0,1]
	v_pk_mul_f32 v[224:225], v[88:89], v[142:143] op_sel_hi:[0,1]
	v_mul_f32_e64 v230, v88, v116
	v_pk_mul_f32 v[220:221], v[88:89], v[136:137] op_sel:[1,0]
	v_pk_mul_f32 v[226:227], v[88:89], v[142:143] op_sel:[1,0]
	v_mul_f32_e64 v232, v89, v116
	v_pk_fma_f32 v[130:131], v[88:89], v[118:119], v[130:131] op_sel_hi:[0,1,1]
	v_pk_fma_f32 v[222:223], v[88:89], v[120:121], v[222:223] op_sel_hi:[0,1,1]
	v_fma_f32 v228, v88, v122, v228
	v_pk_fma_f32 v[148:149], v[90:91], v[118:119], v[148:149] op_sel_hi:[0,1,1]
	v_pk_fma_f32 v[224:225], v[90:91], v[120:121], v[224:225] op_sel_hi:[0,1,1]
	v_fma_f32 v230, v90, v122, v230
	v_pk_fma_f32 v[220:221], v[90:91], v[118:119], v[220:221] op_sel:[1,0,0]
	v_pk_fma_f32 v[226:227], v[90:91], v[120:121], v[226:227] op_sel:[1,0,0]
	v_fma_f32 v232, v91, v122, v232
	v_pk_fma_f32 v[130:131], v[88:89], v[124:125], v[130:131] op_sel:[1,0,0]
	v_pk_fma_f32 v[222:223], v[88:89], v[126:127], v[222:223] op_sel:[1,0,0]
	v_fma_f32 v228, v89, v128, v228
	v_pk_fma_f32 v[148:149], v[90:91], v[124:125], v[148:149] op_sel:[1,0,0]
	v_pk_fma_f32 v[224:225], v[90:91], v[126:127], v[224:225] op_sel:[1,0,0]
	v_fma_f32 v230, v91, v128, v230
	s_waitcnt lgkmcnt(0)
	v_pk_fma_f32 v[220:221], v[216:217], v[124:125], v[220:221] op_sel_hi:[0,1,1]
	v_pk_fma_f32 v[226:227], v[216:217], v[126:127], v[226:227] op_sel_hi:[0,1,1]
	v_fma_f32 v232, v216, v128, v232
	v_pk_mul_f32 v[234:235], v[84:85], v[130:131] op_sel_hi:[0,1]
	v_pk_mul_f32 v[236:237], v[84:85], v[222:223] op_sel_hi:[0,1]
	v_mul_f32_e64 v238, v84, v228
	v_pk_fma_f32 v[234:235], v[84:85], v[148:149], v[234:235] op_sel:[1,0,0]
	v_pk_fma_f32 v[236:237], v[84:85], v[224:225], v[236:237] op_sel:[1,0,0]
	v_fma_f32 v238, v85, v230, v238
	v_pk_fma_f32 v[234:235], v[86:87], v[220:221], v[234:235] op_sel_hi:[0,1,1]
	v_pk_fma_f32 v[236:237], v[86:87], v[226:227], v[236:237] op_sel_hi:[0,1,1]
	v_fma_f32 v238, v86, v232, v238
	v_pk_fma_f32 v[234:235], v[216:217], v[108:109], v[234:235] op_sel:[1,0,0] neg_lo:[0,0,1] neg_hi:[0,0,1]
	v_pk_fma_f32 v[236:237], v[216:217], v[46:47], v[236:237] op_sel:[1,0,0] neg_lo:[0,0,1] neg_hi:[0,0,1]
	v_fma_f32 v238, v217, v134, -v238
	v_cmp_eq_u32_e64 s[10:11], 1, v219
	v_cmp_eq_u32_e64 s[14:15], 2, v219
	v_cmp_eq_u32_e64 s[20:21], 3, v219
	v_cmp_eq_u32_e64 s[22:23], 4, v219
	v_cmp_eq_u32_e64 s[30:31], 5, v219
	v_pk_add_f32 v[46:47], v[52:53], v[130:131]
	v_pk_add_f32 v[52:53], v[106:107], v[222:223]
	v_add_f32_e64 v106, v150, v228
	v_pk_add_f32 v[108:109], v[154:155], v[148:149]
	v_pk_add_f32 v[116:117], v[158:159], v[224:225]
	v_add_f32_e64 v118, v162, v230
	v_pk_add_f32 v[120:121], v[166:167], v[220:221]
	v_pk_add_f32 v[122:123], v[170:171], v[226:227]
	v_add_f32_e64 v124, v176, v232
	v_pk_add_f32 v[126:127], v[180:181], v[234:235]
	v_pk_add_f32 v[128:129], v[184:185], v[236:237]
	v_add_f32_e64 v134, v188, v238
	v_pk_fma_f32 v[136:137], v[76:77], v[46:47], v[126:127] op_sel_hi:[0,1,1]
	v_pk_fma_f32 v[142:143], v[76:77], v[52:53], v[128:129] op_sel_hi:[0,1,1]
	v_fma_f32 v150, v76, v106, v134
	v_pk_fma_f32 v[154:155], v[92:93], v[46:47], v[126:127] op_sel_hi:[0,1,1]
	v_pk_fma_f32 v[158:159], v[92:93], v[52:53], v[128:129] op_sel_hi:[0,1,1]
	v_fma_f32 v162, v92, v106, v134
	v_pk_fma_f32 v[136:137], v[76:77], v[108:109], v[136:137] op_sel:[1,0,0]
	v_pk_fma_f32 v[142:143], v[76:77], v[116:117], v[142:143] op_sel:[1,0,0]
	v_fma_f32 v150, v77, v118, v150
	v_pk_fma_f32 v[154:155], v[92:93], v[108:109], v[154:155] op_sel:[1,0,0]
	v_pk_fma_f32 v[158:159], v[92:93], v[116:117], v[158:159] op_sel:[1,0,0]
	v_fma_f32 v162, v93, v118, v162
	v_pk_fma_f32 v[136:137], v[78:79], v[120:121], v[136:137] op_sel_hi:[0,1,1]
	v_pk_fma_f32 v[142:143], v[78:79], v[122:123], v[142:143] op_sel_hi:[0,1,1]
	v_fma_f32 v150, v78, v124, v150
	v_pk_fma_f32 v[154:155], v[94:95], v[120:121], v[154:155] op_sel_hi:[0,1,1]
	v_pk_fma_f32 v[158:159], v[94:95], v[122:123], v[158:159] op_sel_hi:[0,1,1]
	v_fma_f32 v162, v94, v124, v162
	v_pk_fma_f32 v[126:127], v[36:37], v[46:47], v[126:127] op_sel_hi:[0,1,1]
	v_pk_fma_f32 v[128:129], v[36:37], v[52:53], v[128:129] op_sel_hi:[0,1,1]
	v_fma_f32 v134, v36, v106, v134
	v_pk_fma_f32 v[126:127], v[36:37], v[108:109], v[126:127] op_sel:[1,0,0]
	v_pk_fma_f32 v[128:129], v[36:37], v[116:117], v[128:129] op_sel:[1,0,0]
	v_fma_f32 v134, v37, v118, v134
	v_pk_fma_f32 v[126:127], v[38:39], v[120:121], v[126:127] op_sel_hi:[0,1,1]
	v_pk_fma_f32 v[128:129], v[38:39], v[122:123], v[128:129] op_sel_hi:[0,1,1]
	v_fma_f32 v134, v38, v124, v134
	v_cndmask_b32_e64 v166, 0, v1, s[10:11]
	v_cndmask_b32_e64 v167, 0, v1, s[14:15]
	v_cndmask_b32_e64 v170, 0, v1, s[20:21]
	v_cndmask_b32_e64 v171, 0, v1, s[22:23]
	v_cndmask_b32_e64 v176, 0, v1, s[30:31]
	v_add_f32_dpp v126, v136, v126 wave_shl:1 row_mask:0xf bank_mask:0xf bound_ctrl:1
	v_add_f32_dpp v127, v137, v127 wave_shl:1 row_mask:0xf bank_mask:0xf bound_ctrl:1
	v_add_f32_dpp v128, v142, v128 wave_shl:1 row_mask:0xf bank_mask:0xf bound_ctrl:1
	v_add_f32_dpp v129, v143, v129 wave_shl:1 row_mask:0xf bank_mask:0xf bound_ctrl:1
	v_add_f32_dpp v134, v150, v134 wave_shl:1 row_mask:0xf bank_mask:0xf bound_ctrl:1
	s_add_i32 s4, s34, 5
	s_cmpk_lt_i32 s4, 0x201
	s_cselect_b64 s[12:13], s[0:1], 0
	v_add_f32_dpp v126, v154, v126 wave_shr:1 row_mask:0xf bank_mask:0xf bound_ctrl:1
	v_add_f32_dpp v127, v155, v127 wave_shr:1 row_mask:0xf bank_mask:0xf bound_ctrl:1
	v_add_f32_dpp v128, v158, v128 wave_shr:1 row_mask:0xf bank_mask:0xf bound_ctrl:1
	v_add_f32_dpp v129, v159, v129 wave_shr:1 row_mask:0xf bank_mask:0xf bound_ctrl:1
	v_add_f32_dpp v134, v162, v134 wave_shr:1 row_mask:0xf bank_mask:0xf bound_ctrl:1
	v_pk_fma_f32 v[126:127], v[20:21], v[218:219], v[126:127] op_sel_hi:[1,0,1] neg_lo:[0,0,1] neg_hi:[0,0,1]
	v_pk_fma_f32 v[128:129], v[24:25], v[218:219], v[128:129] op_sel_hi:[1,0,1] neg_lo:[0,0,1] neg_hi:[0,0,1]
	v_fma_f32 v134, v30, v218, -v134
	v_pk_add_f32 v[126:127], v[126:127], v[166:167] neg_lo:[0,1] neg_hi:[0,1]
	v_pk_add_f32 v[128:129], v[128:129], v[170:171] neg_lo:[0,1] neg_hi:[0,1]
	v_add_f32_e64 v134, v134, -v176
	v_pk_mul_f32 v[180:181], v[126:127], v[126:127]
	v_pk_fma_f32 v[180:181], v[128:129], v[128:129], v[180:181]
	v_add_f32_e32 v180, v180, v181
	v_fma_f32 v180, v134, v134, v180
	v_cndmask_b32_e64 v181, 0, v180, s[12:13]
	v_add_f32_e32 v0, v0, v181
	s_add_i32 s4, s34, 10
	s_min_i32 s4, s4, 0x200
	s_mul_i32 s5, s4, 0x804
	s_add_i32 s5, s5, s35
	s_add_i32 s6, s5, 0x0
	s_add_i32 s7, s5, 0x101004
	s_add_i32 s8, s5, 0x202008
	s_add_i32 s11, s5, 0x30300c
	s_add_i32 s15, s5, 0x404010
	s_mul_i32 s9, s4, 0x180c
	s_add_i32 s9, s9, s33
	buffer_load_dword v20, v28, s[16:19], s6 offen nt
	buffer_load_dword v21, v28, s[16:19], s7 offen nt
	buffer_load_dword v24, v28, s[16:19], s8 offen nt
	buffer_load_dword v25, v28, s[16:19], s11 offen nt
	buffer_load_dword v30, v28, s[16:19], s15 offen nt
	buffer_load_dwordx3 v[36:38], v27, s[24:27], s9 offen nt
	s_waitcnt vmcnt(12)
	v_mov_b32_dpp v76, v8 wave_shr:1 row_mask:0xf bank_mask:0xf bound_ctrl:1
	v_mov_b32_dpp v77, v9 wave_shr:1 row_mask:0xf bank_mask:0xf bound_ctrl:1
	v_mov_b32_dpp v78, v10 wave_shr:1 row_mask:0xf bank_mask:0xf bound_ctrl:1
	v_mov_b32_dpp v84, v8 wave_shl:1 row_mask:0xf bank_mask:0xf bound_ctrl:1
	v_mov_b32_dpp v85, v9 wave_shl:1 row_mask:0xf bank_mask:0xf bound_ctrl:1
	v_mov_b32_dpp v86, v10 wave_shl:1 row_mask:0xf bank_mask:0xf bound_ctrl:1
	v_mov_b32_dpp v46, v2 wave_shr:1 row_mask:0xf bank_mask:0xf bound_ctrl:1
	v_mov_b32_dpp v47, v3 wave_shr:1 row_mask:0xf bank_mask:0xf bound_ctrl:1
	v_mov_b32_dpp v52, v4 wave_shr:1 row_mask:0xf bank_mask:0xf bound_ctrl:1
	v_mov_b32_dpp v53, v5 wave_shr:1 row_mask:0xf bank_mask:0xf bound_ctrl:1
	v_mov_b32_dpp v88, v6 wave_shr:1 row_mask:0xf bank_mask:0xf bound_ctrl:1
	v_mov_b32_dpp v90, v2 wave_shl:1 row_mask:0xf bank_mask:0xf bound_ctrl:1
	v_mov_b32_dpp v91, v3 wave_shl:1 row_mask:0xf bank_mask:0xf bound_ctrl:1
	v_mov_b32_dpp v92, v4 wave_shl:1 row_mask:0xf bank_mask:0xf bound_ctrl:1
	v_mov_b32_dpp v93, v5 wave_shl:1 row_mask:0xf bank_mask:0xf bound_ctrl:1
	v_mov_b32_dpp v94, v6 wave_shl:1 row_mask:0xf bank_mask:0xf bound_ctrl:1
	v_pk_mul_f32 v[106:107], v[2:3], v[8:9] op_sel_hi:[1,0]
	v_pk_mul_f32 v[108:109], v[4:5], v[8:9] op_sel_hi:[1,0]
	v_mul_f32_e64 v116, v6, v8
	v_pk_mul_f32 v[118:119], v[2:3], v[8:9] op_sel:[0,1]
	v_pk_mul_f32 v[120:121], v[4:5], v[8:9] op_sel:[0,1]
	v_mul_f32_e64 v122, v6, v9
	v_pk_mul_f32 v[124:125], v[2:3], v[10:11] op_sel_hi:[1,0]
	v_pk_mul_f32 v[126:127], v[4:5], v[10:11] op_sel_hi:[1,0]
	v_mul_f32_e64 v128, v6, v10
	v_pk_add_f32 v[134:135], v[2:3], v[46:47]
	v_pk_add_f32 v[136:137], v[4:5], v[52:53]
	v_add_f32_e64 v142, v6, v88
	v_pk_fma_f32 v[106:107], v[46:47], v[76:77], v[106:107] op_sel_hi:[1,0,1]
	v_pk_fma_f32 v[108:109], v[52:53], v[76:77], v[108:109] op_sel_hi:[1,0,1]
	v_fma_f32 v116, v88, v76, v116
	v_pk_fma_f32 v[118:119], v[46:47], v[76:77], v[118:119] op_sel:[0,1,0]
	v_pk_fma_f32 v[120:121], v[52:53], v[76:77], v[120:121] op_sel:[0,1,0]
	v_fma_f32 v122, v88, v77, v122
	v_pk_fma_f32 v[124:125], v[46:47], v[78:79], v[124:125] op_sel_hi:[1,0,1]
	v_pk_fma_f32 v[126:127], v[52:53], v[78:79], v[126:127] op_sel_hi:[1,0,1]
	v_fma_f32 v128, v88, v78, v128
	v_pk_add_f32 v[134:135], v[134:135], v[90:91]
	v_pk_add_f32 v[136:137], v[136:137], v[92:93]
	v_add_f32_e64 v142, v142, v94
	v_pk_fma_f32 v[106:107], v[90:91], v[84:85], v[106:107] op_sel_hi:[1,0,1]
	v_pk_fma_f32 v[108:109], v[92:93], v[84:85], v[108:109] op_sel_hi:[1,0,1]
	v_fma_f32 v116, v94, v84, v116
	v_pk_fma_f32 v[118:119], v[90:91], v[84:85], v[118:119] op_sel:[0,1,0]
	v_pk_fma_f32 v[120:121], v[92:93], v[84:85], v[120:121] op_sel:[0,1,0]
	v_fma_f32 v122, v94, v85, v122
	v_pk_fma_f32 v[124:125], v[90:91], v[86:87], v[124:125] op_sel_hi:[1,0,1]
	v_pk_fma_f32 v[126:127], v[92:93], v[86:87], v[126:127] op_sel_hi:[1,0,1]
	v_fma_f32 v128, v94, v86, v128
	s_barrier
	ds_read_b128 v[88:91], v23 offset:0
	ds_read_b128 v[92:95], v23 offset:1024
	ds_read_b128 v[216:219], v23 offset:2048
	v_pk_add_f32 v[46:47], v[190:191], v[134:135]
	v_pk_add_f32 v[52:53], v[140:141], v[46:47]
	v_pk_add_f32 v[140:141], v[192:193], v[136:137]
	v_pk_add_f32 v[150:151], v[144:145], v[140:141]
	v_add_f32_e64 v144, v194, v142
	v_add_f32_e64 v154, v146, v144
	v_pk_add_f32 v[146:147], v[152:153], v[106:107]
	v_pk_add_f32 v[158:159], v[96:97], v[146:147]
	v_pk_add_f32 v[96:97], v[156:157], v[108:109]
	v_pk_add_f32 v[152:153], v[98:99], v[96:97]
	v_add_f32_e64 v98, v160, v116
	v_add_f32_e64 v156, v100, v98
	v_pk_add_f32 v[100:101], v[164:165], v[118:119]
	v_pk_add_f32 v[160:161], v[102:103], v[100:101]
	v_pk_add_f32 v[102:103], v[168:169], v[120:121]
	v_pk_add_f32 v[162:163], v[104:105], v[102:103]
	v_add_f32_e64 v104, v174, v122
	v_add_f32_e64 v164, v110, v104
	v_pk_add_f32 v[110:111], v[178:179], v[124:125]
	v_pk_add_f32 v[166:167], v[112:113], v[110:111]
	v_pk_add_f32 v[112:113], v[182:183], v[126:127]
	v_pk_add_f32 v[168:169], v[114:115], v[112:113]
	v_add_f32_e64 v114, v186, v128
	v_add_f32_e64 v170, v138, v114
	s_waitcnt lgkmcnt(2)
	v_pk_fma_f32 v[158:159], v[88:89], v[52:53], v[158:159] op_sel_hi:[0,1,1] neg_lo:[1,0,0] neg_hi:[1,0,0]
	v_pk_fma_f32 v[152:153], v[88:89], v[150:151], v[152:153] op_sel_hi:[0,1,1] neg_lo:[1,0,0] neg_hi:[1,0,0]
	v_fma_f32 v156, -v88, v154, v156
	v_pk_fma_f32 v[160:161], v[88:89], v[52:53], v[160:161] op_sel:[1,0,0] neg_lo:[1,0,0] neg_hi:[1,0,0]
	v_pk_fma_f32 v[162:163], v[88:89], v[150:151], v[162:163] op_sel:[1,0,0] neg_lo:[1,0,0] neg_hi:[1,0,0]
	v_fma_f32 v164, -v89, v154, v164
	v_pk_fma_f32 v[166:167], v[90:91], v[52:53], v[166:167] op_sel_hi:[0,1,1] neg_lo:[1,0,0] neg_hi:[1,0,0]
	v_pk_fma_f32 v[168:169], v[90:91], v[150:151], v[168:169] op_sel_hi:[0,1,1] neg_lo:[1,0,0] neg_hi:[1,0,0]
	v_fma_f32 v170, -v90, v154, v170
	v_pk_mul_f32 v[138:139], v[90:91], v[158:159] op_sel:[1,0]
	v_pk_mul_f32 v[178:179], v[90:91], v[152:153] op_sel:[1,0]
	v_mul_f32_e64 v184, v91, v156
	s_waitcnt lgkmcnt(1)
	v_pk_mul_f32 v[174:175], v[92:93], v[158:159] op_sel_hi:[0,1]
	v_pk_mul_f32 v[180:181], v[92:93], v[152:153] op_sel_hi:[0,1]
	v_mul_f32_e64 v186, v92, v156
	v_pk_mul_f32 v[176:177], v[92:93], v[158:159] op_sel:[1,0]
	v_pk_mul_f32 v[182:183], v[92:93], v[152:153] op_sel:[1,0]
	v_mul_f32_e64 v188, v93, v156
	v_pk_fma_f32 v[138:139], v[92:93], v[160:161], v[138:139] op_sel_hi:[0,1,1]
	v_pk_fma_f32 v[178:179], v[92:93], v[162:163], v[178:179] op_sel_hi:[0,1,1]
	v_fma_f32 v184, v92, v164, v184
	v_pk_fma_f32 v[174:175], v[94:95], v[160:161], v[174:175] op_sel_hi:[0,1,1]
	v_pk_fma_f32 v[180:181], v[94:95], v[162:163], v[180:181] op_sel_hi:[0,1,1]
	v_fma_f32 v186, v94, v164, v186
	v_pk_fma_f32 v[176:177], v[94:95], v[160:161], v[176:177] op_sel:[1,0,0]
	v_pk_fma_f32 v[182:183], v[94:95], v[162:163], v[182:183] op_sel:[1,0,0]
	v_fma_f32 v188, v95, v164, v188
	v_pk_fma_f32 v[138:139], v[92:93], v[166:167], v[138:139] op_sel:[1,0,0]
	v_pk_fma_f32 v[178:179], v[92:93], v[168:169], v[178:179] op_sel:[1,0,0]
	v_fma_f32 v184, v93, v170, v184
	v_pk_fma_f32 v[174:175], v[94:95], v[166:167], v[174:175] op_sel:[1,0,0]
	v_pk_fma_f32 v[180:181], v[94:95], v[168:169], v[180:181] op_sel:[1,0,0]
	v_fma_f32 v186, v95, v170, v186
	s_waitcnt lgkmcnt(0)
	v_pk_fma_f32 v[176:177], v[216:217], v[166:167], v[176:177] op_sel_hi:[0,1,1]
	v_pk_fma_f32 v[182:183], v[216:217], v[168:169], v[182:183] op_sel_hi:[0,1,1]
	v_fma_f32 v188, v216, v170, v188
	v_pk_mul_f32 v[190:191], v[88:89], v[138:139] op_sel_hi:[0,1]
	v_pk_mul_f32 v[192:193], v[88:89], v[178:179] op_sel_hi:[0,1]
	v_mul_f32_e64 v194, v88, v184
	v_pk_fma_f32 v[190:191], v[88:89], v[174:175], v[190:191] op_sel:[1,0,0]
	v_pk_fma_f32 v[192:193], v[88:89], v[180:181], v[192:193] op_sel:[1,0,0]
	v_fma_f32 v194, v89, v186, v194
	v_pk_fma_f32 v[190:191], v[90:91], v[176:177], v[190:191] op_sel_hi:[0,1,1]
	v_pk_fma_f32 v[192:193], v[90:91], v[182:183], v[192:193] op_sel_hi:[0,1,1]
	v_fma_f32 v194, v90, v188, v194
	v_pk_fma_f32 v[190:191], v[216:217], v[52:53], v[190:191] op_sel:[1,0,0] neg_lo:[0,0,1] neg_hi:[0,0,1]
	v_pk_fma_f32 v[192:193], v[216:217], v[150:151], v[192:193] op_sel:[1,0,0] neg_lo:[0,0,1] neg_hi:[0,0,1]
	v_fma_f32 v194, v217, v154, -v194
	v_cmp_eq_u32_e64 s[10:11], 1, v219
	v_cmp_eq_u32_e64 s[14:15], 2, v219
	v_cmp_eq_u32_e64 s[20:21], 3, v219
	v_cmp_eq_u32_e64 s[22:23], 4, v219
	v_cmp_eq_u32_e64 s[30:31], 5, v219
	v_pk_add_f32 v[52:53], v[130:131], v[138:139]
	v_pk_add_f32 v[150:151], v[132:133], v[52:53]
	v_pk_add_f32 v[130:131], v[222:223], v[178:179]
	v_pk_add_f32 v[132:133], v[198:199], v[130:131]
	v_add_f32_e64 v152, v228, v184
	v_add_f32_e64 v154, v204, v152
	v_pk_add_f32 v[156:157], v[148:149], v[174:175]
	v_pk_add_f32 v[158:159], v[172:173], v[156:157]
	v_pk_add_f32 v[148:149], v[224:225], v[180:181]
	v_pk_add_f32 v[160:161], v[200:201], v[148:149]
	v_add_f32_e64 v162, v230, v186
	v_add_f32_e64 v164, v206, v162
	v_pk_add_f32 v[166:167], v[220:221], v[176:177]
	v_pk_add_f32 v[168:169], v[196:197], v[166:167]
	v_pk_add_f32 v[170:171], v[226:227], v[182:183]
	v_pk_add_f32 v[172:173], v[202:203], v[170:171]
	v_add_f32_e64 v196, v232, v188
	v_add_f32_e64 v198, v208, v196
	v_pk_add_f32 v[200:201], v[234:235], v[190:191]
	v_pk_add_f32 v[202:203], v[210:211], v[200:201]
	v_pk_add_f32 v[204:205], v[236:237], v[192:193]
	v_pk_add_f32 v[206:207], v[212:213], v[204:205]
	v_add_f32_e64 v208, v238, v194
	v_add_f32_e64 v210, v214, v208
	v_pk_fma_f32 v[212:213], v[68:69], v[150:151], v[202:203] op_sel_hi:[0,1,1]
	v_pk_fma_f32 v[214:215], v[68:69], v[132:133], v[206:207] op_sel_hi:[0,1,1]
	v_fma_f32 v220, v68, v154, v210
	v_pk_fma_f32 v[222:223], v[80:81], v[150:151], v[202:203] op_sel_hi:[0,1,1]
	v_pk_fma_f32 v[224:225], v[80:81], v[132:133], v[206:207] op_sel_hi:[0,1,1]
	v_fma_f32 v226, v80, v154, v210
	v_pk_fma_f32 v[212:213], v[68:69], v[158:159], v[212:213] op_sel:[1,0,0]
	v_pk_fma_f32 v[214:215], v[68:69], v[160:161], v[214:215] op_sel:[1,0,0]
	v_fma_f32 v220, v69, v164, v220
	v_pk_fma_f32 v[222:223], v[80:81], v[158:159], v[222:223] op_sel:[1,0,0]
	v_pk_fma_f32 v[224:225], v[80:81], v[160:161], v[224:225] op_sel:[1,0,0]
	v_fma_f32 v226, v81, v164, v226
	v_pk_fma_f32 v[212:213], v[70:71], v[168:169], v[212:213] op_sel_hi:[0,1,1]
	v_pk_fma_f32 v[214:215], v[70:71], v[172:173], v[214:215] op_sel_hi:[0,1,1]
	v_fma_f32 v220, v70, v198, v220
	v_pk_fma_f32 v[222:223], v[82:83], v[168:169], v[222:223] op_sel_hi:[0,1,1]
	v_pk_fma_f32 v[224:225], v[82:83], v[172:173], v[224:225] op_sel_hi:[0,1,1]
	v_fma_f32 v226, v82, v198, v226
	v_pk_fma_f32 v[202:203], v[48:49], v[150:151], v[202:203] op_sel_hi:[0,1,1]
	v_pk_fma_f32 v[206:207], v[48:49], v[132:133], v[206:207] op_sel_hi:[0,1,1]
	v_fma_f32 v210, v48, v154, v210
	v_pk_fma_f32 v[202:203], v[48:49], v[158:159], v[202:203] op_sel:[1,0,0]
	v_pk_fma_f32 v[206:207], v[48:49], v[160:161], v[206:207] op_sel:[1,0,0]
	v_fma_f32 v210, v49, v164, v210
	v_pk_fma_f32 v[202:203], v[50:51], v[168:169], v[202:203] op_sel_hi:[0,1,1]
	v_pk_fma_f32 v[206:207], v[50:51], v[172:173], v[206:207] op_sel_hi:[0,1,1]
	v_fma_f32 v210, v50, v198, v210
	v_cndmask_b32_e64 v228, 0, v1, s[10:11]
	v_cndmask_b32_e64 v229, 0, v1, s[14:15]
	v_cndmask_b32_e64 v230, 0, v1, s[20:21]
	v_cndmask_b32_e64 v231, 0, v1, s[22:23]
	v_cndmask_b32_e64 v232, 0, v1, s[30:31]
	v_add_f32_dpp v202, v212, v202 wave_shl:1 row_mask:0xf bank_mask:0xf bound_ctrl:1
	v_add_f32_dpp v203, v213, v203 wave_shl:1 row_mask:0xf bank_mask:0xf bound_ctrl:1
	v_add_f32_dpp v206, v214, v206 wave_shl:1 row_mask:0xf bank_mask:0xf bound_ctrl:1
	v_add_f32_dpp v207, v215, v207 wave_shl:1 row_mask:0xf bank_mask:0xf bound_ctrl:1
	v_add_f32_dpp v210, v220, v210 wave_shl:1 row_mask:0xf bank_mask:0xf bound_ctrl:1
	s_add_i32 s4, s34, 6
	s_cmpk_lt_i32 s4, 0x201
	s_cselect_b64 s[12:13], s[0:1], 0
	v_add_f32_dpp v202, v222, v202 wave_shr:1 row_mask:0xf bank_mask:0xf bound_ctrl:1
	v_add_f32_dpp v203, v223, v203 wave_shr:1 row_mask:0xf bank_mask:0xf bound_ctrl:1
	v_add_f32_dpp v206, v224, v206 wave_shr:1 row_mask:0xf bank_mask:0xf bound_ctrl:1
	v_add_f32_dpp v207, v225, v207 wave_shr:1 row_mask:0xf bank_mask:0xf bound_ctrl:1
	v_add_f32_dpp v210, v226, v210 wave_shr:1 row_mask:0xf bank_mask:0xf bound_ctrl:1
	v_pk_fma_f32 v[202:203], v[40:41], v[218:219], v[202:203] op_sel_hi:[1,0,1] neg_lo:[0,0,1] neg_hi:[0,0,1]
	v_pk_fma_f32 v[206:207], v[42:43], v[218:219], v[206:207] op_sel_hi:[1,0,1] neg_lo:[0,0,1] neg_hi:[0,0,1]
	v_fma_f32 v210, v44, v218, -v210
	v_pk_add_f32 v[202:203], v[202:203], v[228:229] neg_lo:[0,1] neg_hi:[0,1]
	v_pk_add_f32 v[206:207], v[206:207], v[230:231] neg_lo:[0,1] neg_hi:[0,1]
	v_add_f32_e64 v210, v210, -v232
	v_pk_mul_f32 v[234:235], v[202:203], v[202:203]
	v_pk_fma_f32 v[234:235], v[206:207], v[206:207], v[234:235]
	v_add_f32_e32 v234, v234, v235
	v_fma_f32 v234, v210, v210, v234
	v_cndmask_b32_e64 v235, 0, v234, s[12:13]
	v_add_f32_e32 v0, v0, v235
	s_add_i32 s4, s34, 11
	s_min_i32 s4, s4, 0x200
	s_mul_i32 s5, s4, 0x804
	s_add_i32 s5, s5, s35
	s_add_i32 s6, s5, 0x0
	s_add_i32 s7, s5, 0x101004
	s_add_i32 s8, s5, 0x202008
	s_add_i32 s11, s5, 0x30300c
	s_add_i32 s15, s5, 0x404010
	s_mul_i32 s9, s4, 0x180c
	s_add_i32 s9, s9, s33
	buffer_load_dword v40, v28, s[16:19], s6 offen nt
	buffer_load_dword v41, v28, s[16:19], s7 offen nt
	buffer_load_dword v42, v28, s[16:19], s8 offen nt
	buffer_load_dword v43, v28, s[16:19], s11 offen nt
	buffer_load_dword v44, v28, s[16:19], s15 offen nt
	buffer_load_dwordx3 v[48:50], v27, s[24:27], s9 offen nt
	s_waitcnt vmcnt(12)
	v_mov_b32_dpp v68, v32 wave_shr:1 row_mask:0xf bank_mask:0xf bound_ctrl:1
	v_mov_b32_dpp v69, v33 wave_shr:1 row_mask:0xf bank_mask:0xf bound_ctrl:1
	v_mov_b32_dpp v70, v34 wave_shr:1 row_mask:0xf bank_mask:0xf bound_ctrl:1
	v_mov_b32_dpp v80, v32 wave_shl:1 row_mask:0xf bank_mask:0xf bound_ctrl:1
	v_mov_b32_dpp v81, v33 wave_shl:1 row_mask:0xf bank_mask:0xf bound_ctrl:1
	v_mov_b32_dpp v82, v34 wave_shl:1 row_mask:0xf bank_mask:0xf bound_ctrl:1
	v_mov_b32_dpp v88, v12 wave_shr:1 row_mask:0xf bank_mask:0xf bound_ctrl:1
	v_mov_b32_dpp v89, v13 wave_shr:1 row_mask:0xf bank_mask:0xf bound_ctrl:1
	v_mov_b32_dpp v90, v14 wave_shr:1 row_mask:0xf bank_mask:0xf bound_ctrl:1
	v_mov_b32_dpp v91, v15 wave_shr:1 row_mask:0xf bank_mask:0xf bound_ctrl:1
	v_mov_b32_dpp v92, v16 wave_shr:1 row_mask:0xf bank_mask:0xf bound_ctrl:1
	v_mov_b32_dpp v94, v12 wave_shl:1 row_mask:0xf bank_mask:0xf bound_ctrl:1
	v_mov_b32_dpp v95, v13 wave_shl:1 row_mask:0xf bank_mask:0xf bound_ctrl:1
	v_mov_b32_dpp v132, v14 wave_shl:1 row_mask:0xf bank_mask:0xf bound_ctrl:1
	v_mov_b32_dpp v133, v15 wave_shl:1 row_mask:0xf bank_mask:0xf bound_ctrl:1
	v_mov_b32_dpp v150, v16 wave_shl:1 row_mask:0xf bank_mask:0xf bound_ctrl:1
	v_pk_mul_f32 v[154:155], v[12:13], v[32:33] op_sel_hi:[1,0]
	v_pk_mul_f32 v[158:159], v[14:15], v[32:33] op_sel_hi:[1,0]
	v_mul_f32_e64 v160, v16, v32
	v_pk_mul_f32 v[164:165], v[12:13], v[32:33] op_sel:[0,1]
	v_pk_mul_f32 v[168:169], v[14:15], v[32:33] op_sel:[0,1]
	v_mul_f32_e64 v172, v16, v33
	v_pk_mul_f32 v[198:199], v[12:13], v[34:35] op_sel_hi:[1,0]
	v_pk_mul_f32 v[202:203], v[14:15], v[34:35] op_sel_hi:[1,0]
	v_mul_f32_e64 v206, v16, v34
	v_pk_add_f32 v[210:211], v[12:13], v[88:89]
	v_pk_add_f32 v[212:213], v[14:15], v[90:91]
	v_add_f32_e64 v214, v16, v92
	v_pk_fma_f32 v[154:155], v[88:89], v[68:69], v[154:155] op_sel_hi:[1,0,1]
	v_pk_fma_f32 v[158:159], v[90:91], v[68:69], v[158:159] op_sel_hi:[1,0,1]
	v_fma_f32 v160, v92, v68, v160
	v_pk_fma_f32 v[164:165], v[88:89], v[68:69], v[164:165] op_sel:[0,1,0]
	v_pk_fma_f32 v[168:169], v[90:91], v[68:69], v[168:169] op_sel:[0,1,0]
	v_fma_f32 v172, v92, v69, v172
	v_pk_fma_f32 v[198:199], v[88:89], v[70:71], v[198:199] op_sel_hi:[1,0,1]
	v_pk_fma_f32 v[202:203], v[90:91], v[70:71], v[202:203] op_sel_hi:[1,0,1]
	v_fma_f32 v206, v92, v70, v206
	v_pk_add_f32 v[210:211], v[210:211], v[94:95]
	v_pk_add_f32 v[212:213], v[212:213], v[132:133]
	v_add_f32_e64 v214, v214, v150
	v_pk_fma_f32 v[154:155], v[94:95], v[80:81], v[154:155] op_sel_hi:[1,0,1]
	v_pk_fma_f32 v[158:159], v[132:133], v[80:81], v[158:159] op_sel_hi:[1,0,1]
	v_fma_f32 v160, v150, v80, v160
	v_pk_fma_f32 v[164:165], v[94:95], v[80:81], v[164:165] op_sel:[0,1,0]
	v_pk_fma_f32 v[168:169], v[132:133], v[80:81], v[168:169] op_sel:[0,1,0]
	v_fma_f32 v172, v150, v81, v172
	v_pk_fma_f32 v[198:199], v[94:95], v[82:83], v[198:199] op_sel_hi:[1,0,1]
	v_pk_fma_f32 v[202:203], v[132:133], v[82:83], v[202:203] op_sel_hi:[1,0,1]
	v_fma_f32 v206, v150, v82, v206
	s_barrier
	ds_read_b128 v[88:91], v23 offset:3072
	ds_read_b128 v[92:95], v23 offset:4096
	ds_read_b128 v[216:219], v23 offset:5120
	v_pk_add_f32 v[132:133], v[46:47], v[210:211]
	v_pk_add_f32 v[46:47], v[140:141], v[212:213]
	v_add_f32_e64 v140, v144, v214
	v_pk_add_f32 v[144:145], v[146:147], v[154:155]
	v_pk_add_f32 v[146:147], v[96:97], v[158:159]
	v_add_f32_e64 v96, v98, v160
	v_pk_add_f32 v[98:99], v[100:101], v[164:165]
	v_pk_add_f32 v[100:101], v[102:103], v[168:169]
	v_add_f32_e64 v102, v104, v172
	v_pk_add_f32 v[104:105], v[110:111], v[198:199]
	v_pk_add_f32 v[110:111], v[112:113], v[202:203]
	v_add_f32_e64 v112, v114, v206
	s_waitcnt lgkmcnt(2)
	v_pk_fma_f32 v[144:145], v[88:89], v[132:133], v[144:145] op_sel_hi:[0,1,1] neg_lo:[1,0,0] neg_hi:[1,0,0]
	v_pk_fma_f32 v[146:147], v[88:89], v[46:47], v[146:147] op_sel_hi:[0,1,1] neg_lo:[1,0,0] neg_hi:[1,0,0]
	v_fma_f32 v96, -v88, v140, v96
	v_pk_fma_f32 v[98:99], v[88:89], v[132:133], v[98:99] op_sel:[1,0,0] neg_lo:[1,0,0] neg_hi:[1,0,0]
	v_pk_fma_f32 v[100:101], v[88:89], v[46:47], v[100:101] op_sel:[1,0,0] neg_lo:[1,0,0] neg_hi:[1,0,0]
	v_fma_f32 v102, -v89, v140, v102
	v_pk_fma_f32 v[104:105], v[90:91], v[132:133], v[104:105] op_sel_hi:[0,1,1] neg_lo:[1,0,0] neg_hi:[1,0,0]
	v_pk_fma_f32 v[110:111], v[90:91], v[46:47], v[110:111] op_sel_hi:[0,1,1] neg_lo:[1,0,0] neg_hi:[1,0,0]
	v_fma_f32 v112, -v90, v140, v112
	v_pk_mul_f32 v[114:115], v[90:91], v[144:145] op_sel:[1,0]
	v_pk_mul_f32 v[222:223], v[90:91], v[146:147] op_sel:[1,0]
	v_mul_f32_e64 v228, v91, v96
	s_waitcnt lgkmcnt(1)
	v_pk_mul_f32 v[150:151], v[92:93], v[144:145] op_sel_hi:[0,1]
	v_pk_mul_f32 v[224:225], v[92:93], v[146:147] op_sel_hi:[0,1]
	v_mul_f32_e64 v230, v92, v96
	v_pk_mul_f32 v[220:221], v[92:93], v[144:145] op_sel:[1,0]
	v_pk_mul_f32 v[226:227], v[92:93], v[146:147] op_sel:[1,0]
	v_mul_f32_e64 v232, v93, v96
	v_pk_fma_f32 v[114:115], v[92:93], v[98:99], v[114:115] op_sel_hi:[0,1,1]
	v_pk_fma_f32 v[222:223], v[92:93], v[100:101], v[222:223] op_sel_hi:[0,1,1]
	v_fma_f32 v228, v92, v102, v228
	v_pk_fma_f32 v[150:151], v[94:95], v[98:99], v[150:151] op_sel_hi:[0,1,1]
	v_pk_fma_f32 v[224:225], v[94:95], v[100:101], v[224:225] op_sel_hi:[0,1,1]
	v_fma_f32 v230, v94, v102, v230
	v_pk_fma_f32 v[220:221], v[94:95], v[98:99], v[220:221] op_sel:[1,0,0]
	v_pk_fma_f32 v[226:227], v[94:95], v[100:101], v[226:227] op_sel:[1,0,0]
	v_fma_f32 v232, v95, v102, v232
	v_pk_fma_f32 v[114:115], v[92:93], v[104:105], v[114:115] op_sel:[1,0,0]
	v_pk_fma_f32 v[222:223], v[92:93], v[110:111], v[222:223] op_sel:[1,0,0]
	v_fma_f32 v228, v93, v112, v228
	v_pk_fma_f32 v[150:151], v[94:95], v[104:105], v[150:151] op_sel:[1,0,0]
	v_pk_fma_f32 v[224:225], v[94:95], v[110:111], v[224:225] op_sel:[1,0,0]
	v_fma_f32 v230, v95, v112, v230
	s_waitcnt lgkmcnt(0)
	v_pk_fma_f32 v[220:221], v[216:217], v[104:105], v[220:221] op_sel_hi:[0,1,1]
	v_pk_fma_f32 v[226:227], v[216:217], v[110:111], v[226:227] op_sel_hi:[0,1,1]
	v_fma_f32 v232, v216, v112, v232
	v_pk_mul_f32 v[234:235], v[88:89], v[114:115] op_sel_hi:[0,1]
	v_pk_mul_f32 v[236:237], v[88:89], v[222:223] op_sel_hi:[0,1]
	v_mul_f32_e64 v238, v88, v228
	v_pk_fma_f32 v[234:235], v[88:89], v[150:151], v[234:235] op_sel:[1,0,0]
	v_pk_fma_f32 v[236:237], v[88:89], v[224:225], v[236:237] op_sel:[1,0,0]
	v_fma_f32 v238, v89, v230, v238
	v_pk_fma_f32 v[234:235], v[90:91], v[220:221], v[234:235] op_sel_hi:[0,1,1]
	v_pk_fma_f32 v[236:237], v[90:91], v[226:227], v[236:237] op_sel_hi:[0,1,1]
	v_fma_f32 v238, v90, v232, v238
	v_pk_fma_f32 v[234:235], v[216:217], v[132:133], v[234:235] op_sel:[1,0,0] neg_lo:[0,0,1] neg_hi:[0,0,1]
	v_pk_fma_f32 v[236:237], v[216:217], v[46:47], v[236:237] op_sel:[1,0,0] neg_lo:[0,0,1] neg_hi:[0,0,1]
	v_fma_f32 v238, v217, v140, -v238
	v_cmp_eq_u32_e64 s[10:11], 1, v219
	v_cmp_eq_u32_e64 s[14:15], 2, v219
	v_cmp_eq_u32_e64 s[20:21], 3, v219
	v_cmp_eq_u32_e64 s[22:23], 4, v219
	v_cmp_eq_u32_e64 s[30:31], 5, v219
	v_pk_add_f32 v[46:47], v[52:53], v[114:115]
	v_pk_add_f32 v[52:53], v[130:131], v[222:223]
	v_add_f32_e64 v96, v152, v228
	v_pk_add_f32 v[98:99], v[156:157], v[150:151]
	v_pk_add_f32 v[100:101], v[148:149], v[224:225]
	v_add_f32_e64 v102, v162, v230
	v_pk_add_f32 v[104:105], v[166:167], v[220:221]
	v_pk_add_f32 v[110:111], v[170:171], v[226:227]
	v_add_f32_e64 v112, v196, v232
	v_pk_add_f32 v[130:131], v[200:201], v[234:235]
	v_pk_add_f32 v[132:133], v[204:205], v[236:237]
	v_add_f32_e64 v140, v208, v238
	v_pk_fma_f32 v[144:145], v[56:57], v[46:47], v[130:131] op_sel_hi:[0,1,1]
	v_pk_fma_f32 v[146:147], v[56:57], v[52:53], v[132:133] op_sel_hi:[0,1,1]
	v_fma_f32 v148, v56, v96, v140
	v_pk_fma_f32 v[152:153], v[72:73], v[46:47], v[130:131] op_sel_hi:[0,1,1]
	v_pk_fma_f32 v[156:157], v[72:73], v[52:53], v[132:133] op_sel_hi:[0,1,1]
	v_fma_f32 v162, v72, v96, v140
	v_pk_fma_f32 v[144:145], v[56:57], v[98:99], v[144:145] op_sel:[1,0,0]
	v_pk_fma_f32 v[146:147], v[56:57], v[100:101], v[146:147] op_sel:[1,0,0]
	v_fma_f32 v148, v57, v102, v148
	v_pk_fma_f32 v[152:153], v[72:73], v[98:99], v[152:153] op_sel:[1,0,0]
	v_pk_fma_f32 v[156:157], v[72:73], v[100:101], v[156:157] op_sel:[1,0,0]
	v_fma_f32 v162, v73, v102, v162
	v_pk_fma_f32 v[144:145], v[58:59], v[104:105], v[144:145] op_sel_hi:[0,1,1]
	v_pk_fma_f32 v[146:147], v[58:59], v[110:111], v[146:147] op_sel_hi:[0,1,1]
	v_fma_f32 v148, v58, v112, v148
	v_pk_fma_f32 v[152:153], v[74:75], v[104:105], v[152:153] op_sel_hi:[0,1,1]
	v_pk_fma_f32 v[156:157], v[74:75], v[110:111], v[156:157] op_sel_hi:[0,1,1]
	v_fma_f32 v162, v74, v112, v162
	v_pk_fma_f32 v[130:131], v[64:65], v[46:47], v[130:131] op_sel_hi:[0,1,1]
	v_pk_fma_f32 v[132:133], v[64:65], v[52:53], v[132:133] op_sel_hi:[0,1,1]
	v_fma_f32 v140, v64, v96, v140
	v_pk_fma_f32 v[130:131], v[64:65], v[98:99], v[130:131] op_sel:[1,0,0]
	v_pk_fma_f32 v[132:133], v[64:65], v[100:101], v[132:133] op_sel:[1,0,0]
	v_fma_f32 v140, v65, v102, v140
	v_pk_fma_f32 v[130:131], v[66:67], v[104:105], v[130:131] op_sel_hi:[0,1,1]
	v_pk_fma_f32 v[132:133], v[66:67], v[110:111], v[132:133] op_sel_hi:[0,1,1]
	v_fma_f32 v140, v66, v112, v140
	v_cndmask_b32_e64 v166, 0, v1, s[10:11]
	v_cndmask_b32_e64 v167, 0, v1, s[14:15]
	v_cndmask_b32_e64 v170, 0, v1, s[20:21]
	v_cndmask_b32_e64 v171, 0, v1, s[22:23]
	v_cndmask_b32_e64 v196, 0, v1, s[30:31]
	v_add_f32_dpp v130, v144, v130 wave_shl:1 row_mask:0xf bank_mask:0xf bound_ctrl:1
	v_add_f32_dpp v131, v145, v131 wave_shl:1 row_mask:0xf bank_mask:0xf bound_ctrl:1
	v_add_f32_dpp v132, v146, v132 wave_shl:1 row_mask:0xf bank_mask:0xf bound_ctrl:1
	v_add_f32_dpp v133, v147, v133 wave_shl:1 row_mask:0xf bank_mask:0xf bound_ctrl:1
	v_add_f32_dpp v140, v148, v140 wave_shl:1 row_mask:0xf bank_mask:0xf bound_ctrl:1
	s_add_i32 s4, s34, 7
	s_cmpk_lt_i32 s4, 0x201
	s_cselect_b64 s[12:13], s[0:1], 0
	v_add_f32_dpp v130, v152, v130 wave_shr:1 row_mask:0xf bank_mask:0xf bound_ctrl:1
	v_add_f32_dpp v131, v153, v131 wave_shr:1 row_mask:0xf bank_mask:0xf bound_ctrl:1
	v_add_f32_dpp v132, v156, v132 wave_shr:1 row_mask:0xf bank_mask:0xf bound_ctrl:1
	v_add_f32_dpp v133, v157, v133 wave_shr:1 row_mask:0xf bank_mask:0xf bound_ctrl:1
	v_add_f32_dpp v140, v162, v140 wave_shr:1 row_mask:0xf bank_mask:0xf bound_ctrl:1
	v_pk_fma_f32 v[130:131], v[54:55], v[218:219], v[130:131] op_sel_hi:[1,0,1] neg_lo:[0,0,1] neg_hi:[0,0,1]
	v_pk_fma_f32 v[132:133], v[60:61], v[218:219], v[132:133] op_sel_hi:[1,0,1] neg_lo:[0,0,1] neg_hi:[0,0,1]
	v_fma_f32 v140, v62, v218, -v140
	v_pk_add_f32 v[130:131], v[130:131], v[166:167] neg_lo:[0,1] neg_hi:[0,1]
	v_pk_add_f32 v[132:133], v[132:133], v[170:171] neg_lo:[0,1] neg_hi:[0,1]
	v_add_f32_e64 v140, v140, -v196
	v_pk_mul_f32 v[200:201], v[130:131], v[130:131]
	v_pk_fma_f32 v[200:201], v[132:133], v[132:133], v[200:201]
	v_add_f32_e32 v200, v200, v201
	v_fma_f32 v200, v140, v140, v200
	v_cndmask_b32_e64 v201, 0, v200, s[12:13]
	v_add_f32_e32 v0, v0, v201
	s_waitcnt vmcnt(6)
	v_mov_b32_dpp v52, v36 wave_shr:1 row_mask:0xf bank_mask:0xf bound_ctrl:1
	v_mov_b32_dpp v53, v37 wave_shr:1 row_mask:0xf bank_mask:0xf bound_ctrl:1
	v_mov_b32_dpp v54, v38 wave_shr:1 row_mask:0xf bank_mask:0xf bound_ctrl:1
	v_mov_b32_dpp v56, v36 wave_shl:1 row_mask:0xf bank_mask:0xf bound_ctrl:1
	v_mov_b32_dpp v57, v37 wave_shl:1 row_mask:0xf bank_mask:0xf bound_ctrl:1
	v_mov_b32_dpp v58, v38 wave_shl:1 row_mask:0xf bank_mask:0xf bound_ctrl:1
	v_mov_b32_dpp v46, v20 wave_shr:1 row_mask:0xf bank_mask:0xf bound_ctrl:1
	v_mov_b32_dpp v47, v21 wave_shr:1 row_mask:0xf bank_mask:0xf bound_ctrl:1
	v_mov_b32_dpp v60, v24 wave_shr:1 row_mask:0xf bank_mask:0xf bound_ctrl:1
	v_mov_b32_dpp v61, v25 wave_shr:1 row_mask:0xf bank_mask:0xf bound_ctrl:1
	v_mov_b32_dpp v62, v30 wave_shr:1 row_mask:0xf bank_mask:0xf bound_ctrl:1
	v_mov_b32_dpp v64, v20 wave_shl:1 row_mask:0xf bank_mask:0xf bound_ctrl:1
	v_mov_b32_dpp v65, v21 wave_shl:1 row_mask:0xf bank_mask:0xf bound_ctrl:1
	v_mov_b32_dpp v66, v24 wave_shl:1 row_mask:0xf bank_mask:0xf bound_ctrl:1
	v_mov_b32_dpp v67, v25 wave_shl:1 row_mask:0xf bank_mask:0xf bound_ctrl:1
	v_mov_b32_dpp v72, v30 wave_shl:1 row_mask:0xf bank_mask:0xf bound_ctrl:1
	v_pk_mul_f32 v[74:75], v[20:21], v[36:37] op_sel_hi:[1,0]
	v_pk_mul_f32 v[88:89], v[24:25], v[36:37] op_sel_hi:[1,0]
	v_mul_f32_e64 v90, v30, v36
	v_pk_mul_f32 v[92:93], v[20:21], v[36:37] op_sel:[0,1]
	v_pk_mul_f32 v[94:95], v[24:25], v[36:37] op_sel:[0,1]
	v_mul_f32_e64 v96, v30, v37
	v_pk_mul_f32 v[98:99], v[20:21], v[38:39] op_sel_hi:[1,0]
	v_pk_mul_f32 v[100:101], v[24:25], v[38:39] op_sel_hi:[1,0]
	v_mul_f32_e64 v102, v30, v38
	v_pk_add_f32 v[104:105], v[20:21], v[46:47]
	v_pk_add_f32 v[110:111], v[24:25], v[60:61]
	v_add_f32_e64 v112, v30, v62
	v_pk_fma_f32 v[74:75], v[46:47], v[52:53], v[74:75] op_sel_hi:[1,0,1]
	v_pk_fma_f32 v[88:89], v[60:61], v[52:53], v[88:89] op_sel_hi:[1,0,1]
	v_fma_f32 v90, v62, v52, v90
	v_pk_fma_f32 v[92:93], v[46:47], v[52:53], v[92:93] op_sel:[0,1,0]
	v_pk_fma_f32 v[94:95], v[60:61], v[52:53], v[94:95] op_sel:[0,1,0]
	v_fma_f32 v96, v62, v53, v96
	v_pk_fma_f32 v[98:99], v[46:47], v[54:55], v[98:99] op_sel_hi:[1,0,1]
	v_pk_fma_f32 v[100:101], v[60:61], v[54:55], v[100:101] op_sel_hi:[1,0,1]
	v_fma_f32 v102, v62, v54, v102
	v_pk_add_f32 v[104:105], v[104:105], v[64:65]
	v_pk_add_f32 v[110:111], v[110:111], v[66:67]
	v_add_f32_e64 v112, v112, v72
	v_pk_fma_f32 v[74:75], v[64:65], v[56:57], v[74:75] op_sel_hi:[1,0,1]
	v_pk_fma_f32 v[88:89], v[66:67], v[56:57], v[88:89] op_sel_hi:[1,0,1]
	v_fma_f32 v90, v72, v56, v90
	v_pk_fma_f32 v[92:93], v[64:65], v[56:57], v[92:93] op_sel:[0,1,0]
	v_pk_fma_f32 v[94:95], v[66:67], v[56:57], v[94:95] op_sel:[0,1,0]
	v_fma_f32 v96, v72, v57, v96
	v_pk_fma_f32 v[98:99], v[64:65], v[58:59], v[98:99] op_sel_hi:[1,0,1]
	v_pk_fma_f32 v[100:101], v[66:67], v[58:59], v[100:101] op_sel_hi:[1,0,1]
	v_fma_f32 v102, v72, v58, v102
	s_barrier
	ds_read_b128 v[60:63], v23 offset:0
	ds_read_b128 v[64:67], v23 offset:1024
	ds_read_b128 v[144:147], v23 offset:2048
	v_pk_add_f32 v[46:47], v[210:211], v[104:105]
	v_pk_add_f32 v[72:73], v[134:135], v[46:47]
	v_pk_add_f32 v[130:131], v[212:213], v[110:111]
	v_pk_add_f32 v[132:133], v[136:137], v[130:131]
	v_add_f32_e64 v134, v214, v112
	v_add_f32_e64 v136, v142, v134
	v_pk_add_f32 v[140:141], v[154:155], v[74:75]
	v_pk_add_f32 v[142:143], v[106:107], v[140:141]
	v_pk_add_f32 v[106:107], v[158:159], v[88:89]
	v_pk_add_f32 v[148:149], v[108:109], v[106:107]
	v_add_f32_e64 v108, v160, v90
	v_add_f32_e64 v152, v116, v108
	v_pk_add_f32 v[116:117], v[164:165], v[92:93]
	v_pk_add_f32 v[154:155], v[118:119], v[116:117]
	v_pk_add_f32 v[118:119], v[168:169], v[94:95]
	v_pk_add_f32 v[156:157], v[120:121], v[118:119]
	v_add_f32_e64 v120, v172, v96
	v_add_f32_e64 v158, v122, v120
	v_pk_add_f32 v[122:123], v[198:199], v[98:99]
	v_pk_add_f32 v[160:161], v[124:125], v[122:123]
	v_pk_add_f32 v[124:125], v[202:203], v[100:101]
	v_pk_add_f32 v[162:163], v[126:127], v[124:125]
	v_add_f32_e64 v126, v206, v102
	v_add_f32_e64 v164, v128, v126
	s_waitcnt lgkmcnt(2)
	v_pk_fma_f32 v[142:143], v[60:61], v[72:73], v[142:143] op_sel_hi:[0,1,1] neg_lo:[1,0,0] neg_hi:[1,0,0]
	v_pk_fma_f32 v[148:149], v[60:61], v[132:133], v[148:149] op_sel_hi:[0,1,1] neg_lo:[1,0,0] neg_hi:[1,0,0]
	v_fma_f32 v152, -v60, v136, v152
	v_pk_fma_f32 v[154:155], v[60:61], v[72:73], v[154:155] op_sel:[1,0,0] neg_lo:[1,0,0] neg_hi:[1,0,0]
	v_pk_fma_f32 v[156:157], v[60:61], v[132:133], v[156:157] op_sel:[1,0,0] neg_lo:[1,0,0] neg_hi:[1,0,0]
	v_fma_f32 v158, -v61, v136, v158
	v_pk_fma_f32 v[160:161], v[62:63], v[72:73], v[160:161] op_sel_hi:[0,1,1] neg_lo:[1,0,0] neg_hi:[1,0,0]
	v_pk_fma_f32 v[162:163], v[62:63], v[132:133], v[162:163] op_sel_hi:[0,1,1] neg_lo:[1,0,0] neg_hi:[1,0,0]
	v_fma_f32 v164, -v62, v136, v164
	v_pk_mul_f32 v[128:129], v[62:63], v[142:143] op_sel:[1,0]
	v_pk_mul_f32 v[170:171], v[62:63], v[148:149] op_sel:[1,0]
	v_mul_f32_e64 v198, v63, v152
	s_waitcnt lgkmcnt(1)
	v_pk_mul_f32 v[166:167], v[64:65], v[142:143] op_sel_hi:[0,1]
	v_pk_mul_f32 v[172:173], v[64:65], v[148:149] op_sel_hi:[0,1]
	v_mul_f32_e64 v200, v64, v152
	v_pk_mul_f32 v[168:169], v[64:65], v[142:143] op_sel:[1,0]
	v_pk_mul_f32 v[196:197], v[64:65], v[148:149] op_sel:[1,0]
	v_mul_f32_e64 v202, v65, v152
	v_pk_fma_f32 v[128:129], v[64:65], v[154:155], v[128:129] op_sel_hi:[0,1,1]
	v_pk_fma_f32 v[170:171], v[64:65], v[156:157], v[170:171] op_sel_hi:[0,1,1]
	v_fma_f32 v198, v64, v158, v198
	v_pk_fma_f32 v[166:167], v[66:67], v[154:155], v[166:167] op_sel_hi:[0,1,1]
	v_pk_fma_f32 v[172:173], v[66:67], v[156:157], v[172:173] op_sel_hi:[0,1,1]
	v_fma_f32 v200, v66, v158, v200
	v_pk_fma_f32 v[168:169], v[66:67], v[154:155], v[168:169] op_sel:[1,0,0]
	v_pk_fma_f32 v[196:197], v[66:67], v[156:157], v[196:197] op_sel:[1,0,0]
	v_fma_f32 v202, v67, v158, v202
	v_pk_fma_f32 v[128:129], v[64:65], v[160:161], v[128:129] op_sel:[1,0,0]
	v_pk_fma_f32 v[170:171], v[64:65], v[162:163], v[170:171] op_sel:[1,0,0]
	v_fma_f32 v198, v65, v164, v198
	v_pk_fma_f32 v[166:167], v[66:67], v[160:161], v[166:167] op_sel:[1,0,0]
	v_pk_fma_f32 v[172:173], v[66:67], v[162:163], v[172:173] op_sel:[1,0,0]
	v_fma_f32 v200, v67, v164, v200
	s_waitcnt lgkmcnt(0)
	v_pk_fma_f32 v[168:169], v[144:145], v[160:161], v[168:169] op_sel_hi:[0,1,1]
	v_pk_fma_f32 v[196:197], v[144:145], v[162:163], v[196:197] op_sel_hi:[0,1,1]
	v_fma_f32 v202, v144, v164, v202
	v_pk_mul_f32 v[204:205], v[60:61], v[128:129] op_sel_hi:[0,1]
	v_pk_mul_f32 v[206:207], v[60:61], v[170:171] op_sel_hi:[0,1]
	v_mul_f32_e64 v208, v60, v198
	v_pk_fma_f32 v[204:205], v[60:61], v[166:167], v[204:205] op_sel:[1,0,0]
	v_pk_fma_f32 v[206:207], v[60:61], v[172:173], v[206:207] op_sel:[1,0,0]
	v_fma_f32 v208, v61, v200, v208
	v_pk_fma_f32 v[204:205], v[62:63], v[168:169], v[204:205] op_sel_hi:[0,1,1]
	v_pk_fma_f32 v[206:207], v[62:63], v[196:197], v[206:207] op_sel_hi:[0,1,1]
	v_fma_f32 v208, v62, v202, v208
	v_pk_fma_f32 v[204:205], v[144:145], v[72:73], v[204:205] op_sel:[1,0,0] neg_lo:[0,0,1] neg_hi:[0,0,1]
	v_pk_fma_f32 v[206:207], v[144:145], v[132:133], v[206:207] op_sel:[1,0,0] neg_lo:[0,0,1] neg_hi:[0,0,1]
	v_fma_f32 v208, v145, v136, -v208
	v_cmp_eq_u32_e64 s[10:11], 1, v147
	v_cmp_eq_u32_e64 s[14:15], 2, v147
	v_cmp_eq_u32_e64 s[20:21], 3, v147
	v_cmp_eq_u32_e64 s[22:23], 4, v147
	v_cmp_eq_u32_e64 s[30:31], 5, v147
	v_pk_add_f32 v[72:73], v[114:115], v[128:129]
	v_pk_add_f32 v[132:133], v[138:139], v[72:73]
	v_pk_add_f32 v[114:115], v[222:223], v[170:171]
	v_pk_add_f32 v[136:137], v[178:179], v[114:115]
	v_add_f32_e64 v138, v228, v198
	v_add_f32_e64 v142, v184, v138
	v_pk_add_f32 v[148:149], v[150:151], v[166:167]
	v_pk_add_f32 v[152:153], v[174:175], v[148:149]
	v_pk_add_f32 v[150:151], v[224:225], v[172:173]
	v_pk_add_f32 v[154:155], v[180:181], v[150:151]
	v_add_f32_e64 v156, v230, v200
	v_add_f32_e64 v158, v186, v156
	v_pk_add_f32 v[160:161], v[220:221], v[168:169]
	v_pk_add_f32 v[162:163], v[176:177], v[160:161]
	v_pk_add_f32 v[164:165], v[226:227], v[196:197]
	v_pk_add_f32 v[174:175], v[182:183], v[164:165]
	v_add_f32_e64 v176, v232, v202
	v_add_f32_e64 v178, v188, v176
	v_pk_add_f32 v[180:181], v[234:235], v[204:205]
	v_pk_add_f32 v[182:183], v[190:191], v[180:181]
	v_pk_add_f32 v[184:185], v[236:237], v[206:207]
	v_pk_add_f32 v[186:187], v[192:193], v[184:185]
	v_add_f32_e64 v188, v238, v208
	v_add_f32_e64 v190, v194, v188
	v_pk_fma_f32 v[192:193], v[76:77], v[132:133], v[182:183] op_sel_hi:[0,1,1]
	v_pk_fma_f32 v[194:195], v[76:77], v[136:137], v[186:187] op_sel_hi:[0,1,1]
	v_fma_f32 v210, v76, v142, v190
	v_pk_fma_f32 v[212:213], v[84:85], v[132:133], v[182:183] op_sel_hi:[0,1,1]
	v_pk_fma_f32 v[214:215], v[84:85], v[136:137], v[186:187] op_sel_hi:[0,1,1]
	v_fma_f32 v216, v84, v142, v190
	v_pk_fma_f32 v[192:193], v[76:77], v[152:153], v[192:193] op_sel:[1,0,0]
	v_pk_fma_f32 v[194:195], v[76:77], v[154:155], v[194:195] op_sel:[1,0,0]
	v_fma_f32 v210, v77, v158, v210
	v_pk_fma_f32 v[212:213], v[84:85], v[152:153], v[212:213] op_sel:[1,0,0]
	v_pk_fma_f32 v[214:215], v[84:85], v[154:155], v[214:215] op_sel:[1,0,0]
	v_fma_f32 v216, v85, v158, v216
	v_pk_fma_f32 v[192:193], v[78:79], v[162:163], v[192:193] op_sel_hi:[0,1,1]
	v_pk_fma_f32 v[194:195], v[78:79], v[174:175], v[194:195] op_sel_hi:[0,1,1]
	v_fma_f32 v210, v78, v178, v210
	v_pk_fma_f32 v[212:213], v[86:87], v[162:163], v[212:213] op_sel_hi:[0,1,1]
	v_pk_fma_f32 v[214:215], v[86:87], v[174:175], v[214:215] op_sel_hi:[0,1,1]
	v_fma_f32 v216, v86, v178, v216
	v_pk_fma_f32 v[182:183], v[8:9], v[132:133], v[182:183] op_sel_hi:[0,1,1]
	v_pk_fma_f32 v[186:187], v[8:9], v[136:137], v[186:187] op_sel_hi:[0,1,1]
	v_fma_f32 v190, v8, v142, v190
	v_pk_fma_f32 v[182:183], v[8:9], v[152:153], v[182:183] op_sel:[1,0,0]
	v_pk_fma_f32 v[186:187], v[8:9], v[154:155], v[186:187] op_sel:[1,0,0]
	v_fma_f32 v190, v9, v158, v190
	v_pk_fma_f32 v[182:183], v[10:11], v[162:163], v[182:183] op_sel_hi:[0,1,1]
	v_pk_fma_f32 v[186:187], v[10:11], v[174:175], v[186:187] op_sel_hi:[0,1,1]
	v_fma_f32 v190, v10, v178, v190
	v_cndmask_b32_e64 v218, 0, v1, s[10:11]
	v_cndmask_b32_e64 v219, 0, v1, s[14:15]
	v_cndmask_b32_e64 v220, 0, v1, s[20:21]
	v_cndmask_b32_e64 v221, 0, v1, s[22:23]
	v_cndmask_b32_e64 v222, 0, v1, s[30:31]
	v_add_f32_dpp v182, v192, v182 wave_shl:1 row_mask:0xf bank_mask:0xf bound_ctrl:1
	v_add_f32_dpp v183, v193, v183 wave_shl:1 row_mask:0xf bank_mask:0xf bound_ctrl:1
	v_add_f32_dpp v186, v194, v186 wave_shl:1 row_mask:0xf bank_mask:0xf bound_ctrl:1
	v_add_f32_dpp v187, v195, v187 wave_shl:1 row_mask:0xf bank_mask:0xf bound_ctrl:1
	v_add_f32_dpp v190, v210, v190 wave_shl:1 row_mask:0xf bank_mask:0xf bound_ctrl:1
	s_add_i32 s4, s34, 8
	s_cmpk_lt_i32 s4, 0x201
	s_cselect_b64 s[12:13], s[0:1], 0
	v_add_f32_dpp v182, v212, v182 wave_shr:1 row_mask:0xf bank_mask:0xf bound_ctrl:1
	v_add_f32_dpp v183, v213, v183 wave_shr:1 row_mask:0xf bank_mask:0xf bound_ctrl:1
	v_add_f32_dpp v186, v214, v186 wave_shr:1 row_mask:0xf bank_mask:0xf bound_ctrl:1
	v_add_f32_dpp v187, v215, v187 wave_shr:1 row_mask:0xf bank_mask:0xf bound_ctrl:1
	v_add_f32_dpp v190, v216, v190 wave_shr:1 row_mask:0xf bank_mask:0xf bound_ctrl:1
	v_pk_fma_f32 v[182:183], v[2:3], v[146:147], v[182:183] op_sel_hi:[1,0,1] neg_lo:[0,0,1] neg_hi:[0,0,1]
	v_pk_fma_f32 v[186:187], v[4:5], v[146:147], v[186:187] op_sel_hi:[1,0,1] neg_lo:[0,0,1] neg_hi:[0,0,1]
	v_fma_f32 v190, v6, v146, -v190
	v_pk_add_f32 v[182:183], v[182:183], v[218:219] neg_lo:[0,1] neg_hi:[0,1]
	v_pk_add_f32 v[186:187], v[186:187], v[220:221] neg_lo:[0,1] neg_hi:[0,1]
	v_add_f32_e64 v190, v190, -v222
	v_pk_mul_f32 v[224:225], v[182:183], v[182:183]
	v_pk_fma_f32 v[224:225], v[186:187], v[186:187], v[224:225]
	v_add_f32_e32 v224, v224, v225
	v_fma_f32 v224, v190, v190, v224
	v_cndmask_b32_e64 v225, 0, v224, s[12:13]
	v_add_f32_e32 v0, v0, v225
	s_waitcnt vmcnt(0)
	v_mov_b32_dpp v4, v48 wave_shr:1 row_mask:0xf bank_mask:0xf bound_ctrl:1
	v_mov_b32_dpp v5, v49 wave_shr:1 row_mask:0xf bank_mask:0xf bound_ctrl:1
	v_mov_b32_dpp v6, v50 wave_shr:1 row_mask:0xf bank_mask:0xf bound_ctrl:1
	v_mov_b32_dpp v8, v48 wave_shl:1 row_mask:0xf bank_mask:0xf bound_ctrl:1
	v_mov_b32_dpp v9, v49 wave_shl:1 row_mask:0xf bank_mask:0xf bound_ctrl:1
	v_mov_b32_dpp v10, v50 wave_shl:1 row_mask:0xf bank_mask:0xf bound_ctrl:1
	v_mov_b32_dpp v2, v40 wave_shr:1 row_mask:0xf bank_mask:0xf bound_ctrl:1
	v_mov_b32_dpp v3, v41 wave_shr:1 row_mask:0xf bank_mask:0xf bound_ctrl:1
	v_mov_b32_dpp v60, v42 wave_shr:1 row_mask:0xf bank_mask:0xf bound_ctrl:1
	v_mov_b32_dpp v61, v43 wave_shr:1 row_mask:0xf bank_mask:0xf bound_ctrl:1
	v_mov_b32_dpp v62, v44 wave_shr:1 row_mask:0xf bank_mask:0xf bound_ctrl:1
	v_mov_b32_dpp v64, v40 wave_shl:1 row_mask:0xf bank_mask:0xf bound_ctrl:1
	v_mov_b32_dpp v65, v41 wave_shl:1 row_mask:0xf bank_mask:0xf bound_ctrl:1
	v_mov_b32_dpp v66, v42 wave_shl:1 row_mask:0xf bank_mask:0xf bound_ctrl:1
	v_mov_b32_dpp v67, v43 wave_shl:1 row_mask:0xf bank_mask:0xf bound_ctrl:1
	v_mov_b32_dpp v76, v44 wave_shl:1 row_mask:0xf bank_mask:0xf bound_ctrl:1
	v_pk_mul_f32 v[78:79], v[40:41], v[48:49] op_sel_hi:[1,0]
	v_pk_mul_f32 v[84:85], v[42:43], v[48:49] op_sel_hi:[1,0]
	v_mul_f32_e64 v86, v44, v48
	v_pk_mul_f32 v[132:133], v[40:41], v[48:49] op_sel:[0,1]
	v_pk_mul_f32 v[136:137], v[42:43], v[48:49] op_sel:[0,1]
	v_mul_f32_e64 v142, v44, v49
	v_pk_mul_f32 v[144:145], v[40:41], v[50:51] op_sel_hi:[1,0]
	v_pk_mul_f32 v[146:147], v[42:43], v[50:51] op_sel_hi:[1,0]
	v_mul_f32_e64 v152, v44, v50
	v_pk_add_f32 v[154:155], v[40:41], v[2:3]
	v_pk_add_f32 v[158:159], v[42:43], v[60:61]
	v_add_f32_e64 v162, v44, v62
	v_pk_fma_f32 v[78:79], v[2:3], v[4:5], v[78:79] op_sel_hi:[1,0,1]
	v_pk_fma_f32 v[84:85], v[60:61], v[4:5], v[84:85] op_sel_hi:[1,0,1]
	v_fma_f32 v86, v62, v4, v86
	v_pk_fma_f32 v[132:133], v[2:3], v[4:5], v[132:133] op_sel:[0,1,0]
	v_pk_fma_f32 v[136:137], v[60:61], v[4:5], v[136:137] op_sel:[0,1,0]
	v_fma_f32 v142, v62, v5, v142
	v_pk_fma_f32 v[144:145], v[2:3], v[6:7], v[144:145] op_sel_hi:[1,0,1]
	v_pk_fma_f32 v[146:147], v[60:61], v[6:7], v[146:147] op_sel_hi:[1,0,1]
	v_fma_f32 v152, v62, v6, v152
	v_pk_add_f32 v[154:155], v[154:155], v[64:65]
	v_pk_add_f32 v[158:159], v[158:159], v[66:67]
	v_add_f32_e64 v162, v162, v76
	v_pk_fma_f32 v[78:79], v[64:65], v[8:9], v[78:79] op_sel_hi:[1,0,1]
	v_pk_fma_f32 v[84:85], v[66:67], v[8:9], v[84:85] op_sel_hi:[1,0,1]
	v_fma_f32 v86, v76, v8, v86
	v_pk_fma_f32 v[132:133], v[64:65], v[8:9], v[132:133] op_sel:[0,1,0]
	v_pk_fma_f32 v[136:137], v[66:67], v[8:9], v[136:137] op_sel:[0,1,0]
	v_fma_f32 v142, v76, v9, v142
	v_pk_fma_f32 v[144:145], v[64:65], v[10:11], v[144:145] op_sel_hi:[1,0,1]
	v_pk_fma_f32 v[146:147], v[66:67], v[10:11], v[146:147] op_sel_hi:[1,0,1]
	v_fma_f32 v152, v76, v10, v152
	s_barrier
	ds_read_b128 v[60:63], v23 offset:3072
	ds_read_b128 v[64:67], v23 offset:4096
	ds_read_b128 v[192:195], v23 offset:5120
	v_pk_add_f32 v[2:3], v[46:47], v[154:155]
	v_pk_add_f32 v[46:47], v[130:131], v[158:159]
	v_add_f32_e64 v76, v134, v162
	v_pk_add_f32 v[130:131], v[140:141], v[78:79]
	v_pk_add_f32 v[134:135], v[106:107], v[84:85]
	v_add_f32_e64 v106, v108, v86
	v_pk_add_f32 v[108:109], v[116:117], v[132:133]
	v_pk_add_f32 v[116:117], v[118:119], v[136:137]
	v_add_f32_e64 v118, v120, v142
	v_pk_add_f32 v[120:121], v[122:123], v[144:145]
	v_pk_add_f32 v[122:123], v[124:125], v[146:147]
	v_add_f32_e64 v124, v126, v152
	s_waitcnt lgkmcnt(2)
	v_pk_fma_f32 v[130:131], v[60:61], v[2:3], v[130:131] op_sel_hi:[0,1,1] neg_lo:[1,0,0] neg_hi:[1,0,0]
	v_pk_fma_f32 v[134:135], v[60:61], v[46:47], v[134:135] op_sel_hi:[0,1,1] neg_lo:[1,0,0] neg_hi:[1,0,0]
	v_fma_f32 v106, -v60, v76, v106
	v_pk_fma_f32 v[108:109], v[60:61], v[2:3], v[108:109] op_sel:[1,0,0] neg_lo:[1,0,0] neg_hi:[1,0,0]
	v_pk_fma_f32 v[116:117], v[60:61], v[46:47], v[116:117] op_sel:[1,0,0] neg_lo:[1,0,0] neg_hi:[1,0,0]
	v_fma_f32 v118, -v61, v76, v118
	v_pk_fma_f32 v[120:121], v[62:63], v[2:3], v[120:121] op_sel_hi:[0,1,1] neg_lo:[1,0,0] neg_hi:[1,0,0]
	v_pk_fma_f32 v[122:123], v[62:63], v[46:47], v[122:123] op_sel_hi:[0,1,1] neg_lo:[1,0,0] neg_hi:[1,0,0]
	v_fma_f32 v124, -v62, v76, v124
	v_pk_mul_f32 v[126:127], v[62:63], v[130:131] op_sel:[1,0]
	v_pk_mul_f32 v[178:179], v[62:63], v[134:135] op_sel:[1,0]
	v_mul_f32_e64 v190, v63, v106
	s_waitcnt lgkmcnt(1)
	v_pk_mul_f32 v[140:141], v[64:65], v[130:131] op_sel_hi:[0,1]
	v_pk_mul_f32 v[182:183], v[64:65], v[134:135] op_sel_hi:[0,1]
	v_mul_f32_e64 v210, v64, v106
	v_pk_mul_f32 v[174:175], v[64:65], v[130:131] op_sel:[1,0]
	v_pk_mul_f32 v[186:187], v[64:65], v[134:135] op_sel:[1,0]
	v_mul_f32_e64 v212, v65, v106
	v_pk_fma_f32 v[126:127], v[64:65], v[108:109], v[126:127] op_sel_hi:[0,1,1]
	v_pk_fma_f32 v[178:179], v[64:65], v[116:117], v[178:179] op_sel_hi:[0,1,1]
	v_fma_f32 v190, v64, v118, v190
	v_pk_fma_f32 v[140:141], v[66:67], v[108:109], v[140:141] op_sel_hi:[0,1,1]
	v_pk_fma_f32 v[182:183], v[66:67], v[116:117], v[182:183] op_sel_hi:[0,1,1]
	v_fma_f32 v210, v66, v118, v210
	v_pk_fma_f32 v[174:175], v[66:67], v[108:109], v[174:175] op_sel:[1,0,0]
	v_pk_fma_f32 v[186:187], v[66:67], v[116:117], v[186:187] op_sel:[1,0,0]
	v_fma_f32 v212, v67, v118, v212
	v_pk_fma_f32 v[126:127], v[64:65], v[120:121], v[126:127] op_sel:[1,0,0]
	v_pk_fma_f32 v[178:179], v[64:65], v[122:123], v[178:179] op_sel:[1,0,0]
	v_fma_f32 v190, v65, v124, v190
	v_pk_fma_f32 v[140:141], v[66:67], v[120:121], v[140:141] op_sel:[1,0,0]
	v_pk_fma_f32 v[182:183], v[66:67], v[122:123], v[182:183] op_sel:[1,0,0]
	v_fma_f32 v210, v67, v124, v210
	s_waitcnt lgkmcnt(0)
	v_pk_fma_f32 v[174:175], v[192:193], v[120:121], v[174:175] op_sel_hi:[0,1,1]
	v_pk_fma_f32 v[186:187], v[192:193], v[122:123], v[186:187] op_sel_hi:[0,1,1]
	v_fma_f32 v212, v192, v124, v212
	v_pk_mul_f32 v[214:215], v[60:61], v[126:127] op_sel_hi:[0,1]
	v_pk_mul_f32 v[216:217], v[60:61], v[178:179] op_sel_hi:[0,1]
	v_mul_f32_e64 v218, v60, v190
	v_pk_fma_f32 v[214:215], v[60:61], v[140:141], v[214:215] op_sel:[1,0,0]
	v_pk_fma_f32 v[216:217], v[60:61], v[182:183], v[216:217] op_sel:[1,0,0]
	v_fma_f32 v218, v61, v210, v218
	v_pk_fma_f32 v[214:215], v[62:63], v[174:175], v[214:215] op_sel_hi:[0,1,1]
	v_pk_fma_f32 v[216:217], v[62:63], v[186:187], v[216:217] op_sel_hi:[0,1,1]
	v_fma_f32 v218, v62, v212, v218
	v_pk_fma_f32 v[214:215], v[192:193], v[2:3], v[214:215] op_sel:[1,0,0] neg_lo:[0,0,1] neg_hi:[0,0,1]
	v_pk_fma_f32 v[216:217], v[192:193], v[46:47], v[216:217] op_sel:[1,0,0] neg_lo:[0,0,1] neg_hi:[0,0,1]
	v_fma_f32 v218, v193, v76, -v218
	v_cmp_eq_u32_e64 s[10:11], 1, v195
	v_cmp_eq_u32_e64 s[14:15], 2, v195
	v_cmp_eq_u32_e64 s[20:21], 3, v195
	v_cmp_eq_u32_e64 s[22:23], 4, v195
	v_cmp_eq_u32_e64 s[30:31], 5, v195
	v_pk_add_f32 v[2:3], v[72:73], v[126:127]
	v_pk_add_f32 v[46:47], v[114:115], v[178:179]
	v_add_f32_e64 v72, v138, v190
	v_pk_add_f32 v[76:77], v[148:149], v[140:141]
	v_pk_add_f32 v[106:107], v[150:151], v[182:183]
	v_add_f32_e64 v108, v156, v210
	v_pk_add_f32 v[114:115], v[160:161], v[174:175]
	v_pk_add_f32 v[116:117], v[164:165], v[186:187]
	v_add_f32_e64 v118, v176, v212
	v_pk_add_f32 v[120:121], v[180:181], v[214:215]
	v_pk_add_f32 v[122:123], v[184:185], v[216:217]
	v_add_f32_e64 v124, v188, v218
	v_pk_fma_f32 v[130:131], v[68:69], v[2:3], v[120:121] op_sel_hi:[0,1,1]
	v_pk_fma_f32 v[134:135], v[68:69], v[46:47], v[122:123] op_sel_hi:[0,1,1]
	v_fma_f32 v138, v68, v72, v124
	v_pk_fma_f32 v[148:149], v[80:81], v[2:3], v[120:121] op_sel_hi:[0,1,1]
	v_pk_fma_f32 v[150:151], v[80:81], v[46:47], v[122:123] op_sel_hi:[0,1,1]
	v_fma_f32 v156, v80, v72, v124
	v_pk_fma_f32 v[130:131], v[68:69], v[76:77], v[130:131] op_sel:[1,0,0]
	v_pk_fma_f32 v[134:135], v[68:69], v[106:107], v[134:135] op_sel:[1,0,0]
	v_fma_f32 v138, v69, v108, v138
	v_pk_fma_f32 v[148:149], v[80:81], v[76:77], v[148:149] op_sel:[1,0,0]
	v_pk_fma_f32 v[150:151], v[80:81], v[106:107], v[150:151] op_sel:[1,0,0]
	v_fma_f32 v156, v81, v108, v156
	v_pk_fma_f32 v[130:131], v[70:71], v[114:115], v[130:131] op_sel_hi:[0,1,1]
	v_pk_fma_f32 v[134:135], v[70:71], v[116:117], v[134:135] op_sel_hi:[0,1,1]
	v_fma_f32 v138, v70, v118, v138
	v_pk_fma_f32 v[148:149], v[82:83], v[114:115], v[148:149] op_sel_hi:[0,1,1]
	v_pk_fma_f32 v[150:151], v[82:83], v[116:117], v[150:151] op_sel_hi:[0,1,1]
	v_fma_f32 v156, v82, v118, v156
	v_pk_fma_f32 v[120:121], v[32:33], v[2:3], v[120:121] op_sel_hi:[0,1,1]
	v_pk_fma_f32 v[122:123], v[32:33], v[46:47], v[122:123] op_sel_hi:[0,1,1]
	v_fma_f32 v124, v32, v72, v124
	v_pk_fma_f32 v[120:121], v[32:33], v[76:77], v[120:121] op_sel:[1,0,0]
	v_pk_fma_f32 v[122:123], v[32:33], v[106:107], v[122:123] op_sel:[1,0,0]
	v_fma_f32 v124, v33, v108, v124
	v_pk_fma_f32 v[120:121], v[34:35], v[114:115], v[120:121] op_sel_hi:[0,1,1]
	v_pk_fma_f32 v[122:123], v[34:35], v[116:117], v[122:123] op_sel_hi:[0,1,1]
	v_fma_f32 v124, v34, v118, v124
	v_cndmask_b32_e64 v160, 0, v1, s[10:11]
	v_cndmask_b32_e64 v161, 0, v1, s[14:15]
	v_cndmask_b32_e64 v164, 0, v1, s[20:21]
	v_cndmask_b32_e64 v165, 0, v1, s[22:23]
	v_cndmask_b32_e64 v176, 0, v1, s[30:31]
	v_add_f32_dpp v120, v130, v120 wave_shl:1 row_mask:0xf bank_mask:0xf bound_ctrl:1
	v_add_f32_dpp v121, v131, v121 wave_shl:1 row_mask:0xf bank_mask:0xf bound_ctrl:1
	v_add_f32_dpp v122, v134, v122 wave_shl:1 row_mask:0xf bank_mask:0xf bound_ctrl:1
	v_add_f32_dpp v123, v135, v123 wave_shl:1 row_mask:0xf bank_mask:0xf bound_ctrl:1
	v_add_f32_dpp v124, v138, v124 wave_shl:1 row_mask:0xf bank_mask:0xf bound_ctrl:1
	s_add_i32 s4, s34, 9
	s_cmpk_lt_i32 s4, 0x201
	s_cselect_b64 s[12:13], s[0:1], 0
	v_add_f32_dpp v120, v148, v120 wave_shr:1 row_mask:0xf bank_mask:0xf bound_ctrl:1
	v_add_f32_dpp v121, v149, v121 wave_shr:1 row_mask:0xf bank_mask:0xf bound_ctrl:1
	v_add_f32_dpp v122, v150, v122 wave_shr:1 row_mask:0xf bank_mask:0xf bound_ctrl:1
	v_add_f32_dpp v123, v151, v123 wave_shr:1 row_mask:0xf bank_mask:0xf bound_ctrl:1
	v_add_f32_dpp v124, v156, v124 wave_shr:1 row_mask:0xf bank_mask:0xf bound_ctrl:1
	v_pk_fma_f32 v[120:121], v[12:13], v[194:195], v[120:121] op_sel_hi:[1,0,1] neg_lo:[0,0,1] neg_hi:[0,0,1]
	v_pk_fma_f32 v[122:123], v[14:15], v[194:195], v[122:123] op_sel_hi:[1,0,1] neg_lo:[0,0,1] neg_hi:[0,0,1]
	v_fma_f32 v124, v16, v194, -v124
	v_pk_add_f32 v[120:121], v[120:121], v[160:161] neg_lo:[0,1] neg_hi:[0,1]
	v_pk_add_f32 v[122:123], v[122:123], v[164:165] neg_lo:[0,1] neg_hi:[0,1]
	v_add_f32_e64 v124, v124, -v176
	v_pk_mul_f32 v[180:181], v[120:121], v[120:121]
	v_pk_fma_f32 v[180:181], v[122:123], v[122:123], v[180:181]
	v_add_f32_e32 v180, v180, v181
	v_fma_f32 v180, v124, v124, v180
	v_cndmask_b32_e64 v181, 0, v180, s[12:13]
	v_add_f32_e32 v0, v0, v181

	.amdhsa_kernel _Z16closed_form_mainPKfS0_PKiPf
		.amdhsa_group_segment_fixed_size 6144
		.amdhsa_private_segment_fixed_size 0
		.amdhsa_kernarg_size 32
		.amdhsa_user_sgpr_count 2
		.amdhsa_user_sgpr_dispatch_ptr 0
		.amdhsa_user_sgpr_queue_ptr 0
		.amdhsa_user_sgpr_kernarg_segment_ptr 1
		.amdhsa_user_sgpr_dispatch_id 0
		.amdhsa_user_sgpr_kernarg_preload_length 0
		.amdhsa_user_sgpr_kernarg_preload_offset 0
		.amdhsa_user_sgpr_private_segment_size 0
		.amdhsa_uses_dynamic_stack 0
		.amdhsa_enable_private_segment 0
		.amdhsa_system_sgpr_workgroup_id_x 1
		.amdhsa_system_sgpr_workgroup_id_y 0
		.amdhsa_system_sgpr_workgroup_id_z 0
		.amdhsa_system_sgpr_workgroup_info 0
		.amdhsa_system_vgpr_workitem_id 0
		.amdhsa_next_free_vgpr 240
		.amdhsa_next_free_sgpr 48
		.amdhsa_accum_offset 240
		.amdhsa_reserve_vcc 1
		.amdhsa_float_round_mode_32 0
		.amdhsa_float_round_mode_16_64 0
		.amdhsa_float_denorm_mode_32 3
		.amdhsa_float_denorm_mode_16_64 3
		.amdhsa_dx10_clamp 1
		.amdhsa_ieee_mode 1
		.amdhsa_fp16_overflow 0
		.amdhsa_tg_split 0
		.amdhsa_exception_fp_ieee_invalid_op 0
		.amdhsa_exception_fp_denorm_src 0
		.amdhsa_exception_fp_ieee_div_zero 0
		.amdhsa_exception_fp_ieee_overflow 0
		.amdhsa_exception_fp_ieee_underflow 0
		.amdhsa_exception_fp_ieee_inexact 0
		.amdhsa_exception_int_div_zero 0
	.end_amdhsa_kernel

amdhsa.kernels:
  - .agpr_count:     0
    .args:
      - .address_space:  global
        .offset:         0
        .size:           8
        .value_kind:     global_buffer
      - .address_space:  global
        .offset:         8
        .size:           8
        .value_kind:     global_buffer
      - .address_space:  global
        .offset:         16
        .size:           8
        .value_kind:     global_buffer
      - .address_space:  global
        .offset:         24
        .size:           8
        .value_kind:     global_buffer
    .group_segment_fixed_size: 6144
    .kernarg_segment_align: 8
    .kernarg_segment_size: 32
    .language:       OpenCL C
    .language_version:
      - 2
      - 0
    .max_flat_workgroup_size: 128
    .name:           _Z16closed_form_mainPKfS0_PKiPf
    .private_segment_fixed_size: 0
    .sgpr_count:     54
    .sgpr_spill_count: 0
    .symbol:         _Z16closed_form_mainPKfS0_PKiPf.kd
    .uniform_work_group_size: 1
    .uses_dynamic_stack: false
    .vgpr_count:     240
    .vgpr_spill_count: 0
    .wavefront_size: 64
  - .agpr_count:     0
    .args:
      - .actual_access:  read_only
        .address_space:  global
        .offset:         0
        .size:           8
        .value_kind:     global_buffer
      - .actual_access:  write_only
        .address_space:  global
        .offset:         8
        .size:           8
        .value_kind:     global_buffer
    .group_segment_fixed_size: 0
    .kernarg_segment_align: 8
    .kernarg_segment_size: 16
    .language:       OpenCL C
    .language_version:
      - 2
      - 0
    .max_flat_workgroup_size: 64
    .name:           _Z17closed_form_finalPK15HIP_vector_typeIfLj4EEPf
    .private_segment_fixed_size: 0
    .sgpr_count:     10
    .sgpr_spill_count: 0
    .symbol:         _Z17closed_form_finalPK15HIP_vector_typeIfLj4EEPf.kd
    .uniform_work_group_size: 1
    .uses_dynamic_stack: false
    .vgpr_count:     36
    .vgpr_spill_count: 0
    .wavefront_size: 64
